# plus ph_lo/ph_hi and ws pointer kept in spare SGPRs (removes 180 kernarg scalar loads from phase gates)
# baseline (speedup 1.0000x reference)
; #define LAS __attribute__((address_space(3)))
; __device__ __forceinline__ int otid() { int t = threadIdx.x; asm volatile("" : "+v"(t)); return t; }
; __device__ __forceinline__ unsigned xb_add(unsigned* p, unsigned v) { return __hip_atomic_fetch_add(p, v, __ATOMIC_RELAXED, __HIP_MEMORY_SCOPE_AGENT); }
; __device__ __forceinline__ unsigned xb_xcc_id() { return (unsigned)__builtin_amdgcn_s_getreg((3 << 11) | 20) & 0xFu; }
; __device__ __forceinline__ CArgs* fresh_args() { CArgs* p = (CArgs*)__builtin_amdgcn_kernarg_segment_ptr(); asm volatile("" : "+s"(p)); return p; }
; __device__ __forceinline__ XcdBarrier xcd_barrier_post(unsigned* bar, volatile LAS unsigned* st) {
;     XcdBarrier b; b.bar = bar; b.x = xb_xcc_id(); b.st = st;
;     if (otid() == 0) (void)xb_add(&bar[XB_XCNT(b.x)], 1u);
;     return b;
; __global__ void __launch_bounds__(NTHREADS, 2) fwd_kernel(const Args A_unused) {
;     ...
;     { volatile LAS unsigned* MISC = (volatile LAS unsigned*)(lds + LDS_TAB);
;       const int t0 = otid(); if (t0 < 64) MISC[t0] = 0u;
;       __syncthreads();
;       CArgs* A0 = fresh_args();
;       if (A0->ph_hi - A0->ph_lo > 1) (void)xcd_barrier_post((unsigned*)(A0->ws + WS_CTL) + CW_BAR, MISC + 8); }
.Lzc_done:
	s_load_dwordx2 s[100:101], s[0:1], 0xd8
	s_load_dwordx2 s[98:99], s[0:1], 0xd0
	s_load_dwordx2 s[2:3], s[0:1], 0xd8
	s_waitcnt lgkmcnt(0)
	s_sub_i32 s2, s3, s2
	s_cmp_lt_i32 s2, 2
	s_cbranch_scc1 .LBB0_7
	v_mov_b32_e32 v1, v0
	s_getreg_b32 s6, hwreg(HW_REG_XCC_ID, 0, 4)
	s_nop 0
	v_cmp_eq_u32_e32 vcc, 0, v1
	s_and_saveexec_b64 s[2:3], vcc
	s_cbranch_execz .LBB0_6
	s_mov_b64 s[4:5], exec
	v_mbcnt_lo_u32_b32 v1, s4, 0
	v_mbcnt_hi_u32_b32 v1, s5, v1
	v_cmp_eq_u32_e32 vcc, 0, v1
	s_and_b64 s[8:9], exec, vcc
	s_mov_b64 exec, s[8:9]
	s_cbranch_execz .LBB0_6
	s_mov_b64 s[0:1], s[98:99]
	s_lshl_b32 s6, s6, 8
	s_and_b32 s6, s6, 0xf00
	v_mov_b32_e32 v1, 0x4000
	s_waitcnt lgkmcnt(0)
	s_add_u32 s0, s0, s6
	s_addc_u32 s1, s1, 0
	s_bcnt1_i32_b64 s4, s[4:5]
	v_mov_b32_e32 v2, s4
	global_atomic_add v1, v2, s[0:1] offset:1024

; #define LAS __attribute__((address_space(3)))
; __device__ __forceinline__ void prologue_phase(CArgs& A, LAS unsigned char* lds, int vcu, int G) {
;     int tid = threadIdx.x; asm volatile("" : "+v"(tid));
;     const int lane = tid & 63, wave = __builtin_amdgcn_readfirstlane(tid >> 6);
;     const int gw = vcu * NWAVES + wave, NGW = G * NWAVES;
;     unsigned char* ws = A.ws;
;     LAS unsigned* scr = (LAS unsigned*)(lds + wave * 8320);
;     if (blockIdx.x < DEPTH * (NMOD * DM / 256)) {
;         constexpr int NJ = NMOD * DM / 256;
;         const int l = blockIdx.x / NJ, jc = blockIdx.x % NJ;
;         float* modacc = (float*)(ws + WS_CTL) + CW_MOD;
;         const float* w = A.in[I_WADA] + ((size_t)l * DM + wave * 256) * (NMOD * DM) + jc * 256 + lane * 4;
.LBB0_7:
	s_ashr_i32 s0, s95, 31
	v_writelane_b32 v255, s0, 2
	s_lshr_b32 s0, s0, 29
	v_readlane_b32 s24, v255, 0
	v_readlane_b32 s25, v255, 1
	s_add_i32 s2, s95, s0
	s_mov_b64 s[0:1], s[24:25]
	s_mov_b32 s0, s100
	s_ashr_i32 s96, s2, 3
	v_writelane_b32 v255, s2, 4
	s_lshl_b32 s2, s95, 5
	s_mul_i32 s1, s96, 0xffffff01
	s_add_i32 s97, s1, s2
	v_writelane_b32 v255, s2, 5
	s_waitcnt lgkmcnt(0)
	s_cmp_gt_i32 s0, 0
	s_cbranch_scc1 .LBB0_409
	s_mov_b64 s[0:1], s[24:25]
	s_mov_b32 s0, s101
	s_waitcnt lgkmcnt(0)
	s_cmp_lt_i32 s0, 1
	s_cbranch_scc1 .LBB0_409
	s_mov_b64 s[16:17], s[24:25]
	v_mov_b32_e32 v1, v0
	s_mov_b64 s[18:19], s[98:99]
	v_and_b32_e32 v108, 63, v1
	v_ashrrev_i32_e32 v138, 6, v1
	s_cmpk_gt_u32 s95, 0x5f
	v_readfirstlane_b32 s46, v138
	v_lshlrev_b32_e32 v2, 4, v108
	s_cbranch_scc1 .LBB0_13
	s_cmp_gt_u32 s95, 47
	s_cselect_b64 s[2:3], -1, 0
	s_lshl_b32 s0, s95, 8
	s_add_i32 s1, s0, 0xffffd000
	s_cmp_lt_u32 s95, 48
	s_cselect_b32 s0, s0, s1
	s_and_b64 s[4:5], s[2:3], exec
	s_cselect_b32 s10, 0x800, 0
	s_lshl_b32 s8, s46, 8
	s_ashr_i32 s9, s8, 31
	s_load_dwordx2 s[4:5], s[16:17], 0x8
	s_load_dwordx2 s[6:7], s[16:17], 0x18
	s_add_u32 s10, s10, s8
	s_addc_u32 s11, 0, s9
	s_mul_i32 s11, s11, 0xc000
	s_mul_hi_u32 s12, s10, 0xc000
	s_add_i32 s11, s12, s11
	s_lshl_b64 s[8:9], s[8:9], 2
	s_mov_b32 s1, 0
	s_waitcnt lgkmcnt(0)
	s_add_u32 s12, s4, s8
	s_addc_u32 s13, s5, s9
	s_lshl_b64 s[4:5], s[0:1], 2
	s_add_u32 s0, s6, s4
	s_mul_i32 s10, s10, 0xc000
	s_addc_u32 s1, s7, s5
	s_add_u32 s0, s0, s10
	v_mov_b32_e32 v3, 0
	s_addc_u32 s1, s1, s11
	v_lshl_add_u64 v[4:5], s[0:1], 0, v[2:3]
	s_mov_b64 s[0:1], 0x54000
	v_lshl_add_u64 v[12:13], v[4:5], 0, s[0:1]
	s_mov_b64 s[6:7], 0
	v_mov_b32_e32 v14, 0x2000
	s_mov_b32 s14, 0xfffb8000
	s_mov_b32 s15, 0xfffc4000
	s_mov_b32 s20, 0xfffd0000
	s_mov_b32 s21, 0xfffdc000
	s_mov_b32 s22, 0xfffe8000
	s_mov_b32 s23, 0xffff4000
	s_mov_b64 s[8:9], 0x60000
	v_mov_b32_e32 v4, 0
	v_mov_b32_e32 v5, v3
	v_mov_b32_e32 v6, 0
	v_mov_b32_e32 v7, v3
	v_mov_b32_e32 v8, 0
	v_mov_b32_e32 v9, v3
	v_mov_b32_e32 v10, 0
	v_mov_b32_e32 v11, v3

; __device__ __forceinline__ int otid() { int t = threadIdx.x; asm volatile("" : "+v"(t)); return t; }
; __device__ __forceinline__ unsigned xb_ld(unsigned* p)              { return __hip_atomic_load(p, __ATOMIC_RELAXED, __HIP_MEMORY_SCOPE_AGENT); }
; __device__ __forceinline__ unsigned xb_add(unsigned* p, unsigned v) { return __hip_atomic_fetch_add(p, v, __ATOMIC_RELAXED, __HIP_MEMORY_SCOPE_AGENT); }
; __device__ __forceinline__ void xcd_barrier_complete(unsigned* bar, unsigned x, unsigned& nloc, unsigned& nx) {
;     const unsigned G = gridDim.x * gridDim.y * gridDim.z;
;     unsigned sum, cnt, mine, sp = 0u;
;     for (;;) {
;         sum = 0u; cnt = 0u; mine = 0u;
; #pragma unroll
;         for (unsigned j = 0; j < 16; ++j) { const unsigned c = xb_ld(&bar[XB_XCNT(j)]); sum += c; cnt += (c > 0u) ? 1u : 0u; mine = (j == x) ? c : mine; }
;         if (sum == G) break;
;         __builtin_amdgcn_s_sleep(1);
;         if ((++sp & 255u) == 0u) { if (xb_ld(&bar[XB_TMO])) break; if (sp > XB_SPIN_CAP) { atomicAdd(&bar[XB_TMO], 1u); break; } }
;     }
;     nloc = mine > 0u ? mine : 1u; nx = cnt > 0u ? cnt : 1u;
; }
; __device__ __forceinline__ void xcd_barrier(const XcdBarrier& b) {
;     asm volatile("s_waitcnt vmcnt(0)" ::: "memory");
;     __syncthreads();
;     if (otid() == 0) {
;         unsigned* bar = b.bar;
;         __builtin_amdgcn_s_waitcnt(0);
;         unsigned nloc = b.st[0], nx = b.st[1];
;         if (nloc == 0u) { xcd_barrier_complete(bar, b.x, nloc, nx); b.st[0] = nloc; b.st[1] = nx; }
;         const unsigned old = xb_add(&bar[XB_XSUB(b.x)], 1u);
;         const unsigned gen = old / nloc;
;         if (old + 1u == (gen + 1u) * nloc) {
;             __builtin_amdgcn_fence(__ATOMIC_RELEASE, "agent");
;             asm volatile("s_waitcnt vmcnt(0)" ::: "memory");
;             const unsigned og = xb_add(&bar[XB_TOP], 1u);
.LBB0_409:
	s_mov_b64 s[0:1], s[24:25]
	s_mov_b32 s0, s100
	s_waitcnt lgkmcnt(0)
	s_cmp_gt_i32 s0, 0
	s_cbranch_scc1 .LBB0_467
	s_mov_b64 s[0:1], s[24:25]
	s_mov_b32 s0, s101
	s_waitcnt lgkmcnt(0)
	s_cmp_lt_i32 s0, 1
	s_cbranch_scc1 .LBB0_466
	v_readlane_b32 s0, v255, 0
	v_readlane_b32 s1, v255, 1
	s_mov_b32 s0, s100
	s_waitcnt lgkmcnt(0)
	s_cmp_gt_i32 s0, 1
	s_cbranch_scc1 .LBB0_466
	v_readlane_b32 s0, v255, 0
	v_readlane_b32 s1, v255, 1
	s_mov_b32 s0, s101
	s_waitcnt lgkmcnt(0)
	s_cmp_lt_i32 s0, 2
	s_cbranch_scc1 .LBB0_466
	v_readlane_b32 s2, v255, 0
	v_readlane_b32 s3, v255, 1
	s_getreg_b32 s4, hwreg(HW_REG_XCC_ID, 0, 4)
	s_waitcnt vmcnt(0)
	v_mov_b32_e32 v1, v0
	s_barrier
	s_nop 0
	v_cmp_eq_u32_e32 vcc, 0, v1
	s_and_saveexec_b64 s[0:1], vcc
	s_cbranch_execz .LBB0_465
	s_add_i32 s5, 0, 0x20020
	v_mov_b32_e32 v1, s5
	s_mov_b64 s[2:3], s[98:99]
	s_waitcnt vmcnt(0) expcnt(0) lgkmcnt(0)
	ds_read_b32 v3, v1
	s_add_i32 s5, 0, 0x20024
	v_mov_b32_e32 v1, s5
	ds_read_b32 v1, v1
	s_and_b32 s33, s4, 15
	s_waitcnt lgkmcnt(1)
	v_cmp_ne_u32_e32 vcc, 0, v3
	s_cbranch_vccnz .LBB0_429
	v_readlane_b32 s4, v255, 0
	v_readlane_b32 s5, v255, 1
	s_load_dwordx2 s[8:9], s[4:5], 0xe0
	s_load_dword s7, s[4:5], 0xe8
	s_add_u32 s4, s2, 0x4200
	s_addc_u32 s5, s3, 0
	s_add_u32 s6, s2, 0x4400
	s_waitcnt lgkmcnt(0)
	s_mul_i32 s46, s9, s8
	s_mul_i32 s46, s46, s7
	s_addc_u32 s7, s3, 0
	s_add_u32 s8, s2, 0x4500
	s_addc_u32 s9, s3, 0
	s_add_u32 s10, s2, 0x4600
	s_addc_u32 s11, s3, 0
	s_add_u32 s12, s2, 0x4700
	s_addc_u32 s13, s3, 0
	s_add_u32 s14, s2, 0x4800
	s_addc_u32 s15, s3, 0
	s_add_u32 s16, s2, 0x4900
	s_addc_u32 s17, s3, 0
	s_add_u32 s18, s2, 0x4a00
	s_addc_u32 s19, s3, 0
	s_add_u32 s20, s2, 0x4b00
	s_addc_u32 s21, s3, 0
	s_add_u32 s22, s2, 0x4c00
	s_addc_u32 s23, s3, 0
	s_add_u32 s24, s2, 0x4d00
	s_addc_u32 s25, s3, 0
	s_add_u32 s26, s2, 0x4e00
	s_addc_u32 s27, s3, 0
	s_add_u32 s28, s2, 0x4f00
	s_addc_u32 s29, s3, 0
	s_add_u32 s30, s2, 0x5000
	s_addc_u32 s31, s3, 0
	s_add_u32 s34, s2, 0x5100
	s_addc_u32 s35, s3, 0
	s_add_u32 s36, s2, 0x5200
	s_addc_u32 s37, s3, 0
	s_add_u32 s38, s2, 0x5300
	s_addc_u32 s39, s3, 0
	s_mov_b32 s47, 1
	v_mov_b32_e32 v17, 0
	s_branch .LBB0_417

; #define REP(k) for (int rep_ = 0; rep_ < ((REP_KIND == (k)) ? REP_N : 1); ++rep_)
; #define IN(k) (fresh_args()->ph_lo <= (k) && (k) < fresh_args()->ph_hi)
; #define SEAM(k) do { if (IN(k) && IN((k) + 1)) { XcdBarrier bar; bar.bar = (unsigned*)(fresh_args()->ws + WS_CTL) + CW_BAR; bar.x = xb_xcc_id(); bar.st = (volatile LAS unsigned*)(lds + LDS_TAB) + 8; xcd_barrier(bar); } } while (0)
; #define PHASE_ARGS() CArgs* A_p = fresh_args(); CArgs& A = *A_p; unsigned char* ws = A.ws; (void)ws;
; __device__ __forceinline__ void row_norm_mod_store(const Row& x, const float* g, ModPtr sh, ModPtr sc, bf16* hrow, int lane, unsigned char* h8row = nullptr) {
;     const float rstd = row_rstd(x);
;     Row o;
; #pragma unroll
;     for (int j = 0; j < 4; ++j) { const int c0 = 512 * j + 8 * lane;
; #pragma unroll
;         for (int q4 = 0; q4 < 2; ++q4) { const int c = c0 + 4 * q4;
;             const f32x4 gv = *(const f32x4*)(g + c), sa = *(const f32x4*)(sh.acc + c), ca = *(const f32x4*)(sc.acc + c);
; #pragma unroll
;             for (int q = 0; q < 4; ++q) o.v[j][4 * q4 + q] = (x.v[j][4 * q4 + q] * rstd * gv[q]) * (1.0f + ca[q]) + sa[q]; }
;         asm volatile("" ::: "memory"); }
;     if (hrow) row_store_bf16(o, hrow, lane);
;     if (h8row) {
; #pragma unroll
;         for (int j = 0; j < 4; ++j) *(u32x2*)(h8row + 512 * j + 8 * lane) = pack8_fp8((f32x4){o.v[j][0], o.v[j][1], o.v[j][2], o.v[j][3]}, (f32x4){o.v[j][4], o.v[j][5], o.v[j][6], o.v[j][7]}); }
; }
; __device__ __forceinline__ void norm_mod_phase(CArgs& A, const float* xin, const float* g, int l, int wsh, int wsc, int vcu, int G) {
;     int tid = threadIdx.x; asm volatile("" : "+v"(tid));
;     const int lane = tid & 63, wave = __builtin_amdgcn_readfirstlane(tid >> 6);
;     bf16* H = (bf16*)(A.ws + WS_H);
;     for (int t = vcu * NWAVES + wave; t < NT; t += G * NWAVES) {
;         const int b = t / SEQ; Row x; row_load_f32(x, xin + (size_t)t * DM, lane);
;         row_norm_mod_store(x, g, mod_ptr(A, l, b, wsh), mod_ptr(A, l, b, wsc), H + (size_t)t * DM, lane, A.ws + WS_H8 + (size_t)t * DM);
;     }
; }
; __global__ void __launch_bounds__(NTHREADS, 2) fwd_kernel(const Args A_unused) {
;     ...
;     if (KEN(1) && IN(1)) REP(1) { PHASE_ARGS(); norm_mod_phase(A, A.in[I_X], A.in[I_GMIX], 0, 0, 1, vcu, G); } SEAM(1);
.LBB0_467:
	s_mov_b64 s[0:1], s[24:25]
	s_mov_b32 s0, s100
	s_waitcnt lgkmcnt(0)
	s_cmp_gt_i32 s0, 1
	s_cbranch_scc1 .LBB0_473
	s_mov_b64 s[0:1], s[24:25]
	s_mov_b32 s0, s101
	s_waitcnt lgkmcnt(0)
	s_cmp_lt_i32 s0, 2
	s_cbranch_scc1 .LBB0_472
	v_readlane_b32 s4, v255, 0
	v_readlane_b32 s5, v255, 1
	v_mov_b32_e32 v1, v0
	s_lshl_b32 s0, s97, 3
	v_readfirstlane_b32 s1, v1
	s_ashr_i32 s1, s1, 6
	s_add_i32 s0, s1, s0
	s_cmpk_gt_i32 s0, 0x1fff
	s_cbranch_scc1 .LBB0_472
	s_load_dwordx2 s[6:7], s[4:5], 0x0
	s_mov_b64 s[2:3], s[98:99]
	s_load_dwordx2 s[8:9], s[4:5], 0x28
	v_lshlrev_b32_e32 v2, 3, v1
	v_and_b32_e32 v2, 0x1f8, v2
	v_mov_b32_e32 v5, 0
	s_waitcnt lgkmcnt(0)
	s_add_u32 s10, s2, 0x10000
	s_addc_u32 s11, s3, 0
	v_lshlrev_b32_e32 v4, 2, v2
	v_or_b32_e32 v8, 0x400, v2
	s_ashr_i32 s1, s0, 31
	v_lshl_add_u64 v[42:43], s[8:9], 0, v[4:5]
	v_lshlrev_b32_e32 v4, 2, v8
	v_or_b32_e32 v10, 0x600, v2
	s_lshl_b64 s[4:5], s[0:1], 13
	v_lshl_add_u64 v[44:45], s[8:9], 0, v[4:5]
	v_lshlrev_b32_e32 v4, 2, v10
	v_and_b32_e32 v1, 63, v1
	s_add_u32 s4, s6, s4
	v_lshl_add_u64 v[46:47], s[8:9], 0, v[4:5]
	v_lshlrev_b32_e32 v4, 5, v1
	s_addc_u32 s5, s7, s5
	v_lshl_add_u64 v[4:5], s[4:5], 0, v[4:5]
	s_mov_b64 s[4:5], 0x1000
	v_lshl_add_u64 v[48:49], v[4:5], 0, s[4:5]
	s_lshl_b64 s[4:5], s[0:1], 11
	v_or_b32_e32 v6, 0x200, v2
	v_or_b32_e32 v50, s4, v2
	v_mov_b32_e32 v51, s5
	s_lshl_b64 s[4:5], s[0:1], 12
	v_lshl_or_b32 v52, v1, 4, s4
	v_mov_b32_e32 v53, s5
	v_mov_b32_e32 v1, 0x358637bd
	s_mov_b32 s1, 0x800000
	v_lshlrev_b32_e32 v64, 2, v2
	v_lshlrev_b32_e32 v65, 2, v6
	v_lshlrev_b32_e32 v66, 2, v8
	v_lshlrev_b32_e32 v67, 2, v10
	s_mov_b32 s12, 0x3c400000
	s_mov_b32 s13, 0x30c00000
	s_mov_b64 s[4:5], 0x1000000
	s_mov_b64 s[6:7], 0x400000
	s_mov_b64 s[8:9], 0x800000

; __device__ __forceinline__ int otid() { int t = threadIdx.x; asm volatile("" : "+v"(t)); return t; }
; __device__ __forceinline__ unsigned xb_ld(unsigned* p)              { return __hip_atomic_load(p, __ATOMIC_RELAXED, __HIP_MEMORY_SCOPE_AGENT); }
; __device__ __forceinline__ unsigned xb_add(unsigned* p, unsigned v) { return __hip_atomic_fetch_add(p, v, __ATOMIC_RELAXED, __HIP_MEMORY_SCOPE_AGENT); }
; __device__ __forceinline__ void xcd_barrier_complete(unsigned* bar, unsigned x, unsigned& nloc, unsigned& nx) {
;     const unsigned G = gridDim.x * gridDim.y * gridDim.z;
;     unsigned sum, cnt, mine, sp = 0u;
;     for (;;) {
;         sum = 0u; cnt = 0u; mine = 0u;
; #pragma unroll
;         for (unsigned j = 0; j < 16; ++j) { const unsigned c = xb_ld(&bar[XB_XCNT(j)]); sum += c; cnt += (c > 0u) ? 1u : 0u; mine = (j == x) ? c : mine; }
;         if (sum == G) break;
;         __builtin_amdgcn_s_sleep(1);
;         if ((++sp & 255u) == 0u) { if (xb_ld(&bar[XB_TMO])) break; if (sp > XB_SPIN_CAP) { atomicAdd(&bar[XB_TMO], 1u); break; } }
;     }
;     nloc = mine > 0u ? mine : 1u; nx = cnt > 0u ? cnt : 1u;
; }
; __device__ __forceinline__ void xcd_barrier(const XcdBarrier& b) {
;     asm volatile("s_waitcnt vmcnt(0)" ::: "memory");
;     __syncthreads();
;     if (otid() == 0) {
;         unsigned* bar = b.bar;
;         __builtin_amdgcn_s_waitcnt(0);
;         unsigned nloc = b.st[0], nx = b.st[1];
;         if (nloc == 0u) { xcd_barrier_complete(bar, b.x, nloc, nx); b.st[0] = nloc; b.st[1] = nx; }
;         const unsigned old = xb_add(&bar[XB_XSUB(b.x)], 1u);
;         const unsigned gen = old / nloc;
;         if (old + 1u == (gen + 1u) * nloc) {
;             __builtin_amdgcn_fence(__ATOMIC_RELEASE, "agent");
;             asm volatile("s_waitcnt vmcnt(0)" ::: "memory");
;             const unsigned og = xb_add(&bar[XB_TOP], 1u);
.LBB0_473:
	s_mov_b64 s[0:1], s[24:25]
	s_mov_b32 s0, s100
	s_waitcnt lgkmcnt(0)
	s_cmp_gt_i32 s0, 1
	s_cbranch_scc1 .LBB0_531
	s_mov_b64 s[0:1], s[24:25]
	s_mov_b32 s0, s101
	s_waitcnt lgkmcnt(0)
	s_cmp_lt_i32 s0, 2
	s_cbranch_scc1 .LBB0_530
	v_readlane_b32 s0, v255, 0
	v_readlane_b32 s1, v255, 1
	s_mov_b32 s0, s100
	s_waitcnt lgkmcnt(0)
	s_cmp_gt_i32 s0, 2
	s_cbranch_scc1 .LBB0_530
	v_readlane_b32 s0, v255, 0
	v_readlane_b32 s1, v255, 1
	s_mov_b32 s0, s101
	s_waitcnt lgkmcnt(0)
	s_cmp_lt_i32 s0, 3
	s_cbranch_scc1 .LBB0_530
	v_readlane_b32 s2, v255, 0
	v_readlane_b32 s3, v255, 1
	s_getreg_b32 s4, hwreg(HW_REG_XCC_ID, 0, 4)
	s_waitcnt vmcnt(0)
	v_mov_b32_e32 v1, v0
	s_barrier
	s_nop 0
	v_cmp_eq_u32_e32 vcc, 0, v1
	s_and_saveexec_b64 s[0:1], vcc
	s_cbranch_execz .LBB0_529
	s_add_i32 s5, 0, 0x20020
	v_mov_b32_e32 v1, s5
	s_mov_b64 s[2:3], s[98:99]
	s_waitcnt vmcnt(0) expcnt(0) lgkmcnt(0)
	ds_read_b32 v3, v1
	s_add_i32 s5, 0, 0x20024
	v_mov_b32_e32 v1, s5
	ds_read_b32 v1, v1
	s_and_b32 s33, s4, 15
	s_waitcnt lgkmcnt(1)
	v_cmp_ne_u32_e32 vcc, 0, v3
	s_cbranch_vccnz .LBB0_493
	v_readlane_b32 s4, v255, 0
	v_readlane_b32 s5, v255, 1
	s_load_dwordx2 s[8:9], s[4:5], 0xe0
	s_load_dword s7, s[4:5], 0xe8
	s_add_u32 s4, s2, 0x4200
	s_addc_u32 s5, s3, 0
	s_add_u32 s6, s2, 0x4400
	s_waitcnt lgkmcnt(0)
	s_mul_i32 s46, s9, s8
	s_mul_i32 s46, s46, s7
	s_addc_u32 s7, s3, 0
	s_add_u32 s8, s2, 0x4500
	s_addc_u32 s9, s3, 0
	s_add_u32 s10, s2, 0x4600
	s_addc_u32 s11, s3, 0
	s_add_u32 s12, s2, 0x4700
	s_addc_u32 s13, s3, 0
	s_add_u32 s14, s2, 0x4800
	s_addc_u32 s15, s3, 0
	s_add_u32 s16, s2, 0x4900
	s_addc_u32 s17, s3, 0
	s_add_u32 s18, s2, 0x4a00
	s_addc_u32 s19, s3, 0
	s_add_u32 s20, s2, 0x4b00
	s_addc_u32 s21, s3, 0
	s_add_u32 s22, s2, 0x4c00
	s_addc_u32 s23, s3, 0
	s_add_u32 s24, s2, 0x4d00
	s_addc_u32 s25, s3, 0
	s_add_u32 s26, s2, 0x4e00
	s_addc_u32 s27, s3, 0
	s_add_u32 s28, s2, 0x4f00
	s_addc_u32 s29, s3, 0
	s_add_u32 s30, s2, 0x5000
	s_addc_u32 s31, s3, 0
	s_add_u32 s34, s2, 0x5100
	s_addc_u32 s35, s3, 0
	s_add_u32 s36, s2, 0x5200
	s_addc_u32 s37, s3, 0
	s_add_u32 s38, s2, 0x5300
	s_addc_u32 s39, s3, 0
	s_mov_b32 s47, 1
	v_mov_b32_e32 v17, 0
	s_branch .LBB0_481

; template <class P, class MK = NoChain>
; __device__ __forceinline__ void gemm_phase(LAS unsigned char* lds, const P& p, const MK& mk = MK(), bool chain_out = false, bool chained_in = false) {
;     ...
;     int tid = threadIdx.x; asm volatile("" : "+v"(tid));
;     const int wid = __builtin_amdgcn_readfirstlane(tid >> 6), lane = tid & 63, wr = wid >> 2, wc = wid & 3, fr = lane & 15, fq = lane >> 4;
;     unsigned voffB[2], vA[2][2], nvA[2][2], nvB[2]; typedef decltype(mk()) NP; constexpr int NES = NP::FP8 ? 1 : 2; constexpr int NBMODE = bmode_of<NP>::value; constexpr size_t nhstepB = (size_t)(NBMODE == 1 ? 8 : (NBMODE == 2 ? 16 : HALF)) * NP::LDB * NES;
;     constexpr size_t kstep = (size_t)(BK * 2);
;     constexpr int BMODE = bmode_of<P>::value;
;     constexpr size_t hstep = (size_t)(BMODE == 1 ? 8 : (BMODE == 2 ? 16 : HALF)) * LDB * ES, hstepA = (size_t)HALF * LDA * ES;
; #pragma unroll
;     for (int i = 0; i < 2; ++i) { int R, C; stage_rc(tid * 16 + i * 8192, R, C); const int rho_ = R & 31;
;         const int fq_ = (rho_ & 15) >> 2, n_ = rho_ >> 4, q_ = rho_ & 3;
;         const int Rb = BMODE == 1 ? ((R >> 5) * 64 + fq_ * 16 + 4 * n_ + q_) : (BMODE == 2 ? ((R >> 5) * 64 + 32 * (fq_ >> 1) + 8 * n_ + 4 * (fq_ & 1) + q_) : (P::PERM ? ((R & ~31) + perm32(R & 31)) : R));
;         voffB[i] = (unsigned)(Rb * LDB * ES + C * 2); vA[0][i] = (unsigned)(R * LDA * ES + C * 2); vA[1][i] = vA[0][i] + (unsigned)hstepA; nvA[0][i] = vA[0][i]; nvA[1][i] = vA[1][i]; nvB[i] = voffB[i]; }
;     const unsigned ldsw = (unsigned)wid * 1024u;
;     const int aoff = lds_byte(wr * 64 + fr, fq * 8), boff = lds_byte(wc * 32 + fr, fq * 8); const int aoff1 = aoff ^ 64, boff1 = boff ^ 64;
;     ...
;     Unit cur, nxt; int ui = 0;
;     if (!p.next(0, cur)) return;
;     Acc acc;
;     if constexpr (!PEEL) {
; #pragma unroll
;     for (int a = 0; a < 2; ++a)
; #pragma unroll
;         for (int b = 0; b < 2; ++b)
; #pragma unroll
;             for (int m = 0; m < 4; ++m)
; #pragma unroll
;                 for (int n = 0; n < 2; ++n) { typedef double d2_ __attribute__((ext_vector_type(2))); d2_ z_; asm volatile("v_mov_b64 %0, 0" : "=v"(z_.x)); asm volatile("v_mov_b64 %0, 0" : "=v"(z_.y)); acc[a][b][m][n] = __builtin_bit_cast(f32x4, z_); }
;     }
;     typedef int v8i_ __attribute__((ext_vector_type(8))); typedef int v4i_ __attribute__((ext_vector_type(4)));
.LBB0_531:
	s_mov_b64 s[0:1], s[24:25]
	s_mov_b32 s0, s100
	s_waitcnt lgkmcnt(0)
	s_cmp_gt_i32 s0, 2
	s_cbranch_scc1 .LBB0_601
	s_mov_b64 s[0:1], s[24:25]
	s_mov_b32 s0, s101
	s_waitcnt lgkmcnt(0)
	s_cmp_lt_i32 s0, 3
	s_cbranch_scc1 .LBB0_601
	s_cmpk_lt_i32 s95, 0x400
	s_mov_b64 s[2:3], s[24:25]
	v_mov_b32_e32 v2, v0
	s_cselect_b64 s[4:5], -1, 0
	s_cmpk_gt_i32 s95, 0x3ff
	s_nop 0
	v_readfirstlane_b32 s13, v2
	s_cbranch_scc1 .LBB0_535
	v_readlane_b32 s0, v255, 4
	s_and_b32 s0, s0, -8
	s_sub_i32 s0, s95, s0
	s_lshl_b32 s6, s0, 7
	s_mul_i32 s1, s0, 0x81
	s_cmp_lt_i32 s0, 0
	s_cselect_b32 s0, s1, s6
	s_add_i32 s0, s0, s96
	s_ashr_i32 s1, s0, 31
	s_lshr_b32 s1, s1, 24
	s_add_i32 s1, s0, s1
	s_ashr_i32 s6, s1, 8
	s_and_b32 s1, s1, 0xffffff00
	s_sub_i32 s0, s0, s1
	s_sext_i32_i16 s1, s0
	s_bfe_u32 s1, s1, 0x3001c
	s_add_i32 s1, s0, s1
	s_sext_i32_i16 s7, s1
	s_and_b32 s1, s1, 0xfff8
	s_sub_i32 s0, s0, s1
	s_lshl_b32 s6, s6, 3
	s_sext_i32_i16 s0, s0
	s_add_i32 s15, s6, s0
	s_ashr_i32 s0, s7, 3
.LBB0_535:
	v_readlane_b32 s24, v255, 0
	s_andn2_b64 vcc, exec, s[4:5]
	v_readlane_b32 s25, v255, 1
	s_cbranch_vccnz .LBB0_601
	v_lshrrev_b32_e32 v3, 4, v2
	v_ashrrev_i32_e32 v4, 3, v2
	s_mov_b64 s[2:3], s[98:99]
	v_xor_b32_e32 v1, v3, v2
	v_lshlrev_b32_e32 v5, 1, v4
	v_lshrrev_b32_e32 v6, 2, v4
	v_lshlrev_b32_e32 v1, 4, v1
	v_and_b32_e32 v5, 24, v5
	v_and_b32_e32 v6, 4, v6
	v_and_b32_e32 v7, 0x1fffe3, v4
	v_and_b32_e32 v1, 0x70, v1
	v_or3_b32 v5, v7, v6, v5
	v_lshl_or_b32 v194, v5, 11, v1
	v_mov_b32_e32 v5, 0x2000
	v_lshl_add_u32 v5, v2, 4, v5
	s_waitcnt lgkmcnt(0)
	s_add_u32 s4, s2, 0x30c00000
	v_ashrrev_i32_e32 v5, 7, v5
	s_addc_u32 s5, s3, 0
	v_lshlrev_b32_e32 v6, 1, v5
	v_lshrrev_b32_e32 v7, 2, v5
	s_add_u32 s30, s2, 0x32400000
	v_and_b32_e32 v6, 24, v6
	v_and_b32_e32 v7, 4, v7
	v_and_b32_e32 v8, 0x1fffe3, v5
	s_addc_u32 s31, s3, 0
	v_or3_b32 v6, v8, v7, v6
	s_ashr_i32 s10, s13, 6
	s_ashr_i32 s1, s0, 31
	s_ashr_i32 s6, s13, 8
	v_lshl_or_b32 v196, v6, 11, v1
	s_lshl_b32 s35, s10, 10
	s_lshl_b64 s[8:9], s[0:1], 19
	v_mov_b32_e32 v6, v0
	v_mov_b64 v[186:187], 0
	v_mov_b64 v[188:189], 0
	v_mov_b64 v[190:191], 0
	v_mov_b64 v[192:193], 0
	v_mov_b64 v[174:175], 0
	v_mov_b64 v[176:177], 0
	v_mov_b64 v[170:171], 0
	v_mov_b64 v[172:173], 0
	v_mov_b64 v[158:159], 0
	v_mov_b64 v[160:161], 0
	v_mov_b64 v[154:155], 0
	v_mov_b64 v[156:157], 0
	v_mov_b64 v[142:143], 0
	v_mov_b64 v[144:145], 0
	v_mov_b64 v[138:139], 0
	v_mov_b64 v[140:141], 0
	v_mov_b64 v[182:183], 0
	v_mov_b64 v[184:185], 0
	v_mov_b64 v[178:179], 0
	v_mov_b64 v[180:181], 0
	v_mov_b64 v[166:167], 0
	v_mov_b64 v[168:169], 0
	v_mov_b64 v[162:163], 0
	v_mov_b64 v[164:165], 0
	v_mov_b64 v[150:151], 0
	v_mov_b64 v[152:153], 0
	v_mov_b64 v[146:147], 0
	v_mov_b64 v[148:149], 0
	v_mov_b64 v[134:135], 0
	v_mov_b64 v[136:137], 0
	v_mov_b64 v[130:131], 0
	v_mov_b64 v[132:133], 0
	v_mov_b64 v[126:127], 0
	v_mov_b64 v[128:129], 0
	v_mov_b64 v[122:123], 0
	v_mov_b64 v[124:125], 0
	v_mov_b64 v[110:111], 0
	v_mov_b64 v[112:113], 0
	v_mov_b64 v[106:107], 0
	v_mov_b64 v[108:109], 0
	v_mov_b64 v[94:95], 0
	v_mov_b64 v[96:97], 0
	v_mov_b64 v[90:91], 0
	v_mov_b64 v[92:93], 0
	v_mov_b64 v[78:79], 0
	v_mov_b64 v[80:81], 0
	v_mov_b64 v[74:75], 0
	v_mov_b64 v[76:77], 0
	v_mov_b64 v[118:119], 0
	v_mov_b64 v[120:121], 0
	v_mov_b64 v[114:115], 0
	v_mov_b64 v[116:117], 0
	v_mov_b64 v[102:103], 0
	v_mov_b64 v[104:105], 0
	v_mov_b64 v[98:99], 0
	v_mov_b64 v[100:101], 0
	v_mov_b64 v[86:87], 0
	v_mov_b64 v[88:89], 0
	v_mov_b64 v[82:83], 0
	v_mov_b64 v[84:85], 0
	v_mov_b64 v[70:71], 0
	v_mov_b64 v[72:73], 0
	v_mov_b64 v[66:67], 0
	v_mov_b64 v[68:69], 0
	s_add_u32 s20, s30, s8
	s_addc_u32 s21, s31, s9
	v_lshlrev_b32_e32 v7, 4, v6
	v_xor_b32_e32 v7, v7, v6
	v_lshlrev_b32_e32 v6, 8, v6
	s_add_i32 s36, s35, 0
	v_and_b32_e32 v6, 0xfffff800, v6
	s_mov_b64 s[8:9], s[20:21]
	s_add_i32 m0, s36, 0x10000
	s_movk_i32 s34, 0x70
	v_lshl_add_u32 v6, s15, 19, v6
	v_and_or_b32 v198, v7, s34, v6
	global_load_lds_dwordx4 v194, s[8:9]
	s_add_i32 m0, s36, 0x12000
	s_add_i32 s37, s36, 0x2000
	global_load_lds_dwordx4 v196, s[8:9]
	s_mov_b64 s[8:9], s[4:5]
	s_mov_b32 m0, s36
	v_add_u32_e32 v208, 0x20000, v198
	v_add_u32_e32 v212, 0x40000, v198
	global_load_lds_dwordx4 v198, s[8:9]
	s_mov_b32 m0, s37
	v_add_u32_e32 v210, 0x60000, v198
	global_load_lds_dwordx4 v208, s[8:9]
	s_add_u32 s8, s20, 0x40000
	s_addc_u32 s9, s21, 0
	s_add_i32 s38, s36, 0x14000
	s_mov_b32 m0, s38
	s_add_i32 s39, s36, 0x16000
	s_add_i32 s40, s36, 0x4000
	global_load_lds_dwordx4 v194, s[8:9]
	s_mov_b32 m0, s39
	s_add_i32 s41, s36, 0x6000
	global_load_lds_dwordx4 v196, s[8:9]
	s_mov_b64 s[8:9], s[4:5]
	s_mov_b32 m0, s40
	v_mov_b32_e32 v199, 0
	global_load_lds_dwordx4 v212, s[8:9]
	s_mov_b32 m0, s41
	s_mov_b32 s7, 0
	global_load_lds_dwordx4 v210, s[8:9]
	v_mov_b32_e32 v195, v199
	v_mov_b32_e32 v197, v199
	s_cmp_lg_u32 s6, 1
	v_mov_b32_e32 v209, v199
	s_cbranch_scc1 .LBB0_538
	s_barrier

; __device__ __forceinline__ int otid() { int t = threadIdx.x; asm volatile("" : "+v"(t)); return t; }
; __device__ __forceinline__ unsigned xb_ld(unsigned* p)              { return __hip_atomic_load(p, __ATOMIC_RELAXED, __HIP_MEMORY_SCOPE_AGENT); }
; __device__ __forceinline__ unsigned xb_add(unsigned* p, unsigned v) { return __hip_atomic_fetch_add(p, v, __ATOMIC_RELAXED, __HIP_MEMORY_SCOPE_AGENT); }
; __device__ __forceinline__ void xcd_barrier_complete(unsigned* bar, unsigned x, unsigned& nloc, unsigned& nx) {
;     const unsigned G = gridDim.x * gridDim.y * gridDim.z;
;     unsigned sum, cnt, mine, sp = 0u;
;     for (;;) {
;         sum = 0u; cnt = 0u; mine = 0u;
; #pragma unroll
;         for (unsigned j = 0; j < 16; ++j) { const unsigned c = xb_ld(&bar[XB_XCNT(j)]); sum += c; cnt += (c > 0u) ? 1u : 0u; mine = (j == x) ? c : mine; }
;         if (sum == G) break;
;         __builtin_amdgcn_s_sleep(1);
;         if ((++sp & 255u) == 0u) { if (xb_ld(&bar[XB_TMO])) break; if (sp > XB_SPIN_CAP) { atomicAdd(&bar[XB_TMO], 1u); break; } }
;     }
;     nloc = mine > 0u ? mine : 1u; nx = cnt > 0u ? cnt : 1u;
; }
; __device__ __forceinline__ void xcd_barrier(const XcdBarrier& b) {
;     asm volatile("s_waitcnt vmcnt(0)" ::: "memory");
;     __syncthreads();
;     if (otid() == 0) {
;         unsigned* bar = b.bar;
;         __builtin_amdgcn_s_waitcnt(0);
;         unsigned nloc = b.st[0], nx = b.st[1];
;         if (nloc == 0u) { xcd_barrier_complete(bar, b.x, nloc, nx); b.st[0] = nloc; b.st[1] = nx; }
;         const unsigned old = xb_add(&bar[XB_XSUB(b.x)], 1u);
;         const unsigned gen = old / nloc;
;         if (old + 1u == (gen + 1u) * nloc) {
;             __builtin_amdgcn_fence(__ATOMIC_RELEASE, "agent");
;             asm volatile("s_waitcnt vmcnt(0)" ::: "memory");
;             const unsigned og = xb_add(&bar[XB_TOP], 1u);
.LBB0_601:
	s_mov_b64 s[0:1], s[24:25]
	s_mov_b32 s0, s100
	s_waitcnt lgkmcnt(0)
	s_cmp_gt_i32 s0, 2
	s_cbranch_scc1 .LBB0_659
	s_mov_b64 s[0:1], s[24:25]
	s_mov_b32 s0, s101
	s_waitcnt lgkmcnt(0)
	s_cmp_lt_i32 s0, 3
	s_cbranch_scc1 .LBB0_658
	v_readlane_b32 s0, v255, 0
	v_readlane_b32 s1, v255, 1
	s_mov_b32 s0, s100
	s_waitcnt lgkmcnt(0)
	s_cmp_gt_i32 s0, 3
	s_cbranch_scc1 .LBB0_658
	v_readlane_b32 s0, v255, 0
	v_readlane_b32 s1, v255, 1
	s_mov_b32 s0, s101
	s_waitcnt lgkmcnt(0)
	s_cmp_lt_i32 s0, 4
	s_cbranch_scc1 .LBB0_658
	v_readlane_b32 s2, v255, 0
	v_readlane_b32 s3, v255, 1
	s_getreg_b32 s4, hwreg(HW_REG_XCC_ID, 0, 4)
	s_waitcnt vmcnt(0)
	v_mov_b32_e32 v1, v0
	s_waitcnt vmcnt(0)
	s_barrier
	s_nop 0
	v_cmp_eq_u32_e32 vcc, 0, v1
	s_and_saveexec_b64 s[0:1], vcc
	s_cbranch_execz .LBB0_657
	s_add_i32 s5, 0, 0x20020
	v_mov_b32_e32 v1, s5
	s_mov_b64 s[2:3], s[98:99]
	s_waitcnt vmcnt(0) expcnt(0) lgkmcnt(0)
	ds_read_b32 v3, v1
	s_add_i32 s5, 0, 0x20024
	v_mov_b32_e32 v1, s5
	ds_read_b32 v1, v1
	s_and_b32 s33, s4, 15
	s_waitcnt lgkmcnt(1)
	v_cmp_ne_u32_e32 vcc, 0, v3
	s_cbranch_vccnz .LBB0_621
	v_readlane_b32 s4, v255, 0
	v_readlane_b32 s5, v255, 1
	s_load_dwordx2 s[8:9], s[4:5], 0xe0
	s_load_dword s7, s[4:5], 0xe8
	s_add_u32 s4, s2, 0x4200
	s_addc_u32 s5, s3, 0
	s_add_u32 s6, s2, 0x4400
	s_waitcnt lgkmcnt(0)
	s_mul_i32 s46, s9, s8
	s_mul_i32 s46, s46, s7
	s_addc_u32 s7, s3, 0
	s_add_u32 s8, s2, 0x4500
	s_addc_u32 s9, s3, 0
	s_add_u32 s10, s2, 0x4600
	s_addc_u32 s11, s3, 0
	s_add_u32 s12, s2, 0x4700
	s_addc_u32 s13, s3, 0
	s_add_u32 s14, s2, 0x4800
	s_addc_u32 s15, s3, 0
	s_add_u32 s16, s2, 0x4900
	s_addc_u32 s17, s3, 0
	s_add_u32 s18, s2, 0x4a00
	s_addc_u32 s19, s3, 0
	s_add_u32 s20, s2, 0x4b00
	s_addc_u32 s21, s3, 0
	s_add_u32 s22, s2, 0x4c00
	s_addc_u32 s23, s3, 0
	s_add_u32 s24, s2, 0x4d00
	s_addc_u32 s25, s3, 0
	s_add_u32 s26, s2, 0x4e00
	s_addc_u32 s27, s3, 0
	s_add_u32 s28, s2, 0x4f00
	s_addc_u32 s29, s3, 0
	s_add_u32 s30, s2, 0x5000
	s_addc_u32 s31, s3, 0
	s_add_u32 s34, s2, 0x5100
	s_addc_u32 s35, s3, 0
	s_add_u32 s36, s2, 0x5200
	s_addc_u32 s37, s3, 0
	s_add_u32 s38, s2, 0x5300
	s_addc_u32 s39, s3, 0
	s_mov_b32 s47, 1
	v_mov_b32_e32 v17, 0
	s_branch .LBB0_609

; __device__ __forceinline__ float bflo(unsigned w) { return __uint_as_float(w << 16); }
; __device__ __forceinline__ void postproj_phase(CArgs& A, int l, int vcu, int G) {
;     int tid = threadIdx.x; asm volatile("" : "+v"(tid));
;     const int lane = tid & 63, wave = __builtin_amdgcn_readfirstlane(tid >> 6);
;     const bf16* P = (const bf16*)(A.ws + WS_PROJ);
;     bf16* CQN = (bf16*)(A.ws + WS_CQN); bf16* CKVN = (bf16*)(A.ws + WS_CKVN); bf16* CZ = (bf16*)(A.ws + WS_CZ); unsigned char* Kb = A.ws + WS_K;
;     const f32x2* cs = (const f32x2*)(A.ws + WS_CS);
;     const float* gq = A.in[I_GQ] + l * QL; const float* gkv = A.in[I_GKV] + l * KVL; const float* cw = A.in[I_CONVW] + (size_t)l * 3 * CW;
;     for (int t = vcu * NWAVES + wave; t < NT; t += G * NWAVES) {
;         const int b = t / SEQ, s = t % SEQ; const bf16* pr = P + (size_t)t * NINP;
;         {
;             const u32x4 w = *(const u32x4*)(pr + PC_CQ + 8 * lane); float v[8] = {bflo(w.x), bfhi(w.x), bflo(w.y), bfhi(w.y), bflo(w.z), bfhi(w.z), bflo(w.w), bfhi(w.w)};
;             float ss = 0.f;
; #pragma unroll
;             for (int q = 0; q < 8; ++q) ss += v[q] * v[q];
;             const float rstd = rsqrtf(wave_sum(ss) * (1.0f / QL) + EPS);
;             const f32x4 g0 = *(const f32x4*)(gq + 8 * lane), g1 = *(const f32x4*)(gq + 8 * lane + 4);
;             u32x4 o; o.x = cvtpk(v[0] * rstd * g0.x, v[1] * rstd * g0.y); o.y = cvtpk(v[2] * rstd * g0.z, v[3] * rstd * g0.w); o.z = cvtpk(v[4] * rstd * g1.x, v[5] * rstd * g1.y); o.w = cvtpk(v[6] * rstd * g1.z, v[7] * rstd * g1.w);
;             *(u32x2*)((unsigned char*)CQN + (size_t)t * QL + 8 * lane) = pack8_fp8((f32x4){v[0] * rstd * g0.x, v[1] * rstd * g0.y, v[2] * rstd * g0.z, v[3] * rstd * g0.w}, (f32x4){v[4] * rstd * g1.x, v[5] * rstd * g1.y, v[6] * rstd * g1.z, v[7] * rstd * g1.w});
;         }
;         {
;             const u32x2 w = *(const u32x2*)(pr + PC_CKV + 4 * lane); float v[4] = {bflo(w.x), bfhi(w.x), bflo(w.y), bfhi(w.y)};
;             const float rstd = rsqrtf(wave_sum(v[0] * v[0] + v[1] * v[1] + v[2] * v[2] + v[3] * v[3]) * (1.0f / KVL) + EPS);
;             const f32x4 g0 = *(const f32x4*)(gkv + 4 * lane);
;             u32x2 o; o.x = cvtpk(v[0] * rstd * g0.x, v[1] * rstd * g0.y); o.y = cvtpk(v[2] * rstd * g0.z, v[3] * rstd * g0.w);
;             *(u32x2*)(CKVN + (size_t)t * KVL + 4 * lane) = o;
;         }
;         {
.LBB0_659:
	s_mov_b64 s[0:1], s[24:25]
	s_mov_b32 s0, s100
	s_waitcnt lgkmcnt(0)
	s_cmp_gt_i32 s0, 3
	s_cbranch_scc1 .LBB0_672
	s_mov_b64 s[0:1], s[24:25]
	s_mov_b32 s0, s101
	s_waitcnt lgkmcnt(0)
	s_cmp_lt_i32 s0, 4
	s_cbranch_scc1 .LBB0_671
	v_readlane_b32 s0, v255, 0
	v_readlane_b32 s1, v255, 1
	v_mov_b32_e32 v1, v0
	s_lshl_b32 s2, s97, 3
	v_readfirstlane_b32 s3, v1
	s_ashr_i32 s3, s3, 6
	s_add_i32 s6, s3, s2
	s_cmpk_gt_i32 s6, 0x1fff
	s_cbranch_scc1 .LBB0_671
	s_mov_b64 s[4:5], s[98:99]
	s_load_dwordx2 s[2:3], s[0:1], 0x38
	s_load_dwordx2 s[10:11], s[0:1], 0x48
	s_load_dwordx2 s[12:13], s[0:1], 0x60
	v_and_b32_e32 v6, 1, v1
	v_and_b32_e32 v8, 63, v1
	v_mov_b32_e32 v3, 0
	v_cmp_eq_u32_e64 s[0:1], 0, v6
	v_lshlrev_b32_e32 v6, 2, v1
	v_lshlrev_b32_e32 v2, 5, v8
	v_and_b32_e32 v54, 60, v6
	v_lshlrev_b32_e32 v6, 6, v8
	v_mov_b32_e32 v7, v3
	s_waitcnt lgkmcnt(0)
	s_add_u32 s8, s4, 0x200000
	v_lshl_add_u64 v[50:51], s[2:3], 0, v[2:3]
	v_lshl_add_u64 v[56:57], s[12:13], 0, v[6:7]
	s_mov_b64 s[2:3], 0x1000
	s_addc_u32 s9, s5, 0
	v_lshl_add_u64 v[58:59], v[56:57], 0, s[2:3]
	s_mov_b64 s[2:3], 0x2000
	s_ashr_i32 s7, s6, 31
	v_lshl_add_u64 v[60:61], v[56:57], 0, s[2:3]
	s_lshl_b64 s[2:3], s[6:7], 11
	v_lshlrev_b32_e32 v9, 3, v8
	v_or_b32_e32 v64, s2, v2
	v_mov_b32_e32 v65, s3
	s_lshl_b64 s[2:3], s[6:7], 9
	v_lshlrev_b32_e32 v4, 4, v8
	v_mov_b32_e32 v5, v3
	v_or_b32_e32 v66, s2, v9
	v_mov_b32_e32 v67, s3
	s_lshl_b64 s[2:3], s[6:7], 14
	v_lshl_add_u64 v[52:53], s[10:11], 0, v[4:5]
	v_mov_b32_e32 v55, v3
	v_or_b32_e32 v68, s2, v2
	v_or_b32_e32 v2, s2, v9
	v_mov_b32_e32 v3, s3
	s_mov_b64 s[10:11], 0x3e400400
	v_lshl_add_u64 v[70:71], v[2:3], 0, s[10:11]
	v_lshl_or_b32 v2, v8, 1, s2
	s_mov_b64 s[10:11], 0x3e400600
	v_mov_b32_e32 v69, s3
	v_lshl_add_u64 v[72:73], v[2:3], 0, s[10:11]
	v_or_b32_e32 v2, s2, v4
	s_mov_b64 s[2:3], 0x3e400000
	v_lshl_add_u64 v[74:75], v[2:3], 0, s[2:3]
	v_mbcnt_lo_u32_b32 v2, -1, 0
	v_mbcnt_hi_u32_b32 v97, -1, v2
	v_and_b32_e32 v2, 64, v97
	v_bfe_u32 v5, v1, 1, 5
	v_add_u32_e32 v99, 64, v2
	v_or_b32_e32 v2, v2, v54
	v_bfe_u32 v1, v1, 4, 2
	v_lshl_or_b32 v62, s6, 5, v5
	v_mov_b32_e32 v96, 0x358637bd
	s_mov_b32 s7, 0x800000
	s_mov_b32 s30, 0x46400000
	s_mov_b32 s31, 0x46c00000
	s_movk_i32 s33, 0xc0
	s_mov_b32 s34, 0x4b000000
	s_mov_b32 s35, 0x4b300000
	s_mov_b64 s[10:11], 0x3e3fd000
	s_mov_b64 s[12:13], 0x3e3fd800
	s_mov_b64 s[14:15], 0x3e401000
	s_mov_b64 s[16:17], 0x3e401800
	s_mov_b64 s[18:19], 0x3e405000
	s_mov_b64 s[20:21], 0x3e405800
	s_mov_b64 s[22:23], 0x3e400800
	s_mov_b32 s36, 0x3e400000
	s_mov_b32 s37, 0x47000000
	s_mov_b64 s[24:25], 0x400000
	s_mov_b64 s[26:27], 0x100000
	s_mov_b64 s[28:29], 0x2000000
	v_xor_b32_e32 v98, 1, v97
	v_lshlrev_b32_e32 v100, 2, v2
	v_mov_b64_e32 v[76:77], s[4:5]
	s_branch .LBB0_664

; __device__ __forceinline__ int otid() { int t = threadIdx.x; asm volatile("" : "+v"(t)); return t; }
; __device__ __forceinline__ unsigned xb_ld(unsigned* p)              { return __hip_atomic_load(p, __ATOMIC_RELAXED, __HIP_MEMORY_SCOPE_AGENT); }
; __device__ __forceinline__ unsigned xb_add(unsigned* p, unsigned v) { return __hip_atomic_fetch_add(p, v, __ATOMIC_RELAXED, __HIP_MEMORY_SCOPE_AGENT); }
; __device__ __forceinline__ void xcd_barrier_complete(unsigned* bar, unsigned x, unsigned& nloc, unsigned& nx) {
;     const unsigned G = gridDim.x * gridDim.y * gridDim.z;
;     unsigned sum, cnt, mine, sp = 0u;
;     for (;;) {
;         sum = 0u; cnt = 0u; mine = 0u;
; #pragma unroll
;         for (unsigned j = 0; j < 16; ++j) { const unsigned c = xb_ld(&bar[XB_XCNT(j)]); sum += c; cnt += (c > 0u) ? 1u : 0u; mine = (j == x) ? c : mine; }
;         if (sum == G) break;
;         __builtin_amdgcn_s_sleep(1);
;         if ((++sp & 255u) == 0u) { if (xb_ld(&bar[XB_TMO])) break; if (sp > XB_SPIN_CAP) { atomicAdd(&bar[XB_TMO], 1u); break; } }
;     }
;     nloc = mine > 0u ? mine : 1u; nx = cnt > 0u ? cnt : 1u;
; }
; __device__ __forceinline__ void xcd_barrier(const XcdBarrier& b) {
;     asm volatile("s_waitcnt vmcnt(0)" ::: "memory");
;     __syncthreads();
;     if (otid() == 0) {
;         unsigned* bar = b.bar;
;         __builtin_amdgcn_s_waitcnt(0);
;         unsigned nloc = b.st[0], nx = b.st[1];
;         if (nloc == 0u) { xcd_barrier_complete(bar, b.x, nloc, nx); b.st[0] = nloc; b.st[1] = nx; }
;         const unsigned old = xb_add(&bar[XB_XSUB(b.x)], 1u);
;         const unsigned gen = old / nloc;
;         if (old + 1u == (gen + 1u) * nloc) {
;             __builtin_amdgcn_fence(__ATOMIC_RELEASE, "agent");
;             asm volatile("s_waitcnt vmcnt(0)" ::: "memory");
;             const unsigned og = xb_add(&bar[XB_TOP], 1u);
.LBB0_672:
	s_mov_b64 s[0:1], s[24:25]
	s_mov_b32 s0, s100
	s_waitcnt lgkmcnt(0)
	s_cmp_gt_i32 s0, 3
	s_cbranch_scc1 .LBB0_730
	s_mov_b64 s[0:1], s[24:25]
	s_mov_b32 s0, s101
	s_waitcnt lgkmcnt(0)
	s_cmp_lt_i32 s0, 4
	s_cbranch_scc1 .LBB0_729
	v_readlane_b32 s0, v255, 0
	v_readlane_b32 s1, v255, 1
	s_mov_b32 s0, s100
	s_waitcnt lgkmcnt(0)
	s_cmp_gt_i32 s0, 4
	s_cbranch_scc1 .LBB0_729
	v_readlane_b32 s0, v255, 0
	v_readlane_b32 s1, v255, 1
	s_mov_b32 s0, s101
	s_waitcnt lgkmcnt(0)
	s_cmp_lt_i32 s0, 5
	s_cbranch_scc1 .LBB0_729
	v_readlane_b32 s2, v255, 0
	v_readlane_b32 s3, v255, 1
	s_getreg_b32 s4, hwreg(HW_REG_XCC_ID, 0, 4)
	s_waitcnt vmcnt(0)
	v_mov_b32_e32 v1, v0
	s_waitcnt vmcnt(0)
	s_barrier
	s_nop 0
	v_cmp_eq_u32_e32 vcc, 0, v1
	s_and_saveexec_b64 s[0:1], vcc
	s_cbranch_execz .LBB0_728
	s_add_i32 s5, 0, 0x20020
	v_mov_b32_e32 v1, s5
	s_mov_b64 s[2:3], s[98:99]
	s_waitcnt vmcnt(0) expcnt(0) lgkmcnt(0)
	ds_read_b32 v3, v1
	s_add_i32 s5, 0, 0x20024
	v_mov_b32_e32 v1, s5
	ds_read_b32 v1, v1
	s_and_b32 s33, s4, 15
	s_waitcnt lgkmcnt(1)
	v_cmp_ne_u32_e32 vcc, 0, v3
	s_cbranch_vccnz .LBB0_692
	v_readlane_b32 s4, v255, 0
	v_readlane_b32 s5, v255, 1
	s_load_dwordx2 s[8:9], s[4:5], 0xe0
	s_load_dword s7, s[4:5], 0xe8
	s_add_u32 s4, s2, 0x4200
	s_addc_u32 s5, s3, 0
	s_add_u32 s6, s2, 0x4400
	s_waitcnt lgkmcnt(0)
	s_mul_i32 s46, s9, s8
	s_mul_i32 s46, s46, s7
	s_addc_u32 s7, s3, 0
	s_add_u32 s8, s2, 0x4500
	s_addc_u32 s9, s3, 0
	s_add_u32 s10, s2, 0x4600
	s_addc_u32 s11, s3, 0
	s_add_u32 s12, s2, 0x4700
	s_addc_u32 s13, s3, 0
	s_add_u32 s14, s2, 0x4800
	s_addc_u32 s15, s3, 0
	s_add_u32 s16, s2, 0x4900
	s_addc_u32 s17, s3, 0
	s_add_u32 s18, s2, 0x4a00
	s_addc_u32 s19, s3, 0
	s_add_u32 s20, s2, 0x4b00
	s_addc_u32 s21, s3, 0
	s_add_u32 s22, s2, 0x4c00
	s_addc_u32 s23, s3, 0
	s_add_u32 s24, s2, 0x4d00
	s_addc_u32 s25, s3, 0
	s_add_u32 s26, s2, 0x4e00
	s_addc_u32 s27, s3, 0
	s_add_u32 s28, s2, 0x4f00
	s_addc_u32 s29, s3, 0
	s_add_u32 s30, s2, 0x5000
	s_addc_u32 s31, s3, 0
	s_add_u32 s34, s2, 0x5100
	s_addc_u32 s35, s3, 0
	s_add_u32 s36, s2, 0x5200
	s_addc_u32 s37, s3, 0
	s_add_u32 s38, s2, 0x5300
	s_addc_u32 s39, s3, 0
	s_mov_b32 s47, 1
	v_mov_b32_e32 v17, 0
	s_branch .LBB0_680

; template <class P, class MK = NoChain>
; __device__ __forceinline__ void gemm_phase(LAS unsigned char* lds, const P& p, const MK& mk = MK(), bool chain_out = false, bool chained_in = false) {
;     ...
;     int tid = threadIdx.x; asm volatile("" : "+v"(tid));
;     const int wid = __builtin_amdgcn_readfirstlane(tid >> 6), lane = tid & 63, wr = wid >> 2, wc = wid & 3, fr = lane & 15, fq = lane >> 4;
;     unsigned voffB[2], vA[2][2], nvA[2][2], nvB[2]; typedef decltype(mk()) NP; constexpr int NES = NP::FP8 ? 1 : 2; constexpr int NBMODE = bmode_of<NP>::value; constexpr size_t nhstepB = (size_t)(NBMODE == 1 ? 8 : (NBMODE == 2 ? 16 : HALF)) * NP::LDB * NES;
;     constexpr size_t kstep = (size_t)(BK * 2);
;     constexpr int BMODE = bmode_of<P>::value;
;     constexpr size_t hstep = (size_t)(BMODE == 1 ? 8 : (BMODE == 2 ? 16 : HALF)) * LDB * ES, hstepA = (size_t)HALF * LDA * ES;
; #pragma unroll
;     for (int i = 0; i < 2; ++i) { int R, C; stage_rc(tid * 16 + i * 8192, R, C); const int rho_ = R & 31;
;         const int fq_ = (rho_ & 15) >> 2, n_ = rho_ >> 4, q_ = rho_ & 3;
;         const int Rb = BMODE == 1 ? ((R >> 5) * 64 + fq_ * 16 + 4 * n_ + q_) : (BMODE == 2 ? ((R >> 5) * 64 + 32 * (fq_ >> 1) + 8 * n_ + 4 * (fq_ & 1) + q_) : (P::PERM ? ((R & ~31) + perm32(R & 31)) : R));
;         voffB[i] = (unsigned)(Rb * LDB * ES + C * 2); vA[0][i] = (unsigned)(R * LDA * ES + C * 2); vA[1][i] = vA[0][i] + (unsigned)hstepA; nvA[0][i] = vA[0][i]; nvA[1][i] = vA[1][i]; nvB[i] = voffB[i]; }
;     const unsigned ldsw = (unsigned)wid * 1024u;
;     const int aoff = lds_byte(wr * 64 + fr, fq * 8), boff = lds_byte(wc * 32 + fr, fq * 8); const int aoff1 = aoff ^ 64, boff1 = boff ^ 64;
;     ...
;     Unit cur, nxt; int ui = 0;
;     if (!p.next(0, cur)) return;
;     Acc acc;
;     if constexpr (!PEEL) {
; #pragma unroll
;     for (int a = 0; a < 2; ++a)
; #pragma unroll
;         for (int b = 0; b < 2; ++b)
; #pragma unroll
;             for (int m = 0; m < 4; ++m)
; #pragma unroll
;                 for (int n = 0; n < 2; ++n) { typedef double d2_ __attribute__((ext_vector_type(2))); d2_ z_; asm volatile("v_mov_b64 %0, 0" : "=v"(z_.x)); asm volatile("v_mov_b64 %0, 0" : "=v"(z_.y)); acc[a][b][m][n] = __builtin_bit_cast(f32x4, z_); }
;     }
;     typedef int v8i_ __attribute__((ext_vector_type(8))); typedef int v4i_ __attribute__((ext_vector_type(4)));
.LBB0_730:
	s_mov_b64 s[0:1], s[24:25]
	s_mov_b32 s0, s100
	s_waitcnt lgkmcnt(0)
	s_cmp_gt_i32 s0, 4
	s_cbranch_scc1 .LBB0_816
	s_mov_b64 s[0:1], s[24:25]
	s_mov_b32 s0, s101
	s_waitcnt lgkmcnt(0)
	s_cmp_lt_i32 s0, 5
	s_cbranch_scc1 .LBB0_816
	s_cmpk_lt_i32 s95, 0x100
	v_readlane_b32 s2, v255, 4
	s_cselect_b64 s[0:1], -1, 0
	s_and_b32 s2, s2, -8
	s_sub_i32 s4, s95, s2
	s_mov_b64 s[2:3], s[24:25]
	v_mov_b32_e32 v130, v0
	s_mov_b32 s67, s97
	s_cmpk_gt_i32 s95, 0xff
	s_nop 0
	v_readfirstlane_b32 s10, v130
	s_cbranch_scc1 .LBB0_734
	s_lshl_b32 s6, s4, 5
	s_mul_i32 s5, s4, 33
	s_cmp_lt_i32 s4, 0
	s_cselect_b32 s5, s5, s6
	s_add_i32 s5, s5, s96
	s_ashr_i32 s6, s5, 31
	s_lshr_b32 s6, s6, 26
	s_add_i32 s6, s5, s6
	s_ashr_i32 s7, s6, 6
	s_andn2_b32 s6, s6, 63
	s_sub_i32 s5, s5, s6
	s_bfe_i32 s6, s5, 0x80000
	s_bfe_u32 s6, s6, 0x3000c
	s_add_i32 s6, s5, s6
	s_bfe_i32 s8, s6, 0x80000
	s_and_b32 s6, s6, 0xf8
	s_sub_i32 s5, s5, s6
	s_lshl_b32 s7, s7, 3
	s_sext_i32_i16 s8, s8
	s_sext_i32_i8 s5, s5
	s_add_i32 s28, s7, s5
	s_ashr_i32 s26, s8, 3
.LBB0_734:
	s_ashr_i32 s97, s96, 31
	s_ashr_i32 s5, s4, 31
	s_lshl_b64 s[6:7], s[96:97], 17
	s_andn2_b64 vcc, exec, s[0:1]
	s_lshl_b64 s[8:9], s[4:5], 17
	s_cbranch_vccnz .LBB0_781
	s_mov_b64 s[0:1], s[98:99]
	v_lshrrev_b32_e32 v139, 4, v130
	v_xor_b32_e32 v1, v139, v130
	v_ashrrev_i32_e32 v132, 3, v130
	v_lshlrev_b32_e32 v1, 4, v1
	s_waitcnt lgkmcnt(0)
	s_add_u32 s5, s0, 0x47000000
	v_lshlrev_b32_e32 v134, 1, v132
	v_lshrrev_b32_e32 v2, 2, v132
	s_addc_u32 s46, s1, 0
	v_and_b32_e32 v131, 0x70, v1
	v_and_b32_e32 v1, 24, v134
	v_and_b32_e32 v135, 4, v2
	v_and_b32_e32 v2, 0x1fffe3, v132
	s_add_u32 s47, s0, 0x5e00000
	v_or3_b32 v1, v2, v1, v135
	s_addc_u32 s48, s1, 0
	v_lshl_or_b32 v194, v1, 11, v131
	v_mov_b32_e32 v1, 0x2000
	s_ashr_i32 s3, s10, 6
	s_ashr_i32 s29, s28, 31
	s_ashr_i32 s27, s26, 31
	s_ashr_i32 s2, s10, 8
	v_lshl_add_u32 v136, v130, 4, v1
	s_lshl_b32 s14, s3, 10
	s_lshl_b64 s[10:11], s[28:29], 19
	s_lshl_b64 s[12:13], s[26:27], 19
	v_ashrrev_i32_e32 v133, 7, v136
	s_add_u32 s38, s47, s12
	v_lshlrev_b32_e32 v137, 1, v133
	v_lshrrev_b32_e32 v2, 2, v133
	s_addc_u32 s39, s48, s13
	s_add_i32 s27, s14, 0
	v_and_b32_e32 v1, 24, v137
	v_and_b32_e32 v138, 4, v2
	v_and_b32_e32 v2, 0x1fffe3, v133
	s_add_i32 s29, s27, 0x10000
	s_add_i32 s49, s27, 0x12000
	v_or3_b32 v1, v2, v1, v138
	s_mov_b64 s[12:13], s[38:39]
	s_mov_b32 m0, s29
	s_add_u32 s30, s5, s10
	v_lshl_or_b32 v200, v1, 11, v131
	v_mov_b64 v[106:107], 0
	v_mov_b64 v[108:109], 0
	v_mov_b64 v[110:111], 0
	v_mov_b64 v[112:113], 0
	v_mov_b64 v[98:99], 0
	v_mov_b64 v[100:101], 0
	v_mov_b64 v[102:103], 0
	v_mov_b64 v[104:105], 0
	v_mov_b64 v[82:83], 0
	v_mov_b64 v[84:85], 0
	v_mov_b64 v[86:87], 0
	v_mov_b64 v[88:89], 0
	v_mov_b64 v[70:71], 0
	v_mov_b64 v[72:73], 0
	v_mov_b64 v[66:67], 0
	v_mov_b64 v[68:69], 0
	v_mov_b64 v[122:123], 0
	v_mov_b64 v[124:125], 0
	v_mov_b64 v[126:127], 0
	v_mov_b64 v[128:129], 0
	v_mov_b64 v[114:115], 0
	v_mov_b64 v[116:117], 0
	v_mov_b64 v[118:119], 0
	v_mov_b64 v[120:121], 0
	v_mov_b64 v[94:95], 0
	v_mov_b64 v[96:97], 0
	v_mov_b64 v[90:91], 0
	v_mov_b64 v[92:93], 0
	v_mov_b64 v[78:79], 0
	v_mov_b64 v[80:81], 0
	v_mov_b64 v[74:75], 0
	v_mov_b64 v[76:77], 0
	v_mov_b64 v[54:55], 0
	v_mov_b64 v[56:57], 0
	v_mov_b64 v[50:51], 0
	v_mov_b64 v[52:53], 0
	v_mov_b64 v[38:39], 0
	v_mov_b64 v[40:41], 0
	v_mov_b64 v[34:35], 0
	v_mov_b64 v[36:37], 0
	v_mov_b64 v[22:23], 0
	v_mov_b64 v[24:25], 0
	v_mov_b64 v[18:19], 0
	v_mov_b64 v[20:21], 0
	v_mov_b64 v[6:7], 0
	v_mov_b64 v[8:9], 0
	v_mov_b64 v[2:3], 0
	v_mov_b64 v[4:5], 0
	v_mov_b64 v[62:63], 0
	v_mov_b64 v[64:65], 0
	v_mov_b64 v[58:59], 0
	v_mov_b64 v[60:61], 0
	v_mov_b64 v[46:47], 0
	v_mov_b64 v[48:49], 0
	v_mov_b64 v[42:43], 0
	v_mov_b64 v[44:45], 0
	v_mov_b64 v[30:31], 0
	v_mov_b64 v[32:33], 0
	v_mov_b64 v[26:27], 0
	v_mov_b64 v[28:29], 0
	v_mov_b64 v[14:15], 0
	v_mov_b64 v[16:17], 0
	v_mov_b64 v[10:11], 0
	v_mov_b64 v[12:13], 0
	s_addc_u32 s31, s46, s11
	global_load_lds_dwordx4 v194, s[12:13]
	s_mov_b32 m0, s49
	v_lshl_or_b32 v196, v132, 11, v131
	global_load_lds_dwordx4 v200, s[12:13]
	s_mov_b64 s[10:11], s[30:31]
	s_mov_b32 m0, s27
	s_add_i32 s50, s27, 0x2000
	v_lshl_or_b32 v202, v133, 11, v131
	v_add_u32_e32 v198, 0x40000, v196
	global_load_lds_dwordx4 v196, s[10:11]
	s_mov_b32 m0, s50
	v_add_u32_e32 v204, 0x40000, v202
	global_load_lds_dwordx4 v202, s[10:11]
	s_add_u32 s10, s38, 0x40000
	s_addc_u32 s11, s39, 0
	s_add_i32 s51, s27, 0x14000
	s_mov_b32 m0, s51
	s_add_i32 s52, s27, 0x16000
	s_add_i32 s53, s27, 0x4000
	global_load_lds_dwordx4 v194, s[10:11]
	s_mov_b32 m0, s52
	s_add_i32 s54, s27, 0x6000
	global_load_lds_dwordx4 v200, s[10:11]
	s_mov_b64 s[10:11], s[30:31]
	s_mov_b32 m0, s53
	v_mov_b32_e32 v207, 0
	global_load_lds_dwordx4 v198, s[10:11]
	s_mov_b32 m0, s54
	v_mov_b32_e32 v195, v207
	global_load_lds_dwordx4 v204, s[10:11]
	s_mov_b32 s11, 0
	v_mov_b32_e32 v201, v207
	v_mov_b32_e32 v197, v207
	s_cmp_lg_u32 s2, 1
	v_mov_b32_e32 v203, v207
	s_cbranch_scc1 .LBB0_737
	s_barrier

;     __device__ __forceinline__ bool next(int i, pg::Unit& u) const { u.aux = 0; u.aux2 = 0; u.half = 0; return ord.get(i, u.pm, u.pn); }
;     __device__ __forceinline__ bool next(int i, pg::Unit& u) const { u.aux = 0; u.aux2 = 0; u.half = 0; return ord.get(i, u.pm, u.pn); }
; __device__ __forceinline__ CArgs* fresh_args() { CArgs* p = (CArgs*)__builtin_amdgcn_kernarg_segment_ptr(); asm volatile("" : "+s"(p)); return p; }
; template <class P, class MK = NoChain>
; __device__ __forceinline__ void gemm_phase(LAS unsigned char* lds, const P& p, const MK& mk = MK(), bool chain_out = false, bool chained_in = false) {
;     ...
;         const bool has_next = p.next(ui + 1, nxt);
;         const char* nA = has_next ? p.a_base(nxt) : cA; const char* nB = has_next ? p.b_base(nxt) : cB;
;         const bool chain_now = CHAIN && chain_out && !has_next;
;         if constexpr (CHAIN) { if (chain_now) { const auto np = mk(); Unit nu; (void)np.next(0, nu); nA = np.a_base(nu); nB = np.b_base(nu); } }
; template <int l> __device__ __forceinline__ void layer_body(LAS unsigned char* lds, unsigned char* lds_raw, int bx, int vcu) {
;     ...
;             const auto mkK = [=]() { unsigned char* ws = fresh_args()->ws; DenseP<KVL, EpiK, pg::ListOrder> P; P.A = (const char*)(ws + WS_CKVN); P.Bt = (const char*)(ws + WS_WUKV) + (size_t)l * NH * 128 * KVL * 2; P.ord.nN = NH / 2; P.ord.first = bx; P.ord.n = 1; P.e.Kb = ws + WS_K; return P; };
.LBB0_745:
	s_ashr_i32 s19, s18, 31
	s_lshl_b64 s[22:23], s[18:19], 19
	s_add_u32 s22, s5, s22
	s_addc_u32 s23, s46, s23
	s_ashr_i32 s21, s20, 31
	s_lshl_b64 s[24:25], s[20:21], 19
	s_add_u32 s24, s47, s24
	s_addc_u32 s25, s48, s25
	s_andn2_b64 vcc, exec, s[0:1]
	s_cbranch_vccnz .LBB0_747
	v_readlane_b32 s0, v255, 0
	v_readlane_b32 s1, v255, 1
	s_mov_b64 s[0:1], s[98:99]
	s_waitcnt lgkmcnt(0)
	s_add_u32 s17, s0, s6
	s_addc_u32 s19, s1, s7
	s_add_u32 s22, s17, 0x46c00000
	s_addc_u32 s23, s19, 0
	s_add_u32 s0, s0, s8
	s_addc_u32 s1, s1, s9
	s_add_u32 s24, s0, 0x4a00000
	s_addc_u32 s25, s1, 0

.LBB0_811:
	s_lshl_b32 s0, s5, 6
	s_lshl_b32 s6, s4, 1
	s_and_b32 s0, s0, 64
	s_add_u32 s8, s16, 0x4b000000
	v_mov_b32_e32 v131, 0
	s_addc_u32 s9, s17, 0
	s_lshr_b32 s5, s5, 1
	s_mov_b32 s4, 0x3e800000
	v_pk_mul_f32 v[114:115], v[114:115], s[4:5] op_sel_hi:[1,0]
	v_pk_mul_f32 v[134:135], v[118:119], s[4:5] op_sel_hi:[1,0]
	v_mov_b32_e32 v118, v131
	v_cvt_pk_fp8_f32 v118, v114, v115
	v_mov_b32_e32 v119, v131
	v_pk_mul_f32 v[114:115], v[116:117], s[4:5] op_sel_hi:[1,0]
	v_lshl_add_u32 v1, s96, 8, v1
	v_cvt_pk_fp8_f32 v119, v134, v135
	v_pk_mul_f32 v[116:117], v[120:121], s[4:5] op_sel_hi:[1,0]
	v_cvt_pk_fp8_f32 v118, v114, v115 op_sel:[0,0,1]
	v_pk_mul_f32 v[114:115], v[122:123], s[4:5] op_sel_hi:[1,0]
	v_mov_b32_e32 v120, v131
	v_ashrrev_i32_e32 v132, 31, v1
	v_cvt_pk_fp8_f32 v120, v114, v115
	v_lshrrev_b32_e32 v132, 20, v132
	v_add_u32_e32 v132, v1, v132
	v_ashrrev_i32_e32 v133, 12, v132
	v_cvt_pk_fp8_f32 v119, v116, v117 op_sel:[0,0,1]
	v_pk_mul_f32 v[116:117], v[126:127], s[4:5] op_sel_hi:[1,0]
	v_mov_b32_e32 v121, v131
	v_pk_mul_f32 v[114:115], v[124:125], s[4:5] op_sel_hi:[1,0]
	v_cvt_pk_fp8_f32 v121, v116, v117
	v_cvt_pk_fp8_f32 v120, v114, v115 op_sel:[0,0,1]
	v_lshl_add_u32 v114, v133, 4, s6
	v_mul_i32_i24_e32 v132, 0x1000, v133
	v_or_b32_e32 v114, s5, v114
	v_sub_u32_e32 v132, v1, v132
	v_ashrrev_i32_e32 v115, 31, v114
	v_pk_mul_f32 v[116:117], v[128:129], s[4:5] op_sel_hi:[1,0]
	v_lshlrev_b64 v[114:115], 12, v[114:115]
	v_ashrrev_i32_e32 v133, 31, v132
	v_cvt_pk_fp8_f32 v121, v116, v117 op_sel:[0,0,1]
	v_lshl_add_u64 v[116:117], v[114:115], 0, v[132:133]
	s_movk_i32 s7, 0xc0
	v_mov_b64_e32 v[114:115], s[8:9]
	v_mad_u64_u32 v[122:123], s[8:9], v116, s7, v[114:115]
	s_mov_b32 s1, 0
	v_mad_i32_i24 v123, v117, s7, v123
	v_lshlrev_b32_e32 v130, 4, v212
	v_lshl_add_u64 v[116:117], v[122:123], 0, s[0:1]
	v_lshl_add_u64 v[116:117], v[116:117], 0, v[130:131]
	global_store_dwordx4 v[116:117], v[118:121], off
	v_add_u32_e32 v116, 16, v1
	v_ashrrev_i32_e32 v117, 31, v116
	v_lshrrev_b32_e32 v117, 20, v117
	v_add_u32_e32 v117, v116, v117
	v_ashrrev_i32_e32 v117, 12, v117
	v_mul_i32_i24_e32 v118, 0x1000, v117
	v_sub_u32_e32 v116, v116, v118
	v_pk_mul_f32 v[118:119], v[98:99], s[4:5] op_sel_hi:[1,0]
	v_pk_mul_f32 v[102:103], v[102:103], s[4:5] op_sel_hi:[1,0]
	v_mov_b32_e32 v98, v131
	v_mov_b32_e32 v99, v131
	v_cvt_pk_fp8_f32 v98, v118, v119
	v_cvt_pk_fp8_f32 v99, v102, v103
	v_pk_mul_f32 v[100:101], v[100:101], s[4:5] op_sel_hi:[1,0]
	v_pk_mul_f32 v[102:103], v[104:105], s[4:5] op_sel_hi:[1,0]
	v_cvt_pk_fp8_f32 v98, v100, v101 op_sel:[0,0,1]
	v_cvt_pk_fp8_f32 v99, v102, v103 op_sel:[0,0,1]
	v_pk_mul_f32 v[102:103], v[106:107], s[4:5] op_sel_hi:[1,0]
	v_mov_b32_e32 v100, v131
	v_cvt_pk_fp8_f32 v100, v102, v103
	v_pk_mul_f32 v[102:103], v[108:109], s[4:5] op_sel_hi:[1,0]
	v_pk_mul_f32 v[104:105], v[110:111], s[4:5] op_sel_hi:[1,0]
	v_mov_b32_e32 v101, v131
	v_cvt_pk_fp8_f32 v100, v102, v103 op_sel:[0,0,1]
	v_lshl_add_u32 v102, v117, 4, s6
	v_cvt_pk_fp8_f32 v101, v104, v105
	v_or_b32_e32 v102, s5, v102
	v_ashrrev_i32_e32 v103, 31, v102
	v_lshlrev_b64 v[102:103], 12, v[102:103]
	v_ashrrev_i32_e32 v117, 31, v116
	v_pk_mul_f32 v[104:105], v[112:113], s[4:5] op_sel_hi:[1,0]
	v_lshl_add_u64 v[102:103], v[102:103], 0, v[116:117]
	v_cvt_pk_fp8_f32 v101, v104, v105 op_sel:[0,0,1]
	v_mad_u64_u32 v[104:105], s[8:9], v102, s7, v[114:115]
	v_mad_i32_i24 v105, v103, s7, v105
	v_lshl_add_u64 v[102:103], v[104:105], 0, s[0:1]
	v_lshl_add_u64 v[102:103], v[102:103], 0, v[130:131]
	global_store_dwordx4 v[102:103], v[98:101], off
	v_pk_mul_f32 v[86:87], v[86:87], s[4:5] op_sel_hi:[1,0]
	v_pk_mul_f32 v[84:85], v[84:85], s[4:5] op_sel_hi:[1,0]
	v_add_u32_e32 v98, 32, v1
	v_ashrrev_i32_e32 v99, 31, v98
	v_lshrrev_b32_e32 v99, 20, v99
	v_add_u32_e32 v99, v98, v99
	v_ashrrev_i32_e32 v99, 12, v99
	v_mul_i32_i24_e32 v100, 0x1000, v99
	v_sub_u32_e32 v98, v98, v100
	v_pk_mul_f32 v[100:101], v[82:83], s[4:5] op_sel_hi:[1,0]
	v_mov_b32_e32 v82, v131
	v_mov_b32_e32 v83, v131
	v_cvt_pk_fp8_f32 v82, v100, v101
	v_cvt_pk_fp8_f32 v83, v86, v87
	v_pk_mul_f32 v[86:87], v[88:89], s[4:5] op_sel_hi:[1,0]
	v_pk_mul_f32 v[88:89], v[94:95], s[4:5] op_sel_hi:[1,0]
	v_cvt_pk_fp8_f32 v82, v84, v85 op_sel:[0,0,1]
	v_cvt_pk_fp8_f32 v83, v86, v87 op_sel:[0,0,1]
	v_pk_mul_f32 v[86:87], v[90:91], s[4:5] op_sel_hi:[1,0]
	v_mov_b32_e32 v84, v131
	v_cvt_pk_fp8_f32 v84, v86, v87
	v_pk_mul_f32 v[86:87], v[92:93], s[4:5] op_sel_hi:[1,0]
	v_mov_b32_e32 v85, v131
	v_cvt_pk_fp8_f32 v85, v88, v89
	v_cvt_pk_fp8_f32 v84, v86, v87 op_sel:[0,0,1]
	v_lshl_add_u32 v86, v99, 4, s6
	v_or_b32_e32 v86, s5, v86
	v_ashrrev_i32_e32 v87, 31, v86
	v_lshlrev_b64 v[86:87], 12, v[86:87]
	v_ashrrev_i32_e32 v99, 31, v98
	v_pk_mul_f32 v[88:89], v[96:97], s[4:5] op_sel_hi:[1,0]
	v_lshl_add_u64 v[86:87], v[86:87], 0, v[98:99]
	v_cvt_pk_fp8_f32 v85, v88, v89 op_sel:[0,0,1]
	v_mad_u64_u32 v[88:89], s[8:9], v86, s7, v[114:115]
	v_mad_i32_i24 v89, v87, s7, v89
	v_lshl_add_u64 v[86:87], v[88:89], 0, s[0:1]
	v_lshl_add_u64 v[86:87], v[86:87], 0, v[130:131]
	global_store_dwordx4 v[86:87], v[82:85], off
	v_pk_mul_f32 v[62:63], v[62:63], s[4:5] op_sel_hi:[1,0]
	v_pk_mul_f32 v[60:61], v[60:61], s[4:5] op_sel_hi:[1,0]
	v_add_u32_e32 v82, 48, v1
	v_ashrrev_i32_e32 v83, 31, v82
	v_lshrrev_b32_e32 v83, 20, v83
	v_add_u32_e32 v83, v82, v83
	v_ashrrev_i32_e32 v83, 12, v83
	v_mul_i32_i24_e32 v84, 0x1000, v83
	v_sub_u32_e32 v82, v82, v84
	v_pk_mul_f32 v[84:85], v[58:59], s[4:5] op_sel_hi:[1,0]
	v_mov_b32_e32 v58, v131
	v_mov_b32_e32 v59, v131
	v_cvt_pk_fp8_f32 v58, v84, v85
	v_cvt_pk_fp8_f32 v59, v62, v63
	v_pk_mul_f32 v[62:63], v[64:65], s[4:5] op_sel_hi:[1,0]
	v_pk_mul_f32 v[64:65], v[78:79], s[4:5] op_sel_hi:[1,0]
	v_cvt_pk_fp8_f32 v58, v60, v61 op_sel:[0,0,1]
	v_cvt_pk_fp8_f32 v59, v62, v63 op_sel:[0,0,1]
	v_pk_mul_f32 v[62:63], v[74:75], s[4:5] op_sel_hi:[1,0]
	v_mov_b32_e32 v60, v131
	v_cvt_pk_fp8_f32 v60, v62, v63
	v_pk_mul_f32 v[62:63], v[76:77], s[4:5] op_sel_hi:[1,0]
	v_mov_b32_e32 v61, v131
	v_cvt_pk_fp8_f32 v61, v64, v65
	v_cvt_pk_fp8_f32 v60, v62, v63 op_sel:[0,0,1]
	v_lshl_add_u32 v62, v83, 4, s6
	v_or_b32_e32 v62, s5, v62
	v_ashrrev_i32_e32 v63, 31, v62
	v_lshlrev_b64 v[62:63], 12, v[62:63]
	v_ashrrev_i32_e32 v83, 31, v82
	v_pk_mul_f32 v[64:65], v[80:81], s[4:5] op_sel_hi:[1,0]
	v_lshl_add_u64 v[62:63], v[62:63], 0, v[82:83]
	v_cvt_pk_fp8_f32 v61, v64, v65 op_sel:[0,0,1]
	v_mad_u64_u32 v[64:65], s[8:9], v62, s7, v[114:115]
	v_mad_i32_i24 v65, v63, s7, v65
	v_lshl_add_u64 v[62:63], v[64:65], 0, s[0:1]
	v_lshl_add_u64 v[62:63], v[62:63], 0, v[130:131]
	global_store_dwordx4 v[62:63], v[58:61], off
	v_pk_mul_f32 v[54:55], v[54:55], s[4:5] op_sel_hi:[1,0]
	v_pk_mul_f32 v[52:53], v[52:53], s[4:5] op_sel_hi:[1,0]
	v_add_u32_e32 v58, 0x80, v1
	v_ashrrev_i32_e32 v59, 31, v58
	v_lshrrev_b32_e32 v59, 20, v59
	v_add_u32_e32 v59, v58, v59
	v_ashrrev_i32_e32 v59, 12, v59
	v_mul_i32_i24_e32 v60, 0x1000, v59
	v_sub_u32_e32 v58, v58, v60
	v_pk_mul_f32 v[60:61], v[50:51], s[4:5] op_sel_hi:[1,0]
	v_mov_b32_e32 v50, v131
	v_mov_b32_e32 v51, v131
	v_cvt_pk_fp8_f32 v50, v60, v61
	v_cvt_pk_fp8_f32 v51, v54, v55
	v_pk_mul_f32 v[54:55], v[56:57], s[4:5] op_sel_hi:[1,0]
	v_pk_mul_f32 v[56:57], v[70:71], s[4:5] op_sel_hi:[1,0]
	v_cvt_pk_fp8_f32 v50, v52, v53 op_sel:[0,0,1]
	v_cvt_pk_fp8_f32 v51, v54, v55 op_sel:[0,0,1]
	v_pk_mul_f32 v[54:55], v[66:67], s[4:5] op_sel_hi:[1,0]
	v_mov_b32_e32 v52, v131
	v_cvt_pk_fp8_f32 v52, v54, v55
	v_pk_mul_f32 v[54:55], v[68:69], s[4:5] op_sel_hi:[1,0]
	v_mov_b32_e32 v53, v131
	v_cvt_pk_fp8_f32 v53, v56, v57
	v_cvt_pk_fp8_f32 v52, v54, v55 op_sel:[0,0,1]
	v_lshl_add_u32 v54, v59, 4, s6
	v_or_b32_e32 v54, s5, v54
	v_ashrrev_i32_e32 v55, 31, v54
	v_lshlrev_b64 v[54:55], 12, v[54:55]
	v_ashrrev_i32_e32 v59, 31, v58
	v_pk_mul_f32 v[56:57], v[72:73], s[4:5] op_sel_hi:[1,0]
	v_lshl_add_u64 v[54:55], v[54:55], 0, v[58:59]
	v_cvt_pk_fp8_f32 v53, v56, v57 op_sel:[0,0,1]
	v_mad_u64_u32 v[56:57], s[8:9], v54, s7, v[114:115]
	v_mad_i32_i24 v57, v55, s7, v57
	v_lshl_add_u64 v[54:55], v[56:57], 0, s[0:1]
	v_lshl_add_u64 v[54:55], v[54:55], 0, v[130:131]
	global_store_dwordx4 v[54:55], v[50:53], off
	v_pk_mul_f32 v[38:39], v[38:39], s[4:5] op_sel_hi:[1,0]
	v_pk_mul_f32 v[36:37], v[36:37], s[4:5] op_sel_hi:[1,0]
	v_add_u32_e32 v50, 0x90, v1
	v_ashrrev_i32_e32 v51, 31, v50
	v_lshrrev_b32_e32 v51, 20, v51
	v_add_u32_e32 v51, v50, v51
	v_ashrrev_i32_e32 v51, 12, v51
	v_mul_i32_i24_e32 v52, 0x1000, v51
	v_sub_u32_e32 v50, v50, v52
	v_pk_mul_f32 v[52:53], v[34:35], s[4:5] op_sel_hi:[1,0]
	v_mov_b32_e32 v34, v131
	v_mov_b32_e32 v35, v131
	v_cvt_pk_fp8_f32 v34, v52, v53
	v_cvt_pk_fp8_f32 v35, v38, v39
	v_pk_mul_f32 v[38:39], v[40:41], s[4:5] op_sel_hi:[1,0]
	v_pk_mul_f32 v[40:41], v[46:47], s[4:5] op_sel_hi:[1,0]
	v_cvt_pk_fp8_f32 v34, v36, v37 op_sel:[0,0,1]
	v_cvt_pk_fp8_f32 v35, v38, v39 op_sel:[0,0,1]
	v_pk_mul_f32 v[38:39], v[42:43], s[4:5] op_sel_hi:[1,0]
	v_mov_b32_e32 v36, v131
	v_cvt_pk_fp8_f32 v36, v38, v39
	v_pk_mul_f32 v[38:39], v[44:45], s[4:5] op_sel_hi:[1,0]
	v_mov_b32_e32 v37, v131
	v_cvt_pk_fp8_f32 v37, v40, v41
	v_cvt_pk_fp8_f32 v36, v38, v39 op_sel:[0,0,1]
	v_lshl_add_u32 v38, v51, 4, s6
	v_or_b32_e32 v38, s5, v38
	v_ashrrev_i32_e32 v39, 31, v38
	v_lshlrev_b64 v[38:39], 12, v[38:39]
	v_ashrrev_i32_e32 v51, 31, v50
	v_pk_mul_f32 v[40:41], v[48:49], s[4:5] op_sel_hi:[1,0]
	v_lshl_add_u64 v[38:39], v[38:39], 0, v[50:51]
	v_cvt_pk_fp8_f32 v37, v40, v41 op_sel:[0,0,1]
	v_mad_u64_u32 v[40:41], s[8:9], v38, s7, v[114:115]
	v_mad_i32_i24 v41, v39, s7, v41
	v_lshl_add_u64 v[38:39], v[40:41], 0, s[0:1]
	v_lshl_add_u64 v[38:39], v[38:39], 0, v[130:131]
	global_store_dwordx4 v[38:39], v[34:37], off
	v_pk_mul_f32 v[22:23], v[22:23], s[4:5] op_sel_hi:[1,0]
	v_pk_mul_f32 v[20:21], v[20:21], s[4:5] op_sel_hi:[1,0]
	v_add_u32_e32 v34, 0xa0, v1
	v_ashrrev_i32_e32 v35, 31, v34
	v_lshrrev_b32_e32 v35, 20, v35
	v_add_u32_e32 v35, v34, v35
	v_ashrrev_i32_e32 v35, 12, v35
	v_mul_i32_i24_e32 v36, 0x1000, v35
	v_sub_u32_e32 v34, v34, v36
	v_pk_mul_f32 v[36:37], v[18:19], s[4:5] op_sel_hi:[1,0]
	v_mov_b32_e32 v18, v131
	v_mov_b32_e32 v19, v131
	v_cvt_pk_fp8_f32 v18, v36, v37
	v_cvt_pk_fp8_f32 v19, v22, v23
	v_pk_mul_f32 v[22:23], v[24:25], s[4:5] op_sel_hi:[1,0]
	v_pk_mul_f32 v[24:25], v[30:31], s[4:5] op_sel_hi:[1,0]
	v_cvt_pk_fp8_f32 v18, v20, v21 op_sel:[0,0,1]
	v_cvt_pk_fp8_f32 v19, v22, v23 op_sel:[0,0,1]
	v_pk_mul_f32 v[22:23], v[26:27], s[4:5] op_sel_hi:[1,0]
	v_mov_b32_e32 v20, v131
	v_cvt_pk_fp8_f32 v20, v22, v23
	v_pk_mul_f32 v[22:23], v[28:29], s[4:5] op_sel_hi:[1,0]
	v_mov_b32_e32 v21, v131
	v_cvt_pk_fp8_f32 v21, v24, v25
	v_cvt_pk_fp8_f32 v20, v22, v23 op_sel:[0,0,1]
	v_lshl_add_u32 v22, v35, 4, s6
	v_or_b32_e32 v22, s5, v22
	v_ashrrev_i32_e32 v23, 31, v22
	v_lshlrev_b64 v[22:23], 12, v[22:23]
	v_ashrrev_i32_e32 v35, 31, v34
	v_pk_mul_f32 v[24:25], v[32:33], s[4:5] op_sel_hi:[1,0]
	v_lshl_add_u64 v[22:23], v[22:23], 0, v[34:35]
	v_cvt_pk_fp8_f32 v21, v24, v25 op_sel:[0,0,1]
; template <class P, class MK = NoChain>
; __device__ __forceinline__ void gemm_phase(LAS unsigned char* lds, const P& p, const MK& mk = MK(), bool chain_out = false, bool chained_in = false) {
;     ...
;     int tid = threadIdx.x; asm volatile("" : "+v"(tid));
;     const int wid = __builtin_amdgcn_readfirstlane(tid >> 6), lane = tid & 63, wr = wid >> 2, wc = wid & 3, fr = lane & 15, fq = lane >> 4;
;     unsigned voffB[2], vA[2][2], nvA[2][2], nvB[2]; typedef decltype(mk()) NP; constexpr int NES = NP::FP8 ? 1 : 2; constexpr int NBMODE = bmode_of<NP>::value; constexpr size_t nhstepB = (size_t)(NBMODE == 1 ? 8 : (NBMODE == 2 ? 16 : HALF)) * NP::LDB * NES;
;     constexpr size_t kstep = (size_t)(BK * 2);
;     constexpr int BMODE = bmode_of<P>::value;
;     constexpr size_t hstep = (size_t)(BMODE == 1 ? 8 : (BMODE == 2 ? 16 : HALF)) * LDB * ES, hstepA = (size_t)HALF * LDA * ES;
; #pragma unroll
;     for (int i = 0; i < 2; ++i) { int R, C; stage_rc(tid * 16 + i * 8192, R, C); const int rho_ = R & 31;
;         const int fq_ = (rho_ & 15) >> 2, n_ = rho_ >> 4, q_ = rho_ & 3;
;         const int Rb = BMODE == 1 ? ((R >> 5) * 64 + fq_ * 16 + 4 * n_ + q_) : (BMODE == 2 ? ((R >> 5) * 64 + 32 * (fq_ >> 1) + 8 * n_ + 4 * (fq_ & 1) + q_) : (P::PERM ? ((R & ~31) + perm32(R & 31)) : R));
;         voffB[i] = (unsigned)(Rb * LDB * ES + C * 2); vA[0][i] = (unsigned)(R * LDA * ES + C * 2); vA[1][i] = vA[0][i] + (unsigned)hstepA; nvA[0][i] = vA[0][i]; nvA[1][i] = vA[1][i]; nvB[i] = voffB[i]; }
;     const unsigned ldsw = (unsigned)wid * 1024u;
;     const int aoff = lds_byte(wr * 64 + fr, fq * 8), boff = lds_byte(wc * 32 + fr, fq * 8); const int aoff1 = aoff ^ 64, boff1 = boff ^ 64;
;     ...
;     Unit cur, nxt; int ui = 0;
;     if (!p.next(0, cur)) return;
;     Acc acc;
;     if constexpr (!PEEL) {
; #pragma unroll
;     for (int a = 0; a < 2; ++a)
; #pragma unroll
;         for (int b = 0; b < 2; ++b)
; #pragma unroll
;             for (int m = 0; m < 4; ++m)
; #pragma unroll
;                 for (int n = 0; n < 2; ++n) { typedef double d2_ __attribute__((ext_vector_type(2))); d2_ z_; asm volatile("v_mov_b64 %0, 0" : "=v"(z_.x)); asm volatile("v_mov_b64 %0, 0" : "=v"(z_.y)); acc[a][b][m][n] = __builtin_bit_cast(f32x4, z_); }
;     }
;     typedef int v8i_ __attribute__((ext_vector_type(8))); typedef int v4i_ __attribute__((ext_vector_type(4)));
	v_mad_u64_u32 v[24:25], s[8:9], v22, s7, v[114:115]
	v_mad_i32_i24 v25, v23, s7, v25
	v_lshl_add_u64 v[22:23], v[24:25], 0, s[0:1]
	v_lshl_add_u64 v[22:23], v[22:23], 0, v[130:131]
	global_store_dwordx4 v[22:23], v[18:21], off
	v_pk_mul_f32 v[6:7], v[6:7], s[4:5] op_sel_hi:[1,0]
	v_add_u32_e32 v1, 0xb0, v1
	v_pk_mul_f32 v[20:21], v[2:3], s[4:5] op_sel_hi:[1,0]
	v_mov_b32_e32 v2, v131
	v_mov_b32_e32 v3, v131
	v_cvt_pk_fp8_f32 v2, v20, v21
	v_cvt_pk_fp8_f32 v3, v6, v7
	v_ashrrev_i32_e32 v18, 31, v1
	v_pk_mul_f32 v[4:5], v[4:5], s[4:5] op_sel_hi:[1,0]
	v_pk_mul_f32 v[6:7], v[8:9], s[4:5] op_sel_hi:[1,0]
	v_lshrrev_b32_e32 v18, 20, v18
	v_cvt_pk_fp8_f32 v2, v4, v5 op_sel:[0,0,1]
	v_cvt_pk_fp8_f32 v3, v6, v7 op_sel:[0,0,1]
	v_pk_mul_f32 v[6:7], v[10:11], s[4:5] op_sel_hi:[1,0]
	v_mov_b32_e32 v4, v131
	v_add_u32_e32 v18, v1, v18
	v_cvt_pk_fp8_f32 v4, v6, v7
	v_ashrrev_i32_e32 v19, 12, v18
	v_mul_i32_i24_e32 v18, 0x1000, v19
	v_sub_u32_e32 v18, v1, v18
	v_pk_mul_f32 v[8:9], v[14:15], s[4:5] op_sel_hi:[1,0]
	v_mov_b32_e32 v5, v131
	v_pk_mul_f32 v[6:7], v[12:13], s[4:5] op_sel_hi:[1,0]
	v_lshl_add_u32 v1, v19, 4, s6
	v_cvt_pk_fp8_f32 v5, v8, v9
	v_cvt_pk_fp8_f32 v4, v6, v7 op_sel:[0,0,1]
	v_or_b32_e32 v6, s5, v1
	v_ashrrev_i32_e32 v7, 31, v6
	v_lshlrev_b64 v[6:7], 12, v[6:7]
	v_ashrrev_i32_e32 v19, 31, v18
	v_pk_mul_f32 v[8:9], v[16:17], s[4:5] op_sel_hi:[1,0]
	v_lshl_add_u64 v[6:7], v[6:7], 0, v[18:19]
	v_cvt_pk_fp8_f32 v5, v8, v9 op_sel:[0,0,1]
	v_mad_u64_u32 v[8:9], s[4:5], v6, s7, v[114:115]
	v_mad_i32_i24 v9, v7, s7, v9
	v_lshl_add_u64 v[6:7], v[8:9], 0, s[0:1]
	v_readlane_b32 s0, v255, 0
	v_lshl_add_u64 v[6:7], v[6:7], 0, v[130:131]
	v_readlane_b32 s1, v255, 1
	global_store_dwordx4 v[6:7], v[2:5], off
	s_mov_b64 s[0:1], s[98:99]
	v_mov_b32_e32 v135, v131
	v_mov_b32_e32 v2, v0
	v_mov_b32_e32 v141, v131
	v_readfirstlane_b32 s20, v2
	s_ashr_i32 s21, s20, 2
	s_ashr_i32 s4, s20, 6
	v_and_b32_e32 v1, 15, v2
	v_lshrrev_b32_e32 v4, 4, v2
	v_bfe_u32 v5, v2, 1, 3
	s_and_b32 s22, s4, 3
	v_lshlrev_b32_e32 v3, 7, v1
	v_bitop3_b32 v5, v4, v5, 3 bitop3:0x6c
	s_and_b32 s5, s21, 0xffffffc0
	v_lshl_or_b32 v3, s22, 12, v3
	v_lshlrev_b32_e32 v5, 4, v5
	v_or_b32_e32 v1, s5, v1
	v_or_b32_e32 v143, v3, v5
	v_bitop3_b32 v144, v3, 64, v5 bitop3:0x36
	v_lshlrev_b32_e32 v3, 7, v1
	v_or_b32_e32 v145, v3, v5
	v_bitop3_b32 v146, v3, 64, v5 bitop3:0x36
	s_lshl_b32 s23, s4, 10
	v_mov_b32_e32 v3, 0x2000
	v_xor_b32_e32 v4, v4, v2
	v_lshl_add_u32 v3, v2, 4, v3
	v_lshlrev_b32_e32 v4, 4, v4
	s_waitcnt lgkmcnt(0)
	s_add_u32 s4, s0, s12
	v_ashrrev_i32_e32 v3, 7, v3
	v_and_b32_e32 v4, 0x70, v4
	s_addc_u32 s5, s1, s13
	v_lshl_or_b32 v132, v3, 9, v4
	v_lshlrev_b32_e32 v5, 2, v3
	v_and_b32_e32 v6, 7, v3
	v_lshlrev_b32_e32 v7, 1, v3
	v_lshrrev_b32_e32 v3, 1, v3
	s_add_u32 s24, s4, 0x4c00000
	v_and_b32_e32 v7, 0x7fffc0, v7
	v_and_b32_e32 v3, 8, v3
	v_and_or_b32 v5, v5, 32, v6
	s_addc_u32 s25, s5, 0
	v_bfe_u32 v142, v2, 4, 2
	v_or3_b32 v3, v5, v7, v3
	v_ashrrev_i32_e32 v2, 3, v2
	s_add_u32 s4, s0, s14
	v_lshl_or_b32 v136, v3, 9, v4
	v_lshl_or_b32 v138, v2, 9, v4
	v_lshlrev_b32_e32 v3, 2, v2
	v_and_b32_e32 v5, 7, v2
	v_lshlrev_b32_e32 v6, 1, v2
	v_lshrrev_b32_e32 v2, 1, v2
	s_addc_u32 s5, s1, s15
	v_and_b32_e32 v6, 0x7fffc0, v6
	v_and_b32_e32 v2, 8, v2
	v_and_or_b32 v3, v3, 32, v5
	s_add_u32 s26, s4, 0x46c00000
	v_or3_b32 v2, v3, v6, v2
	s_addc_u32 s27, s5, 0
	s_add_i32 s28, s23, 0
	s_add_i32 s31, s41, s23
	v_add_u32_e32 v134, 0x10000, v132
	v_add_u32_e32 v130, 0x10000, v138
	v_lshl_or_b32 v140, v2, 9, v4
	v_mov_b32_e32 v137, v131
	v_mov_b32_e32 v139, v131
	v_mov_b32_e32 v133, v131
	s_mov_b64 s[8:9], 0
	s_mov_b64 s[4:5], -1
	s_mov_b64 s[6:7], 0
	v_add_u32_e32 v145, 0, v145
	v_add_u32_e32 v146, 0, v146
	s_add_i32 s29, s28, 0xc000
	s_add_i32 s30, s28, 0xe000
	s_add_i32 s33, s31, 0x2000
	s_add_i32 s34, s28, 0x2000
	v_mov_b64 v[90:91], 0
	v_mov_b64 v[92:93], 0
	v_mov_b64 v[94:95], 0
	v_mov_b64 v[96:97], 0
	v_mov_b64 v[66:67], 0
	v_mov_b64 v[68:69], 0
	v_mov_b64 v[70:71], 0
	v_mov_b64 v[72:73], 0
	v_mov_b64 v[42:43], 0
	v_mov_b64 v[44:45], 0
	v_mov_b64 v[46:47], 0
	v_mov_b64 v[48:49], 0
	v_mov_b64 v[18:19], 0
	v_mov_b64 v[20:21], 0
	v_mov_b64 v[30:31], 0
	v_mov_b64 v[32:33], 0
	v_mov_b64 v[122:123], 0
	v_mov_b64 v[124:125], 0
	v_mov_b64 v[126:127], 0
	v_mov_b64 v[128:129], 0
	v_mov_b64 v[114:115], 0
	v_mov_b64 v[116:117], 0
	v_mov_b64 v[118:119], 0
	v_mov_b64 v[120:121], 0
	v_mov_b64 v[98:99], 0
	v_mov_b64 v[100:101], 0
	v_mov_b64 v[102:103], 0
	v_mov_b64 v[104:105], 0
	v_mov_b64 v[74:75], 0
	v_mov_b64 v[76:77], 0
	v_mov_b64 v[78:79], 0
	v_mov_b64 v[80:81], 0
	v_mov_b64 v[50:51], 0
	v_mov_b64 v[52:53], 0
	v_mov_b64 v[62:63], 0
	v_mov_b64 v[64:65], 0
	v_mov_b64 v[26:27], 0
	v_mov_b64 v[28:29], 0
	v_mov_b64 v[38:39], 0
	v_mov_b64 v[40:41], 0
	v_mov_b64 v[10:11], 0
	v_mov_b64 v[12:13], 0
	v_mov_b64 v[14:15], 0
	v_mov_b64 v[16:17], 0
	v_mov_b64 v[2:3], 0
	v_mov_b64 v[4:5], 0
	v_mov_b64 v[6:7], 0
	v_mov_b64 v[8:9], 0
	v_mov_b64 v[106:107], 0
	v_mov_b64 v[108:109], 0
	v_mov_b64 v[110:111], 0
	v_mov_b64 v[112:113], 0
	v_mov_b64 v[82:83], 0
	v_mov_b64 v[84:85], 0
	v_mov_b64 v[86:87], 0
	v_mov_b64 v[88:89], 0
	v_mov_b64 v[54:55], 0
	v_mov_b64 v[56:57], 0
	v_mov_b64 v[58:59], 0
	v_mov_b64 v[60:61], 0
	v_mov_b64 v[22:23], 0
	v_mov_b64 v[24:25], 0
	v_mov_b64 v[34:35], 0
	v_mov_b64 v[36:37], 0

; __device__ __forceinline__ int otid() { int t = threadIdx.x; asm volatile("" : "+v"(t)); return t; }
; __device__ __forceinline__ unsigned xb_ld(unsigned* p)              { return __hip_atomic_load(p, __ATOMIC_RELAXED, __HIP_MEMORY_SCOPE_AGENT); }
; __device__ __forceinline__ unsigned xb_add(unsigned* p, unsigned v) { return __hip_atomic_fetch_add(p, v, __ATOMIC_RELAXED, __HIP_MEMORY_SCOPE_AGENT); }
; __device__ __forceinline__ void xcd_barrier_complete(unsigned* bar, unsigned x, unsigned& nloc, unsigned& nx) {
;     const unsigned G = gridDim.x * gridDim.y * gridDim.z;
;     unsigned sum, cnt, mine, sp = 0u;
;     for (;;) {
;         sum = 0u; cnt = 0u; mine = 0u;
; #pragma unroll
;         for (unsigned j = 0; j < 16; ++j) { const unsigned c = xb_ld(&bar[XB_XCNT(j)]); sum += c; cnt += (c > 0u) ? 1u : 0u; mine = (j == x) ? c : mine; }
;         if (sum == G) break;
;         __builtin_amdgcn_s_sleep(1);
;         if ((++sp & 255u) == 0u) { if (xb_ld(&bar[XB_TMO])) break; if (sp > XB_SPIN_CAP) { atomicAdd(&bar[XB_TMO], 1u); break; } }
;     }
;     nloc = mine > 0u ? mine : 1u; nx = cnt > 0u ? cnt : 1u;
; }
; __device__ __forceinline__ void xcd_barrier(const XcdBarrier& b) {
;     asm volatile("s_waitcnt vmcnt(0)" ::: "memory");
;     __syncthreads();
;     if (otid() == 0) {
;         unsigned* bar = b.bar;
;         __builtin_amdgcn_s_waitcnt(0);
;         unsigned nloc = b.st[0], nx = b.st[1];
;         if (nloc == 0u) { xcd_barrier_complete(bar, b.x, nloc, nx); b.st[0] = nloc; b.st[1] = nx; }
;         const unsigned old = xb_add(&bar[XB_XSUB(b.x)], 1u);
;         const unsigned gen = old / nloc;
;         if (old + 1u == (gen + 1u) * nloc) {
;             __builtin_amdgcn_fence(__ATOMIC_RELEASE, "agent");
;             asm volatile("s_waitcnt vmcnt(0)" ::: "memory");
;             const unsigned og = xb_add(&bar[XB_TOP], 1u);
.LBB0_816:
	s_mov_b64 s[0:1], s[24:25]
	s_mov_b32 s0, s100
	s_waitcnt lgkmcnt(0)
	s_cmp_gt_i32 s0, 4
	s_cbranch_scc1 .LBB0_874
	s_mov_b64 s[0:1], s[24:25]
	s_mov_b32 s0, s101
	s_waitcnt lgkmcnt(0)
	s_cmp_lt_i32 s0, 5
	s_cbranch_scc1 .LBB0_873
	v_readlane_b32 s0, v255, 0
	v_readlane_b32 s1, v255, 1
	s_mov_b32 s0, s100
	s_waitcnt lgkmcnt(0)
	s_cmp_gt_i32 s0, 5
	s_cbranch_scc1 .LBB0_873
	v_readlane_b32 s0, v255, 0
	v_readlane_b32 s1, v255, 1
	s_mov_b32 s0, s101
	s_waitcnt lgkmcnt(0)
	s_cmp_lt_i32 s0, 6
	s_cbranch_scc1 .LBB0_873
	v_readlane_b32 s2, v255, 0
	v_readlane_b32 s3, v255, 1
	s_getreg_b32 s4, hwreg(HW_REG_XCC_ID, 0, 4)
	s_waitcnt vmcnt(0)
	v_mov_b32_e32 v1, v0
	s_waitcnt vmcnt(0)
	s_barrier
	s_nop 0
	v_cmp_eq_u32_e32 vcc, 0, v1
	s_and_saveexec_b64 s[0:1], vcc
	s_cbranch_execz .LBB0_872
	s_add_i32 s5, 0, 0x20020
	v_mov_b32_e32 v1, s5
	s_mov_b64 s[2:3], s[98:99]
	s_waitcnt vmcnt(0) expcnt(0) lgkmcnt(0)
	ds_read_b32 v3, v1
	s_add_i32 s5, 0, 0x20024
	v_mov_b32_e32 v1, s5
	ds_read_b32 v1, v1
	s_and_b32 s33, s4, 15
	s_waitcnt lgkmcnt(1)
	v_cmp_ne_u32_e32 vcc, 0, v3
	s_cbranch_vccnz .LBB0_836
	v_readlane_b32 s4, v255, 0
	v_readlane_b32 s5, v255, 1
	s_load_dwordx2 s[8:9], s[4:5], 0xe0
	s_load_dword s7, s[4:5], 0xe8
	s_add_u32 s4, s2, 0x4200
	s_addc_u32 s5, s3, 0
	s_add_u32 s6, s2, 0x4400
	s_waitcnt lgkmcnt(0)
	s_mul_i32 s46, s9, s8
	s_mul_i32 s46, s46, s7
	s_addc_u32 s7, s3, 0
	s_add_u32 s8, s2, 0x4500
	s_addc_u32 s9, s3, 0
	s_add_u32 s10, s2, 0x4600
	s_addc_u32 s11, s3, 0
	s_add_u32 s12, s2, 0x4700
	s_addc_u32 s13, s3, 0
	s_add_u32 s14, s2, 0x4800
	s_addc_u32 s15, s3, 0
	s_add_u32 s16, s2, 0x4900
	s_addc_u32 s17, s3, 0
	s_add_u32 s18, s2, 0x4a00
	s_addc_u32 s19, s3, 0
	s_add_u32 s20, s2, 0x4b00
	s_addc_u32 s21, s3, 0
	s_add_u32 s22, s2, 0x4c00
	s_addc_u32 s23, s3, 0
	s_add_u32 s24, s2, 0x4d00
	s_addc_u32 s25, s3, 0
	s_add_u32 s26, s2, 0x4e00
	s_addc_u32 s27, s3, 0
	s_add_u32 s28, s2, 0x4f00
	s_addc_u32 s29, s3, 0
	s_add_u32 s30, s2, 0x5000
	s_addc_u32 s31, s3, 0
	s_add_u32 s34, s2, 0x5100
	s_addc_u32 s35, s3, 0
	s_add_u32 s36, s2, 0x5200
	s_addc_u32 s37, s3, 0
	s_add_u32 s38, s2, 0x5300
	s_addc_u32 s39, s3, 0
	s_mov_b32 s47, 1
	v_mov_b32_e32 v17, 0
	s_branch .LBB0_824

; #define REP(k) for (int rep_ = 0; rep_ < ((REP_KIND == (k)) ? REP_N : 1); ++rep_)
; #define IN(k) (fresh_args()->ph_lo <= (k) && (k) < fresh_args()->ph_hi)
; #define SEAM(k) do { if (IN(k) && IN((k) + 1)) { XcdBarrier bar; bar.bar = (unsigned*)(fresh_args()->ws + WS_CTL) + CW_BAR; bar.x = xb_xcc_id(); bar.st = (volatile LAS unsigned*)(lds + LDS_TAB) + 8; xcd_barrier(bar); } } while (0)
; #define PHASE_ARGS() CArgs* A_p = fresh_args(); CArgs& A = *A_p; unsigned char* ws = A.ws; (void)ws;
; __device__ __forceinline__ void attn_phase(CArgs& A, unsigned char* lds, int l) {
;     constexpr int G = 256;
;     const unsigned char* Kb = A.ws + WS_K; const unsigned char* Vb = A.ws + WS_V; bf16* O = (bf16*)(A.ws + WS_O);
;     constexpr int NQB = SEQ / 256, NU = NB * NH * NQB;
;     const int c = blockIdx.x;
;     for (int i = 0; i * G < NU; ++i) {
;         int L;
;         { const int x = c & 7, j = c >> 3; L = (i * 16 + x * 2 + (j >> 4)) * NQB + (j & 15); }
;         if (L >= NU) break;
;         const int bh = L / NQB, qb = L % NQB, b = bh / NH, h = bh % NH;
;         att::attn_unit(A.ws + WS_CQN + ((size_t)b * SEQ + qb * 256) * QL, A.ws + WS_WUQ + ((size_t)l * NH * DQK + (size_t)h * DQK) * QL, (const f32x2*)(A.ws + WS_CS) + ((size_t)b * SEQ + qb * 256) * 32, Kb + (size_t)bh * SEQ * DQK, Vb + (size_t)bh * SEQ * DV, FP8_WO ? (bf16*)((unsigned char*)(A.ws + WS_O8) + ((size_t)b * SEQ + qb * 256) * DM + h * DV) : O + ((size_t)b * SEQ + qb * 256) * DM + h * DV, (char*)lds);
; template <int l> __device__ __forceinline__ void layer_body(LAS unsigned char* lds, unsigned char* lds_raw, int bx, int vcu) {
;     ...
;         if (KEN(5) && IN(pb + 3)) REP(5) { PHASE_ARGS(); attn_phase(A, lds_raw, l); } SEAM(pb + 3);
.LBB0_874:
	s_mov_b64 s[0:1], s[24:25]
	s_mov_b32 s0, s100
	s_waitcnt lgkmcnt(0)
	s_cmp_gt_i32 s0, 5
	s_cbranch_scc1 .LBB0_1090
	s_mov_b64 s[0:1], s[24:25]
	s_mov_b32 s0, s101
	s_waitcnt lgkmcnt(0)
	s_cmp_lt_i32 s0, 6
	s_cbranch_scc1 .LBB0_1090
	s_lshl_b32 s0, s95, 1
	s_and_b32 s2, s0, 14
	s_mov_b64 s[0:1], s[24:25]
	s_mov_b64 s[6:7], s[98:99]
	s_ashr_i32 s3, s95, 7
	s_add_i32 s2, s2, s3
	s_bfe_u32 s0, s95, 0x40003
	s_lshl_b32 s1, s2, 4
	s_or_b32 s68, s1, s0
	s_waitcnt lgkmcnt(0)
	s_add_u32 s69, s6, 0x4b000000
	s_addc_u32 s70, s7, 0
	s_add_u32 s71, s6, 0x4e000000
	s_addc_u32 s72, s7, 0
	s_add_u32 s73, s6, 0x46400000
	s_addc_u32 s74, s7, 0
	s_add_u32 s75, s6, 0x4400000
	s_addc_u32 s76, s7, 0
	s_add_u32 s77, s6, 0x200000
	s_addc_u32 s78, s7, 0
	s_add_u32 s79, s6, 0x35400000
	v_mbcnt_lo_u32_b32 v1, -1, 0
	s_addc_u32 s80, s7, 0
	s_mov_b32 s8, 0
	s_mov_b64 s[28:29], 0
	s_movk_i32 s81, 0xc0
	s_movk_i32 s82, 0xffc0
	s_mov_b32 s83, 0x2aaaaaab
	v_mov_b32_e32 v163, 0
	s_movk_i32 s84, 0xf000
	s_mov_b64 s[24:25], 0x4b006000
	s_mov_b64 s[26:27], 0x4e000080
	s_mov_b32 s85, 0x40e6d4ca
	s_mov_b64 s[30:31], 0x4b009000
	s_mov_b64 s[34:35], 0x4e0000c0
	s_mov_b64 s[36:37], 0x4b00c000
	s_mov_b64 s[38:39], 0x4e000100
	s_mov_b64 s[40:41], 0x4b00f000
	s_mov_b64 s[42:43], 0x4e000140
	s_mov_b64 s[44:45], 0x4b012000
	s_mov_b64 s[46:47], 0x4e000180
	s_mov_b64 s[48:49], 0x4b015000
	s_mov_b64 s[50:51], 0x4e0001c0
	s_mov_b64 s[52:53], 0x180
	s_mov_b64 s[54:55], 0x12000
	s_mov_b64 s[56:57], 0xf80
	s_mov_b64 s[58:59], 0xfc0
	v_mbcnt_hi_u32_b32 v1, -1, v1
	v_mov_b32_e32 v254, 0x1000
	v_mov_b32_e32 v186, 0x9000
	v_mov_b32_e32 v187, 0xc000
	v_mov_b32_e32 v188, 0xd000
	s_mov_b32 s2, 0
	s_branch .LBB0_879

; __device__ __forceinline__ int otid() { int t = threadIdx.x; asm volatile("" : "+v"(t)); return t; }
; __device__ __forceinline__ unsigned xb_ld(unsigned* p)              { return __hip_atomic_load(p, __ATOMIC_RELAXED, __HIP_MEMORY_SCOPE_AGENT); }
; __device__ __forceinline__ unsigned xb_add(unsigned* p, unsigned v) { return __hip_atomic_fetch_add(p, v, __ATOMIC_RELAXED, __HIP_MEMORY_SCOPE_AGENT); }
; __device__ __forceinline__ void xcd_barrier_complete(unsigned* bar, unsigned x, unsigned& nloc, unsigned& nx) {
;     const unsigned G = gridDim.x * gridDim.y * gridDim.z;
;     unsigned sum, cnt, mine, sp = 0u;
;     for (;;) {
;         sum = 0u; cnt = 0u; mine = 0u;
; #pragma unroll
;         for (unsigned j = 0; j < 16; ++j) { const unsigned c = xb_ld(&bar[XB_XCNT(j)]); sum += c; cnt += (c > 0u) ? 1u : 0u; mine = (j == x) ? c : mine; }
;         if (sum == G) break;
;         __builtin_amdgcn_s_sleep(1);
;         if ((++sp & 255u) == 0u) { if (xb_ld(&bar[XB_TMO])) break; if (sp > XB_SPIN_CAP) { atomicAdd(&bar[XB_TMO], 1u); break; } }
;     }
;     nloc = mine > 0u ? mine : 1u; nx = cnt > 0u ? cnt : 1u;
; }
; __device__ __forceinline__ void xcd_barrier(const XcdBarrier& b) {
;     asm volatile("s_waitcnt vmcnt(0)" ::: "memory");
;     __syncthreads();
;     if (otid() == 0) {
;         unsigned* bar = b.bar;
;         __builtin_amdgcn_s_waitcnt(0);
;         unsigned nloc = b.st[0], nx = b.st[1];
;         if (nloc == 0u) { xcd_barrier_complete(bar, b.x, nloc, nx); b.st[0] = nloc; b.st[1] = nx; }
;         const unsigned old = xb_add(&bar[XB_XSUB(b.x)], 1u);
;         const unsigned gen = old / nloc;
;         if (old + 1u == (gen + 1u) * nloc) {
;             __builtin_amdgcn_fence(__ATOMIC_RELEASE, "agent");
;             asm volatile("s_waitcnt vmcnt(0)" ::: "memory");
;             const unsigned og = xb_add(&bar[XB_TOP], 1u);
.LBB0_1090:
	s_mov_b64 s[0:1], s[24:25]
	s_mov_b32 s0, s100
	s_waitcnt lgkmcnt(0)
	s_cmp_gt_i32 s0, 5
	s_cbranch_scc1 .LBB0_1148
	s_mov_b64 s[0:1], s[24:25]
	s_mov_b32 s0, s101
	s_waitcnt lgkmcnt(0)
	s_cmp_lt_i32 s0, 6
	s_cbranch_scc1 .LBB0_1147
	v_readlane_b32 s0, v255, 0
	v_readlane_b32 s1, v255, 1
	s_mov_b32 s0, s100
	s_waitcnt lgkmcnt(0)
	s_cmp_gt_i32 s0, 6
	s_cbranch_scc1 .LBB0_1147
	v_readlane_b32 s0, v255, 0
	v_readlane_b32 s1, v255, 1
	s_mov_b32 s0, s101
	s_waitcnt lgkmcnt(0)
	s_cmp_lt_i32 s0, 7
	s_cbranch_scc1 .LBB0_1147
	v_readlane_b32 s2, v255, 0
	v_readlane_b32 s3, v255, 1
	s_getreg_b32 s4, hwreg(HW_REG_XCC_ID, 0, 4)
	s_waitcnt vmcnt(0)
	v_mov_b32_e32 v1, v0
	s_waitcnt vmcnt(0)
	s_barrier
	s_nop 0
	v_cmp_eq_u32_e32 vcc, 0, v1
	s_and_saveexec_b64 s[0:1], vcc
	s_cbranch_execz .LBB0_1146
	s_add_i32 s5, 0, 0x20020
	v_mov_b32_e32 v1, s5
	s_mov_b64 s[2:3], s[98:99]
	s_waitcnt vmcnt(0) expcnt(0) lgkmcnt(0)
	ds_read_b32 v3, v1
	s_add_i32 s5, 0, 0x20024
	v_mov_b32_e32 v1, s5
	ds_read_b32 v1, v1
	s_and_b32 s33, s4, 15
	s_waitcnt lgkmcnt(1)
	v_cmp_ne_u32_e32 vcc, 0, v3
	s_cbranch_vccnz .LBB0_1110
	v_readlane_b32 s4, v255, 0
	v_readlane_b32 s5, v255, 1
	s_load_dwordx2 s[8:9], s[4:5], 0xe0
	s_load_dword s7, s[4:5], 0xe8
	s_add_u32 s4, s2, 0x4200
	s_addc_u32 s5, s3, 0
	s_add_u32 s6, s2, 0x4400
	s_waitcnt lgkmcnt(0)
	s_mul_i32 s46, s9, s8
	s_mul_i32 s46, s46, s7
	s_addc_u32 s7, s3, 0
	s_add_u32 s8, s2, 0x4500
	s_addc_u32 s9, s3, 0
	s_add_u32 s10, s2, 0x4600
	s_addc_u32 s11, s3, 0
	s_add_u32 s12, s2, 0x4700
	s_addc_u32 s13, s3, 0
	s_add_u32 s14, s2, 0x4800
	s_addc_u32 s15, s3, 0
	s_add_u32 s16, s2, 0x4900
	s_addc_u32 s17, s3, 0
	s_add_u32 s18, s2, 0x4a00
	s_addc_u32 s19, s3, 0
	s_add_u32 s20, s2, 0x4b00
	s_addc_u32 s21, s3, 0
	s_add_u32 s22, s2, 0x4c00
	s_addc_u32 s23, s3, 0
	s_add_u32 s24, s2, 0x4d00
	s_addc_u32 s25, s3, 0
	s_add_u32 s26, s2, 0x4e00
	s_addc_u32 s27, s3, 0
	s_add_u32 s28, s2, 0x4f00
	s_addc_u32 s29, s3, 0
	s_add_u32 s30, s2, 0x5000
	s_addc_u32 s31, s3, 0
	s_add_u32 s34, s2, 0x5100
	s_addc_u32 s35, s3, 0
	s_add_u32 s36, s2, 0x5200
	s_addc_u32 s37, s3, 0
	s_add_u32 s38, s2, 0x5300
	s_addc_u32 s39, s3, 0
	s_mov_b32 s47, 1
	v_mov_b32_e32 v17, 0
	s_branch .LBB0_1098

; template <class P, class MK = NoChain>
; __device__ __forceinline__ void gemm_phase(LAS unsigned char* lds, const P& p, const MK& mk = MK(), bool chain_out = false, bool chained_in = false) {
;     ...
;     int tid = threadIdx.x; asm volatile("" : "+v"(tid));
;     const int wid = __builtin_amdgcn_readfirstlane(tid >> 6), lane = tid & 63, wr = wid >> 2, wc = wid & 3, fr = lane & 15, fq = lane >> 4;
;     unsigned voffB[2], vA[2][2], nvA[2][2], nvB[2]; typedef decltype(mk()) NP; constexpr int NES = NP::FP8 ? 1 : 2; constexpr int NBMODE = bmode_of<NP>::value; constexpr size_t nhstepB = (size_t)(NBMODE == 1 ? 8 : (NBMODE == 2 ? 16 : HALF)) * NP::LDB * NES;
;     constexpr size_t kstep = (size_t)(BK * 2);
;     constexpr int BMODE = bmode_of<P>::value;
;     constexpr size_t hstep = (size_t)(BMODE == 1 ? 8 : (BMODE == 2 ? 16 : HALF)) * LDB * ES, hstepA = (size_t)HALF * LDA * ES;
; #pragma unroll
;     for (int i = 0; i < 2; ++i) { int R, C; stage_rc(tid * 16 + i * 8192, R, C); const int rho_ = R & 31;
;         const int fq_ = (rho_ & 15) >> 2, n_ = rho_ >> 4, q_ = rho_ & 3;
;         const int Rb = BMODE == 1 ? ((R >> 5) * 64 + fq_ * 16 + 4 * n_ + q_) : (BMODE == 2 ? ((R >> 5) * 64 + 32 * (fq_ >> 1) + 8 * n_ + 4 * (fq_ & 1) + q_) : (P::PERM ? ((R & ~31) + perm32(R & 31)) : R));
;         voffB[i] = (unsigned)(Rb * LDB * ES + C * 2); vA[0][i] = (unsigned)(R * LDA * ES + C * 2); vA[1][i] = vA[0][i] + (unsigned)hstepA; nvA[0][i] = vA[0][i]; nvA[1][i] = vA[1][i]; nvB[i] = voffB[i]; }
;     const unsigned ldsw = (unsigned)wid * 1024u;
;     const int aoff = lds_byte(wr * 64 + fr, fq * 8), boff = lds_byte(wc * 32 + fr, fq * 8); const int aoff1 = aoff ^ 64, boff1 = boff ^ 64;
;     ...
;     Unit cur, nxt; int ui = 0;
;     if (!p.next(0, cur)) return;
;     Acc acc;
;     if constexpr (!PEEL) {
; #pragma unroll
;     for (int a = 0; a < 2; ++a)
; #pragma unroll
;         for (int b = 0; b < 2; ++b)
; #pragma unroll
;             for (int m = 0; m < 4; ++m)
; #pragma unroll
;                 for (int n = 0; n < 2; ++n) { typedef double d2_ __attribute__((ext_vector_type(2))); d2_ z_; asm volatile("v_mov_b64 %0, 0" : "=v"(z_.x)); asm volatile("v_mov_b64 %0, 0" : "=v"(z_.y)); acc[a][b][m][n] = __builtin_bit_cast(f32x4, z_); }
;     }
;     typedef int v8i_ __attribute__((ext_vector_type(8))); typedef int v4i_ __attribute__((ext_vector_type(4)));
.LBB0_1148:
	s_mov_b64 s[0:1], s[24:25]
	s_mov_b32 s0, s100
	s_waitcnt lgkmcnt(0)
	s_cmp_gt_i32 s0, 6
	s_cbranch_scc1 .LBB0_1186
	s_mov_b64 s[0:1], s[24:25]
	s_mov_b32 s0, s101
	s_waitcnt lgkmcnt(0)
	s_cmp_lt_i32 s0, 7
	s_cbranch_scc1 .LBB0_1186
	s_cmpk_lt_i32 s95, 0x100
	s_mov_b64 s[0:1], s[24:25]
	v_mov_b32_e32 v2, v0
	s_cselect_b64 s[2:3], -1, 0
	s_cmpk_gt_i32 s95, 0xff
	s_nop 0
	v_readfirstlane_b32 s17, v2
	s_cbranch_scc1 .LBB0_1152
	v_readlane_b32 s4, v255, 4
	s_and_b32 s4, s4, -8
	s_sub_i32 s4, s95, s4
	s_lshl_b32 s6, s4, 5
	s_mul_i32 s5, s4, 33
	s_cmp_lt_i32 s4, 0
	s_cselect_b32 s4, s5, s6
	s_add_i32 s4, s4, s96
	s_ashr_i32 s5, s4, 31
	s_lshr_b32 s5, s5, 26
	s_add_i32 s5, s4, s5
	s_ashr_i32 s6, s5, 6
	s_andn2_b32 s5, s5, 63
	s_sub_i32 s4, s4, s5
	s_bfe_i32 s5, s4, 0x80000
	s_bfe_u32 s5, s5, 0x3000c
	s_add_i32 s5, s4, s5
	s_bfe_i32 s7, s5, 0x80000
	s_and_b32 s5, s5, 0xf8
	s_sub_i32 s4, s4, s5
	s_lshl_b32 s6, s6, 3
	s_sext_i32_i16 s7, s7
	s_sext_i32_i8 s4, s4
	s_add_i32 s33, s6, s4
	s_ashr_i32 s22, s7, 3
.LBB0_1152:
	v_readlane_b32 s24, v255, 0
	s_andn2_b64 vcc, exec, s[2:3]
	v_readlane_b32 s25, v255, 1
	s_cbranch_vccnz .LBB0_1186
	v_lshrrev_b32_e32 v3, 4, v2
	v_ashrrev_i32_e32 v4, 3, v2
	s_mov_b64 s[2:3], s[98:99]
	v_xor_b32_e32 v1, v3, v2
	v_lshlrev_b32_e32 v5, 1, v4
	v_lshrrev_b32_e32 v6, 2, v4
	v_lshlrev_b32_e32 v1, 4, v1
	v_and_b32_e32 v5, 24, v5
	v_and_b32_e32 v6, 4, v6
	v_and_b32_e32 v7, 0x1fffe3, v4
	v_and_b32_e32 v1, 0x70, v1
	v_or3_b32 v5, v7, v6, v5
	v_lshl_or_b32 v194, v5, 11, v1
	v_mov_b32_e32 v5, 0x2000
	v_lshl_add_u32 v5, v2, 4, v5
	s_waitcnt lgkmcnt(0)
	s_add_u32 s0, s2, 0x35400000
	v_ashrrev_i32_e32 v5, 7, v5
	s_addc_u32 s1, s3, 0
	v_lshlrev_b32_e32 v6, 1, v5
	v_lshrrev_b32_e32 v7, 2, v5
	s_add_u32 s36, s2, 0x34400000
	v_and_b32_e32 v6, 24, v6
	v_and_b32_e32 v7, 4, v7
	v_and_b32_e32 v8, 0x1fffe3, v5
	s_addc_u32 s37, s3, 0
	v_or3_b32 v6, v8, v7, v6
	s_ashr_i32 s12, s17, 6
	s_ashr_i32 s23, s22, 31
	s_ashr_i32 s4, s17, 8
	v_lshl_or_b32 v196, v6, 11, v1
	s_lshl_b32 s39, s12, 10
	s_lshl_b64 s[6:7], s[22:23], 19
	v_mov_b32_e32 v6, v0
	v_mov_b64 v[186:187], 0
	v_mov_b64 v[188:189], 0
	v_mov_b64 v[182:183], 0
	v_mov_b64 v[184:185], 0
	v_mov_b64 v[170:171], 0
	v_mov_b64 v[172:173], 0
	v_mov_b64 v[162:163], 0
	v_mov_b64 v[164:165], 0
	v_mov_b64 v[154:155], 0
	v_mov_b64 v[156:157], 0
	v_mov_b64 v[146:147], 0
	v_mov_b64 v[148:149], 0
	v_mov_b64 v[138:139], 0
	v_mov_b64 v[140:141], 0
	v_mov_b64 v[130:131], 0
	v_mov_b64 v[132:133], 0
	v_mov_b64 v[190:191], 0
	v_mov_b64 v[192:193], 0
	v_mov_b64 v[178:179], 0
	v_mov_b64 v[180:181], 0
	v_mov_b64 v[174:175], 0
	v_mov_b64 v[176:177], 0
	v_mov_b64 v[166:167], 0
	v_mov_b64 v[168:169], 0
	v_mov_b64 v[158:159], 0
	v_mov_b64 v[160:161], 0
	v_mov_b64 v[150:151], 0
	v_mov_b64 v[152:153], 0
	v_mov_b64 v[142:143], 0
	v_mov_b64 v[144:145], 0
	v_mov_b64 v[134:135], 0
	v_mov_b64 v[136:137], 0
	v_mov_b64 v[122:123], 0
	v_mov_b64 v[124:125], 0
	v_mov_b64 v[114:115], 0
	v_mov_b64 v[116:117], 0
	v_mov_b64 v[106:107], 0
	v_mov_b64 v[108:109], 0
	v_mov_b64 v[98:99], 0
	v_mov_b64 v[100:101], 0
	v_mov_b64 v[90:91], 0
	v_mov_b64 v[92:93], 0
	v_mov_b64 v[82:83], 0
	v_mov_b64 v[84:85], 0
	v_mov_b64 v[74:75], 0
	v_mov_b64 v[76:77], 0
	v_mov_b64 v[66:67], 0
	v_mov_b64 v[68:69], 0
	v_mov_b64 v[126:127], 0
	v_mov_b64 v[128:129], 0
	v_mov_b64 v[118:119], 0
	v_mov_b64 v[120:121], 0
	v_mov_b64 v[110:111], 0
	v_mov_b64 v[112:113], 0
	v_mov_b64 v[102:103], 0
	v_mov_b64 v[104:105], 0
	v_mov_b64 v[94:95], 0
	v_mov_b64 v[96:97], 0
	v_mov_b64 v[86:87], 0
	v_mov_b64 v[88:89], 0
	v_mov_b64 v[78:79], 0
	v_mov_b64 v[80:81], 0
	v_mov_b64 v[70:71], 0
	v_mov_b64 v[72:73], 0
	s_add_u32 s24, s36, s6
	s_addc_u32 s25, s37, s7
	v_lshlrev_b32_e32 v7, 4, v6
	v_xor_b32_e32 v7, v7, v6
	v_lshlrev_b32_e32 v6, 8, v6
	s_add_i32 s23, s39, 0
	v_and_b32_e32 v6, 0xfffff800, v6
	s_mov_b64 s[6:7], s[24:25]
	s_add_i32 m0, s23, 0x10000
	s_movk_i32 s38, 0x70
	v_lshl_add_u32 v6, s33, 19, v6
	v_and_or_b32 v198, v7, s38, v6
	global_load_lds_dwordx4 v194, s[6:7]
	s_add_i32 m0, s23, 0x12000
	s_add_i32 s40, s23, 0x2000
	global_load_lds_dwordx4 v196, s[6:7]
	s_mov_b64 s[6:7], s[0:1]
	s_mov_b32 m0, s23
	v_add_u32_e32 v206, 0x20000, v198
	v_add_u32_e32 v210, 0x40000, v198
	global_load_lds_dwordx4 v198, s[6:7]
	s_mov_b32 m0, s40
	v_add_u32_e32 v208, 0x60000, v198
	global_load_lds_dwordx4 v206, s[6:7]
	s_add_u32 s6, s24, 0x40000
	s_addc_u32 s7, s25, 0
	s_add_i32 s41, s23, 0x14000
	s_mov_b32 m0, s41
	s_add_i32 s42, s23, 0x16000
	s_add_i32 s43, s23, 0x4000
	global_load_lds_dwordx4 v194, s[6:7]
	s_mov_b32 m0, s42
	s_add_i32 s44, s23, 0x6000
	global_load_lds_dwordx4 v196, s[6:7]
	s_mov_b64 s[6:7], s[0:1]
	s_mov_b32 m0, s43
	v_mov_b32_e32 v199, 0
	global_load_lds_dwordx4 v210, s[6:7]
	s_mov_b32 m0, s44
	s_mov_b32 s5, 0
	global_load_lds_dwordx4 v208, s[6:7]
	v_mov_b32_e32 v195, v199
	v_mov_b32_e32 v197, v199
	s_cmp_lg_u32 s4, 1
	v_mov_b32_e32 v207, v199
	s_cbranch_scc1 .LBB0_1155
	s_barrier

; __device__ __forceinline__ int otid() { int t = threadIdx.x; asm volatile("" : "+v"(t)); return t; }
; __device__ __forceinline__ unsigned xb_ld(unsigned* p)              { return __hip_atomic_load(p, __ATOMIC_RELAXED, __HIP_MEMORY_SCOPE_AGENT); }
; __device__ __forceinline__ unsigned xb_add(unsigned* p, unsigned v) { return __hip_atomic_fetch_add(p, v, __ATOMIC_RELAXED, __HIP_MEMORY_SCOPE_AGENT); }
; __device__ __forceinline__ void xcd_barrier_complete(unsigned* bar, unsigned x, unsigned& nloc, unsigned& nx) {
;     const unsigned G = gridDim.x * gridDim.y * gridDim.z;
;     unsigned sum, cnt, mine, sp = 0u;
;     for (;;) {
;         sum = 0u; cnt = 0u; mine = 0u;
; #pragma unroll
;         for (unsigned j = 0; j < 16; ++j) { const unsigned c = xb_ld(&bar[XB_XCNT(j)]); sum += c; cnt += (c > 0u) ? 1u : 0u; mine = (j == x) ? c : mine; }
;         if (sum == G) break;
;         __builtin_amdgcn_s_sleep(1);
;         if ((++sp & 255u) == 0u) { if (xb_ld(&bar[XB_TMO])) break; if (sp > XB_SPIN_CAP) { atomicAdd(&bar[XB_TMO], 1u); break; } }
;     }
;     nloc = mine > 0u ? mine : 1u; nx = cnt > 0u ? cnt : 1u;
; }
; __device__ __forceinline__ void xcd_barrier(const XcdBarrier& b) {
;     asm volatile("s_waitcnt vmcnt(0)" ::: "memory");
;     __syncthreads();
;     if (otid() == 0) {
;         unsigned* bar = b.bar;
;         __builtin_amdgcn_s_waitcnt(0);
;         unsigned nloc = b.st[0], nx = b.st[1];
;         if (nloc == 0u) { xcd_barrier_complete(bar, b.x, nloc, nx); b.st[0] = nloc; b.st[1] = nx; }
;         const unsigned old = xb_add(&bar[XB_XSUB(b.x)], 1u);
;         const unsigned gen = old / nloc;
;         if (old + 1u == (gen + 1u) * nloc) {
;             __builtin_amdgcn_fence(__ATOMIC_RELEASE, "agent");
;             asm volatile("s_waitcnt vmcnt(0)" ::: "memory");
;             const unsigned og = xb_add(&bar[XB_TOP], 1u);
.LBB0_1186:
	s_mov_b64 s[0:1], s[24:25]
	s_mov_b32 s0, s100
	s_waitcnt lgkmcnt(0)
	s_cmp_gt_i32 s0, 6
	s_cbranch_scc1 .LBB0_1244
	s_mov_b64 s[0:1], s[24:25]
	s_mov_b32 s0, s101
	s_waitcnt lgkmcnt(0)
	s_cmp_lt_i32 s0, 7
	s_cbranch_scc1 .LBB0_1243
	v_readlane_b32 s0, v255, 0
	v_readlane_b32 s1, v255, 1
	s_mov_b32 s0, s100
	s_waitcnt lgkmcnt(0)
	s_cmp_gt_i32 s0, 7
	s_cbranch_scc1 .LBB0_1243
	v_readlane_b32 s0, v255, 0
	v_readlane_b32 s1, v255, 1
	s_mov_b32 s0, s101
	s_waitcnt lgkmcnt(0)
	s_cmp_lt_i32 s0, 8
	s_cbranch_scc1 .LBB0_1243
	v_readlane_b32 s2, v255, 0
	v_readlane_b32 s3, v255, 1
	s_getreg_b32 s4, hwreg(HW_REG_XCC_ID, 0, 4)
	s_waitcnt vmcnt(0)
	v_mov_b32_e32 v1, v0
	s_waitcnt vmcnt(0)
	s_barrier
	s_nop 0
	v_cmp_eq_u32_e32 vcc, 0, v1
	s_and_saveexec_b64 s[0:1], vcc
	s_cbranch_execz .LBB0_1242
	s_add_i32 s5, 0, 0x20020
	v_mov_b32_e32 v1, s5
	s_mov_b64 s[2:3], s[98:99]
	s_waitcnt vmcnt(0) expcnt(0) lgkmcnt(0)
	ds_read_b32 v3, v1
	s_add_i32 s5, 0, 0x20024
	v_mov_b32_e32 v1, s5
	ds_read_b32 v1, v1
	s_and_b32 s33, s4, 15
	s_waitcnt lgkmcnt(1)
	v_cmp_ne_u32_e32 vcc, 0, v3
	s_cbranch_vccnz .LBB0_1206
	v_readlane_b32 s4, v255, 0
	v_readlane_b32 s5, v255, 1
	s_load_dwordx2 s[8:9], s[4:5], 0xe0
	s_load_dword s7, s[4:5], 0xe8
	s_add_u32 s4, s2, 0x4200
	s_addc_u32 s5, s3, 0
	s_add_u32 s6, s2, 0x4400
	s_waitcnt lgkmcnt(0)
	s_mul_i32 s46, s9, s8
	s_mul_i32 s46, s46, s7
	s_addc_u32 s7, s3, 0
	s_add_u32 s8, s2, 0x4500
	s_addc_u32 s9, s3, 0
	s_add_u32 s10, s2, 0x4600
	s_addc_u32 s11, s3, 0
	s_add_u32 s12, s2, 0x4700
	s_addc_u32 s13, s3, 0
	s_add_u32 s14, s2, 0x4800
	s_addc_u32 s15, s3, 0
	s_add_u32 s16, s2, 0x4900
	s_addc_u32 s17, s3, 0
	s_add_u32 s18, s2, 0x4a00
	s_addc_u32 s19, s3, 0
	s_add_u32 s20, s2, 0x4b00
	s_addc_u32 s21, s3, 0
	s_add_u32 s22, s2, 0x4c00
	s_addc_u32 s23, s3, 0
	s_add_u32 s24, s2, 0x4d00
	s_addc_u32 s25, s3, 0
	s_add_u32 s26, s2, 0x4e00
	s_addc_u32 s27, s3, 0
	s_add_u32 s28, s2, 0x4f00
	s_addc_u32 s29, s3, 0
	s_add_u32 s30, s2, 0x5000
	s_addc_u32 s31, s3, 0
	s_add_u32 s34, s2, 0x5100
	s_addc_u32 s35, s3, 0
	s_add_u32 s36, s2, 0x5200
	s_addc_u32 s37, s3, 0
	s_add_u32 s38, s2, 0x5300
	s_addc_u32 s39, s3, 0
	s_mov_b32 s47, 1
	v_mov_b32_e32 v17, 0
	s_branch .LBB0_1194

; template <class P, class MK = NoChain>
; __device__ __forceinline__ void gemm_phase(LAS unsigned char* lds, const P& p, const MK& mk = MK(), bool chain_out = false, bool chained_in = false) {
;     ...
;     int tid = threadIdx.x; asm volatile("" : "+v"(tid));
;     const int wid = __builtin_amdgcn_readfirstlane(tid >> 6), lane = tid & 63, wr = wid >> 2, wc = wid & 3, fr = lane & 15, fq = lane >> 4;
;     unsigned voffB[2], vA[2][2], nvA[2][2], nvB[2]; typedef decltype(mk()) NP; constexpr int NES = NP::FP8 ? 1 : 2; constexpr int NBMODE = bmode_of<NP>::value; constexpr size_t nhstepB = (size_t)(NBMODE == 1 ? 8 : (NBMODE == 2 ? 16 : HALF)) * NP::LDB * NES;
;     constexpr size_t kstep = (size_t)(BK * 2);
;     constexpr int BMODE = bmode_of<P>::value;
;     constexpr size_t hstep = (size_t)(BMODE == 1 ? 8 : (BMODE == 2 ? 16 : HALF)) * LDB * ES, hstepA = (size_t)HALF * LDA * ES;
; #pragma unroll
;     for (int i = 0; i < 2; ++i) { int R, C; stage_rc(tid * 16 + i * 8192, R, C); const int rho_ = R & 31;
;         const int fq_ = (rho_ & 15) >> 2, n_ = rho_ >> 4, q_ = rho_ & 3;
;         const int Rb = BMODE == 1 ? ((R >> 5) * 64 + fq_ * 16 + 4 * n_ + q_) : (BMODE == 2 ? ((R >> 5) * 64 + 32 * (fq_ >> 1) + 8 * n_ + 4 * (fq_ & 1) + q_) : (P::PERM ? ((R & ~31) + perm32(R & 31)) : R));
;         voffB[i] = (unsigned)(Rb * LDB * ES + C * 2); vA[0][i] = (unsigned)(R * LDA * ES + C * 2); vA[1][i] = vA[0][i] + (unsigned)hstepA; nvA[0][i] = vA[0][i]; nvA[1][i] = vA[1][i]; nvB[i] = voffB[i]; }
;     const unsigned ldsw = (unsigned)wid * 1024u;
;     const int aoff = lds_byte(wr * 64 + fr, fq * 8), boff = lds_byte(wc * 32 + fr, fq * 8); const int aoff1 = aoff ^ 64, boff1 = boff ^ 64;
;     ...
;     Unit cur, nxt; int ui = 0;
;     if (!p.next(0, cur)) return;
;     Acc acc;
;     if constexpr (!PEEL) {
; #pragma unroll
;     for (int a = 0; a < 2; ++a)
; #pragma unroll
;         for (int b = 0; b < 2; ++b)
; #pragma unroll
;             for (int m = 0; m < 4; ++m)
; #pragma unroll
;                 for (int n = 0; n < 2; ++n) { typedef double d2_ __attribute__((ext_vector_type(2))); d2_ z_; asm volatile("v_mov_b64 %0, 0" : "=v"(z_.x)); asm volatile("v_mov_b64 %0, 0" : "=v"(z_.y)); acc[a][b][m][n] = __builtin_bit_cast(f32x4, z_); }
;     }
;     typedef int v8i_ __attribute__((ext_vector_type(8))); typedef int v4i_ __attribute__((ext_vector_type(4)));
.LBB0_1244:
	s_mov_b64 s[0:1], s[24:25]
	s_mov_b32 s0, s100
	s_waitcnt lgkmcnt(0)
	s_cmp_gt_i32 s0, 7
	s_cbranch_scc1 .LBB0_1282
	s_mov_b64 s[0:1], s[24:25]
	s_mov_b32 s0, s101
	s_waitcnt lgkmcnt(0)
	s_cmp_lt_i32 s0, 8
	s_cbranch_scc1 .LBB0_1282
	s_cmpk_lt_i32 s95, 0x100
	s_mov_b64 s[4:5], s[24:25]
	v_mov_b32_e32 v2, v0
	s_cselect_b64 s[0:1], -1, 0
	s_cmpk_gt_i32 s95, 0xff
	s_nop 0
	v_readfirstlane_b32 s15, v2
	s_cbranch_scc1 .LBB0_1248
	v_readlane_b32 s2, v255, 4
	s_and_b32 s2, s2, -8
	s_sub_i32 s2, s95, s2
	s_lshl_b32 s6, s2, 5
	s_mul_i32 s3, s2, 33
	s_cmp_lt_i32 s2, 0
	s_cselect_b32 s2, s3, s6
	s_add_i32 s2, s2, s96
	s_ashr_i32 s3, s2, 31
	s_lshr_b32 s3, s3, 26
	s_add_i32 s3, s2, s3
	s_ashr_i32 s6, s3, 6
	s_andn2_b32 s3, s3, 63
	s_sub_i32 s2, s2, s3
	s_bfe_i32 s3, s2, 0x80000
	s_bfe_u32 s3, s3, 0x3000c
	s_add_i32 s3, s2, s3
	s_bfe_i32 s7, s3, 0x80000
	s_and_b32 s3, s3, 0xf8
	s_sub_i32 s2, s2, s3
	s_lshl_b32 s6, s6, 3
	s_sext_i32_i16 s7, s7
	s_sext_i32_i8 s2, s2
	s_add_i32 s33, s6, s2
	s_ashr_i32 s20, s7, 3
.LBB0_1248:
	v_readlane_b32 s24, v255, 0
	s_andn2_b64 vcc, exec, s[0:1]
	v_readlane_b32 s25, v255, 1
	s_cbranch_vccnz .LBB0_1282
	s_mov_b64 s[2:3], s[98:99]
	s_load_dwordx2 s[0:1], s[4:5], 0x0
	v_lshlrev_b32_e32 v1, 4, v2
	v_lshlrev_b32_e32 v3, 8, v2
	v_xor_b32_e32 v1, v1, v2
	s_waitcnt lgkmcnt(0)
	s_add_u32 s4, s2, 0x36400000
	s_addc_u32 s5, s3, 0
	s_add_u32 s34, s2, 0x34c00000
	s_addc_u32 s35, s3, 0
	v_and_b32_e32 v3, 0xfffff800, v3
	s_movk_i32 s36, 0x70
	s_ashr_i32 s10, s15, 6
	s_ashr_i32 s21, s20, 31
	s_ashr_i32 s6, s15, 8
	v_and_or_b32 v194, v1, s36, v3
	s_lshl_b32 s37, s10, 10
	s_lshl_b64 s[8:9], s[20:21], 19
	v_mov_b32_e32 v1, v0
	v_mov_b64 v[178:179], 0
	v_mov_b64 v[180:181], 0
	v_mov_b64 v[182:183], 0
	v_mov_b64 v[184:185], 0
	v_mov_b64 v[162:163], 0
	v_mov_b64 v[164:165], 0
	v_mov_b64 v[166:167], 0
	v_mov_b64 v[168:169], 0
	v_mov_b64 v[146:147], 0
	v_mov_b64 v[148:149], 0
	v_mov_b64 v[150:151], 0
	v_mov_b64 v[152:153], 0
	v_mov_b64 v[122:123], 0
	v_mov_b64 v[124:125], 0
	v_mov_b64 v[126:127], 0
	v_mov_b64 v[128:129], 0
	v_mov_b64 v[186:187], 0
	v_mov_b64 v[188:189], 0
	v_mov_b64 v[190:191], 0
	v_mov_b64 v[192:193], 0
	v_mov_b64 v[170:171], 0
	v_mov_b64 v[172:173], 0
	v_mov_b64 v[174:175], 0
	v_mov_b64 v[176:177], 0
	v_mov_b64 v[154:155], 0
	v_mov_b64 v[156:157], 0
	v_mov_b64 v[158:159], 0
	v_mov_b64 v[160:161], 0
	v_mov_b64 v[138:139], 0
	v_mov_b64 v[140:141], 0
	v_mov_b64 v[142:143], 0
	v_mov_b64 v[144:145], 0
	v_mov_b64 v[114:115], 0
	v_mov_b64 v[116:117], 0
	v_mov_b64 v[118:119], 0
	v_mov_b64 v[120:121], 0
	v_mov_b64 v[98:99], 0
	v_mov_b64 v[100:101], 0
	v_mov_b64 v[102:103], 0
	v_mov_b64 v[104:105], 0
	v_mov_b64 v[82:83], 0
	v_mov_b64 v[84:85], 0
	v_mov_b64 v[86:87], 0
	v_mov_b64 v[88:89], 0
	v_mov_b64 v[66:67], 0
	v_mov_b64 v[68:69], 0
	v_mov_b64 v[70:71], 0
	v_mov_b64 v[72:73], 0
	v_mov_b64 v[130:131], 0
	v_mov_b64 v[132:133], 0
	v_mov_b64 v[134:135], 0
	v_mov_b64 v[136:137], 0
	v_mov_b64 v[106:107], 0
	v_mov_b64 v[108:109], 0
	v_mov_b64 v[110:111], 0
	v_mov_b64 v[112:113], 0
	v_mov_b64 v[90:91], 0
	v_mov_b64 v[92:93], 0
	v_mov_b64 v[94:95], 0
	v_mov_b64 v[96:97], 0
	v_mov_b64 v[74:75], 0
	v_mov_b64 v[76:77], 0
	v_mov_b64 v[78:79], 0
	v_mov_b64 v[80:81], 0
	s_add_u32 s22, s34, s8
	s_addc_u32 s23, s35, s9
	v_lshlrev_b32_e32 v3, 4, v1
	v_xor_b32_e32 v3, v3, v1
	v_lshlrev_b32_e32 v1, 8, v1
	s_add_i32 s38, s37, 0
	v_and_b32_e32 v1, 0xfffff800, v1
	s_mov_b64 s[8:9], s[22:23]
	s_add_i32 m0, s38, 0x10000
	v_add_u32_e32 v196, 0x20000, v194
	v_lshl_add_u32 v1, s33, 19, v1
	v_and_or_b32 v198, v3, s36, v1
	global_load_lds_dwordx4 v194, s[8:9]
	s_add_i32 m0, s38, 0x12000
	s_add_i32 s39, s38, 0x2000
	global_load_lds_dwordx4 v196, s[8:9]
	s_mov_b64 s[8:9], s[4:5]
	s_mov_b32 m0, s38
	v_add_u32_e32 v208, 0x20000, v198
	v_add_u32_e32 v212, 0x40000, v198
	global_load_lds_dwordx4 v198, s[8:9]
	s_mov_b32 m0, s39
	v_add_u32_e32 v210, 0x60000, v198
	global_load_lds_dwordx4 v208, s[8:9]
	s_add_u32 s8, s22, 0x40000
	s_addc_u32 s9, s23, 0
	s_add_i32 s40, s38, 0x14000
	s_mov_b32 m0, s40
	s_add_i32 s41, s38, 0x16000
	s_add_i32 s42, s38, 0x4000
	global_load_lds_dwordx4 v194, s[8:9]
	s_mov_b32 m0, s41
	s_add_i32 s43, s38, 0x6000
	global_load_lds_dwordx4 v196, s[8:9]
	s_mov_b64 s[8:9], s[4:5]
	s_mov_b32 m0, s42
	v_mov_b32_e32 v199, 0
	global_load_lds_dwordx4 v212, s[8:9]
	s_mov_b32 m0, s43
	s_mov_b32 s7, 0
	global_load_lds_dwordx4 v210, s[8:9]
	v_mov_b32_e32 v195, v199
	v_mov_b32_e32 v197, v199
	s_cmp_lg_u32 s6, 1
	v_mov_b32_e32 v209, v199
	s_cbranch_scc1 .LBB0_1251
	s_barrier

; __device__ __forceinline__ int otid() { int t = threadIdx.x; asm volatile("" : "+v"(t)); return t; }
; __device__ __forceinline__ unsigned xb_ld(unsigned* p)              { return __hip_atomic_load(p, __ATOMIC_RELAXED, __HIP_MEMORY_SCOPE_AGENT); }
; __device__ __forceinline__ unsigned xb_add(unsigned* p, unsigned v) { return __hip_atomic_fetch_add(p, v, __ATOMIC_RELAXED, __HIP_MEMORY_SCOPE_AGENT); }
; __device__ __forceinline__ void xcd_barrier_complete(unsigned* bar, unsigned x, unsigned& nloc, unsigned& nx) {
;     const unsigned G = gridDim.x * gridDim.y * gridDim.z;
;     unsigned sum, cnt, mine, sp = 0u;
;     for (;;) {
;         sum = 0u; cnt = 0u; mine = 0u;
; #pragma unroll
;         for (unsigned j = 0; j < 16; ++j) { const unsigned c = xb_ld(&bar[XB_XCNT(j)]); sum += c; cnt += (c > 0u) ? 1u : 0u; mine = (j == x) ? c : mine; }
;         if (sum == G) break;
;         __builtin_amdgcn_s_sleep(1);
;         if ((++sp & 255u) == 0u) { if (xb_ld(&bar[XB_TMO])) break; if (sp > XB_SPIN_CAP) { atomicAdd(&bar[XB_TMO], 1u); break; } }
;     }
;     nloc = mine > 0u ? mine : 1u; nx = cnt > 0u ? cnt : 1u;
; }
; __device__ __forceinline__ void xcd_barrier(const XcdBarrier& b) {
;     asm volatile("s_waitcnt vmcnt(0)" ::: "memory");
;     __syncthreads();
;     if (otid() == 0) {
;         unsigned* bar = b.bar;
;         __builtin_amdgcn_s_waitcnt(0);
;         unsigned nloc = b.st[0], nx = b.st[1];
;         if (nloc == 0u) { xcd_barrier_complete(bar, b.x, nloc, nx); b.st[0] = nloc; b.st[1] = nx; }
;         const unsigned old = xb_add(&bar[XB_XSUB(b.x)], 1u);
;         const unsigned gen = old / nloc;
;         if (old + 1u == (gen + 1u) * nloc) {
;             __builtin_amdgcn_fence(__ATOMIC_RELEASE, "agent");
;             asm volatile("s_waitcnt vmcnt(0)" ::: "memory");
;             const unsigned og = xb_add(&bar[XB_TOP], 1u);
.LBB0_1282:
	s_mov_b64 s[0:1], s[24:25]
	s_mov_b32 s0, s100
	s_waitcnt lgkmcnt(0)
	s_cmp_gt_i32 s0, 7
	s_cbranch_scc1 .LBB0_1340
	s_mov_b64 s[0:1], s[24:25]
	s_mov_b32 s0, s101
	s_waitcnt lgkmcnt(0)
	s_cmp_lt_i32 s0, 8
	s_cbranch_scc1 .LBB0_1339
	v_readlane_b32 s0, v255, 0
	v_readlane_b32 s1, v255, 1
	s_mov_b32 s0, s100
	s_waitcnt lgkmcnt(0)
	s_cmp_gt_i32 s0, 8
	s_cbranch_scc1 .LBB0_1339
	v_readlane_b32 s0, v255, 0
	v_readlane_b32 s1, v255, 1
	s_mov_b32 s0, s101
	s_waitcnt lgkmcnt(0)
	s_cmp_lt_i32 s0, 9
	s_cbranch_scc1 .LBB0_1339
	v_readlane_b32 s2, v255, 0
	v_readlane_b32 s3, v255, 1
	s_getreg_b32 s4, hwreg(HW_REG_XCC_ID, 0, 4)
	s_waitcnt vmcnt(0)
	v_mov_b32_e32 v1, v0
	s_waitcnt vmcnt(0)
	s_barrier
	s_nop 0
	v_cmp_eq_u32_e32 vcc, 0, v1
	s_and_saveexec_b64 s[0:1], vcc
	s_cbranch_execz .LBB0_1338
	s_add_i32 s5, 0, 0x20020
	v_mov_b32_e32 v1, s5
	s_mov_b64 s[2:3], s[98:99]
	s_waitcnt vmcnt(0) expcnt(0) lgkmcnt(0)
	ds_read_b32 v3, v1
	s_add_i32 s5, 0, 0x20024
	v_mov_b32_e32 v1, s5
	ds_read_b32 v1, v1
	s_and_b32 s33, s4, 15
	s_waitcnt lgkmcnt(1)
	v_cmp_ne_u32_e32 vcc, 0, v3
	s_cbranch_vccnz .LBB0_1302
	v_readlane_b32 s4, v255, 0
	v_readlane_b32 s5, v255, 1
	s_load_dwordx2 s[8:9], s[4:5], 0xe0
	s_load_dword s7, s[4:5], 0xe8
	s_add_u32 s4, s2, 0x4200
	s_addc_u32 s5, s3, 0
	s_add_u32 s6, s2, 0x4400
	s_waitcnt lgkmcnt(0)
	s_mul_i32 s46, s9, s8
	s_mul_i32 s46, s46, s7
	s_addc_u32 s7, s3, 0
	s_add_u32 s8, s2, 0x4500
	s_addc_u32 s9, s3, 0
	s_add_u32 s10, s2, 0x4600
	s_addc_u32 s11, s3, 0
	s_add_u32 s12, s2, 0x4700
	s_addc_u32 s13, s3, 0
	s_add_u32 s14, s2, 0x4800
	s_addc_u32 s15, s3, 0
	s_add_u32 s16, s2, 0x4900
	s_addc_u32 s17, s3, 0
	s_add_u32 s18, s2, 0x4a00
	s_addc_u32 s19, s3, 0
	s_add_u32 s20, s2, 0x4b00
	s_addc_u32 s21, s3, 0
	s_add_u32 s22, s2, 0x4c00
	s_addc_u32 s23, s3, 0
	s_add_u32 s24, s2, 0x4d00
	s_addc_u32 s25, s3, 0
	s_add_u32 s26, s2, 0x4e00
	s_addc_u32 s27, s3, 0
	s_add_u32 s28, s2, 0x4f00
	s_addc_u32 s29, s3, 0
	s_add_u32 s30, s2, 0x5000
	s_addc_u32 s31, s3, 0
	s_add_u32 s34, s2, 0x5100
	s_addc_u32 s35, s3, 0
	s_add_u32 s36, s2, 0x5200
	s_addc_u32 s37, s3, 0
	s_add_u32 s38, s2, 0x5300
	s_addc_u32 s39, s3, 0
	s_mov_b32 s47, 1
	v_mov_b32_e32 v17, 0
	s_branch .LBB0_1290

; #define LAS __attribute__((address_space(3)))
; #define IN(k) (fresh_args()->ph_lo <= (k) && (k) < fresh_args()->ph_hi)
; #define SEAM(k) do { if (IN(k) && IN((k) + 1)) { XcdBarrier bar; bar.bar = (unsigned*)(fresh_args()->ws + WS_CTL) + CW_BAR; bar.x = xb_xcc_id(); bar.st = (volatile LAS unsigned*)(lds + LDS_TAB) + 8; xcd_barrier(bar); } } while (0)
; #define PHASE_ARGS() CArgs* A_p = fresh_args(); CArgs& A = *A_p; unsigned char* ws = A.ws; (void)ws;
; __device__ __forceinline__ void nmr_phase(CArgs& A, const float* xin, int l, int vcu, LAS unsigned char* lds) {
;     int tid = threadIdx.x; asm volatile("" : "+v"(tid));
;     const int lane = tid & 63, wave = __builtin_amdgcn_readfirstlane(tid >> 6);
;     bf16* H = (bf16*)(A.ws + WS_H); int* LIST = (int*)(A.ws + WS_LIST);
;     unsigned* ASG = (unsigned*)(A.ws + WS_ASG); float* ASGW = (float*)(A.ws + WS_ASG + 512 * 1024);
;     unsigned* cnt = (unsigned*)(A.ws + WS_CTL) + CW_CNT + l * 64;
;     const int t0 = vcu * 32;
;     {
;         const float* g = A.in[I_GFFN] + (size_t)l * DM;
;         for (int r = 0; r < 4; ++r) { const int t = t0 + wave * 4 + r; const int b = t / SEQ; Row x; row_load_f32(x, xin + (size_t)t * DM, lane);
;             row_norm_mod_store(x, g, mod_ptr(A, l, b, 3), mod_ptr(A, l, b, 4), H + (size_t)t * DM, lane, A.ws + WS_H8 + (size_t)t * DM); }
; template <int l> __device__ __forceinline__ void layer_body(LAS unsigned char* lds, unsigned char* lds_raw, int bx, int vcu) {
;     ...
;         if (KEN(8) && IN(pb + 6)) { PHASE_ARGS(); nmr_phase(A, (const float*)(ws + WS_X), l, vcu, lds); } SEAM(pb + 6);
.LBB0_1340:
	s_mov_b64 s[0:1], s[24:25]
	s_mov_b32 s0, s100
	s_waitcnt lgkmcnt(0)
	s_cmp_gt_i32 s0, 8
	s_cbranch_scc1 .LBB0_1363
	s_mov_b64 s[0:1], s[24:25]
	s_mov_b32 s0, s101
	s_waitcnt lgkmcnt(0)
	s_cmp_lt_i32 s0, 9
	s_cbranch_scc1 .LBB0_1363
	s_mov_b64 s[4:5], s[24:25]
	s_mov_b64 s[2:3], s[98:99]
	v_mov_b32_e32 v38, v0
	s_lshl_b32 s6, s97, 5
	v_readfirstlane_b32 s0, v38
	s_ashr_i32 s22, s0, 6
	s_load_dwordx2 s[0:1], s[4:5], 0x78
	v_and_b32_e32 v1, 63, v38
	s_lshl_b32 s23, s22, 2
	s_add_i32 s6, s23, s6
	v_lshlrev_b32_e32 v2, 3, v1
	v_mov_b32_e32 v5, 0
	s_waitcnt lgkmcnt(0)
	s_add_u32 s24, s2, 0x10000
	v_or_b32_e32 v8, 0x400, v2
	v_or_b32_e32 v22, 0x600, v2
	s_addc_u32 s25, s3, 0
	v_lshlrev_b32_e32 v4, 5, v1
	v_lshlrev_b32_e32 v12, 2, v8
	v_mov_b32_e32 v13, v5
	v_lshlrev_b32_e32 v14, 2, v22
	v_mov_b32_e32 v15, v5
	s_ashr_i32 s7, s6, 31
	v_lshl_add_u64 v[10:11], s[0:1], 0, v[4:5]
	v_lshl_add_u64 v[12:13], s[0:1], 0, v[12:13]
	v_lshl_add_u64 v[14:15], s[0:1], 0, v[14:15]
	s_lshl_b64 s[0:1], s[6:7], 11
	v_or_b32_e32 v16, s0, v2
	v_mov_b32_e32 v17, s1
	s_lshl_b64 s[0:1], s[6:7], 12
	v_or_b32_e32 v6, 0x200, v2
	v_lshl_or_b32 v18, v1, 4, s0
	v_mov_b32_e32 v19, s1
	s_lshl_b64 s[0:1], s[6:7], 13
	v_or_b32_e32 v20, s0, v4
	v_mov_b32_e32 v21, s1
	s_mov_b32 s7, 0
	s_mov_b64 s[8:9], 0x38400000
	s_mov_b64 s[10:11], 0x38400800
	s_mov_b64 s[12:13], 0x38401000
	s_mov_b32 s26, 0x38401000
	s_mov_b64 s[14:15], 0x38401800
	v_mov_b32_e32 v36, 0x358637bd
	s_mov_b32 s27, 0x800000
	v_lshlrev_b32_e32 v37, 2, v2
	v_lshlrev_b32_e32 v39, 2, v6
	v_lshlrev_b32_e32 v40, 2, v8
	v_lshlrev_b32_e32 v41, 2, v22
	s_mov_b32 s28, 0x3c400000
	s_mov_b32 s29, 0x30c00000
	s_mov_b64 s[16:17], 0x800
	s_mov_b64 s[18:19], 0x1000
	s_mov_b64 s[20:21], 0x2000

; __device__ __forceinline__ int otid() { int t = threadIdx.x; asm volatile("" : "+v"(t)); return t; }
; __device__ __forceinline__ unsigned xb_ld(unsigned* p)              { return __hip_atomic_load(p, __ATOMIC_RELAXED, __HIP_MEMORY_SCOPE_AGENT); }
; __device__ __forceinline__ unsigned xb_add(unsigned* p, unsigned v) { return __hip_atomic_fetch_add(p, v, __ATOMIC_RELAXED, __HIP_MEMORY_SCOPE_AGENT); }
; __device__ __forceinline__ void xcd_barrier_complete(unsigned* bar, unsigned x, unsigned& nloc, unsigned& nx) {
;     const unsigned G = gridDim.x * gridDim.y * gridDim.z;
;     unsigned sum, cnt, mine, sp = 0u;
;     for (;;) {
;         sum = 0u; cnt = 0u; mine = 0u;
; #pragma unroll
;         for (unsigned j = 0; j < 16; ++j) { const unsigned c = xb_ld(&bar[XB_XCNT(j)]); sum += c; cnt += (c > 0u) ? 1u : 0u; mine = (j == x) ? c : mine; }
;         if (sum == G) break;
;         __builtin_amdgcn_s_sleep(1);
;         if ((++sp & 255u) == 0u) { if (xb_ld(&bar[XB_TMO])) break; if (sp > XB_SPIN_CAP) { atomicAdd(&bar[XB_TMO], 1u); break; } }
;     }
;     nloc = mine > 0u ? mine : 1u; nx = cnt > 0u ? cnt : 1u;
; }
; __device__ __forceinline__ void xcd_barrier(const XcdBarrier& b) {
;     asm volatile("s_waitcnt vmcnt(0)" ::: "memory");
;     __syncthreads();
;     if (otid() == 0) {
;         unsigned* bar = b.bar;
;         __builtin_amdgcn_s_waitcnt(0);
;         unsigned nloc = b.st[0], nx = b.st[1];
;         if (nloc == 0u) { xcd_barrier_complete(bar, b.x, nloc, nx); b.st[0] = nloc; b.st[1] = nx; }
;         const unsigned old = xb_add(&bar[XB_XSUB(b.x)], 1u);
;         const unsigned gen = old / nloc;
;         if (old + 1u == (gen + 1u) * nloc) {
;             __builtin_amdgcn_fence(__ATOMIC_RELEASE, "agent");
;             asm volatile("s_waitcnt vmcnt(0)" ::: "memory");
;             const unsigned og = xb_add(&bar[XB_TOP], 1u);
.LBB0_1363:
	s_mov_b64 s[0:1], s[24:25]
	s_mov_b32 s0, s100
	s_waitcnt lgkmcnt(0)
	s_cmp_gt_i32 s0, 8
	s_cbranch_scc1 .LBB0_1421
	s_mov_b64 s[0:1], s[24:25]
	s_mov_b32 s0, s101
	s_waitcnt lgkmcnt(0)
	s_cmp_lt_i32 s0, 9
	s_cbranch_scc1 .LBB0_1420
	v_readlane_b32 s0, v255, 0
	v_readlane_b32 s1, v255, 1
	s_mov_b32 s0, s100
	s_waitcnt lgkmcnt(0)
	s_cmp_gt_i32 s0, 9
	s_cbranch_scc1 .LBB0_1420
	v_readlane_b32 s0, v255, 0
	v_readlane_b32 s1, v255, 1
	s_mov_b32 s0, s101
	s_waitcnt lgkmcnt(0)
	s_cmp_lt_i32 s0, 10
	s_cbranch_scc1 .LBB0_1420
	v_readlane_b32 s2, v255, 0
	v_readlane_b32 s3, v255, 1
	s_getreg_b32 s4, hwreg(HW_REG_XCC_ID, 0, 4)
	s_waitcnt vmcnt(0)
	v_mov_b32_e32 v1, v0
	s_waitcnt vmcnt(0)
	s_barrier
	s_nop 0
	v_cmp_eq_u32_e32 vcc, 0, v1
	s_and_saveexec_b64 s[0:1], vcc
	s_cbranch_execz .LBB0_1419
	s_add_i32 s5, 0, 0x20020
	v_mov_b32_e32 v1, s5
	s_mov_b64 s[2:3], s[98:99]
	s_waitcnt vmcnt(0) expcnt(0) lgkmcnt(0)
	ds_read_b32 v3, v1
	s_add_i32 s5, 0, 0x20024
	v_mov_b32_e32 v1, s5
	ds_read_b32 v1, v1
	s_and_b32 s33, s4, 15
	s_waitcnt lgkmcnt(1)
	v_cmp_ne_u32_e32 vcc, 0, v3
	s_cbranch_vccnz .LBB0_1383
	v_readlane_b32 s4, v255, 0
	v_readlane_b32 s5, v255, 1
	s_load_dwordx2 s[8:9], s[4:5], 0xe0
	s_load_dword s7, s[4:5], 0xe8
	s_add_u32 s4, s2, 0x4200
	s_addc_u32 s5, s3, 0
	s_add_u32 s6, s2, 0x4400
	s_waitcnt lgkmcnt(0)
	s_mul_i32 s46, s9, s8
	s_mul_i32 s46, s46, s7
	s_addc_u32 s7, s3, 0
	s_add_u32 s8, s2, 0x4500
	s_addc_u32 s9, s3, 0
	s_add_u32 s10, s2, 0x4600
	s_addc_u32 s11, s3, 0
	s_add_u32 s12, s2, 0x4700
	s_addc_u32 s13, s3, 0
	s_add_u32 s14, s2, 0x4800
	s_addc_u32 s15, s3, 0
	s_add_u32 s16, s2, 0x4900
	s_addc_u32 s17, s3, 0
	s_add_u32 s18, s2, 0x4a00
	s_addc_u32 s19, s3, 0
	s_add_u32 s20, s2, 0x4b00
	s_addc_u32 s21, s3, 0
	s_add_u32 s22, s2, 0x4c00
	s_addc_u32 s23, s3, 0
	s_add_u32 s24, s2, 0x4d00
	s_addc_u32 s25, s3, 0
	s_add_u32 s26, s2, 0x4e00
	s_addc_u32 s27, s3, 0
	s_add_u32 s28, s2, 0x4f00
	s_addc_u32 s29, s3, 0
	s_add_u32 s30, s2, 0x5000
	s_addc_u32 s31, s3, 0
	s_add_u32 s34, s2, 0x5100
	s_addc_u32 s35, s3, 0
	s_add_u32 s36, s2, 0x5200
	s_addc_u32 s37, s3, 0
	s_add_u32 s38, s2, 0x5300
	s_addc_u32 s39, s3, 0
	s_mov_b32 s47, 1
	v_mov_b32_e32 v17, 0
	s_branch .LBB0_1371

; #define LAS __attribute__((address_space(3)))
; __device__ __forceinline__ int otid() { int t = threadIdx.x; asm volatile("" : "+v"(t)); return t; }
; __device__ __forceinline__ MoeTab moe_tables(CArgs& A, int l, LAS unsigned char* lds, bool want_order) {
;     MoeTab T; T.cnt = (LAS int*)(lds + LDS_TAB + 256); T.ts = T.cnt + 64; T.ord = (LAS int*)(lds + LDS_TAB + 1024) + 1;
;     unsigned* cg = (unsigned*)(A.ws + WS_CTL) + CW_CNT + l * 64;
;     const int tt = otid();
;     __syncthreads();
;     if (tt < 64) {
;         const int e = tt; const int c = (int)__hip_atomic_load(cg + e, RLX_AGENT);
;         T.cnt[e] = c;
;         const int nall = (c + 255) >> 8; const int ia = wave_incl_scan(nall, e);
;         T.ts[e] = ia - nall; if (e == 63) T.ts[64] = ia;
;         if (want_order) {
;             const int nfull = c >> 8, rem = c & 255;
;             const int n1 = nfull + (rem > 128 ? 1 : 0), nh = (rem != 0 && rem <= 128) ? 1 : 0;
;             const int p1 = wave_incl_scan(n1, e), ph = wave_incl_scan(nh, e);
;             const int tot1 = __builtin_amdgcn_readlane(p1, 63), toth = __builtin_amdgcn_readlane(ph, 63);
;             if (e < NT / 256) T.ord[e] = 64 | (e << 8);
;             const int pos = NT / 256 + p1 - n1;
; #pragma nounroll
;             for (int m = 0; m < n1; ++m) T.ord[pos + m] = e | (m << 8);
;             if (nh) T.ord[NT / 256 + tot1 + ph - 1] = e | (nfull << 8) | (1 << 16);
;             if (e == 0) T.ord[-1] = NT / 256 + tot1 + toth;
;         }
;     }
; template <int l> __device__ __forceinline__ void layer_body(LAS unsigned char* lds, unsigned char* lds_raw, int bx, int vcu) {
;     ...
;             Moe1P P; P.H = (const char*)(ws + WS_H8); P.W = (const char*)(ws + WS_W13E) + (size_t)l * NE * 1024 * DM; P.WSH = (const char*)(ws + WS_WSH8) + (size_t)l * 1024 * DM; P.LIST = (const int*)(ws + WS_LIST); P.ACT = (bf16*)(ws + WS_ACT); P.SACT = (bf16*)(ws + WS_SACT); P.T = moe_tables(A, l, lds, true); P.G = G; P.c = bx;
.LBB0_1421:
	s_mov_b64 s[0:1], s[24:25]
	s_mov_b32 s0, s100
	s_waitcnt lgkmcnt(0)
	s_cmp_gt_i32 s0, 9
	s_cbranch_scc1 .LBB0_1535
	s_mov_b64 s[0:1], s[24:25]
	s_mov_b32 s0, s101
	s_waitcnt lgkmcnt(0)
	s_cmp_lt_i32 s0, 10
	s_cbranch_scc1 .LBB0_1535
	s_mov_b64 s[0:1], s[24:25]
	s_mov_b64 s[14:15], s[98:99]
	v_mov_b32_e32 v2, v0
	s_waitcnt vmcnt(0) lgkmcnt(0)
	v_cmp_gt_i32_e32 vcc, 64, v2
	s_barrier
	s_and_saveexec_b64 s[16:17], vcc
	s_cbranch_execz .LBB0_1442
	v_ashrrev_i32_e32 v3, 31, v2
	v_mul_u32_u24_e32 v4, 0x1100, v2
	v_mov_b32_e32 v5, 0
	v_lshl_add_u64 v[4:5], v[4:5], 0, s[14:15]
	v_add_co_u32_e32 v4, vcc, 0x80000, v4
	v_cmp_lt_i32_e64 s[0:1], 0, v2
	s_nop 0
	v_addc_co_u32_e32 v5, vcc, 0, v5, vcc
	global_load_dword v3, v[4:5], off sc1
	v_mbcnt_lo_u32_b32 v4, -1, 0
	v_mbcnt_hi_u32_b32 v4, -1, v4
	v_and_b32_e32 v10, 64, v4
	v_add_u32_e32 v5, -1, v4
	v_cmp_lt_i32_e32 vcc, v5, v10
	v_add_u32_e32 v6, -2, v4
	v_add_u32_e32 v7, -4, v4
	v_cndmask_b32_e32 v5, v5, v4, vcc
	v_lshlrev_b32_e32 v5, 2, v5
	v_cmp_lt_i32_e32 vcc, v6, v10
	v_cmp_gt_i32_e64 s[2:3], 2, v2
	v_add_u32_e32 v8, -8, v4
	v_cndmask_b32_e32 v6, v6, v4, vcc
	v_lshlrev_b32_e32 v6, 2, v6
	v_cmp_lt_i32_e32 vcc, v7, v10
	v_cmp_gt_i32_e64 s[4:5], 4, v2
	v_add_u32_e32 v9, -16, v4
	v_cndmask_b32_e32 v7, v7, v4, vcc
	v_lshlrev_b32_e32 v7, 2, v7
	v_cmp_lt_i32_e32 vcc, v8, v10
	v_cmp_gt_i32_e64 s[6:7], 8, v2
	v_subrev_u32_e32 v11, 32, v4
	v_cndmask_b32_e32 v8, v8, v4, vcc
	v_lshlrev_b32_e32 v8, 2, v8
	v_cmp_lt_i32_e32 vcc, v9, v10
	v_cmp_gt_i32_e64 s[8:9], 16, v2
	v_cmp_gt_i32_e64 s[10:11], 32, v2
	v_cndmask_b32_e32 v9, v9, v4, vcc
	v_lshlrev_b32_e32 v9, 2, v9
	v_cmp_lt_i32_e32 vcc, v11, v10
	v_lshl_add_u32 v1, v2, 2, 0
	s_waitcnt vmcnt(0)
	v_add_u32_e32 v12, 0xff, v3
	v_ashrrev_i32_e32 v12, 8, v12
	ds_bpermute_b32 v13, v5, v12
	v_cndmask_b32_e32 v4, v11, v4, vcc
	v_lshlrev_b32_e32 v10, 2, v4
	v_cmp_eq_u32_e32 vcc, 63, v2
	s_waitcnt lgkmcnt(0)
	v_cndmask_b32_e64 v13, 0, v13, s[0:1]
	v_add_u32_e32 v13, v13, v12
	ds_bpermute_b32 v14, v6, v13
	s_waitcnt lgkmcnt(0)
	v_cndmask_b32_e64 v14, v14, 0, s[2:3]
	v_add_u32_e32 v13, v14, v13
	ds_bpermute_b32 v14, v7, v13
	s_waitcnt lgkmcnt(0)
	v_cndmask_b32_e64 v14, v14, 0, s[4:5]
	v_add_u32_e32 v13, v14, v13
	ds_bpermute_b32 v14, v8, v13
	s_waitcnt lgkmcnt(0)
	v_cndmask_b32_e64 v14, v14, 0, s[6:7]
	v_add_u32_e32 v13, v14, v13
	ds_bpermute_b32 v14, v9, v13
	s_waitcnt lgkmcnt(0)
	v_cndmask_b32_e64 v4, v14, 0, s[8:9]
	v_add_u32_e32 v4, v4, v13
	ds_bpermute_b32 v11, v10, v4
	v_add_u32_e32 v13, 0x20100, v1
	v_add_u32_e32 v14, 0x20200, v1
	ds_write_b32 v13, v3
	s_waitcnt lgkmcnt(1)
	v_cndmask_b32_e64 v11, v11, 0, s[10:11]
	v_add_u32_e32 v4, v11, v4
	v_sub_u32_e32 v11, v4, v12
	ds_write_b32 v14, v11
	s_and_saveexec_b64 s[12:13], vcc
	s_add_i32 s18, 0, 0x20300
	v_mov_b32_e32 v11, s18
	ds_write_b32 v11, v4
	s_or_b64 exec, exec, s[12:13]
	s_movk_i32 s18, 0x80
	v_ashrrev_i32_e32 v12, 8, v3
	v_cmp_gt_u32_sdwa s[12:13], v3, s18 src0_sel:BYTE_0 src1_sel:DWORD
	v_mov_b32_e32 v11, -1
	v_add_u32_sdwa v11, v3, v11 dst_sel:DWORD dst_unused:UNUSED_PAD src0_sel:BYTE_0 src1_sel:DWORD
	v_addc_co_u32_e64 v4, vcc, 0, v12, s[12:13]
	v_cmp_gt_u32_e32 vcc, s18, v11
	ds_bpermute_b32 v13, v5, v4
	s_nop 0
	v_cndmask_b32_e64 v11, 0, 1, vcc
	ds_bpermute_b32 v5, v5, v11
	s_waitcnt lgkmcnt(1)
	v_cndmask_b32_e64 v11, 0, v13, s[0:1]
	v_addc_co_u32_e64 v12, s[12:13], v11, v12, s[12:13]
	s_waitcnt lgkmcnt(0)
	v_cndmask_b32_e64 v5, 0, v5, s[0:1]
	v_addc_co_u32_e64 v14, s[0:1], 0, v5, vcc
	ds_bpermute_b32 v13, v6, v12
	ds_bpermute_b32 v14, v6, v14
	s_waitcnt lgkmcnt(1)
	v_cndmask_b32_e64 v6, v13, 0, s[2:3]
	s_waitcnt lgkmcnt(0)
	v_cndmask_b32_e64 v14, v14, 0, s[2:3]
	v_add_u32_e32 v12, v6, v12
	v_addc_co_u32_e64 v5, s[0:1], v14, v5, vcc
	ds_bpermute_b32 v13, v7, v12
	ds_bpermute_b32 v14, v7, v5
	s_waitcnt lgkmcnt(1)
	v_cndmask_b32_e64 v7, v13, 0, s[4:5]
	s_waitcnt lgkmcnt(0)
	v_cndmask_b32_e64 v14, v14, 0, s[4:5]
	v_add_u32_e32 v13, v7, v12
	v_add_u32_e32 v5, v14, v5
	ds_bpermute_b32 v12, v8, v13
	ds_bpermute_b32 v8, v8, v5
	s_waitcnt lgkmcnt(1)
	v_cndmask_b32_e64 v12, v12, 0, s[6:7]
	s_waitcnt lgkmcnt(0)
	v_cndmask_b32_e64 v8, v8, 0, s[6:7]
	v_add_u32_e32 v13, v12, v13
	v_add_u32_e32 v5, v8, v5
	ds_bpermute_b32 v14, v9, v13
	ds_bpermute_b32 v8, v9, v5
	s_waitcnt lgkmcnt(1)
	v_cndmask_b32_e64 v9, v14, 0, s[8:9]
	s_waitcnt lgkmcnt(0)
	v_cndmask_b32_e64 v8, v8, 0, s[8:9]
	v_add_u32_e32 v13, v9, v13
	v_add_u32_e32 v5, v8, v5
	ds_bpermute_b32 v14, v10, v13
	ds_bpermute_b32 v10, v10, v5
	s_waitcnt lgkmcnt(1)
	v_cndmask_b32_e64 v8, v14, 0, s[10:11]
	s_waitcnt lgkmcnt(0)
	v_cndmask_b32_e64 v10, v10, 0, s[10:11]
	v_add_u32_e32 v13, v8, v13
	v_add_u32_e32 v5, v10, v5
	v_readlane_b32 s8, v13, 63
	v_readlane_b32 s9, v5, 63
	s_and_saveexec_b64 s[0:1], s[10:11]
	v_add_u32_e32 v1, 0x20404, v1
	v_lshl_or_b32 v10, v2, 8, 64
	ds_write_b32 v1, v10
	s_or_b64 exec, exec, s[0:1]
	v_cmp_lt_i32_e64 s[0:1], 0, v4
	s_and_saveexec_b64 s[2:3], s[0:1]
	s_cbranch_execz .LBB0_1438
	v_add3_u32 v1, v11, v6, v7
	s_mov_b32 s10, 1
	v_cmp_ne_u32_e64 s[0:1], 1, v4
	s_mov_b64 s[6:7], 0
	v_add3_u32 v9, v1, v12, v9
	s_and_saveexec_b64 s[4:5], s[0:1]
	s_xor_b64 s[4:5], exec, s[4:5]
	s_cbranch_execnz .LBB0_1432
	s_andn2_saveexec_b64 s[0:1], s[4:5]
	s_cbranch_execnz .LBB0_1435

; __device__ __forceinline__ int otid() { int t = threadIdx.x; asm volatile("" : "+v"(t)); return t; }
; __device__ __forceinline__ unsigned xb_ld(unsigned* p)              { return __hip_atomic_load(p, __ATOMIC_RELAXED, __HIP_MEMORY_SCOPE_AGENT); }
; __device__ __forceinline__ unsigned xb_add(unsigned* p, unsigned v) { return __hip_atomic_fetch_add(p, v, __ATOMIC_RELAXED, __HIP_MEMORY_SCOPE_AGENT); }
; __device__ __forceinline__ void xcd_barrier_complete(unsigned* bar, unsigned x, unsigned& nloc, unsigned& nx) {
;     const unsigned G = gridDim.x * gridDim.y * gridDim.z;
;     unsigned sum, cnt, mine, sp = 0u;
;     for (;;) {
;         sum = 0u; cnt = 0u; mine = 0u;
; #pragma unroll
;         for (unsigned j = 0; j < 16; ++j) { const unsigned c = xb_ld(&bar[XB_XCNT(j)]); sum += c; cnt += (c > 0u) ? 1u : 0u; mine = (j == x) ? c : mine; }
;         if (sum == G) break;
;         __builtin_amdgcn_s_sleep(1);
;         if ((++sp & 255u) == 0u) { if (xb_ld(&bar[XB_TMO])) break; if (sp > XB_SPIN_CAP) { atomicAdd(&bar[XB_TMO], 1u); break; } }
;     }
;     nloc = mine > 0u ? mine : 1u; nx = cnt > 0u ? cnt : 1u;
; }
; __device__ __forceinline__ void xcd_barrier(const XcdBarrier& b) {
;     asm volatile("s_waitcnt vmcnt(0)" ::: "memory");
;     __syncthreads();
;     if (otid() == 0) {
;         unsigned* bar = b.bar;
;         __builtin_amdgcn_s_waitcnt(0);
;         unsigned nloc = b.st[0], nx = b.st[1];
;         if (nloc == 0u) { xcd_barrier_complete(bar, b.x, nloc, nx); b.st[0] = nloc; b.st[1] = nx; }
;         const unsigned old = xb_add(&bar[XB_XSUB(b.x)], 1u);
;         const unsigned gen = old / nloc;
;         if (old + 1u == (gen + 1u) * nloc) {
;             __builtin_amdgcn_fence(__ATOMIC_RELEASE, "agent");
;             asm volatile("s_waitcnt vmcnt(0)" ::: "memory");
;             const unsigned og = xb_add(&bar[XB_TOP], 1u);
.LBB0_1535:
	s_mov_b64 s[0:1], s[24:25]
	s_mov_b32 s0, s100
	s_waitcnt lgkmcnt(0)
	s_cmp_gt_i32 s0, 9
	s_cbranch_scc1 .LBB0_1593
	s_mov_b64 s[0:1], s[24:25]
	s_mov_b32 s0, s101
	s_waitcnt lgkmcnt(0)
	s_cmp_lt_i32 s0, 10
	s_cbranch_scc1 .LBB0_1592
	v_readlane_b32 s0, v255, 0
	v_readlane_b32 s1, v255, 1
	s_mov_b32 s0, s100
	s_waitcnt lgkmcnt(0)
	s_cmp_gt_i32 s0, 10
	s_cbranch_scc1 .LBB0_1592
	v_readlane_b32 s0, v255, 0
	v_readlane_b32 s1, v255, 1
	s_mov_b32 s0, s101
	s_waitcnt lgkmcnt(0)
	s_cmp_lt_i32 s0, 11
	s_cbranch_scc1 .LBB0_1592
	v_readlane_b32 s2, v255, 0
	v_readlane_b32 s3, v255, 1
	s_getreg_b32 s4, hwreg(HW_REG_XCC_ID, 0, 4)
	s_waitcnt vmcnt(0)
	v_mov_b32_e32 v1, v0
	s_waitcnt vmcnt(0)
	s_barrier
	s_nop 0
	v_cmp_eq_u32_e32 vcc, 0, v1
	s_and_saveexec_b64 s[0:1], vcc
	s_cbranch_execz .LBB0_1591
	s_add_i32 s5, 0, 0x20020
	v_mov_b32_e32 v1, s5
	s_mov_b64 s[2:3], s[98:99]
	s_waitcnt vmcnt(0) expcnt(0) lgkmcnt(0)
	ds_read_b32 v3, v1
	s_add_i32 s5, 0, 0x20024
	v_mov_b32_e32 v1, s5
	ds_read_b32 v1, v1
	s_and_b32 s33, s4, 15
	s_waitcnt lgkmcnt(1)
	v_cmp_ne_u32_e32 vcc, 0, v3
	s_cbranch_vccnz .LBB0_1555
	v_readlane_b32 s4, v255, 0
	v_readlane_b32 s5, v255, 1
	s_load_dwordx2 s[8:9], s[4:5], 0xe0
	s_load_dword s7, s[4:5], 0xe8
	s_add_u32 s4, s2, 0x4200
	s_addc_u32 s5, s3, 0
	s_add_u32 s6, s2, 0x4400
	s_waitcnt lgkmcnt(0)
	s_mul_i32 s46, s9, s8
	s_mul_i32 s46, s46, s7
	s_addc_u32 s7, s3, 0
	s_add_u32 s8, s2, 0x4500
	s_addc_u32 s9, s3, 0
	s_add_u32 s10, s2, 0x4600
	s_addc_u32 s11, s3, 0
	s_add_u32 s12, s2, 0x4700
	s_addc_u32 s13, s3, 0
	s_add_u32 s14, s2, 0x4800
	s_addc_u32 s15, s3, 0
	s_add_u32 s16, s2, 0x4900
	s_addc_u32 s17, s3, 0
	s_add_u32 s18, s2, 0x4a00
	s_addc_u32 s19, s3, 0
	s_add_u32 s20, s2, 0x4b00
	s_addc_u32 s21, s3, 0
	s_add_u32 s22, s2, 0x4c00
	s_addc_u32 s23, s3, 0
	s_add_u32 s24, s2, 0x4d00
	s_addc_u32 s25, s3, 0
	s_add_u32 s26, s2, 0x4e00
	s_addc_u32 s27, s3, 0
	s_add_u32 s28, s2, 0x4f00
	s_addc_u32 s29, s3, 0
	s_add_u32 s30, s2, 0x5000
	s_addc_u32 s31, s3, 0
	s_add_u32 s34, s2, 0x5100
	s_addc_u32 s35, s3, 0
	s_add_u32 s36, s2, 0x5200
	s_addc_u32 s37, s3, 0
	s_add_u32 s38, s2, 0x5300
	s_addc_u32 s39, s3, 0
	s_mov_b32 s47, 1
	v_mov_b32_e32 v17, 0
	s_branch .LBB0_1543

; #define LAS __attribute__((address_space(3)))
; __device__ __forceinline__ int otid() { int t = threadIdx.x; asm volatile("" : "+v"(t)); return t; }
; __device__ __forceinline__ MoeTab moe_tables(CArgs& A, int l, LAS unsigned char* lds, bool want_order) {
;     MoeTab T; T.cnt = (LAS int*)(lds + LDS_TAB + 256); T.ts = T.cnt + 64; T.ord = (LAS int*)(lds + LDS_TAB + 1024) + 1;
;     unsigned* cg = (unsigned*)(A.ws + WS_CTL) + CW_CNT + l * 64;
;     const int tt = otid();
;     __syncthreads();
;     if (tt < 64) {
;         const int e = tt; const int c = (int)__hip_atomic_load(cg + e, RLX_AGENT);
;         T.cnt[e] = c;
;         const int nall = (c + 255) >> 8; const int ia = wave_incl_scan(nall, e);
;         T.ts[e] = ia - nall; if (e == 63) T.ts[64] = ia;
;         if (want_order) {
;             const int nfull = c >> 8, rem = c & 255;
;             const int n1 = nfull + (rem > 128 ? 1 : 0), nh = (rem != 0 && rem <= 128) ? 1 : 0;
;             const int p1 = wave_incl_scan(n1, e), ph = wave_incl_scan(nh, e);
;             const int tot1 = __builtin_amdgcn_readlane(p1, 63), toth = __builtin_amdgcn_readlane(ph, 63);
;             if (e < NT / 256) T.ord[e] = 64 | (e << 8);
;             const int pos = NT / 256 + p1 - n1;
; #pragma nounroll
;             for (int m = 0; m < n1; ++m) T.ord[pos + m] = e | (m << 8);
;             if (nh) T.ord[NT / 256 + tot1 + ph - 1] = e | (nfull << 8) | (1 << 16);
;             if (e == 0) T.ord[-1] = NT / 256 + tot1 + toth;
;         }
;     }
; template <int l> __device__ __forceinline__ void layer_body(LAS unsigned char* lds, unsigned char* lds_raw, int bx, int vcu) {
;     ...
;             P.OUT2 = (bf16*)(ws + WS_OUT2); P.T = moe_tables(A, l, lds, true); P.G = G; P.c = bx;
.LBB0_1593:
	s_mov_b64 s[0:1], s[24:25]
	s_mov_b32 s0, s100
	s_waitcnt lgkmcnt(0)
	s_cmp_gt_i32 s0, 10
	s_cbranch_scc1 .LBB0_1669
	s_mov_b64 s[0:1], s[24:25]
	s_mov_b32 s0, s101
	s_waitcnt lgkmcnt(0)
	s_cmp_lt_i32 s0, 11
	s_cbranch_scc1 .LBB0_1669
	s_mov_b64 s[0:1], s[24:25]
	s_mov_b64 s[14:15], s[98:99]
	v_mov_b32_e32 v2, v0
	s_waitcnt vmcnt(0) lgkmcnt(0)
	v_cmp_gt_i32_e32 vcc, 64, v2
	s_barrier
	s_and_saveexec_b64 s[16:17], vcc
	s_cbranch_execz .LBB0_1614
	v_ashrrev_i32_e32 v3, 31, v2
	v_mul_u32_u24_e32 v4, 0x1100, v2
	v_mov_b32_e32 v5, 0
	v_lshl_add_u64 v[4:5], v[4:5], 0, s[14:15]
	v_add_co_u32_e32 v4, vcc, 0x80000, v4
	v_cmp_lt_i32_e64 s[0:1], 0, v2
	s_nop 0
	v_addc_co_u32_e32 v5, vcc, 0, v5, vcc
	global_load_dword v3, v[4:5], off sc1
	v_mbcnt_lo_u32_b32 v4, -1, 0
	v_mbcnt_hi_u32_b32 v4, -1, v4
	v_and_b32_e32 v10, 64, v4
	v_add_u32_e32 v5, -1, v4
	v_cmp_lt_i32_e32 vcc, v5, v10
	v_add_u32_e32 v6, -2, v4
	v_add_u32_e32 v7, -4, v4
	v_cndmask_b32_e32 v5, v5, v4, vcc
	v_lshlrev_b32_e32 v5, 2, v5
	v_cmp_lt_i32_e32 vcc, v6, v10
	v_cmp_gt_i32_e64 s[2:3], 2, v2
	v_add_u32_e32 v8, -8, v4
	v_cndmask_b32_e32 v6, v6, v4, vcc
	v_lshlrev_b32_e32 v6, 2, v6
	v_cmp_lt_i32_e32 vcc, v7, v10
	v_cmp_gt_i32_e64 s[4:5], 4, v2
	v_add_u32_e32 v9, -16, v4
	v_cndmask_b32_e32 v7, v7, v4, vcc
	v_lshlrev_b32_e32 v7, 2, v7
	v_cmp_lt_i32_e32 vcc, v8, v10
	v_cmp_gt_i32_e64 s[6:7], 8, v2
	v_subrev_u32_e32 v11, 32, v4
	v_cndmask_b32_e32 v8, v8, v4, vcc
	v_lshlrev_b32_e32 v8, 2, v8
	v_cmp_lt_i32_e32 vcc, v9, v10
	v_cmp_gt_i32_e64 s[8:9], 16, v2
	v_cmp_gt_i32_e64 s[10:11], 32, v2
	v_cndmask_b32_e32 v9, v9, v4, vcc
	v_lshlrev_b32_e32 v9, 2, v9
	v_cmp_lt_i32_e32 vcc, v11, v10
	v_lshl_add_u32 v1, v2, 2, 0
	s_waitcnt vmcnt(0)
	v_add_u32_e32 v12, 0xff, v3
	v_ashrrev_i32_e32 v12, 8, v12
	ds_bpermute_b32 v13, v5, v12
	v_cndmask_b32_e32 v4, v11, v4, vcc
	v_lshlrev_b32_e32 v10, 2, v4
	v_cmp_eq_u32_e32 vcc, 63, v2
	s_waitcnt lgkmcnt(0)
	v_cndmask_b32_e64 v13, 0, v13, s[0:1]
	v_add_u32_e32 v13, v13, v12
	ds_bpermute_b32 v14, v6, v13
	s_waitcnt lgkmcnt(0)
	v_cndmask_b32_e64 v14, v14, 0, s[2:3]
	v_add_u32_e32 v13, v14, v13
	ds_bpermute_b32 v14, v7, v13
	s_waitcnt lgkmcnt(0)
	v_cndmask_b32_e64 v14, v14, 0, s[4:5]
	v_add_u32_e32 v13, v14, v13
	ds_bpermute_b32 v14, v8, v13
	s_waitcnt lgkmcnt(0)
	v_cndmask_b32_e64 v14, v14, 0, s[6:7]
	v_add_u32_e32 v13, v14, v13
	ds_bpermute_b32 v14, v9, v13
	s_waitcnt lgkmcnt(0)
	v_cndmask_b32_e64 v4, v14, 0, s[8:9]
	v_add_u32_e32 v4, v4, v13
	ds_bpermute_b32 v11, v10, v4
	v_add_u32_e32 v13, 0x20100, v1
	v_add_u32_e32 v14, 0x20200, v1
	ds_write_b32 v13, v3
	s_waitcnt lgkmcnt(1)
	v_cndmask_b32_e64 v11, v11, 0, s[10:11]
	v_add_u32_e32 v4, v11, v4
	v_sub_u32_e32 v11, v4, v12
	ds_write_b32 v14, v11
	s_and_saveexec_b64 s[12:13], vcc
	s_add_i32 s18, 0, 0x20300
	v_mov_b32_e32 v11, s18
	ds_write_b32 v11, v4
	s_or_b64 exec, exec, s[12:13]
	s_movk_i32 s18, 0x80
	v_ashrrev_i32_e32 v12, 8, v3
	v_cmp_gt_u32_sdwa s[12:13], v3, s18 src0_sel:BYTE_0 src1_sel:DWORD
	v_mov_b32_e32 v11, -1
	v_add_u32_sdwa v11, v3, v11 dst_sel:DWORD dst_unused:UNUSED_PAD src0_sel:BYTE_0 src1_sel:DWORD
	v_addc_co_u32_e64 v4, vcc, 0, v12, s[12:13]
	v_cmp_gt_u32_e32 vcc, s18, v11
	ds_bpermute_b32 v13, v5, v4
	s_nop 0
	v_cndmask_b32_e64 v11, 0, 1, vcc
	ds_bpermute_b32 v5, v5, v11
	s_waitcnt lgkmcnt(1)
	v_cndmask_b32_e64 v11, 0, v13, s[0:1]
	v_addc_co_u32_e64 v12, s[12:13], v11, v12, s[12:13]
	s_waitcnt lgkmcnt(0)
	v_cndmask_b32_e64 v5, 0, v5, s[0:1]
	v_addc_co_u32_e64 v14, s[0:1], 0, v5, vcc
	ds_bpermute_b32 v13, v6, v12
	ds_bpermute_b32 v14, v6, v14
	s_waitcnt lgkmcnt(1)
	v_cndmask_b32_e64 v6, v13, 0, s[2:3]
	s_waitcnt lgkmcnt(0)
	v_cndmask_b32_e64 v14, v14, 0, s[2:3]
	v_add_u32_e32 v12, v6, v12
	v_addc_co_u32_e64 v5, s[0:1], v14, v5, vcc
	ds_bpermute_b32 v13, v7, v12
	ds_bpermute_b32 v14, v7, v5
	s_waitcnt lgkmcnt(1)
	v_cndmask_b32_e64 v7, v13, 0, s[4:5]
	s_waitcnt lgkmcnt(0)
	v_cndmask_b32_e64 v14, v14, 0, s[4:5]
	v_add_u32_e32 v13, v7, v12
	v_add_u32_e32 v5, v14, v5
	ds_bpermute_b32 v12, v8, v13
	ds_bpermute_b32 v8, v8, v5
	s_waitcnt lgkmcnt(1)
	v_cndmask_b32_e64 v12, v12, 0, s[6:7]
	s_waitcnt lgkmcnt(0)
	v_cndmask_b32_e64 v8, v8, 0, s[6:7]
	v_add_u32_e32 v13, v12, v13
	v_add_u32_e32 v5, v8, v5
	ds_bpermute_b32 v14, v9, v13
	ds_bpermute_b32 v8, v9, v5
	s_waitcnt lgkmcnt(1)
	v_cndmask_b32_e64 v9, v14, 0, s[8:9]
	s_waitcnt lgkmcnt(0)
	v_cndmask_b32_e64 v8, v8, 0, s[8:9]
	v_add_u32_e32 v13, v9, v13
	v_add_u32_e32 v5, v8, v5
	ds_bpermute_b32 v14, v10, v13
	ds_bpermute_b32 v10, v10, v5
	s_waitcnt lgkmcnt(1)
	v_cndmask_b32_e64 v8, v14, 0, s[10:11]
	s_waitcnt lgkmcnt(0)
	v_cndmask_b32_e64 v10, v10, 0, s[10:11]
	v_add_u32_e32 v13, v8, v13
	v_add_u32_e32 v5, v10, v5
	v_readlane_b32 s8, v13, 63
	v_readlane_b32 s9, v5, 63
	s_and_saveexec_b64 s[0:1], s[10:11]
	v_add_u32_e32 v1, 0x20404, v1
	v_lshl_or_b32 v10, v2, 8, 64
	ds_write_b32 v1, v10
	s_or_b64 exec, exec, s[0:1]
	v_cmp_lt_i32_e64 s[0:1], 0, v4
	s_and_saveexec_b64 s[2:3], s[0:1]
	s_cbranch_execz .LBB0_1610
	v_add3_u32 v1, v11, v6, v7
	s_mov_b32 s10, 1
	v_cmp_ne_u32_e64 s[0:1], 1, v4
	s_mov_b64 s[6:7], 0
	v_add3_u32 v9, v1, v12, v9
	s_and_saveexec_b64 s[4:5], s[0:1]
	s_xor_b64 s[4:5], exec, s[4:5]
	s_cbranch_execnz .LBB0_1604
	s_andn2_saveexec_b64 s[0:1], s[4:5]
	s_cbranch_execnz .LBB0_1607

; __device__ __forceinline__ int otid() { int t = threadIdx.x; asm volatile("" : "+v"(t)); return t; }
; __device__ __forceinline__ unsigned xb_ld(unsigned* p)              { return __hip_atomic_load(p, __ATOMIC_RELAXED, __HIP_MEMORY_SCOPE_AGENT); }
; __device__ __forceinline__ unsigned xb_add(unsigned* p, unsigned v) { return __hip_atomic_fetch_add(p, v, __ATOMIC_RELAXED, __HIP_MEMORY_SCOPE_AGENT); }
; __device__ __forceinline__ void xcd_barrier_complete(unsigned* bar, unsigned x, unsigned& nloc, unsigned& nx) {
;     const unsigned G = gridDim.x * gridDim.y * gridDim.z;
;     unsigned sum, cnt, mine, sp = 0u;
;     for (;;) {
;         sum = 0u; cnt = 0u; mine = 0u;
; #pragma unroll
;         for (unsigned j = 0; j < 16; ++j) { const unsigned c = xb_ld(&bar[XB_XCNT(j)]); sum += c; cnt += (c > 0u) ? 1u : 0u; mine = (j == x) ? c : mine; }
;         if (sum == G) break;
;         __builtin_amdgcn_s_sleep(1);
;         if ((++sp & 255u) == 0u) { if (xb_ld(&bar[XB_TMO])) break; if (sp > XB_SPIN_CAP) { atomicAdd(&bar[XB_TMO], 1u); break; } }
;     }
;     nloc = mine > 0u ? mine : 1u; nx = cnt > 0u ? cnt : 1u;
; }
; __device__ __forceinline__ void xcd_barrier(const XcdBarrier& b) {
;     asm volatile("s_waitcnt vmcnt(0)" ::: "memory");
;     __syncthreads();
;     if (otid() == 0) {
;         unsigned* bar = b.bar;
;         __builtin_amdgcn_s_waitcnt(0);
;         unsigned nloc = b.st[0], nx = b.st[1];
;         if (nloc == 0u) { xcd_barrier_complete(bar, b.x, nloc, nx); b.st[0] = nloc; b.st[1] = nx; }
;         const unsigned old = xb_add(&bar[XB_XSUB(b.x)], 1u);
;         const unsigned gen = old / nloc;
;         if (old + 1u == (gen + 1u) * nloc) {
;             __builtin_amdgcn_fence(__ATOMIC_RELEASE, "agent");
;             asm volatile("s_waitcnt vmcnt(0)" ::: "memory");
;             const unsigned og = xb_add(&bar[XB_TOP], 1u);
.LBB0_1669:
	s_mov_b64 s[0:1], s[24:25]
	s_mov_b32 s0, s100
	s_waitcnt lgkmcnt(0)
	s_cmp_gt_i32 s0, 10
	s_cbranch_scc1 .LBB0_1727
	s_mov_b64 s[0:1], s[24:25]
	s_mov_b32 s0, s101
	s_waitcnt lgkmcnt(0)
	s_cmp_lt_i32 s0, 11
	s_cbranch_scc1 .LBB0_1726
	v_readlane_b32 s0, v255, 0
	v_readlane_b32 s1, v255, 1
	s_mov_b32 s0, s100
	s_waitcnt lgkmcnt(0)
	s_cmp_gt_i32 s0, 11
	s_cbranch_scc1 .LBB0_1726
	v_readlane_b32 s0, v255, 0
	v_readlane_b32 s1, v255, 1
	s_mov_b32 s0, s101
	s_waitcnt lgkmcnt(0)
	s_cmp_lt_i32 s0, 12
	s_cbranch_scc1 .LBB0_1726
	v_readlane_b32 s2, v255, 0
	v_readlane_b32 s3, v255, 1
	s_getreg_b32 s4, hwreg(HW_REG_XCC_ID, 0, 4)
	s_waitcnt vmcnt(0)
	v_mov_b32_e32 v1, v0
	s_waitcnt vmcnt(0)
	s_barrier
	s_nop 0
	v_cmp_eq_u32_e32 vcc, 0, v1
	s_and_saveexec_b64 s[0:1], vcc
	s_cbranch_execz .LBB0_1725
	s_add_i32 s5, 0, 0x20020
	v_mov_b32_e32 v1, s5
	s_mov_b64 s[2:3], s[98:99]
	s_waitcnt vmcnt(0) expcnt(0) lgkmcnt(0)
	ds_read_b32 v3, v1
	s_add_i32 s5, 0, 0x20024
	v_mov_b32_e32 v1, s5
	ds_read_b32 v1, v1
	s_and_b32 s33, s4, 15
	s_waitcnt lgkmcnt(1)
	v_cmp_ne_u32_e32 vcc, 0, v3
	s_cbranch_vccnz .LBB0_1689
	v_readlane_b32 s4, v255, 0
	v_readlane_b32 s5, v255, 1
	s_load_dwordx2 s[8:9], s[4:5], 0xe0
	s_load_dword s7, s[4:5], 0xe8
	s_add_u32 s4, s2, 0x4200
	s_addc_u32 s5, s3, 0
	s_add_u32 s6, s2, 0x4400
	s_waitcnt lgkmcnt(0)
	s_mul_i32 s46, s9, s8
	s_mul_i32 s46, s46, s7
	s_addc_u32 s7, s3, 0
	s_add_u32 s8, s2, 0x4500
	s_addc_u32 s9, s3, 0
	s_add_u32 s10, s2, 0x4600
	s_addc_u32 s11, s3, 0
	s_add_u32 s12, s2, 0x4700
	s_addc_u32 s13, s3, 0
	s_add_u32 s14, s2, 0x4800
	s_addc_u32 s15, s3, 0
	s_add_u32 s16, s2, 0x4900
	s_addc_u32 s17, s3, 0
	s_add_u32 s18, s2, 0x4a00
	s_addc_u32 s19, s3, 0
	s_add_u32 s20, s2, 0x4b00
	s_addc_u32 s21, s3, 0
	s_add_u32 s22, s2, 0x4c00
	s_addc_u32 s23, s3, 0
	s_add_u32 s24, s2, 0x4d00
	s_addc_u32 s25, s3, 0
	s_add_u32 s26, s2, 0x4e00
	s_addc_u32 s27, s3, 0
	s_add_u32 s28, s2, 0x4f00
	s_addc_u32 s29, s3, 0
	s_add_u32 s30, s2, 0x5000
	s_addc_u32 s31, s3, 0
	s_add_u32 s34, s2, 0x5100
	s_addc_u32 s35, s3, 0
	s_add_u32 s36, s2, 0x5200
	s_addc_u32 s37, s3, 0
	s_add_u32 s38, s2, 0x5300
	s_addc_u32 s39, s3, 0
	s_mov_b32 s47, 1
	v_mov_b32_e32 v17, 0
	s_branch .LBB0_1677

; #define LAS __attribute__((address_space(3)))
; __device__ __forceinline__ int otid() { int t = threadIdx.x; asm volatile("" : "+v"(t)); return t; }
; #define REP(k) for (int rep_ = 0; rep_ < ((REP_KIND == (k)) ? REP_N : 1); ++rep_)
; #define IN(k) (fresh_args()->ph_lo <= (k) && (k) < fresh_args()->ph_hi)
; #define SEAM(k) do { if (IN(k) && IN((k) + 1)) { XcdBarrier bar; bar.bar = (unsigned*)(fresh_args()->ws + WS_CTL) + CW_BAR; bar.x = xb_xcc_id(); bar.st = (volatile LAS unsigned*)(lds + LDS_TAB) + 8; xcd_barrier(bar); } } while (0)
; #define PHASE_ARGS() CArgs* A_p = fresh_args(); CArgs& A = *A_p; unsigned char* ws = A.ws; (void)ws;
; __device__ __forceinline__ MoeTab moe_tables(CArgs& A, int l, LAS unsigned char* lds, bool want_order) {
;     MoeTab T; T.cnt = (LAS int*)(lds + LDS_TAB + 256); T.ts = T.cnt + 64; T.ord = (LAS int*)(lds + LDS_TAB + 1024) + 1;
;     unsigned* cg = (unsigned*)(A.ws + WS_CTL) + CW_CNT + l * 64;
;     const int tt = otid();
;     __syncthreads();
;     if (tt < 64) {
;         const int e = tt; const int c = (int)__hip_atomic_load(cg + e, RLX_AGENT);
;         T.cnt[e] = c;
;         const int nall = (c + 255) >> 8; const int ia = wave_incl_scan(nall, e);
;         T.ts[e] = ia - nall; if (e == 63) T.ts[64] = ia;
; template <int l> __device__ __forceinline__ void layer_body(LAS unsigned char* lds, unsigned char* lds_raw, int bx, int vcu) {
;     ...
;         if (KEN(11) && IN(pb + 9)) REP(11) { PHASE_ARGS(); combine_phase(A, l, (const float*)(ws + WS_X), lds, vcu, G); } SEAM(pb + 9);
.LBB0_1727:
	s_mov_b64 s[0:1], s[24:25]
	s_mov_b32 s0, s100
	s_waitcnt lgkmcnt(0)
	s_cmp_gt_i32 s0, 11
	s_cbranch_scc1 .LBB0_1736
	s_mov_b64 s[0:1], s[24:25]
	s_mov_b32 s0, s101
	s_waitcnt lgkmcnt(0)
	s_cmp_lt_i32 s0, 12
	s_cbranch_scc1 .LBB0_1736
	s_mov_b64 s[6:7], s[24:25]
	s_mov_b64 s[0:1], s[98:99]
	v_mov_b32_e32 v1, v0
	v_mov_b32_e32 v2, v0
	s_waitcnt vmcnt(0) lgkmcnt(0)
	v_readfirstlane_b32 s4, v1
	v_cmp_gt_i32_e32 vcc, 64, v2
	s_barrier
	s_and_saveexec_b64 s[2:3], vcc
	s_cbranch_execz .LBB0_1732
	v_ashrrev_i32_e32 v3, 31, v2
	v_mul_u32_u24_e32 v4, 0x1100, v2
	v_mov_b32_e32 v5, 0
	v_lshl_add_u64 v[4:5], v[4:5], 0, s[0:1]
	v_add_co_u32_e32 v4, vcc, 0x80000, v4
	s_nop 1
	v_addc_co_u32_e32 v5, vcc, 0, v5, vcc
	global_load_dword v3, v[4:5], off sc1
	v_mbcnt_lo_u32_b32 v5, -1, 0
	v_mbcnt_hi_u32_b32 v5, -1, v5
	v_and_b32_e32 v6, 64, v5
	v_add_u32_e32 v7, -1, v5
	v_cmp_lt_i32_e32 vcc, v7, v6
	v_add_u32_e32 v8, -2, v5
	v_add_u32_e32 v9, -4, v5
	v_cndmask_b32_e32 v7, v7, v5, vcc
	v_lshlrev_b32_e32 v7, 2, v7
	v_cmp_lt_i32_e32 vcc, v8, v6
	v_add_u32_e32 v10, -8, v5
	v_add_u32_e32 v11, -16, v5
	v_cndmask_b32_e32 v8, v8, v5, vcc
	v_cmp_lt_i32_e32 vcc, 0, v2
	v_lshlrev_b32_e32 v8, 2, v8
	v_subrev_u32_e32 v12, 32, v5
	v_lshl_add_u32 v4, v2, 2, 0
	s_waitcnt vmcnt(0)
	v_add_u32_e32 v13, 0xff, v3
	v_ashrrev_i32_e32 v13, 8, v13
	ds_bpermute_b32 v7, v7, v13
	s_waitcnt lgkmcnt(0)
	v_cndmask_b32_e32 v7, 0, v7, vcc
	v_add_u32_e32 v7, v7, v13
	ds_bpermute_b32 v8, v8, v7
	v_cmp_lt_i32_e32 vcc, v9, v6
	s_nop 1
	v_cndmask_b32_e32 v9, v9, v5, vcc
	v_cmp_lt_i32_e32 vcc, 1, v2
	v_lshlrev_b32_e32 v9, 2, v9
	s_waitcnt lgkmcnt(0)
	v_cndmask_b32_e32 v8, 0, v8, vcc
	v_add_u32_e32 v7, v8, v7
	ds_bpermute_b32 v8, v9, v7
	v_cmp_lt_i32_e32 vcc, v10, v6
	s_nop 1
	v_cndmask_b32_e32 v9, v10, v5, vcc
	v_cmp_lt_i32_e32 vcc, 3, v2
	v_lshlrev_b32_e32 v9, 2, v9
	s_waitcnt lgkmcnt(0)
	v_cndmask_b32_e32 v8, 0, v8, vcc
	v_add_u32_e32 v7, v8, v7
	ds_bpermute_b32 v8, v9, v7
	v_cmp_lt_i32_e32 vcc, v11, v6
	s_nop 1
	v_cndmask_b32_e32 v9, v11, v5, vcc
	v_cmp_lt_i32_e32 vcc, 7, v2
	v_lshlrev_b32_e32 v9, 2, v9
	s_waitcnt lgkmcnt(0)
	v_cndmask_b32_e32 v8, 0, v8, vcc
	v_add_u32_e32 v7, v8, v7
	ds_bpermute_b32 v8, v9, v7
	v_cmp_lt_i32_e32 vcc, v12, v6
	s_nop 1
	v_cndmask_b32_e32 v5, v12, v5, vcc
	v_cmp_lt_i32_e32 vcc, 15, v2
	v_lshlrev_b32_e32 v5, 2, v5
	s_waitcnt lgkmcnt(0)
	v_cndmask_b32_e32 v6, 0, v8, vcc
	v_add_u32_e32 v6, v6, v7
	ds_bpermute_b32 v5, v5, v6
	v_add_u32_e32 v7, 0x20100, v4
	v_cmp_lt_i32_e32 vcc, 31, v2
	ds_write_b32 v7, v3
	v_add_u32_e32 v4, 0x20200, v4
	s_waitcnt lgkmcnt(1)
	v_cndmask_b32_e32 v3, 0, v5, vcc
	v_add_u32_e32 v3, v3, v6
	v_sub_u32_e32 v5, v3, v13
	v_cmp_eq_u32_e32 vcc, 63, v2
	ds_write_b32 v4, v5
	s_and_b64 exec, exec, vcc
	s_add_i32 s5, 0, 0x20300
	v_mov_b32_e32 v2, s5
	ds_write_b32 v2, v3

; __device__ __forceinline__ int otid() { int t = threadIdx.x; asm volatile("" : "+v"(t)); return t; }
; __device__ __forceinline__ unsigned xb_ld(unsigned* p)              { return __hip_atomic_load(p, __ATOMIC_RELAXED, __HIP_MEMORY_SCOPE_AGENT); }
; __device__ __forceinline__ unsigned xb_add(unsigned* p, unsigned v) { return __hip_atomic_fetch_add(p, v, __ATOMIC_RELAXED, __HIP_MEMORY_SCOPE_AGENT); }
; __device__ __forceinline__ void xcd_barrier_complete(unsigned* bar, unsigned x, unsigned& nloc, unsigned& nx) {
;     const unsigned G = gridDim.x * gridDim.y * gridDim.z;
;     unsigned sum, cnt, mine, sp = 0u;
;     for (;;) {
;         sum = 0u; cnt = 0u; mine = 0u;
; #pragma unroll
;         for (unsigned j = 0; j < 16; ++j) { const unsigned c = xb_ld(&bar[XB_XCNT(j)]); sum += c; cnt += (c > 0u) ? 1u : 0u; mine = (j == x) ? c : mine; }
;         if (sum == G) break;
;         __builtin_amdgcn_s_sleep(1);
;         if ((++sp & 255u) == 0u) { if (xb_ld(&bar[XB_TMO])) break; if (sp > XB_SPIN_CAP) { atomicAdd(&bar[XB_TMO], 1u); break; } }
;     }
;     nloc = mine > 0u ? mine : 1u; nx = cnt > 0u ? cnt : 1u;
; }
; __device__ __forceinline__ void xcd_barrier(const XcdBarrier& b) {
;     asm volatile("s_waitcnt vmcnt(0)" ::: "memory");
;     __syncthreads();
;     if (otid() == 0) {
;         unsigned* bar = b.bar;
;         __builtin_amdgcn_s_waitcnt(0);
;         unsigned nloc = b.st[0], nx = b.st[1];
;         if (nloc == 0u) { xcd_barrier_complete(bar, b.x, nloc, nx); b.st[0] = nloc; b.st[1] = nx; }
;         const unsigned old = xb_add(&bar[XB_XSUB(b.x)], 1u);
;         const unsigned gen = old / nloc;
;         if (old + 1u == (gen + 1u) * nloc) {
;             __builtin_amdgcn_fence(__ATOMIC_RELEASE, "agent");
;             asm volatile("s_waitcnt vmcnt(0)" ::: "memory");
;             const unsigned og = xb_add(&bar[XB_TOP], 1u);
.LBB0_1736:
	s_mov_b64 s[0:1], s[24:25]
	s_mov_b32 s0, s100
	s_waitcnt lgkmcnt(0)
	s_cmp_gt_i32 s0, 11
	s_cbranch_scc1 .LBB0_1794
	s_mov_b64 s[0:1], s[24:25]
	s_mov_b32 s0, s101
	s_waitcnt lgkmcnt(0)
	s_cmp_lt_i32 s0, 12
	s_cbranch_scc1 .LBB0_1793
	v_readlane_b32 s0, v255, 0
	v_readlane_b32 s1, v255, 1
	s_mov_b32 s0, s100
	s_waitcnt lgkmcnt(0)
	s_cmp_gt_i32 s0, 12
	s_cbranch_scc1 .LBB0_1793
	v_readlane_b32 s0, v255, 0
	v_readlane_b32 s1, v255, 1
	s_mov_b32 s0, s101
	s_waitcnt lgkmcnt(0)
	s_cmp_lt_i32 s0, 13
	s_cbranch_scc1 .LBB0_1793
	v_readlane_b32 s2, v255, 0
	v_readlane_b32 s3, v255, 1
	s_getreg_b32 s4, hwreg(HW_REG_XCC_ID, 0, 4)
	s_waitcnt vmcnt(0)
	v_mov_b32_e32 v1, v0
	s_waitcnt vmcnt(0)
	s_barrier
	s_nop 0
	v_cmp_eq_u32_e32 vcc, 0, v1
	s_and_saveexec_b64 s[0:1], vcc
	s_cbranch_execz .LBB0_1792
	s_add_i32 s5, 0, 0x20020
	v_mov_b32_e32 v1, s5
	s_mov_b64 s[2:3], s[98:99]
	s_waitcnt vmcnt(0) expcnt(0) lgkmcnt(0)
	ds_read_b32 v3, v1
	s_add_i32 s5, 0, 0x20024
	v_mov_b32_e32 v1, s5
	ds_read_b32 v1, v1
	s_and_b32 s33, s4, 15
	s_waitcnt lgkmcnt(1)
	v_cmp_ne_u32_e32 vcc, 0, v3
	s_cbranch_vccnz .LBB0_1756
	v_readlane_b32 s4, v255, 0
	v_readlane_b32 s5, v255, 1
	s_load_dwordx2 s[8:9], s[4:5], 0xe0
	s_load_dword s7, s[4:5], 0xe8
	s_add_u32 s4, s2, 0x4200
	s_addc_u32 s5, s3, 0
	s_add_u32 s6, s2, 0x4400
	s_waitcnt lgkmcnt(0)
	s_mul_i32 s46, s9, s8
	s_mul_i32 s46, s46, s7
	s_addc_u32 s7, s3, 0
	s_add_u32 s8, s2, 0x4500
	s_addc_u32 s9, s3, 0
	s_add_u32 s10, s2, 0x4600
	s_addc_u32 s11, s3, 0
	s_add_u32 s12, s2, 0x4700
	s_addc_u32 s13, s3, 0
	s_add_u32 s14, s2, 0x4800
	s_addc_u32 s15, s3, 0
	s_add_u32 s16, s2, 0x4900
	s_addc_u32 s17, s3, 0
	s_add_u32 s18, s2, 0x4a00
	s_addc_u32 s19, s3, 0
	s_add_u32 s20, s2, 0x4b00
	s_addc_u32 s21, s3, 0
	s_add_u32 s22, s2, 0x4c00
	s_addc_u32 s23, s3, 0
	s_add_u32 s24, s2, 0x4d00
	s_addc_u32 s25, s3, 0
	s_add_u32 s26, s2, 0x4e00
	s_addc_u32 s27, s3, 0
	s_add_u32 s28, s2, 0x4f00
	s_addc_u32 s29, s3, 0
	s_add_u32 s30, s2, 0x5000
	s_addc_u32 s31, s3, 0
	s_add_u32 s34, s2, 0x5100
	s_addc_u32 s35, s3, 0
	s_add_u32 s36, s2, 0x5200
	s_addc_u32 s37, s3, 0
	s_add_u32 s38, s2, 0x5300
	s_addc_u32 s39, s3, 0
	s_mov_b32 s47, 1
	v_mov_b32_e32 v17, 0
	s_branch .LBB0_1744

; template <class P, class MK = NoChain>
; __device__ __forceinline__ void gemm_phase(LAS unsigned char* lds, const P& p, const MK& mk = MK(), bool chain_out = false, bool chained_in = false) {
;     ...
;     int tid = threadIdx.x; asm volatile("" : "+v"(tid));
;     const int wid = __builtin_amdgcn_readfirstlane(tid >> 6), lane = tid & 63, wr = wid >> 2, wc = wid & 3, fr = lane & 15, fq = lane >> 4;
;     unsigned voffB[2], vA[2][2], nvA[2][2], nvB[2]; typedef decltype(mk()) NP; constexpr int NES = NP::FP8 ? 1 : 2; constexpr int NBMODE = bmode_of<NP>::value; constexpr size_t nhstepB = (size_t)(NBMODE == 1 ? 8 : (NBMODE == 2 ? 16 : HALF)) * NP::LDB * NES;
;     constexpr size_t kstep = (size_t)(BK * 2);
;     constexpr int BMODE = bmode_of<P>::value;
;     constexpr size_t hstep = (size_t)(BMODE == 1 ? 8 : (BMODE == 2 ? 16 : HALF)) * LDB * ES, hstepA = (size_t)HALF * LDA * ES;
; #pragma unroll
;     for (int i = 0; i < 2; ++i) { int R, C; stage_rc(tid * 16 + i * 8192, R, C); const int rho_ = R & 31;
;         const int fq_ = (rho_ & 15) >> 2, n_ = rho_ >> 4, q_ = rho_ & 3;
;         const int Rb = BMODE == 1 ? ((R >> 5) * 64 + fq_ * 16 + 4 * n_ + q_) : (BMODE == 2 ? ((R >> 5) * 64 + 32 * (fq_ >> 1) + 8 * n_ + 4 * (fq_ & 1) + q_) : (P::PERM ? ((R & ~31) + perm32(R & 31)) : R));
;         voffB[i] = (unsigned)(Rb * LDB * ES + C * 2); vA[0][i] = (unsigned)(R * LDA * ES + C * 2); vA[1][i] = vA[0][i] + (unsigned)hstepA; nvA[0][i] = vA[0][i]; nvA[1][i] = vA[1][i]; nvB[i] = voffB[i]; }
;     const unsigned ldsw = (unsigned)wid * 1024u;
;     const int aoff = lds_byte(wr * 64 + fr, fq * 8), boff = lds_byte(wc * 32 + fr, fq * 8); const int aoff1 = aoff ^ 64, boff1 = boff ^ 64;
;     ...
;     Unit cur, nxt; int ui = 0;
;     if (!p.next(0, cur)) return;
;     Acc acc;
;     if constexpr (!PEEL) {
; #pragma unroll
;     for (int a = 0; a < 2; ++a)
; #pragma unroll
;         for (int b = 0; b < 2; ++b)
; #pragma unroll
;             for (int m = 0; m < 4; ++m)
; #pragma unroll
;                 for (int n = 0; n < 2; ++n) { typedef double d2_ __attribute__((ext_vector_type(2))); d2_ z_; asm volatile("v_mov_b64 %0, 0" : "=v"(z_.x)); asm volatile("v_mov_b64 %0, 0" : "=v"(z_.y)); acc[a][b][m][n] = __builtin_bit_cast(f32x4, z_); }
;     }
;     typedef int v8i_ __attribute__((ext_vector_type(8))); typedef int v4i_ __attribute__((ext_vector_type(4)));
.LBB0_1794:
	s_mov_b64 s[0:1], s[24:25]
	s_mov_b32 s0, s100
	s_waitcnt lgkmcnt(0)
	s_cmp_gt_i32 s0, 12
	s_cbranch_scc1 .LBB0_1864
	s_mov_b64 s[0:1], s[24:25]
	s_mov_b32 s0, s101
	s_waitcnt lgkmcnt(0)
	s_cmp_lt_i32 s0, 13
	s_cbranch_scc1 .LBB0_1864
	s_cmpk_lt_i32 s95, 0x400
	s_mov_b64 s[2:3], s[24:25]
	v_mov_b32_e32 v2, v0
	s_cselect_b64 s[4:5], -1, 0
	s_cmpk_gt_i32 s95, 0x3ff
	s_nop 0
	v_readfirstlane_b32 s13, v2
	s_cbranch_scc1 .LBB0_1798
	v_readlane_b32 s0, v255, 4
	s_and_b32 s0, s0, -8
	s_sub_i32 s0, s95, s0
	s_lshl_b32 s6, s0, 7
	s_mul_i32 s1, s0, 0x81
	s_cmp_lt_i32 s0, 0
	s_cselect_b32 s0, s1, s6
	s_add_i32 s0, s0, s96
	s_ashr_i32 s1, s0, 31
	s_lshr_b32 s1, s1, 24
	s_add_i32 s1, s0, s1
	s_ashr_i32 s6, s1, 8
	s_and_b32 s1, s1, 0xffffff00
	s_sub_i32 s0, s0, s1
	s_sext_i32_i16 s1, s0
	s_bfe_u32 s1, s1, 0x3001c
	s_add_i32 s1, s0, s1
	s_sext_i32_i16 s7, s1
	s_and_b32 s1, s1, 0xfff8
	s_sub_i32 s0, s0, s1
	s_lshl_b32 s6, s6, 3
	s_sext_i32_i16 s0, s0
	s_add_i32 s15, s6, s0
	s_ashr_i32 s0, s7, 3
.LBB0_1798:
	v_readlane_b32 s24, v255, 0
	s_andn2_b64 vcc, exec, s[4:5]
	v_readlane_b32 s25, v255, 1
	s_cbranch_vccnz .LBB0_1864
	v_lshrrev_b32_e32 v3, 4, v2
	v_ashrrev_i32_e32 v4, 3, v2
	s_mov_b64 s[2:3], s[98:99]
	v_xor_b32_e32 v1, v3, v2
	v_lshlrev_b32_e32 v5, 1, v4
	v_lshrrev_b32_e32 v6, 2, v4
	v_lshlrev_b32_e32 v1, 4, v1
	v_and_b32_e32 v5, 24, v5
	v_and_b32_e32 v6, 4, v6
	v_and_b32_e32 v7, 0x1fffe3, v4
	v_and_b32_e32 v1, 0x70, v1
	v_or3_b32 v5, v7, v6, v5
	v_lshl_or_b32 v194, v5, 11, v1
	v_mov_b32_e32 v5, 0x2000
	v_lshl_add_u32 v5, v2, 4, v5
	s_waitcnt lgkmcnt(0)
	s_add_u32 s4, s2, 0x30c00000
	v_ashrrev_i32_e32 v5, 7, v5
	s_addc_u32 s5, s3, 0
	v_lshlrev_b32_e32 v6, 1, v5
	v_lshrrev_b32_e32 v7, 2, v5
	s_add_u32 s30, s2, 0x33400000
	v_and_b32_e32 v6, 24, v6
	v_and_b32_e32 v7, 4, v7
	v_and_b32_e32 v8, 0x1fffe3, v5
	s_addc_u32 s31, s3, 0
	v_or3_b32 v6, v8, v7, v6
	s_ashr_i32 s10, s13, 6
	s_ashr_i32 s1, s0, 31
	s_ashr_i32 s6, s13, 8
	v_lshl_or_b32 v196, v6, 11, v1
	s_lshl_b32 s35, s10, 10
	s_lshl_b64 s[8:9], s[0:1], 19
	v_mov_b32_e32 v6, v0
	v_mov_b64 v[186:187], 0
	v_mov_b64 v[188:189], 0
	v_mov_b64 v[190:191], 0
	v_mov_b64 v[192:193], 0
	v_mov_b64 v[174:175], 0
	v_mov_b64 v[176:177], 0
	v_mov_b64 v[170:171], 0
	v_mov_b64 v[172:173], 0
	v_mov_b64 v[158:159], 0
	v_mov_b64 v[160:161], 0
	v_mov_b64 v[154:155], 0
	v_mov_b64 v[156:157], 0
	v_mov_b64 v[142:143], 0
	v_mov_b64 v[144:145], 0
	v_mov_b64 v[138:139], 0
	v_mov_b64 v[140:141], 0
	v_mov_b64 v[182:183], 0
	v_mov_b64 v[184:185], 0
	v_mov_b64 v[178:179], 0
	v_mov_b64 v[180:181], 0
	v_mov_b64 v[166:167], 0
	v_mov_b64 v[168:169], 0
	v_mov_b64 v[162:163], 0
	v_mov_b64 v[164:165], 0
	v_mov_b64 v[150:151], 0
	v_mov_b64 v[152:153], 0
	v_mov_b64 v[146:147], 0
	v_mov_b64 v[148:149], 0
	v_mov_b64 v[134:135], 0
	v_mov_b64 v[136:137], 0
	v_mov_b64 v[130:131], 0
	v_mov_b64 v[132:133], 0
	v_mov_b64 v[126:127], 0
	v_mov_b64 v[128:129], 0
	v_mov_b64 v[122:123], 0
	v_mov_b64 v[124:125], 0
	v_mov_b64 v[110:111], 0
	v_mov_b64 v[112:113], 0
	v_mov_b64 v[106:107], 0
	v_mov_b64 v[108:109], 0
	v_mov_b64 v[94:95], 0
	v_mov_b64 v[96:97], 0
	v_mov_b64 v[90:91], 0
	v_mov_b64 v[92:93], 0
	v_mov_b64 v[78:79], 0
	v_mov_b64 v[80:81], 0
	v_mov_b64 v[74:75], 0
	v_mov_b64 v[76:77], 0
	v_mov_b64 v[118:119], 0
	v_mov_b64 v[120:121], 0
	v_mov_b64 v[114:115], 0
	v_mov_b64 v[116:117], 0
	v_mov_b64 v[102:103], 0
	v_mov_b64 v[104:105], 0
	v_mov_b64 v[98:99], 0
	v_mov_b64 v[100:101], 0
	v_mov_b64 v[86:87], 0
	v_mov_b64 v[88:89], 0
	v_mov_b64 v[82:83], 0
	v_mov_b64 v[84:85], 0
	v_mov_b64 v[70:71], 0
	v_mov_b64 v[72:73], 0
	v_mov_b64 v[66:67], 0
	v_mov_b64 v[68:69], 0
	s_add_u32 s20, s30, s8
	s_addc_u32 s21, s31, s9
	v_lshlrev_b32_e32 v7, 4, v6
	v_xor_b32_e32 v7, v7, v6
	v_lshlrev_b32_e32 v6, 8, v6
	s_add_i32 s36, s35, 0
	v_and_b32_e32 v6, 0xfffff800, v6
	s_mov_b64 s[8:9], s[20:21]
	s_add_i32 m0, s36, 0x10000
	s_movk_i32 s34, 0x70
	v_lshl_add_u32 v6, s15, 19, v6
	v_and_or_b32 v198, v7, s34, v6
	global_load_lds_dwordx4 v194, s[8:9]
	s_add_i32 m0, s36, 0x12000
	s_add_i32 s37, s36, 0x2000
	global_load_lds_dwordx4 v196, s[8:9]
	s_mov_b64 s[8:9], s[4:5]
	s_mov_b32 m0, s36
	v_add_u32_e32 v208, 0x20000, v198
	v_add_u32_e32 v212, 0x40000, v198
	global_load_lds_dwordx4 v198, s[8:9]
	s_mov_b32 m0, s37
	v_add_u32_e32 v210, 0x60000, v198
	global_load_lds_dwordx4 v208, s[8:9]
	s_add_u32 s8, s20, 0x40000
	s_addc_u32 s9, s21, 0
	s_add_i32 s38, s36, 0x14000
	s_mov_b32 m0, s38
	s_add_i32 s39, s36, 0x16000
	s_add_i32 s40, s36, 0x4000
	global_load_lds_dwordx4 v194, s[8:9]
	s_mov_b32 m0, s39
	s_add_i32 s41, s36, 0x6000
	global_load_lds_dwordx4 v196, s[8:9]
	s_mov_b64 s[8:9], s[4:5]
	s_mov_b32 m0, s40
	v_mov_b32_e32 v199, 0
	global_load_lds_dwordx4 v212, s[8:9]
	s_mov_b32 m0, s41
	s_mov_b32 s7, 0
	global_load_lds_dwordx4 v210, s[8:9]
	v_mov_b32_e32 v195, v199
	v_mov_b32_e32 v197, v199
	s_cmp_lg_u32 s6, 1
	v_mov_b32_e32 v209, v199
	s_cbranch_scc1 .LBB0_1801
	s_barrier

; __device__ __forceinline__ int otid() { int t = threadIdx.x; asm volatile("" : "+v"(t)); return t; }
; __device__ __forceinline__ unsigned xb_ld(unsigned* p)              { return __hip_atomic_load(p, __ATOMIC_RELAXED, __HIP_MEMORY_SCOPE_AGENT); }
; __device__ __forceinline__ unsigned xb_add(unsigned* p, unsigned v) { return __hip_atomic_fetch_add(p, v, __ATOMIC_RELAXED, __HIP_MEMORY_SCOPE_AGENT); }
; __device__ __forceinline__ void xcd_barrier_complete(unsigned* bar, unsigned x, unsigned& nloc, unsigned& nx) {
;     const unsigned G = gridDim.x * gridDim.y * gridDim.z;
;     unsigned sum, cnt, mine, sp = 0u;
;     for (;;) {
;         sum = 0u; cnt = 0u; mine = 0u;
; #pragma unroll
;         for (unsigned j = 0; j < 16; ++j) { const unsigned c = xb_ld(&bar[XB_XCNT(j)]); sum += c; cnt += (c > 0u) ? 1u : 0u; mine = (j == x) ? c : mine; }
;         if (sum == G) break;
;         __builtin_amdgcn_s_sleep(1);
;         if ((++sp & 255u) == 0u) { if (xb_ld(&bar[XB_TMO])) break; if (sp > XB_SPIN_CAP) { atomicAdd(&bar[XB_TMO], 1u); break; } }
;     }
;     nloc = mine > 0u ? mine : 1u; nx = cnt > 0u ? cnt : 1u;
; }
; __device__ __forceinline__ void xcd_barrier(const XcdBarrier& b) {
;     asm volatile("s_waitcnt vmcnt(0)" ::: "memory");
;     __syncthreads();
;     if (otid() == 0) {
;         unsigned* bar = b.bar;
;         __builtin_amdgcn_s_waitcnt(0);
;         unsigned nloc = b.st[0], nx = b.st[1];
;         if (nloc == 0u) { xcd_barrier_complete(bar, b.x, nloc, nx); b.st[0] = nloc; b.st[1] = nx; }
;         const unsigned old = xb_add(&bar[XB_XSUB(b.x)], 1u);
;         const unsigned gen = old / nloc;
;         if (old + 1u == (gen + 1u) * nloc) {
;             __builtin_amdgcn_fence(__ATOMIC_RELEASE, "agent");
;             asm volatile("s_waitcnt vmcnt(0)" ::: "memory");
;             const unsigned og = xb_add(&bar[XB_TOP], 1u);
.LBB0_1864:
	s_mov_b64 s[0:1], s[24:25]
	s_mov_b32 s0, s100
	s_waitcnt lgkmcnt(0)
	s_cmp_gt_i32 s0, 12
	s_cbranch_scc1 .LBB0_1922
	s_mov_b64 s[0:1], s[24:25]
	s_mov_b32 s0, s101
	s_waitcnt lgkmcnt(0)
	s_cmp_lt_i32 s0, 13
	s_cbranch_scc1 .LBB0_1921
	v_readlane_b32 s0, v255, 0
	v_readlane_b32 s1, v255, 1
	s_mov_b32 s0, s100
	s_waitcnt lgkmcnt(0)
	s_cmp_gt_i32 s0, 13
	s_cbranch_scc1 .LBB0_1921
	v_readlane_b32 s0, v255, 0
	v_readlane_b32 s1, v255, 1
	s_mov_b32 s0, s101
	s_waitcnt lgkmcnt(0)
	s_cmp_lt_i32 s0, 14
	s_cbranch_scc1 .LBB0_1921
	v_readlane_b32 s2, v255, 0
	v_readlane_b32 s3, v255, 1
	s_getreg_b32 s4, hwreg(HW_REG_XCC_ID, 0, 4)
	s_waitcnt vmcnt(0)
	v_mov_b32_e32 v1, v0
	s_waitcnt vmcnt(0)
	s_barrier
	s_nop 0
	v_cmp_eq_u32_e32 vcc, 0, v1
	s_and_saveexec_b64 s[0:1], vcc
	s_cbranch_execz .LBB0_1920
	s_add_i32 s5, 0, 0x20020
	v_mov_b32_e32 v1, s5
	s_mov_b64 s[2:3], s[98:99]
	s_waitcnt vmcnt(0) expcnt(0) lgkmcnt(0)
	ds_read_b32 v3, v1
	s_add_i32 s5, 0, 0x20024
	v_mov_b32_e32 v1, s5
	ds_read_b32 v1, v1
	s_and_b32 s33, s4, 15
	s_waitcnt lgkmcnt(1)
	v_cmp_ne_u32_e32 vcc, 0, v3
	s_cbranch_vccnz .LBB0_1884
	v_readlane_b32 s4, v255, 0
	v_readlane_b32 s5, v255, 1
	s_load_dwordx2 s[8:9], s[4:5], 0xe0
	s_load_dword s7, s[4:5], 0xe8
	s_add_u32 s4, s2, 0x4200
	s_addc_u32 s5, s3, 0
	s_add_u32 s6, s2, 0x4400
	s_waitcnt lgkmcnt(0)
	s_mul_i32 s46, s9, s8
	s_mul_i32 s46, s46, s7
	s_addc_u32 s7, s3, 0
	s_add_u32 s8, s2, 0x4500
	s_addc_u32 s9, s3, 0
	s_add_u32 s10, s2, 0x4600
	s_addc_u32 s11, s3, 0
	s_add_u32 s12, s2, 0x4700
	s_addc_u32 s13, s3, 0
	s_add_u32 s14, s2, 0x4800
	s_addc_u32 s15, s3, 0
	s_add_u32 s16, s2, 0x4900
	s_addc_u32 s17, s3, 0
	s_add_u32 s18, s2, 0x4a00
	s_addc_u32 s19, s3, 0
	s_add_u32 s20, s2, 0x4b00
	s_addc_u32 s21, s3, 0
	s_add_u32 s22, s2, 0x4c00
	s_addc_u32 s23, s3, 0
	s_add_u32 s24, s2, 0x4d00
	s_addc_u32 s25, s3, 0
	s_add_u32 s26, s2, 0x4e00
	s_addc_u32 s27, s3, 0
	s_add_u32 s28, s2, 0x4f00
	s_addc_u32 s29, s3, 0
	s_add_u32 s30, s2, 0x5000
	s_addc_u32 s31, s3, 0
	s_add_u32 s34, s2, 0x5100
	s_addc_u32 s35, s3, 0
	s_add_u32 s36, s2, 0x5200
	s_addc_u32 s37, s3, 0
	s_add_u32 s38, s2, 0x5300
	s_addc_u32 s39, s3, 0
	s_mov_b32 s47, 1
	v_mov_b32_e32 v17, 0
	s_branch .LBB0_1872

; __device__ __forceinline__ float bflo(unsigned w) { return __uint_as_float(w << 16); }
; __device__ __forceinline__ void postproj_phase(CArgs& A, int l, int vcu, int G) {
;     int tid = threadIdx.x; asm volatile("" : "+v"(tid));
;     const int lane = tid & 63, wave = __builtin_amdgcn_readfirstlane(tid >> 6);
;     const bf16* P = (const bf16*)(A.ws + WS_PROJ);
;     bf16* CQN = (bf16*)(A.ws + WS_CQN); bf16* CKVN = (bf16*)(A.ws + WS_CKVN); bf16* CZ = (bf16*)(A.ws + WS_CZ); unsigned char* Kb = A.ws + WS_K;
;     const f32x2* cs = (const f32x2*)(A.ws + WS_CS);
;     const float* gq = A.in[I_GQ] + l * QL; const float* gkv = A.in[I_GKV] + l * KVL; const float* cw = A.in[I_CONVW] + (size_t)l * 3 * CW;
;     for (int t = vcu * NWAVES + wave; t < NT; t += G * NWAVES) {
;         const int b = t / SEQ, s = t % SEQ; const bf16* pr = P + (size_t)t * NINP;
;         {
;             const u32x4 w = *(const u32x4*)(pr + PC_CQ + 8 * lane); float v[8] = {bflo(w.x), bfhi(w.x), bflo(w.y), bfhi(w.y), bflo(w.z), bfhi(w.z), bflo(w.w), bfhi(w.w)};
;             float ss = 0.f;
; #pragma unroll
;             for (int q = 0; q < 8; ++q) ss += v[q] * v[q];
;             const float rstd = rsqrtf(wave_sum(ss) * (1.0f / QL) + EPS);
;             const f32x4 g0 = *(const f32x4*)(gq + 8 * lane), g1 = *(const f32x4*)(gq + 8 * lane + 4);
;             u32x4 o; o.x = cvtpk(v[0] * rstd * g0.x, v[1] * rstd * g0.y); o.y = cvtpk(v[2] * rstd * g0.z, v[3] * rstd * g0.w); o.z = cvtpk(v[4] * rstd * g1.x, v[5] * rstd * g1.y); o.w = cvtpk(v[6] * rstd * g1.z, v[7] * rstd * g1.w);
;             *(u32x2*)((unsigned char*)CQN + (size_t)t * QL + 8 * lane) = pack8_fp8((f32x4){v[0] * rstd * g0.x, v[1] * rstd * g0.y, v[2] * rstd * g0.z, v[3] * rstd * g0.w}, (f32x4){v[4] * rstd * g1.x, v[5] * rstd * g1.y, v[6] * rstd * g1.z, v[7] * rstd * g1.w});
;         }
;         {
;             const u32x2 w = *(const u32x2*)(pr + PC_CKV + 4 * lane); float v[4] = {bflo(w.x), bfhi(w.x), bflo(w.y), bfhi(w.y)};
;             const float rstd = rsqrtf(wave_sum(v[0] * v[0] + v[1] * v[1] + v[2] * v[2] + v[3] * v[3]) * (1.0f / KVL) + EPS);
;             const f32x4 g0 = *(const f32x4*)(gkv + 4 * lane);
;             u32x2 o; o.x = cvtpk(v[0] * rstd * g0.x, v[1] * rstd * g0.y); o.y = cvtpk(v[2] * rstd * g0.z, v[3] * rstd * g0.w);
;             *(u32x2*)(CKVN + (size_t)t * KVL + 4 * lane) = o;
;         }
;         {
.LBB0_1922:
	s_mov_b64 s[0:1], s[24:25]
	s_mov_b32 s0, s100
	s_waitcnt lgkmcnt(0)
	s_cmp_gt_i32 s0, 13
	s_cbranch_scc1 .LBB0_1935
	s_mov_b64 s[0:1], s[24:25]
	s_mov_b32 s0, s101
	s_waitcnt lgkmcnt(0)
	s_cmp_lt_i32 s0, 14
	s_cbranch_scc1 .LBB0_1934
	v_readlane_b32 s0, v255, 0
	v_readlane_b32 s1, v255, 1
	v_mov_b32_e32 v1, v0
	s_lshl_b32 s2, s97, 3
	v_readfirstlane_b32 s3, v1
	s_ashr_i32 s3, s3, 6
	s_add_i32 s6, s3, s2
	s_cmpk_gt_i32 s6, 0x1fff
	s_cbranch_scc1 .LBB0_1934
	s_mov_b64 s[4:5], s[98:99]
	s_load_dwordx2 s[2:3], s[0:1], 0x38
	s_load_dwordx2 s[10:11], s[0:1], 0x48
	s_load_dwordx2 s[12:13], s[0:1], 0x60
	v_and_b32_e32 v6, 1, v1
	v_and_b32_e32 v8, 63, v1
	v_mov_b32_e32 v3, 0
	v_cmp_eq_u32_e64 s[0:1], 0, v6
	v_lshlrev_b32_e32 v6, 2, v1
	v_lshlrev_b32_e32 v2, 5, v8
	v_and_b32_e32 v54, 60, v6
	v_lshlrev_b32_e32 v6, 6, v8
	v_mov_b32_e32 v7, v3
	s_waitcnt lgkmcnt(0)
	v_lshl_add_u64 v[50:51], s[2:3], 0, v[2:3]
	v_lshl_add_u64 v[6:7], s[12:13], 0, v[6:7]
	s_mov_b64 s[2:3], 0x3000
	s_add_u32 s8, s4, 0x200000
	v_lshl_add_u64 v[56:57], v[6:7], 0, s[2:3]
	s_mov_b64 s[2:3], 0x4000
	s_addc_u32 s9, s5, 0
	v_lshl_add_u64 v[58:59], v[6:7], 0, s[2:3]
	s_mov_b64 s[2:3], 0x5000
	s_ashr_i32 s7, s6, 31
	v_lshl_add_u64 v[60:61], v[6:7], 0, s[2:3]
	s_lshl_b64 s[2:3], s[6:7], 11
	v_lshlrev_b32_e32 v9, 3, v8
	v_or_b32_e32 v64, s2, v2
	v_mov_b32_e32 v65, s3
	s_lshl_b64 s[2:3], s[6:7], 9
	v_lshlrev_b32_e32 v4, 4, v8
	v_mov_b32_e32 v5, v3
	v_or_b32_e32 v66, s2, v9
	v_mov_b32_e32 v67, s3
	s_lshl_b64 s[2:3], s[6:7], 14
	v_lshl_add_u64 v[52:53], s[10:11], 0, v[4:5]
	v_mov_b32_e32 v55, v3
	v_or_b32_e32 v68, s2, v2
	v_or_b32_e32 v2, s2, v9
	v_mov_b32_e32 v3, s3
	s_mov_b64 s[10:11], 0x3e400400
	v_lshl_add_u64 v[70:71], v[2:3], 0, s[10:11]
	v_lshl_or_b32 v2, v8, 1, s2
	s_mov_b64 s[10:11], 0x3e400600
	v_mov_b32_e32 v69, s3
	v_lshl_add_u64 v[72:73], v[2:3], 0, s[10:11]
	v_or_b32_e32 v2, s2, v4
	s_mov_b64 s[2:3], 0x3e400000
	v_lshl_add_u64 v[74:75], v[2:3], 0, s[2:3]
	v_mbcnt_lo_u32_b32 v2, -1, 0
	v_mbcnt_hi_u32_b32 v97, -1, v2
	v_and_b32_e32 v2, 64, v97
	v_bfe_u32 v5, v1, 1, 5
	v_add_u32_e32 v99, 64, v2
	v_or_b32_e32 v2, v2, v54
	v_bfe_u32 v1, v1, 4, 2
	v_lshl_or_b32 v62, s6, 5, v5
	v_mov_b32_e32 v96, 0x358637bd
	s_mov_b32 s7, 0x800000
	s_mov_b32 s30, 0x46400000
	s_mov_b32 s31, 0x46c00000
	s_movk_i32 s33, 0xc0
	s_mov_b32 s34, 0x4b000000
	s_mov_b32 s35, 0x4b300000
	s_mov_b64 s[10:11], 0x3e3fd000
	s_mov_b64 s[12:13], 0x3e3fd800
	s_mov_b64 s[14:15], 0x3e401000
	s_mov_b64 s[16:17], 0x3e401800
	s_mov_b64 s[18:19], 0x3e405000
	s_mov_b64 s[20:21], 0x3e405800
	s_mov_b64 s[22:23], 0x3e400800
	s_mov_b32 s36, 0x3e400000
	s_mov_b32 s37, 0x47000000
	s_mov_b64 s[24:25], 0x400000
	s_mov_b64 s[26:27], 0x100000
	s_mov_b64 s[28:29], 0x2000000
	v_xor_b32_e32 v98, 1, v97
	v_lshlrev_b32_e32 v100, 2, v2
	v_mov_b64_e32 v[76:77], s[4:5]
	s_branch .LBB0_1927

; __device__ __forceinline__ int otid() { int t = threadIdx.x; asm volatile("" : "+v"(t)); return t; }
; __device__ __forceinline__ unsigned xb_ld(unsigned* p)              { return __hip_atomic_load(p, __ATOMIC_RELAXED, __HIP_MEMORY_SCOPE_AGENT); }
; __device__ __forceinline__ unsigned xb_add(unsigned* p, unsigned v) { return __hip_atomic_fetch_add(p, v, __ATOMIC_RELAXED, __HIP_MEMORY_SCOPE_AGENT); }
; __device__ __forceinline__ void xcd_barrier_complete(unsigned* bar, unsigned x, unsigned& nloc, unsigned& nx) {
;     const unsigned G = gridDim.x * gridDim.y * gridDim.z;
;     unsigned sum, cnt, mine, sp = 0u;
;     for (;;) {
;         sum = 0u; cnt = 0u; mine = 0u;
; #pragma unroll
;         for (unsigned j = 0; j < 16; ++j) { const unsigned c = xb_ld(&bar[XB_XCNT(j)]); sum += c; cnt += (c > 0u) ? 1u : 0u; mine = (j == x) ? c : mine; }
;         if (sum == G) break;
;         __builtin_amdgcn_s_sleep(1);
;         if ((++sp & 255u) == 0u) { if (xb_ld(&bar[XB_TMO])) break; if (sp > XB_SPIN_CAP) { atomicAdd(&bar[XB_TMO], 1u); break; } }
;     }
;     nloc = mine > 0u ? mine : 1u; nx = cnt > 0u ? cnt : 1u;
; }
; __device__ __forceinline__ void xcd_barrier(const XcdBarrier& b) {
;     asm volatile("s_waitcnt vmcnt(0)" ::: "memory");
;     __syncthreads();
;     if (otid() == 0) {
;         unsigned* bar = b.bar;
;         __builtin_amdgcn_s_waitcnt(0);
;         unsigned nloc = b.st[0], nx = b.st[1];
;         if (nloc == 0u) { xcd_barrier_complete(bar, b.x, nloc, nx); b.st[0] = nloc; b.st[1] = nx; }
;         const unsigned old = xb_add(&bar[XB_XSUB(b.x)], 1u);
;         const unsigned gen = old / nloc;
;         if (old + 1u == (gen + 1u) * nloc) {
;             __builtin_amdgcn_fence(__ATOMIC_RELEASE, "agent");
;             asm volatile("s_waitcnt vmcnt(0)" ::: "memory");
;             const unsigned og = xb_add(&bar[XB_TOP], 1u);
.LBB0_1935:
	s_mov_b64 s[0:1], s[24:25]
	s_mov_b32 s0, s100
	s_waitcnt lgkmcnt(0)
	s_cmp_gt_i32 s0, 13
	s_cbranch_scc1 .LBB0_1993
	s_mov_b64 s[0:1], s[24:25]
	s_mov_b32 s0, s101
	s_waitcnt lgkmcnt(0)
	s_cmp_lt_i32 s0, 14
	s_cbranch_scc1 .LBB0_1992
	v_readlane_b32 s0, v255, 0
	v_readlane_b32 s1, v255, 1
	s_mov_b32 s0, s100
	s_waitcnt lgkmcnt(0)
	s_cmp_gt_i32 s0, 14
	s_cbranch_scc1 .LBB0_1992
	v_readlane_b32 s0, v255, 0
	v_readlane_b32 s1, v255, 1
	s_mov_b32 s0, s101
	s_waitcnt lgkmcnt(0)
	s_cmp_lt_i32 s0, 15
	s_cbranch_scc1 .LBB0_1992
	v_readlane_b32 s2, v255, 0
	v_readlane_b32 s3, v255, 1
	s_getreg_b32 s4, hwreg(HW_REG_XCC_ID, 0, 4)
	s_waitcnt vmcnt(0)
	v_mov_b32_e32 v1, v0
	s_waitcnt vmcnt(0)
	s_barrier
	s_nop 0
	v_cmp_eq_u32_e32 vcc, 0, v1
	s_and_saveexec_b64 s[0:1], vcc
	s_cbranch_execz .LBB0_1991
	s_add_i32 s5, 0, 0x20020
	v_mov_b32_e32 v1, s5
	s_mov_b64 s[2:3], s[98:99]
	s_waitcnt vmcnt(0) expcnt(0) lgkmcnt(0)
	ds_read_b32 v3, v1
	s_add_i32 s5, 0, 0x20024
	v_mov_b32_e32 v1, s5
	ds_read_b32 v1, v1
	s_and_b32 s33, s4, 15
	s_waitcnt lgkmcnt(1)
	v_cmp_ne_u32_e32 vcc, 0, v3
	s_cbranch_vccnz .LBB0_1955
	v_readlane_b32 s4, v255, 0
	v_readlane_b32 s5, v255, 1
	s_load_dwordx2 s[8:9], s[4:5], 0xe0
	s_load_dword s7, s[4:5], 0xe8
	s_add_u32 s4, s2, 0x4200
	s_addc_u32 s5, s3, 0
	s_add_u32 s6, s2, 0x4400
	s_waitcnt lgkmcnt(0)
	s_mul_i32 s46, s9, s8
	s_mul_i32 s46, s46, s7
	s_addc_u32 s7, s3, 0
	s_add_u32 s8, s2, 0x4500
	s_addc_u32 s9, s3, 0
	s_add_u32 s10, s2, 0x4600
	s_addc_u32 s11, s3, 0
	s_add_u32 s12, s2, 0x4700
	s_addc_u32 s13, s3, 0
	s_add_u32 s14, s2, 0x4800
	s_addc_u32 s15, s3, 0
	s_add_u32 s16, s2, 0x4900
	s_addc_u32 s17, s3, 0
	s_add_u32 s18, s2, 0x4a00
	s_addc_u32 s19, s3, 0
	s_add_u32 s20, s2, 0x4b00
	s_addc_u32 s21, s3, 0
	s_add_u32 s22, s2, 0x4c00
	s_addc_u32 s23, s3, 0
	s_add_u32 s24, s2, 0x4d00
	s_addc_u32 s25, s3, 0
	s_add_u32 s26, s2, 0x4e00
	s_addc_u32 s27, s3, 0
	s_add_u32 s28, s2, 0x4f00
	s_addc_u32 s29, s3, 0
	s_add_u32 s30, s2, 0x5000
	s_addc_u32 s31, s3, 0
	s_add_u32 s34, s2, 0x5100
	s_addc_u32 s35, s3, 0
	s_add_u32 s36, s2, 0x5200
	s_addc_u32 s37, s3, 0
	s_add_u32 s38, s2, 0x5300
	s_addc_u32 s39, s3, 0
	s_mov_b32 s47, 1
	v_mov_b32_e32 v17, 0
	s_branch .LBB0_1943

; template <class P, class MK = NoChain>
; __device__ __forceinline__ void gemm_phase(LAS unsigned char* lds, const P& p, const MK& mk = MK(), bool chain_out = false, bool chained_in = false) {
;     ...
;     int tid = threadIdx.x; asm volatile("" : "+v"(tid));
;     const int wid = __builtin_amdgcn_readfirstlane(tid >> 6), lane = tid & 63, wr = wid >> 2, wc = wid & 3, fr = lane & 15, fq = lane >> 4;
;     unsigned voffB[2], vA[2][2], nvA[2][2], nvB[2]; typedef decltype(mk()) NP; constexpr int NES = NP::FP8 ? 1 : 2; constexpr int NBMODE = bmode_of<NP>::value; constexpr size_t nhstepB = (size_t)(NBMODE == 1 ? 8 : (NBMODE == 2 ? 16 : HALF)) * NP::LDB * NES;
;     constexpr size_t kstep = (size_t)(BK * 2);
;     constexpr int BMODE = bmode_of<P>::value;
;     constexpr size_t hstep = (size_t)(BMODE == 1 ? 8 : (BMODE == 2 ? 16 : HALF)) * LDB * ES, hstepA = (size_t)HALF * LDA * ES;
; #pragma unroll
;     for (int i = 0; i < 2; ++i) { int R, C; stage_rc(tid * 16 + i * 8192, R, C); const int rho_ = R & 31;
;         const int fq_ = (rho_ & 15) >> 2, n_ = rho_ >> 4, q_ = rho_ & 3;
;         const int Rb = BMODE == 1 ? ((R >> 5) * 64 + fq_ * 16 + 4 * n_ + q_) : (BMODE == 2 ? ((R >> 5) * 64 + 32 * (fq_ >> 1) + 8 * n_ + 4 * (fq_ & 1) + q_) : (P::PERM ? ((R & ~31) + perm32(R & 31)) : R));
;         voffB[i] = (unsigned)(Rb * LDB * ES + C * 2); vA[0][i] = (unsigned)(R * LDA * ES + C * 2); vA[1][i] = vA[0][i] + (unsigned)hstepA; nvA[0][i] = vA[0][i]; nvA[1][i] = vA[1][i]; nvB[i] = voffB[i]; }
;     const unsigned ldsw = (unsigned)wid * 1024u;
;     const int aoff = lds_byte(wr * 64 + fr, fq * 8), boff = lds_byte(wc * 32 + fr, fq * 8); const int aoff1 = aoff ^ 64, boff1 = boff ^ 64;
;     ...
;     Unit cur, nxt; int ui = 0;
;     if (!p.next(0, cur)) return;
;     Acc acc;
;     if constexpr (!PEEL) {
; #pragma unroll
;     for (int a = 0; a < 2; ++a)
; #pragma unroll
;         for (int b = 0; b < 2; ++b)
; #pragma unroll
;             for (int m = 0; m < 4; ++m)
; #pragma unroll
;                 for (int n = 0; n < 2; ++n) { typedef double d2_ __attribute__((ext_vector_type(2))); d2_ z_; asm volatile("v_mov_b64 %0, 0" : "=v"(z_.x)); asm volatile("v_mov_b64 %0, 0" : "=v"(z_.y)); acc[a][b][m][n] = __builtin_bit_cast(f32x4, z_); }
;     }
;     typedef int v8i_ __attribute__((ext_vector_type(8))); typedef int v4i_ __attribute__((ext_vector_type(4)));
.LBB0_1993:
	s_mov_b64 s[0:1], s[24:25]
	s_mov_b32 s0, s100
	s_waitcnt lgkmcnt(0)
	s_cmp_gt_i32 s0, 14
	s_cbranch_scc1 .LBB0_2079
	s_mov_b64 s[0:1], s[24:25]
	s_mov_b32 s0, s101
	s_waitcnt lgkmcnt(0)
	s_cmp_lt_i32 s0, 15
	s_cbranch_scc1 .LBB0_2079
	s_cmpk_lt_i32 s95, 0x100
	v_readlane_b32 s2, v255, 4
	s_cselect_b64 s[0:1], -1, 0
	s_and_b32 s2, s2, -8
	s_sub_i32 s4, s95, s2
	s_mov_b64 s[2:3], s[24:25]
	v_mov_b32_e32 v130, v0
	s_mov_b32 s67, s97
	s_cmpk_gt_i32 s95, 0xff
	s_nop 0
	v_readfirstlane_b32 s10, v130
	s_cbranch_scc1 .LBB0_1997
	s_lshl_b32 s6, s4, 5
	s_mul_i32 s5, s4, 33
	s_cmp_lt_i32 s4, 0
	s_cselect_b32 s5, s5, s6
	s_add_i32 s5, s5, s96
	s_ashr_i32 s6, s5, 31
	s_lshr_b32 s6, s6, 26
	s_add_i32 s6, s5, s6
	s_ashr_i32 s7, s6, 6
	s_andn2_b32 s6, s6, 63
	s_sub_i32 s5, s5, s6
	s_bfe_i32 s6, s5, 0x80000
	s_bfe_u32 s6, s6, 0x3000c
	s_add_i32 s6, s5, s6
	s_bfe_i32 s8, s6, 0x80000
	s_and_b32 s6, s6, 0xf8
	s_sub_i32 s5, s5, s6
	s_lshl_b32 s7, s7, 3
	s_sext_i32_i16 s8, s8
	s_sext_i32_i8 s5, s5
	s_add_i32 s28, s7, s5
	s_ashr_i32 s26, s8, 3
.LBB0_1997:
	s_ashr_i32 s97, s96, 31
	s_ashr_i32 s5, s4, 31
	s_lshl_b64 s[6:7], s[96:97], 17
	s_andn2_b64 vcc, exec, s[0:1]
	s_lshl_b64 s[8:9], s[4:5], 17
	s_cbranch_vccnz .LBB0_2044
	s_mov_b64 s[0:1], s[98:99]
	v_lshrrev_b32_e32 v139, 4, v130
	v_xor_b32_e32 v1, v139, v130
	v_ashrrev_i32_e32 v132, 3, v130
	v_lshlrev_b32_e32 v1, 4, v1
	s_waitcnt lgkmcnt(0)
	s_add_u32 s5, s0, 0x47000000
	v_lshlrev_b32_e32 v134, 1, v132
	v_lshrrev_b32_e32 v2, 2, v132
	s_addc_u32 s46, s1, 0
	v_and_b32_e32 v131, 0x70, v1
	v_and_b32_e32 v1, 24, v134
	v_and_b32_e32 v135, 4, v2
	v_and_b32_e32 v2, 0x1fffe3, v132
	s_add_u32 s47, s0, 0x6200000
	v_or3_b32 v1, v2, v1, v135
	s_addc_u32 s48, s1, 0
	v_lshl_or_b32 v194, v1, 11, v131
	v_mov_b32_e32 v1, 0x2000
	s_ashr_i32 s3, s10, 6
	s_ashr_i32 s29, s28, 31
	s_ashr_i32 s27, s26, 31
	s_ashr_i32 s2, s10, 8
	v_lshl_add_u32 v136, v130, 4, v1
	s_lshl_b32 s14, s3, 10
	s_lshl_b64 s[10:11], s[28:29], 19
	s_lshl_b64 s[12:13], s[26:27], 19
	v_ashrrev_i32_e32 v133, 7, v136
	s_add_u32 s38, s47, s12
	v_lshlrev_b32_e32 v137, 1, v133
	v_lshrrev_b32_e32 v2, 2, v133
	s_addc_u32 s39, s48, s13
	s_add_i32 s27, s14, 0
	v_and_b32_e32 v1, 24, v137
	v_and_b32_e32 v138, 4, v2
	v_and_b32_e32 v2, 0x1fffe3, v133
	s_add_i32 s29, s27, 0x10000
	s_add_i32 s49, s27, 0x12000
	v_or3_b32 v1, v2, v1, v138
	s_mov_b64 s[12:13], s[38:39]
	s_mov_b32 m0, s29
	s_add_u32 s30, s5, s10
	v_lshl_or_b32 v200, v1, 11, v131
	v_mov_b64 v[106:107], 0
	v_mov_b64 v[108:109], 0
	v_mov_b64 v[110:111], 0
	v_mov_b64 v[112:113], 0
	v_mov_b64 v[98:99], 0
	v_mov_b64 v[100:101], 0
	v_mov_b64 v[102:103], 0
	v_mov_b64 v[104:105], 0
	v_mov_b64 v[82:83], 0
	v_mov_b64 v[84:85], 0
	v_mov_b64 v[86:87], 0
	v_mov_b64 v[88:89], 0
	v_mov_b64 v[70:71], 0
	v_mov_b64 v[72:73], 0
	v_mov_b64 v[66:67], 0
	v_mov_b64 v[68:69], 0
	v_mov_b64 v[122:123], 0
	v_mov_b64 v[124:125], 0
	v_mov_b64 v[126:127], 0
	v_mov_b64 v[128:129], 0
	v_mov_b64 v[114:115], 0
	v_mov_b64 v[116:117], 0
	v_mov_b64 v[118:119], 0
	v_mov_b64 v[120:121], 0
	v_mov_b64 v[94:95], 0
	v_mov_b64 v[96:97], 0
	v_mov_b64 v[90:91], 0
	v_mov_b64 v[92:93], 0
	v_mov_b64 v[78:79], 0
	v_mov_b64 v[80:81], 0
	v_mov_b64 v[74:75], 0
	v_mov_b64 v[76:77], 0
	v_mov_b64 v[54:55], 0
	v_mov_b64 v[56:57], 0
	v_mov_b64 v[50:51], 0
	v_mov_b64 v[52:53], 0
	v_mov_b64 v[38:39], 0
	v_mov_b64 v[40:41], 0
	v_mov_b64 v[34:35], 0
	v_mov_b64 v[36:37], 0
	v_mov_b64 v[22:23], 0
	v_mov_b64 v[24:25], 0
	v_mov_b64 v[18:19], 0
	v_mov_b64 v[20:21], 0
	v_mov_b64 v[6:7], 0
	v_mov_b64 v[8:9], 0
	v_mov_b64 v[2:3], 0
	v_mov_b64 v[4:5], 0
	v_mov_b64 v[62:63], 0
	v_mov_b64 v[64:65], 0
	v_mov_b64 v[58:59], 0
	v_mov_b64 v[60:61], 0
	v_mov_b64 v[46:47], 0
	v_mov_b64 v[48:49], 0
	v_mov_b64 v[42:43], 0
	v_mov_b64 v[44:45], 0
	v_mov_b64 v[30:31], 0
	v_mov_b64 v[32:33], 0
	v_mov_b64 v[26:27], 0
	v_mov_b64 v[28:29], 0
	v_mov_b64 v[14:15], 0
	v_mov_b64 v[16:17], 0
	v_mov_b64 v[10:11], 0
	v_mov_b64 v[12:13], 0
	s_addc_u32 s31, s46, s11
	global_load_lds_dwordx4 v194, s[12:13]
	s_mov_b32 m0, s49
	v_lshl_or_b32 v196, v132, 11, v131
	global_load_lds_dwordx4 v200, s[12:13]
	s_mov_b64 s[10:11], s[30:31]
	s_mov_b32 m0, s27
	s_add_i32 s50, s27, 0x2000
	v_lshl_or_b32 v202, v133, 11, v131
	v_add_u32_e32 v198, 0x40000, v196
	global_load_lds_dwordx4 v196, s[10:11]
	s_mov_b32 m0, s50
	v_add_u32_e32 v204, 0x40000, v202
	global_load_lds_dwordx4 v202, s[10:11]
	s_add_u32 s10, s38, 0x40000
	s_addc_u32 s11, s39, 0
	s_add_i32 s51, s27, 0x14000
	s_mov_b32 m0, s51
	s_add_i32 s52, s27, 0x16000
	s_add_i32 s53, s27, 0x4000
	global_load_lds_dwordx4 v194, s[10:11]
	s_mov_b32 m0, s52
	s_add_i32 s54, s27, 0x6000
	global_load_lds_dwordx4 v200, s[10:11]
	s_mov_b64 s[10:11], s[30:31]
	s_mov_b32 m0, s53
	v_mov_b32_e32 v207, 0
	global_load_lds_dwordx4 v198, s[10:11]
	s_mov_b32 m0, s54
	v_mov_b32_e32 v195, v207
	global_load_lds_dwordx4 v204, s[10:11]
	s_mov_b32 s11, 0
	v_mov_b32_e32 v201, v207
	v_mov_b32_e32 v197, v207
	s_cmp_lg_u32 s2, 1
	v_mov_b32_e32 v203, v207
	s_cbranch_scc1 .LBB0_2000
	s_barrier

;     __device__ __forceinline__ bool next(int i, pg::Unit& u) const { u.aux = 0; u.aux2 = 0; u.half = 0; return ord.get(i, u.pm, u.pn); }
;     __device__ __forceinline__ bool next(int i, pg::Unit& u) const { u.aux = 0; u.aux2 = 0; u.half = 0; return ord.get(i, u.pm, u.pn); }
; __device__ __forceinline__ CArgs* fresh_args() { CArgs* p = (CArgs*)__builtin_amdgcn_kernarg_segment_ptr(); asm volatile("" : "+s"(p)); return p; }
; template <class P, class MK = NoChain>
; __device__ __forceinline__ void gemm_phase(LAS unsigned char* lds, const P& p, const MK& mk = MK(), bool chain_out = false, bool chained_in = false) {
;     ...
;         const bool has_next = p.next(ui + 1, nxt);
;         const char* nA = has_next ? p.a_base(nxt) : cA; const char* nB = has_next ? p.b_base(nxt) : cB;
;         const bool chain_now = CHAIN && chain_out && !has_next;
;         if constexpr (CHAIN) { if (chain_now) { const auto np = mk(); Unit nu; (void)np.next(0, nu); nA = np.a_base(nu); nB = np.b_base(nu); } }
; template <int l> __device__ __forceinline__ void layer_body(LAS unsigned char* lds, unsigned char* lds_raw, int bx, int vcu) {
;     ...
;             const auto mkK = [=]() { unsigned char* ws = fresh_args()->ws; DenseP<KVL, EpiK, pg::ListOrder> P; P.A = (const char*)(ws + WS_CKVN); P.Bt = (const char*)(ws + WS_WUKV) + (size_t)l * NH * 128 * KVL * 2; P.ord.nN = NH / 2; P.ord.first = bx; P.ord.n = 1; P.e.Kb = ws + WS_K; return P; };
.LBB0_2008:
	s_ashr_i32 s19, s18, 31
	s_lshl_b64 s[22:23], s[18:19], 19
	s_add_u32 s22, s5, s22
	s_addc_u32 s23, s46, s23
	s_ashr_i32 s21, s20, 31
	s_lshl_b64 s[24:25], s[20:21], 19
	s_add_u32 s24, s47, s24
	s_addc_u32 s25, s48, s25
	s_andn2_b64 vcc, exec, s[0:1]
	s_cbranch_vccnz .LBB0_2010
	v_readlane_b32 s0, v255, 0
	v_readlane_b32 s1, v255, 1
	s_mov_b64 s[0:1], s[98:99]
	s_waitcnt lgkmcnt(0)
	s_add_u32 s17, s0, s6
	s_addc_u32 s19, s1, s7
	s_add_u32 s22, s17, 0x46c00000
	s_addc_u32 s23, s19, 0
	s_add_u32 s0, s0, s8
	s_addc_u32 s1, s1, s9
	s_add_u32 s24, s0, 0x4b00000
	s_addc_u32 s25, s1, 0

.LBB0_2074:
	s_lshl_b32 s0, s5, 6
	s_lshl_b32 s6, s4, 1
	s_and_b32 s0, s0, 64
	s_add_u32 s8, s16, 0x4b000000
	v_mov_b32_e32 v131, 0
	s_addc_u32 s9, s17, 0
	s_lshr_b32 s5, s5, 1
	s_mov_b32 s4, 0x3e800000
	v_pk_mul_f32 v[114:115], v[114:115], s[4:5] op_sel_hi:[1,0]
	v_pk_mul_f32 v[134:135], v[118:119], s[4:5] op_sel_hi:[1,0]
	v_mov_b32_e32 v118, v131
	v_cvt_pk_fp8_f32 v118, v114, v115
	v_mov_b32_e32 v119, v131
	v_pk_mul_f32 v[114:115], v[116:117], s[4:5] op_sel_hi:[1,0]
	v_lshl_add_u32 v1, s96, 8, v1
	v_cvt_pk_fp8_f32 v119, v134, v135
	v_pk_mul_f32 v[116:117], v[120:121], s[4:5] op_sel_hi:[1,0]
	v_cvt_pk_fp8_f32 v118, v114, v115 op_sel:[0,0,1]
	v_pk_mul_f32 v[114:115], v[122:123], s[4:5] op_sel_hi:[1,0]
	v_mov_b32_e32 v120, v131
	v_ashrrev_i32_e32 v132, 31, v1
	v_cvt_pk_fp8_f32 v120, v114, v115
	v_lshrrev_b32_e32 v132, 20, v132
	v_add_u32_e32 v132, v1, v132
	v_ashrrev_i32_e32 v133, 12, v132
	v_cvt_pk_fp8_f32 v119, v116, v117 op_sel:[0,0,1]
	v_pk_mul_f32 v[116:117], v[126:127], s[4:5] op_sel_hi:[1,0]
	v_mov_b32_e32 v121, v131
	v_pk_mul_f32 v[114:115], v[124:125], s[4:5] op_sel_hi:[1,0]
	v_cvt_pk_fp8_f32 v121, v116, v117
	v_cvt_pk_fp8_f32 v120, v114, v115 op_sel:[0,0,1]
	v_lshl_add_u32 v114, v133, 4, s6
	v_mul_i32_i24_e32 v132, 0x1000, v133
	v_or_b32_e32 v114, s5, v114
	v_sub_u32_e32 v132, v1, v132
	v_ashrrev_i32_e32 v115, 31, v114
	v_pk_mul_f32 v[116:117], v[128:129], s[4:5] op_sel_hi:[1,0]
	v_lshlrev_b64 v[114:115], 12, v[114:115]
	v_ashrrev_i32_e32 v133, 31, v132
	v_cvt_pk_fp8_f32 v121, v116, v117 op_sel:[0,0,1]
	v_lshl_add_u64 v[116:117], v[114:115], 0, v[132:133]
	s_movk_i32 s7, 0xc0
	v_mov_b64_e32 v[114:115], s[8:9]
	v_mad_u64_u32 v[122:123], s[8:9], v116, s7, v[114:115]
	s_mov_b32 s1, 0
	v_mad_i32_i24 v123, v117, s7, v123
	v_lshlrev_b32_e32 v130, 4, v212
	v_lshl_add_u64 v[116:117], v[122:123], 0, s[0:1]
	v_lshl_add_u64 v[116:117], v[116:117], 0, v[130:131]
	global_store_dwordx4 v[116:117], v[118:121], off
	v_add_u32_e32 v116, 16, v1
	v_ashrrev_i32_e32 v117, 31, v116
	v_lshrrev_b32_e32 v117, 20, v117
	v_add_u32_e32 v117, v116, v117
	v_ashrrev_i32_e32 v117, 12, v117
	v_mul_i32_i24_e32 v118, 0x1000, v117
	v_sub_u32_e32 v116, v116, v118
	v_pk_mul_f32 v[118:119], v[98:99], s[4:5] op_sel_hi:[1,0]
	v_pk_mul_f32 v[102:103], v[102:103], s[4:5] op_sel_hi:[1,0]
	v_mov_b32_e32 v98, v131
	v_mov_b32_e32 v99, v131
	v_cvt_pk_fp8_f32 v98, v118, v119
	v_cvt_pk_fp8_f32 v99, v102, v103
	v_pk_mul_f32 v[100:101], v[100:101], s[4:5] op_sel_hi:[1,0]
	v_pk_mul_f32 v[102:103], v[104:105], s[4:5] op_sel_hi:[1,0]
	v_cvt_pk_fp8_f32 v98, v100, v101 op_sel:[0,0,1]
	v_cvt_pk_fp8_f32 v99, v102, v103 op_sel:[0,0,1]
	v_pk_mul_f32 v[102:103], v[106:107], s[4:5] op_sel_hi:[1,0]
	v_mov_b32_e32 v100, v131
	v_cvt_pk_fp8_f32 v100, v102, v103
	v_pk_mul_f32 v[102:103], v[108:109], s[4:5] op_sel_hi:[1,0]
	v_pk_mul_f32 v[104:105], v[110:111], s[4:5] op_sel_hi:[1,0]
	v_mov_b32_e32 v101, v131
	v_cvt_pk_fp8_f32 v100, v102, v103 op_sel:[0,0,1]
	v_lshl_add_u32 v102, v117, 4, s6
	v_cvt_pk_fp8_f32 v101, v104, v105
	v_or_b32_e32 v102, s5, v102
	v_ashrrev_i32_e32 v103, 31, v102
	v_lshlrev_b64 v[102:103], 12, v[102:103]
	v_ashrrev_i32_e32 v117, 31, v116
	v_pk_mul_f32 v[104:105], v[112:113], s[4:5] op_sel_hi:[1,0]
	v_lshl_add_u64 v[102:103], v[102:103], 0, v[116:117]
	v_cvt_pk_fp8_f32 v101, v104, v105 op_sel:[0,0,1]
	v_mad_u64_u32 v[104:105], s[8:9], v102, s7, v[114:115]
	v_mad_i32_i24 v105, v103, s7, v105
	v_lshl_add_u64 v[102:103], v[104:105], 0, s[0:1]
	v_lshl_add_u64 v[102:103], v[102:103], 0, v[130:131]
	global_store_dwordx4 v[102:103], v[98:101], off
	v_pk_mul_f32 v[86:87], v[86:87], s[4:5] op_sel_hi:[1,0]
	v_pk_mul_f32 v[84:85], v[84:85], s[4:5] op_sel_hi:[1,0]
	v_add_u32_e32 v98, 32, v1
	v_ashrrev_i32_e32 v99, 31, v98
	v_lshrrev_b32_e32 v99, 20, v99
	v_add_u32_e32 v99, v98, v99
	v_ashrrev_i32_e32 v99, 12, v99
	v_mul_i32_i24_e32 v100, 0x1000, v99
	v_sub_u32_e32 v98, v98, v100
	v_pk_mul_f32 v[100:101], v[82:83], s[4:5] op_sel_hi:[1,0]
	v_mov_b32_e32 v82, v131
	v_mov_b32_e32 v83, v131
	v_cvt_pk_fp8_f32 v82, v100, v101
	v_cvt_pk_fp8_f32 v83, v86, v87
	v_pk_mul_f32 v[86:87], v[88:89], s[4:5] op_sel_hi:[1,0]
	v_pk_mul_f32 v[88:89], v[94:95], s[4:5] op_sel_hi:[1,0]
	v_cvt_pk_fp8_f32 v82, v84, v85 op_sel:[0,0,1]
	v_cvt_pk_fp8_f32 v83, v86, v87 op_sel:[0,0,1]
	v_pk_mul_f32 v[86:87], v[90:91], s[4:5] op_sel_hi:[1,0]
	v_mov_b32_e32 v84, v131
	v_cvt_pk_fp8_f32 v84, v86, v87
	v_pk_mul_f32 v[86:87], v[92:93], s[4:5] op_sel_hi:[1,0]
	v_mov_b32_e32 v85, v131
	v_cvt_pk_fp8_f32 v85, v88, v89
	v_cvt_pk_fp8_f32 v84, v86, v87 op_sel:[0,0,1]
	v_lshl_add_u32 v86, v99, 4, s6
	v_or_b32_e32 v86, s5, v86
	v_ashrrev_i32_e32 v87, 31, v86
	v_lshlrev_b64 v[86:87], 12, v[86:87]
	v_ashrrev_i32_e32 v99, 31, v98
	v_pk_mul_f32 v[88:89], v[96:97], s[4:5] op_sel_hi:[1,0]
	v_lshl_add_u64 v[86:87], v[86:87], 0, v[98:99]
	v_cvt_pk_fp8_f32 v85, v88, v89 op_sel:[0,0,1]
	v_mad_u64_u32 v[88:89], s[8:9], v86, s7, v[114:115]
	v_mad_i32_i24 v89, v87, s7, v89
	v_lshl_add_u64 v[86:87], v[88:89], 0, s[0:1]
	v_lshl_add_u64 v[86:87], v[86:87], 0, v[130:131]
	global_store_dwordx4 v[86:87], v[82:85], off
	v_pk_mul_f32 v[62:63], v[62:63], s[4:5] op_sel_hi:[1,0]
	v_pk_mul_f32 v[60:61], v[60:61], s[4:5] op_sel_hi:[1,0]
	v_add_u32_e32 v82, 48, v1
	v_ashrrev_i32_e32 v83, 31, v82
	v_lshrrev_b32_e32 v83, 20, v83
	v_add_u32_e32 v83, v82, v83
	v_ashrrev_i32_e32 v83, 12, v83
	v_mul_i32_i24_e32 v84, 0x1000, v83
	v_sub_u32_e32 v82, v82, v84
	v_pk_mul_f32 v[84:85], v[58:59], s[4:5] op_sel_hi:[1,0]
	v_mov_b32_e32 v58, v131
	v_mov_b32_e32 v59, v131
	v_cvt_pk_fp8_f32 v58, v84, v85
	v_cvt_pk_fp8_f32 v59, v62, v63
	v_pk_mul_f32 v[62:63], v[64:65], s[4:5] op_sel_hi:[1,0]
	v_pk_mul_f32 v[64:65], v[78:79], s[4:5] op_sel_hi:[1,0]
	v_cvt_pk_fp8_f32 v58, v60, v61 op_sel:[0,0,1]
	v_cvt_pk_fp8_f32 v59, v62, v63 op_sel:[0,0,1]
	v_pk_mul_f32 v[62:63], v[74:75], s[4:5] op_sel_hi:[1,0]
	v_mov_b32_e32 v60, v131
	v_cvt_pk_fp8_f32 v60, v62, v63
	v_pk_mul_f32 v[62:63], v[76:77], s[4:5] op_sel_hi:[1,0]
	v_mov_b32_e32 v61, v131
	v_cvt_pk_fp8_f32 v61, v64, v65
	v_cvt_pk_fp8_f32 v60, v62, v63 op_sel:[0,0,1]
	v_lshl_add_u32 v62, v83, 4, s6
	v_or_b32_e32 v62, s5, v62
	v_ashrrev_i32_e32 v63, 31, v62
	v_lshlrev_b64 v[62:63], 12, v[62:63]
	v_ashrrev_i32_e32 v83, 31, v82
	v_pk_mul_f32 v[64:65], v[80:81], s[4:5] op_sel_hi:[1,0]
	v_lshl_add_u64 v[62:63], v[62:63], 0, v[82:83]
	v_cvt_pk_fp8_f32 v61, v64, v65 op_sel:[0,0,1]
	v_mad_u64_u32 v[64:65], s[8:9], v62, s7, v[114:115]
	v_mad_i32_i24 v65, v63, s7, v65
	v_lshl_add_u64 v[62:63], v[64:65], 0, s[0:1]
	v_lshl_add_u64 v[62:63], v[62:63], 0, v[130:131]
	global_store_dwordx4 v[62:63], v[58:61], off
	v_pk_mul_f32 v[54:55], v[54:55], s[4:5] op_sel_hi:[1,0]
	v_pk_mul_f32 v[52:53], v[52:53], s[4:5] op_sel_hi:[1,0]
	v_add_u32_e32 v58, 0x80, v1
	v_ashrrev_i32_e32 v59, 31, v58
	v_lshrrev_b32_e32 v59, 20, v59
	v_add_u32_e32 v59, v58, v59
	v_ashrrev_i32_e32 v59, 12, v59
	v_mul_i32_i24_e32 v60, 0x1000, v59
	v_sub_u32_e32 v58, v58, v60
	v_pk_mul_f32 v[60:61], v[50:51], s[4:5] op_sel_hi:[1,0]
	v_mov_b32_e32 v50, v131
	v_mov_b32_e32 v51, v131
	v_cvt_pk_fp8_f32 v50, v60, v61
	v_cvt_pk_fp8_f32 v51, v54, v55
	v_pk_mul_f32 v[54:55], v[56:57], s[4:5] op_sel_hi:[1,0]
	v_pk_mul_f32 v[56:57], v[70:71], s[4:5] op_sel_hi:[1,0]
	v_cvt_pk_fp8_f32 v50, v52, v53 op_sel:[0,0,1]
	v_cvt_pk_fp8_f32 v51, v54, v55 op_sel:[0,0,1]
	v_pk_mul_f32 v[54:55], v[66:67], s[4:5] op_sel_hi:[1,0]
	v_mov_b32_e32 v52, v131
	v_cvt_pk_fp8_f32 v52, v54, v55
	v_pk_mul_f32 v[54:55], v[68:69], s[4:5] op_sel_hi:[1,0]
	v_mov_b32_e32 v53, v131
	v_cvt_pk_fp8_f32 v53, v56, v57
	v_cvt_pk_fp8_f32 v52, v54, v55 op_sel:[0,0,1]
	v_lshl_add_u32 v54, v59, 4, s6
	v_or_b32_e32 v54, s5, v54
	v_ashrrev_i32_e32 v55, 31, v54
	v_lshlrev_b64 v[54:55], 12, v[54:55]
	v_ashrrev_i32_e32 v59, 31, v58
	v_pk_mul_f32 v[56:57], v[72:73], s[4:5] op_sel_hi:[1,0]
	v_lshl_add_u64 v[54:55], v[54:55], 0, v[58:59]
	v_cvt_pk_fp8_f32 v53, v56, v57 op_sel:[0,0,1]
	v_mad_u64_u32 v[56:57], s[8:9], v54, s7, v[114:115]
	v_mad_i32_i24 v57, v55, s7, v57
	v_lshl_add_u64 v[54:55], v[56:57], 0, s[0:1]
	v_lshl_add_u64 v[54:55], v[54:55], 0, v[130:131]
	global_store_dwordx4 v[54:55], v[50:53], off
	v_pk_mul_f32 v[38:39], v[38:39], s[4:5] op_sel_hi:[1,0]
	v_pk_mul_f32 v[36:37], v[36:37], s[4:5] op_sel_hi:[1,0]
	v_add_u32_e32 v50, 0x90, v1
	v_ashrrev_i32_e32 v51, 31, v50
	v_lshrrev_b32_e32 v51, 20, v51
	v_add_u32_e32 v51, v50, v51
	v_ashrrev_i32_e32 v51, 12, v51
	v_mul_i32_i24_e32 v52, 0x1000, v51
	v_sub_u32_e32 v50, v50, v52
	v_pk_mul_f32 v[52:53], v[34:35], s[4:5] op_sel_hi:[1,0]
	v_mov_b32_e32 v34, v131
	v_mov_b32_e32 v35, v131
	v_cvt_pk_fp8_f32 v34, v52, v53
	v_cvt_pk_fp8_f32 v35, v38, v39
	v_pk_mul_f32 v[38:39], v[40:41], s[4:5] op_sel_hi:[1,0]
	v_pk_mul_f32 v[40:41], v[46:47], s[4:5] op_sel_hi:[1,0]
	v_cvt_pk_fp8_f32 v34, v36, v37 op_sel:[0,0,1]
	v_cvt_pk_fp8_f32 v35, v38, v39 op_sel:[0,0,1]
	v_pk_mul_f32 v[38:39], v[42:43], s[4:5] op_sel_hi:[1,0]
	v_mov_b32_e32 v36, v131
	v_cvt_pk_fp8_f32 v36, v38, v39
	v_pk_mul_f32 v[38:39], v[44:45], s[4:5] op_sel_hi:[1,0]
	v_mov_b32_e32 v37, v131
	v_cvt_pk_fp8_f32 v37, v40, v41
	v_cvt_pk_fp8_f32 v36, v38, v39 op_sel:[0,0,1]
	v_lshl_add_u32 v38, v51, 4, s6
	v_or_b32_e32 v38, s5, v38
	v_ashrrev_i32_e32 v39, 31, v38
	v_lshlrev_b64 v[38:39], 12, v[38:39]
	v_ashrrev_i32_e32 v51, 31, v50
	v_pk_mul_f32 v[40:41], v[48:49], s[4:5] op_sel_hi:[1,0]
	v_lshl_add_u64 v[38:39], v[38:39], 0, v[50:51]
	v_cvt_pk_fp8_f32 v37, v40, v41 op_sel:[0,0,1]
	v_mad_u64_u32 v[40:41], s[8:9], v38, s7, v[114:115]
	v_mad_i32_i24 v41, v39, s7, v41
	v_lshl_add_u64 v[38:39], v[40:41], 0, s[0:1]
	v_lshl_add_u64 v[38:39], v[38:39], 0, v[130:131]
	global_store_dwordx4 v[38:39], v[34:37], off
	v_pk_mul_f32 v[22:23], v[22:23], s[4:5] op_sel_hi:[1,0]
	v_pk_mul_f32 v[20:21], v[20:21], s[4:5] op_sel_hi:[1,0]
	v_add_u32_e32 v34, 0xa0, v1
	v_ashrrev_i32_e32 v35, 31, v34
	v_lshrrev_b32_e32 v35, 20, v35
	v_add_u32_e32 v35, v34, v35
	v_ashrrev_i32_e32 v35, 12, v35
	v_mul_i32_i24_e32 v36, 0x1000, v35
	v_sub_u32_e32 v34, v34, v36
	v_pk_mul_f32 v[36:37], v[18:19], s[4:5] op_sel_hi:[1,0]
	v_mov_b32_e32 v18, v131
	v_mov_b32_e32 v19, v131
	v_cvt_pk_fp8_f32 v18, v36, v37
	v_cvt_pk_fp8_f32 v19, v22, v23
	v_pk_mul_f32 v[22:23], v[24:25], s[4:5] op_sel_hi:[1,0]
	v_pk_mul_f32 v[24:25], v[30:31], s[4:5] op_sel_hi:[1,0]
	v_cvt_pk_fp8_f32 v18, v20, v21 op_sel:[0,0,1]
	v_cvt_pk_fp8_f32 v19, v22, v23 op_sel:[0,0,1]
	v_pk_mul_f32 v[22:23], v[26:27], s[4:5] op_sel_hi:[1,0]
	v_mov_b32_e32 v20, v131
	v_cvt_pk_fp8_f32 v20, v22, v23
	v_pk_mul_f32 v[22:23], v[28:29], s[4:5] op_sel_hi:[1,0]
	v_mov_b32_e32 v21, v131
	v_cvt_pk_fp8_f32 v21, v24, v25
	v_cvt_pk_fp8_f32 v20, v22, v23 op_sel:[0,0,1]
	v_lshl_add_u32 v22, v35, 4, s6
	v_or_b32_e32 v22, s5, v22
	v_ashrrev_i32_e32 v23, 31, v22
	v_lshlrev_b64 v[22:23], 12, v[22:23]
	v_ashrrev_i32_e32 v35, 31, v34
	v_pk_mul_f32 v[24:25], v[32:33], s[4:5] op_sel_hi:[1,0]
	v_lshl_add_u64 v[22:23], v[22:23], 0, v[34:35]
	v_cvt_pk_fp8_f32 v21, v24, v25 op_sel:[0,0,1]
; template <class P, class MK = NoChain>
; __device__ __forceinline__ void gemm_phase(LAS unsigned char* lds, const P& p, const MK& mk = MK(), bool chain_out = false, bool chained_in = false) {
;     ...
;     int tid = threadIdx.x; asm volatile("" : "+v"(tid));
;     const int wid = __builtin_amdgcn_readfirstlane(tid >> 6), lane = tid & 63, wr = wid >> 2, wc = wid & 3, fr = lane & 15, fq = lane >> 4;
;     unsigned voffB[2], vA[2][2], nvA[2][2], nvB[2]; typedef decltype(mk()) NP; constexpr int NES = NP::FP8 ? 1 : 2; constexpr int NBMODE = bmode_of<NP>::value; constexpr size_t nhstepB = (size_t)(NBMODE == 1 ? 8 : (NBMODE == 2 ? 16 : HALF)) * NP::LDB * NES;
;     constexpr size_t kstep = (size_t)(BK * 2);
;     constexpr int BMODE = bmode_of<P>::value;
;     constexpr size_t hstep = (size_t)(BMODE == 1 ? 8 : (BMODE == 2 ? 16 : HALF)) * LDB * ES, hstepA = (size_t)HALF * LDA * ES;
; #pragma unroll
;     for (int i = 0; i < 2; ++i) { int R, C; stage_rc(tid * 16 + i * 8192, R, C); const int rho_ = R & 31;
;         const int fq_ = (rho_ & 15) >> 2, n_ = rho_ >> 4, q_ = rho_ & 3;
;         const int Rb = BMODE == 1 ? ((R >> 5) * 64 + fq_ * 16 + 4 * n_ + q_) : (BMODE == 2 ? ((R >> 5) * 64 + 32 * (fq_ >> 1) + 8 * n_ + 4 * (fq_ & 1) + q_) : (P::PERM ? ((R & ~31) + perm32(R & 31)) : R));
;         voffB[i] = (unsigned)(Rb * LDB * ES + C * 2); vA[0][i] = (unsigned)(R * LDA * ES + C * 2); vA[1][i] = vA[0][i] + (unsigned)hstepA; nvA[0][i] = vA[0][i]; nvA[1][i] = vA[1][i]; nvB[i] = voffB[i]; }
;     const unsigned ldsw = (unsigned)wid * 1024u;
;     const int aoff = lds_byte(wr * 64 + fr, fq * 8), boff = lds_byte(wc * 32 + fr, fq * 8); const int aoff1 = aoff ^ 64, boff1 = boff ^ 64;
;     ...
;     Unit cur, nxt; int ui = 0;
;     if (!p.next(0, cur)) return;
;     Acc acc;
;     if constexpr (!PEEL) {
; #pragma unroll
;     for (int a = 0; a < 2; ++a)
; #pragma unroll
;         for (int b = 0; b < 2; ++b)
; #pragma unroll
;             for (int m = 0; m < 4; ++m)
; #pragma unroll
;                 for (int n = 0; n < 2; ++n) { typedef double d2_ __attribute__((ext_vector_type(2))); d2_ z_; asm volatile("v_mov_b64 %0, 0" : "=v"(z_.x)); asm volatile("v_mov_b64 %0, 0" : "=v"(z_.y)); acc[a][b][m][n] = __builtin_bit_cast(f32x4, z_); }
;     }
;     typedef int v8i_ __attribute__((ext_vector_type(8))); typedef int v4i_ __attribute__((ext_vector_type(4)));
	v_mad_u64_u32 v[24:25], s[8:9], v22, s7, v[114:115]
	v_mad_i32_i24 v25, v23, s7, v25
	v_lshl_add_u64 v[22:23], v[24:25], 0, s[0:1]
	v_lshl_add_u64 v[22:23], v[22:23], 0, v[130:131]
	global_store_dwordx4 v[22:23], v[18:21], off
	v_pk_mul_f32 v[6:7], v[6:7], s[4:5] op_sel_hi:[1,0]
	v_add_u32_e32 v1, 0xb0, v1
	v_pk_mul_f32 v[20:21], v[2:3], s[4:5] op_sel_hi:[1,0]
	v_mov_b32_e32 v2, v131
	v_mov_b32_e32 v3, v131
	v_cvt_pk_fp8_f32 v2, v20, v21
	v_cvt_pk_fp8_f32 v3, v6, v7
	v_ashrrev_i32_e32 v18, 31, v1
	v_pk_mul_f32 v[4:5], v[4:5], s[4:5] op_sel_hi:[1,0]
	v_pk_mul_f32 v[6:7], v[8:9], s[4:5] op_sel_hi:[1,0]
	v_lshrrev_b32_e32 v18, 20, v18
	v_cvt_pk_fp8_f32 v2, v4, v5 op_sel:[0,0,1]
	v_cvt_pk_fp8_f32 v3, v6, v7 op_sel:[0,0,1]
	v_pk_mul_f32 v[6:7], v[10:11], s[4:5] op_sel_hi:[1,0]
	v_mov_b32_e32 v4, v131
	v_add_u32_e32 v18, v1, v18
	v_cvt_pk_fp8_f32 v4, v6, v7
	v_ashrrev_i32_e32 v19, 12, v18
	v_mul_i32_i24_e32 v18, 0x1000, v19
	v_sub_u32_e32 v18, v1, v18
	v_pk_mul_f32 v[8:9], v[14:15], s[4:5] op_sel_hi:[1,0]
	v_mov_b32_e32 v5, v131
	v_pk_mul_f32 v[6:7], v[12:13], s[4:5] op_sel_hi:[1,0]
	v_lshl_add_u32 v1, v19, 4, s6
	v_cvt_pk_fp8_f32 v5, v8, v9
	v_cvt_pk_fp8_f32 v4, v6, v7 op_sel:[0,0,1]
	v_or_b32_e32 v6, s5, v1
	v_ashrrev_i32_e32 v7, 31, v6
	v_lshlrev_b64 v[6:7], 12, v[6:7]
	v_ashrrev_i32_e32 v19, 31, v18
	v_pk_mul_f32 v[8:9], v[16:17], s[4:5] op_sel_hi:[1,0]
	v_lshl_add_u64 v[6:7], v[6:7], 0, v[18:19]
	v_cvt_pk_fp8_f32 v5, v8, v9 op_sel:[0,0,1]
	v_mad_u64_u32 v[8:9], s[4:5], v6, s7, v[114:115]
	v_mad_i32_i24 v9, v7, s7, v9
	v_lshl_add_u64 v[6:7], v[8:9], 0, s[0:1]
	v_readlane_b32 s0, v255, 0
	v_lshl_add_u64 v[6:7], v[6:7], 0, v[130:131]
	v_readlane_b32 s1, v255, 1
	global_store_dwordx4 v[6:7], v[2:5], off
	s_mov_b64 s[0:1], s[98:99]
	v_mov_b32_e32 v135, v131
	v_mov_b32_e32 v2, v0
	v_mov_b32_e32 v141, v131
	v_readfirstlane_b32 s20, v2
	s_ashr_i32 s21, s20, 2
	s_ashr_i32 s4, s20, 6
	v_and_b32_e32 v1, 15, v2
	v_lshrrev_b32_e32 v4, 4, v2
	v_bfe_u32 v5, v2, 1, 3
	s_and_b32 s22, s4, 3
	v_lshlrev_b32_e32 v3, 7, v1
	v_bitop3_b32 v5, v4, v5, 3 bitop3:0x6c
	s_and_b32 s5, s21, 0xffffffc0
	v_lshl_or_b32 v3, s22, 12, v3
	v_lshlrev_b32_e32 v5, 4, v5
	v_or_b32_e32 v1, s5, v1
	v_or_b32_e32 v143, v3, v5
	v_bitop3_b32 v144, v3, 64, v5 bitop3:0x36
	v_lshlrev_b32_e32 v3, 7, v1
	v_or_b32_e32 v145, v3, v5
	v_bitop3_b32 v146, v3, 64, v5 bitop3:0x36
	s_lshl_b32 s23, s4, 10
	v_mov_b32_e32 v3, 0x2000
	v_xor_b32_e32 v4, v4, v2
	v_lshl_add_u32 v3, v2, 4, v3
	v_lshlrev_b32_e32 v4, 4, v4
	s_waitcnt lgkmcnt(0)
	s_add_u32 s4, s0, s12
	v_ashrrev_i32_e32 v3, 7, v3
	v_and_b32_e32 v4, 0x70, v4
	s_addc_u32 s5, s1, s13
	v_lshl_or_b32 v132, v3, 9, v4
	v_lshlrev_b32_e32 v5, 2, v3
	v_and_b32_e32 v6, 7, v3
	v_lshlrev_b32_e32 v7, 1, v3
	v_lshrrev_b32_e32 v3, 1, v3
	s_add_u32 s24, s4, 0x4d00000
	v_and_b32_e32 v7, 0x7fffc0, v7
	v_and_b32_e32 v3, 8, v3
	v_and_or_b32 v5, v5, 32, v6
	s_addc_u32 s25, s5, 0
	v_bfe_u32 v142, v2, 4, 2
	v_or3_b32 v3, v5, v7, v3
	v_ashrrev_i32_e32 v2, 3, v2
	s_add_u32 s4, s0, s14
	v_lshl_or_b32 v136, v3, 9, v4
	v_lshl_or_b32 v138, v2, 9, v4
	v_lshlrev_b32_e32 v3, 2, v2
	v_and_b32_e32 v5, 7, v2
	v_lshlrev_b32_e32 v6, 1, v2
	v_lshrrev_b32_e32 v2, 1, v2
	s_addc_u32 s5, s1, s15
	v_and_b32_e32 v6, 0x7fffc0, v6
	v_and_b32_e32 v2, 8, v2
	v_and_or_b32 v3, v3, 32, v5
	s_add_u32 s26, s4, 0x46c00000
	v_or3_b32 v2, v3, v6, v2
	s_addc_u32 s27, s5, 0
	s_add_i32 s28, s23, 0
	s_add_i32 s31, s41, s23
	v_add_u32_e32 v134, 0x10000, v132
	v_add_u32_e32 v130, 0x10000, v138
	v_lshl_or_b32 v140, v2, 9, v4
	v_mov_b32_e32 v137, v131
	v_mov_b32_e32 v139, v131
	v_mov_b32_e32 v133, v131
	s_mov_b64 s[8:9], 0
	s_mov_b64 s[4:5], -1
	s_mov_b64 s[6:7], 0
	v_add_u32_e32 v145, 0, v145
	v_add_u32_e32 v146, 0, v146
	s_add_i32 s29, s28, 0xc000
	s_add_i32 s30, s28, 0xe000
	s_add_i32 s33, s31, 0x2000
	s_add_i32 s34, s28, 0x2000
	v_mov_b64 v[90:91], 0
	v_mov_b64 v[92:93], 0
	v_mov_b64 v[94:95], 0
	v_mov_b64 v[96:97], 0
	v_mov_b64 v[66:67], 0
	v_mov_b64 v[68:69], 0
	v_mov_b64 v[70:71], 0
	v_mov_b64 v[72:73], 0
	v_mov_b64 v[42:43], 0
	v_mov_b64 v[44:45], 0
	v_mov_b64 v[46:47], 0
	v_mov_b64 v[48:49], 0
	v_mov_b64 v[18:19], 0
	v_mov_b64 v[20:21], 0
	v_mov_b64 v[30:31], 0
	v_mov_b64 v[32:33], 0
	v_mov_b64 v[122:123], 0
	v_mov_b64 v[124:125], 0
	v_mov_b64 v[126:127], 0
	v_mov_b64 v[128:129], 0
	v_mov_b64 v[114:115], 0
	v_mov_b64 v[116:117], 0
	v_mov_b64 v[118:119], 0
	v_mov_b64 v[120:121], 0
	v_mov_b64 v[98:99], 0
	v_mov_b64 v[100:101], 0
	v_mov_b64 v[102:103], 0
	v_mov_b64 v[104:105], 0
	v_mov_b64 v[74:75], 0
	v_mov_b64 v[76:77], 0
	v_mov_b64 v[78:79], 0
	v_mov_b64 v[80:81], 0
	v_mov_b64 v[50:51], 0
	v_mov_b64 v[52:53], 0
	v_mov_b64 v[62:63], 0
	v_mov_b64 v[64:65], 0
	v_mov_b64 v[26:27], 0
	v_mov_b64 v[28:29], 0
	v_mov_b64 v[38:39], 0
	v_mov_b64 v[40:41], 0
	v_mov_b64 v[10:11], 0
	v_mov_b64 v[12:13], 0
	v_mov_b64 v[14:15], 0
	v_mov_b64 v[16:17], 0
	v_mov_b64 v[2:3], 0
	v_mov_b64 v[4:5], 0
	v_mov_b64 v[6:7], 0
	v_mov_b64 v[8:9], 0
	v_mov_b64 v[106:107], 0
	v_mov_b64 v[108:109], 0
	v_mov_b64 v[110:111], 0
	v_mov_b64 v[112:113], 0
	v_mov_b64 v[82:83], 0
	v_mov_b64 v[84:85], 0
	v_mov_b64 v[86:87], 0
	v_mov_b64 v[88:89], 0
	v_mov_b64 v[54:55], 0
	v_mov_b64 v[56:57], 0
	v_mov_b64 v[58:59], 0
	v_mov_b64 v[60:61], 0
	v_mov_b64 v[22:23], 0
	v_mov_b64 v[24:25], 0
	v_mov_b64 v[34:35], 0
	v_mov_b64 v[36:37], 0

; __device__ __forceinline__ int otid() { int t = threadIdx.x; asm volatile("" : "+v"(t)); return t; }
; __device__ __forceinline__ unsigned xb_ld(unsigned* p)              { return __hip_atomic_load(p, __ATOMIC_RELAXED, __HIP_MEMORY_SCOPE_AGENT); }
; __device__ __forceinline__ void xcd_barrier_complete(unsigned* bar, unsigned x, unsigned& nloc, unsigned& nx) {
;     const unsigned G = gridDim.x * gridDim.y * gridDim.z;
;     unsigned sum, cnt, mine, sp = 0u;
;     for (;;) {
;         sum = 0u; cnt = 0u; mine = 0u;
; #pragma unroll
;         for (unsigned j = 0; j < 16; ++j) { const unsigned c = xb_ld(&bar[XB_XCNT(j)]); sum += c; cnt += (c > 0u) ? 1u : 0u; mine = (j == x) ? c : mine; }
;         if (sum == G) break;
;         __builtin_amdgcn_s_sleep(1);
;         if ((++sp & 255u) == 0u) { if (xb_ld(&bar[XB_TMO])) break; if (sp > XB_SPIN_CAP) { atomicAdd(&bar[XB_TMO], 1u); break; } }
;     }
;     nloc = mine > 0u ? mine : 1u; nx = cnt > 0u ? cnt : 1u;
; }
; __device__ __forceinline__ void xcd_barrier(const XcdBarrier& b) {
;     asm volatile("s_waitcnt vmcnt(0)" ::: "memory");
;     __syncthreads();
;     if (otid() == 0) {
;         unsigned* bar = b.bar;
;         __builtin_amdgcn_s_waitcnt(0);
;         unsigned nloc = b.st[0], nx = b.st[1];
;         if (nloc == 0u) { xcd_barrier_complete(bar, b.x, nloc, nx); b.st[0] = nloc; b.st[1] = nx; }
.LBB0_2079:
	s_mov_b64 s[0:1], s[24:25]
	s_mov_b32 s0, s100
	s_waitcnt lgkmcnt(0)
	s_cmp_gt_i32 s0, 14
	s_cbranch_scc1 .LBB0_2137
	s_mov_b64 s[0:1], s[24:25]
	s_mov_b32 s0, s101
	s_waitcnt lgkmcnt(0)
	s_cmp_lt_i32 s0, 15
	s_cbranch_scc1 .LBB0_2136
	v_readlane_b32 s0, v255, 0
	v_readlane_b32 s1, v255, 1
	s_mov_b32 s0, s100
	s_waitcnt lgkmcnt(0)
	s_cmp_gt_i32 s0, 15
	s_cbranch_scc1 .LBB0_2136
	v_readlane_b32 s0, v255, 0
	v_readlane_b32 s1, v255, 1
	s_mov_b32 s0, s101
	s_waitcnt lgkmcnt(0)
	s_cmp_lt_i32 s0, 16
	s_cbranch_scc1 .LBB0_2136
	v_readlane_b32 s2, v255, 0
	v_readlane_b32 s3, v255, 1
	s_getreg_b32 s4, hwreg(HW_REG_XCC_ID, 0, 4)
	s_waitcnt vmcnt(0)
	v_mov_b32_e32 v1, v0
	s_waitcnt vmcnt(0)
	s_barrier
	s_nop 0
	v_cmp_eq_u32_e32 vcc, 0, v1
	s_and_saveexec_b64 s[0:1], vcc
	s_cbranch_execz .LBB0_2135
	s_add_i32 s5, 0, 0x20020
	v_mov_b32_e32 v1, s5
	s_mov_b64 s[2:3], s[98:99]
	s_waitcnt vmcnt(0) expcnt(0) lgkmcnt(0)
	ds_read_b32 v3, v1
	s_add_i32 s5, 0, 0x20024
	v_mov_b32_e32 v1, s5
	ds_read_b32 v1, v1
	s_and_b32 s33, s4, 15
	s_waitcnt lgkmcnt(1)
	v_cmp_ne_u32_e32 vcc, 0, v3
	s_cbranch_vccnz .LBB0_2099
	v_readlane_b32 s4, v255, 0
	v_readlane_b32 s5, v255, 1
	s_load_dwordx2 s[8:9], s[4:5], 0xe0
	s_load_dword s7, s[4:5], 0xe8
	s_add_u32 s4, s2, 0x4200
	s_addc_u32 s5, s3, 0
	s_add_u32 s6, s2, 0x4400
	s_waitcnt lgkmcnt(0)
	s_mul_i32 s46, s9, s8
	s_mul_i32 s46, s46, s7
	s_addc_u32 s7, s3, 0
	s_add_u32 s8, s2, 0x4500
	s_addc_u32 s9, s3, 0
	s_add_u32 s10, s2, 0x4600
	s_addc_u32 s11, s3, 0
	s_add_u32 s12, s2, 0x4700
	s_addc_u32 s13, s3, 0
	s_add_u32 s14, s2, 0x4800
	s_addc_u32 s15, s3, 0
	s_add_u32 s16, s2, 0x4900
	s_addc_u32 s17, s3, 0
	s_add_u32 s18, s2, 0x4a00
	s_addc_u32 s19, s3, 0
	s_add_u32 s20, s2, 0x4b00
	s_addc_u32 s21, s3, 0
	s_add_u32 s22, s2, 0x4c00
	s_addc_u32 s23, s3, 0
	s_add_u32 s24, s2, 0x4d00
	s_addc_u32 s25, s3, 0
	s_add_u32 s26, s2, 0x4e00
	s_addc_u32 s27, s3, 0
	s_add_u32 s28, s2, 0x4f00
	s_addc_u32 s29, s3, 0
	s_add_u32 s30, s2, 0x5000
	s_addc_u32 s31, s3, 0
	s_add_u32 s34, s2, 0x5100
	s_addc_u32 s35, s3, 0
	s_add_u32 s36, s2, 0x5200
	s_addc_u32 s37, s3, 0
	s_add_u32 s38, s2, 0x5300
	s_addc_u32 s39, s3, 0
	s_mov_b32 s47, 1
	v_mov_b32_e32 v17, 0
	s_branch .LBB0_2087

; __device__ __forceinline__ void attn_unit(const unsigned char* __restrict__ CQt, const unsigned char* __restrict__ Wh, const f32x2* __restrict__ cst, const unsigned char* __restrict__ Kh, const unsigned char* __restrict__ Vh, bf16* __restrict__ Ob, char* lds) {
;   int tid = threadIdx.x; asm volatile("" : "+v"(tid));
;   const int wid = __builtin_amdgcn_readfirstlane(tid >> 6), lane = tid & 63, r32 = lane & 31, hi = lane >> 5;
;     ...
;   constexpr int WIMG = 32 * 1024;
;   float* wsp = (float*)(lds + 60 * 1024) + wid * 64; float* li_l = wsp; float* al_l = wsp + 32;
;   float m_reg = 0.f, l_reg = 0; f32x16 o[4] = {}; v8i qr[3]; f32x16 nm16 = {};
;   int koff[2], voff[2];
; #pragma unroll
;   for (int i = 0; i < 2; ++i) { const int m = (i * 8 + wid) * 64 + lane, row = m / 12, cp = m % 12; const int c = (cp & ~3) | ((cp & 3) ^ ((row >> 2) & 3)); koff[i] = row * DQK + c * 16; }
;   { const int m = wid * 64 + lane, d = m >> 2, cp = m & 3; voff[0] = d * SEQ + ((cp ^ ((d >> 2) & 3)) << 4); voff[1] = 0; }
; __device__ __forceinline__ void attn_phase(CArgs& A, unsigned char* lds, int l) {
;     constexpr int G = 256;
;     const unsigned char* Kb = A.ws + WS_K; const unsigned char* Vb = A.ws + WS_V; bf16* O = (bf16*)(A.ws + WS_O);
;     constexpr int NQB = SEQ / 256, NU = NB * NH * NQB;
;     const int c = blockIdx.x;
;     for (int i = 0; i * G < NU; ++i) {
;         int L;
;         { const int x = c & 7, j = c >> 3; L = (i * 16 + x * 2 + (j >> 4)) * NQB + (j & 15); }
;         if (L >= NU) break;
;         const int bh = L / NQB, qb = L % NQB, b = bh / NH, h = bh % NH;
;         att::attn_unit(A.ws + WS_CQN + ((size_t)b * SEQ + qb * 256) * QL, A.ws + WS_WUQ + ((size_t)l * NH * DQK + (size_t)h * DQK) * QL, (const f32x2*)(A.ws + WS_CS) + ((size_t)b * SEQ + qb * 256) * 32, Kb + (size_t)bh * SEQ * DQK, Vb + (size_t)bh * SEQ * DV, FP8_WO ? (bf16*)((unsigned char*)(A.ws + WS_O8) + ((size_t)b * SEQ + qb * 256) * DM + h * DV) : O + ((size_t)b * SEQ + qb * 256) * DM + h * DV, (char*)lds);
.LBB0_2137:
	s_mov_b64 s[0:1], s[24:25]
	s_mov_b32 s0, s100
	s_waitcnt lgkmcnt(0)
	s_cmp_gt_i32 s0, 15
	s_cbranch_scc1 .LBB0_2353
	s_mov_b64 s[0:1], s[24:25]
	s_mov_b32 s0, s101
	s_waitcnt lgkmcnt(0)
	s_cmp_lt_i32 s0, 16
	s_cbranch_scc1 .LBB0_2353
	s_lshl_b32 s0, s95, 1
	s_and_b32 s2, s0, 14
	s_mov_b64 s[0:1], s[24:25]
	s_mov_b64 s[6:7], s[98:99]
	s_ashr_i32 s3, s95, 7
	s_add_i32 s2, s2, s3
	s_bfe_u32 s0, s95, 0x40003
	s_lshl_b32 s1, s2, 4
	s_or_b32 s68, s1, s0
	s_waitcnt lgkmcnt(0)
	s_add_u32 s69, s6, 0x4b000000
	s_addc_u32 s70, s7, 0
	s_add_u32 s71, s6, 0x4e000000
	s_addc_u32 s72, s7, 0
	s_add_u32 s73, s6, 0x46400000
	s_addc_u32 s74, s7, 0
	s_add_u32 s75, s6, 0x4400000
	s_addc_u32 s76, s7, 0
	s_add_u32 s77, s6, 0x200000
	s_addc_u32 s78, s7, 0
	s_add_u32 s79, s6, 0x35400000
	v_mbcnt_lo_u32_b32 v1, -1, 0
	s_addc_u32 s80, s7, 0
	s_mov_b32 s9, 0
	s_mov_b64 s[28:29], 0
	s_movk_i32 s81, 0xc0
	s_movk_i32 s82, 0xffc0
	s_mov_b32 s83, 0x2aaaaaab
	v_mov_b32_e32 v163, 0
	s_movk_i32 s84, 0xf000
	s_mov_b64 s[24:25], 0x4b006000
	s_mov_b64 s[26:27], 0x4e000080
	s_mov_b32 s85, 0x40e6d4ca
	s_mov_b64 s[30:31], 0x4b009000
	s_mov_b64 s[34:35], 0x4e0000c0
	s_mov_b64 s[36:37], 0x4b00c000
	s_mov_b64 s[38:39], 0x4e000100
	s_mov_b64 s[40:41], 0x4b00f000
	s_mov_b64 s[42:43], 0x4e000140
	s_mov_b64 s[44:45], 0x4b012000
	s_mov_b64 s[46:47], 0x4e000180
	s_mov_b64 s[48:49], 0x4b015000
	s_mov_b64 s[50:51], 0x4e0001c0
	s_mov_b64 s[52:53], 0x180
	s_mov_b64 s[54:55], 0x12000
	s_mov_b64 s[56:57], 0xf80
	s_mov_b64 s[58:59], 0xfc0
	v_mbcnt_hi_u32_b32 v1, -1, v1
	v_mov_b32_e32 v254, 0x1000
	v_mov_b32_e32 v186, 0x9000
	v_mov_b32_e32 v187, 0xc000
	v_mov_b32_e32 v188, 0xd000
	s_mov_b32 s2, 0
	s_branch .LBB0_2142

; __device__ __forceinline__ int otid() { int t = threadIdx.x; asm volatile("" : "+v"(t)); return t; }
; __device__ __forceinline__ unsigned xb_ld(unsigned* p)              { return __hip_atomic_load(p, __ATOMIC_RELAXED, __HIP_MEMORY_SCOPE_AGENT); }
; __device__ __forceinline__ void xcd_barrier_complete(unsigned* bar, unsigned x, unsigned& nloc, unsigned& nx) {
;     const unsigned G = gridDim.x * gridDim.y * gridDim.z;
;     unsigned sum, cnt, mine, sp = 0u;
;     for (;;) {
;         sum = 0u; cnt = 0u; mine = 0u;
; #pragma unroll
;         for (unsigned j = 0; j < 16; ++j) { const unsigned c = xb_ld(&bar[XB_XCNT(j)]); sum += c; cnt += (c > 0u) ? 1u : 0u; mine = (j == x) ? c : mine; }
;         if (sum == G) break;
;         __builtin_amdgcn_s_sleep(1);
;         if ((++sp & 255u) == 0u) { if (xb_ld(&bar[XB_TMO])) break; if (sp > XB_SPIN_CAP) { atomicAdd(&bar[XB_TMO], 1u); break; } }
;     }
;     nloc = mine > 0u ? mine : 1u; nx = cnt > 0u ? cnt : 1u;
; }
; __device__ __forceinline__ void xcd_barrier(const XcdBarrier& b) {
;     asm volatile("s_waitcnt vmcnt(0)" ::: "memory");
;     __syncthreads();
;     if (otid() == 0) {
;         unsigned* bar = b.bar;
;         __builtin_amdgcn_s_waitcnt(0);
;         unsigned nloc = b.st[0], nx = b.st[1];
;         if (nloc == 0u) { xcd_barrier_complete(bar, b.x, nloc, nx); b.st[0] = nloc; b.st[1] = nx; }
.LBB0_2353:
	s_mov_b64 s[0:1], s[24:25]
	s_mov_b32 s0, s100
	s_waitcnt lgkmcnt(0)
	s_cmp_gt_i32 s0, 15
	s_cbranch_scc1 .LBB0_2411
	s_mov_b64 s[0:1], s[24:25]
	s_mov_b32 s0, s101
	s_waitcnt lgkmcnt(0)
	s_cmp_lt_i32 s0, 16
	s_cbranch_scc1 .LBB0_2410
	v_readlane_b32 s0, v255, 0
	v_readlane_b32 s1, v255, 1
	s_mov_b32 s0, s100
	s_waitcnt lgkmcnt(0)
	s_cmp_gt_i32 s0, 16
	s_cbranch_scc1 .LBB0_2410
	v_readlane_b32 s0, v255, 0
	v_readlane_b32 s1, v255, 1
	s_mov_b32 s0, s101
	s_waitcnt lgkmcnt(0)
	s_cmp_lt_i32 s0, 17
	s_cbranch_scc1 .LBB0_2410
	v_readlane_b32 s2, v255, 0
	v_readlane_b32 s3, v255, 1
	s_getreg_b32 s4, hwreg(HW_REG_XCC_ID, 0, 4)
	s_waitcnt vmcnt(0)
	v_mov_b32_e32 v1, v0
	s_waitcnt vmcnt(0)
	s_barrier
	s_nop 0
	v_cmp_eq_u32_e32 vcc, 0, v1
	s_and_saveexec_b64 s[0:1], vcc
	s_cbranch_execz .LBB0_2409
	s_add_i32 s5, 0, 0x20020
	v_mov_b32_e32 v1, s5
	s_mov_b64 s[2:3], s[98:99]
	s_waitcnt vmcnt(0) expcnt(0) lgkmcnt(0)
	ds_read_b32 v3, v1
	s_add_i32 s5, 0, 0x20024
	v_mov_b32_e32 v1, s5
	ds_read_b32 v1, v1
	s_and_b32 s33, s4, 15
	s_waitcnt lgkmcnt(1)
	v_cmp_ne_u32_e32 vcc, 0, v3
	s_cbranch_vccnz .LBB0_2373
	v_readlane_b32 s4, v255, 0
	v_readlane_b32 s5, v255, 1
	s_load_dwordx2 s[8:9], s[4:5], 0xe0
	s_load_dword s7, s[4:5], 0xe8
	s_add_u32 s4, s2, 0x4200
	s_addc_u32 s5, s3, 0
	s_add_u32 s6, s2, 0x4400
	s_waitcnt lgkmcnt(0)
	s_mul_i32 s46, s9, s8
	s_mul_i32 s46, s46, s7
	s_addc_u32 s7, s3, 0
	s_add_u32 s8, s2, 0x4500
	s_addc_u32 s9, s3, 0
	s_add_u32 s10, s2, 0x4600
	s_addc_u32 s11, s3, 0
	s_add_u32 s12, s2, 0x4700
	s_addc_u32 s13, s3, 0
	s_add_u32 s14, s2, 0x4800
	s_addc_u32 s15, s3, 0
	s_add_u32 s16, s2, 0x4900
	s_addc_u32 s17, s3, 0
	s_add_u32 s18, s2, 0x4a00
	s_addc_u32 s19, s3, 0
	s_add_u32 s20, s2, 0x4b00
	s_addc_u32 s21, s3, 0
	s_add_u32 s22, s2, 0x4c00
	s_addc_u32 s23, s3, 0
	s_add_u32 s24, s2, 0x4d00
	s_addc_u32 s25, s3, 0
	s_add_u32 s26, s2, 0x4e00
	s_addc_u32 s27, s3, 0
	s_add_u32 s28, s2, 0x4f00
	s_addc_u32 s29, s3, 0
	s_add_u32 s30, s2, 0x5000
	s_addc_u32 s31, s3, 0
	s_add_u32 s34, s2, 0x5100
	s_addc_u32 s35, s3, 0
	s_add_u32 s36, s2, 0x5200
	s_addc_u32 s37, s3, 0
	s_add_u32 s38, s2, 0x5300
	s_addc_u32 s39, s3, 0
	s_mov_b32 s47, 1
	v_mov_b32_e32 v17, 0
	s_branch .LBB0_2361

; template <class P, class MK = NoChain>
; __device__ __forceinline__ void gemm_phase(LAS unsigned char* lds, const P& p, const MK& mk = MK(), bool chain_out = false, bool chained_in = false) {
;     ...
;     int tid = threadIdx.x; asm volatile("" : "+v"(tid));
;     const int wid = __builtin_amdgcn_readfirstlane(tid >> 6), lane = tid & 63, wr = wid >> 2, wc = wid & 3, fr = lane & 15, fq = lane >> 4;
;     unsigned voffB[2], vA[2][2], nvA[2][2], nvB[2]; typedef decltype(mk()) NP; constexpr int NES = NP::FP8 ? 1 : 2; constexpr int NBMODE = bmode_of<NP>::value; constexpr size_t nhstepB = (size_t)(NBMODE == 1 ? 8 : (NBMODE == 2 ? 16 : HALF)) * NP::LDB * NES;
;     constexpr size_t kstep = (size_t)(BK * 2);
;     constexpr int BMODE = bmode_of<P>::value;
;     constexpr size_t hstep = (size_t)(BMODE == 1 ? 8 : (BMODE == 2 ? 16 : HALF)) * LDB * ES, hstepA = (size_t)HALF * LDA * ES;
; #pragma unroll
;     for (int i = 0; i < 2; ++i) { int R, C; stage_rc(tid * 16 + i * 8192, R, C); const int rho_ = R & 31;
;         const int fq_ = (rho_ & 15) >> 2, n_ = rho_ >> 4, q_ = rho_ & 3;
;         const int Rb = BMODE == 1 ? ((R >> 5) * 64 + fq_ * 16 + 4 * n_ + q_) : (BMODE == 2 ? ((R >> 5) * 64 + 32 * (fq_ >> 1) + 8 * n_ + 4 * (fq_ & 1) + q_) : (P::PERM ? ((R & ~31) + perm32(R & 31)) : R));
;         voffB[i] = (unsigned)(Rb * LDB * ES + C * 2); vA[0][i] = (unsigned)(R * LDA * ES + C * 2); vA[1][i] = vA[0][i] + (unsigned)hstepA; nvA[0][i] = vA[0][i]; nvA[1][i] = vA[1][i]; nvB[i] = voffB[i]; }
;     const unsigned ldsw = (unsigned)wid * 1024u;
;     const int aoff = lds_byte(wr * 64 + fr, fq * 8), boff = lds_byte(wc * 32 + fr, fq * 8); const int aoff1 = aoff ^ 64, boff1 = boff ^ 64;
;     ...
;     Unit cur, nxt; int ui = 0;
;     if (!p.next(0, cur)) return;
;     Acc acc;
;     if constexpr (!PEEL) {
; #pragma unroll
;     for (int a = 0; a < 2; ++a)
; #pragma unroll
;         for (int b = 0; b < 2; ++b)
; #pragma unroll
;             for (int m = 0; m < 4; ++m)
; #pragma unroll
;                 for (int n = 0; n < 2; ++n) { typedef double d2_ __attribute__((ext_vector_type(2))); d2_ z_; asm volatile("v_mov_b64 %0, 0" : "=v"(z_.x)); asm volatile("v_mov_b64 %0, 0" : "=v"(z_.y)); acc[a][b][m][n] = __builtin_bit_cast(f32x4, z_); }
;     }
;     typedef int v8i_ __attribute__((ext_vector_type(8))); typedef int v4i_ __attribute__((ext_vector_type(4)));
.LBB0_2411:
	s_mov_b64 s[0:1], s[24:25]
	s_mov_b32 s0, s100
	s_waitcnt lgkmcnt(0)
	s_cmp_gt_i32 s0, 16
	s_cbranch_scc1 .LBB0_2449
	s_mov_b64 s[0:1], s[24:25]
	s_mov_b32 s0, s101
	s_waitcnt lgkmcnt(0)
	s_cmp_lt_i32 s0, 17
	s_cbranch_scc1 .LBB0_2449
	s_cmpk_lt_i32 s95, 0x100
	s_mov_b64 s[0:1], s[24:25]
	v_mov_b32_e32 v2, v0
	s_cselect_b64 s[2:3], -1, 0
	s_cmpk_gt_i32 s95, 0xff
	s_nop 0
	v_readfirstlane_b32 s17, v2
	s_cbranch_scc1 .LBB0_2415
	v_readlane_b32 s4, v255, 4
	s_and_b32 s4, s4, -8
	s_sub_i32 s4, s95, s4
	s_lshl_b32 s6, s4, 5
	s_mul_i32 s5, s4, 33
	s_cmp_lt_i32 s4, 0
	s_cselect_b32 s4, s5, s6
	s_add_i32 s4, s4, s96
	s_ashr_i32 s5, s4, 31
	s_lshr_b32 s5, s5, 26
	s_add_i32 s5, s4, s5
	s_ashr_i32 s6, s5, 6
	s_andn2_b32 s5, s5, 63
	s_sub_i32 s4, s4, s5
	s_bfe_i32 s5, s4, 0x80000
	s_bfe_u32 s5, s5, 0x3000c
	s_add_i32 s5, s4, s5
	s_bfe_i32 s7, s5, 0x80000
	s_and_b32 s5, s5, 0xf8
	s_sub_i32 s4, s4, s5
	s_lshl_b32 s6, s6, 3
	s_sext_i32_i16 s7, s7
	s_sext_i32_i8 s4, s4
	s_add_i32 s33, s6, s4
	s_ashr_i32 s22, s7, 3
.LBB0_2415:
	v_readlane_b32 s24, v255, 0
	s_andn2_b64 vcc, exec, s[2:3]
	v_readlane_b32 s25, v255, 1
	s_cbranch_vccnz .LBB0_2449
	v_lshrrev_b32_e32 v3, 4, v2
	v_ashrrev_i32_e32 v4, 3, v2
	s_mov_b64 s[2:3], s[98:99]
	v_xor_b32_e32 v1, v3, v2
	v_lshlrev_b32_e32 v5, 1, v4
	v_lshrrev_b32_e32 v6, 2, v4
	v_lshlrev_b32_e32 v1, 4, v1
	v_and_b32_e32 v5, 24, v5
	v_and_b32_e32 v6, 4, v6
	v_and_b32_e32 v7, 0x1fffe3, v4
	v_and_b32_e32 v1, 0x70, v1
	v_or3_b32 v5, v7, v6, v5
	v_lshl_or_b32 v194, v5, 11, v1
	v_mov_b32_e32 v5, 0x2000
	v_lshl_add_u32 v5, v2, 4, v5
	s_waitcnt lgkmcnt(0)
	s_add_u32 s0, s2, 0x35400000
	v_ashrrev_i32_e32 v5, 7, v5
	s_addc_u32 s1, s3, 0
	v_lshlrev_b32_e32 v6, 1, v5
	v_lshrrev_b32_e32 v7, 2, v5
	s_add_u32 s36, s2, 0x34800000
	v_and_b32_e32 v6, 24, v6
	v_and_b32_e32 v7, 4, v7
	v_and_b32_e32 v8, 0x1fffe3, v5
	s_addc_u32 s37, s3, 0
	v_or3_b32 v6, v8, v7, v6
	s_ashr_i32 s12, s17, 6
	s_ashr_i32 s23, s22, 31
	s_ashr_i32 s4, s17, 8
	v_lshl_or_b32 v196, v6, 11, v1
	s_lshl_b32 s39, s12, 10
	s_lshl_b64 s[6:7], s[22:23], 19
	v_mov_b32_e32 v6, v0
	v_mov_b64 v[186:187], 0
	v_mov_b64 v[188:189], 0
	v_mov_b64 v[182:183], 0
	v_mov_b64 v[184:185], 0
	v_mov_b64 v[170:171], 0
	v_mov_b64 v[172:173], 0
	v_mov_b64 v[162:163], 0
	v_mov_b64 v[164:165], 0
	v_mov_b64 v[154:155], 0
	v_mov_b64 v[156:157], 0
	v_mov_b64 v[146:147], 0
	v_mov_b64 v[148:149], 0
	v_mov_b64 v[138:139], 0
	v_mov_b64 v[140:141], 0
	v_mov_b64 v[130:131], 0
	v_mov_b64 v[132:133], 0
	v_mov_b64 v[190:191], 0
	v_mov_b64 v[192:193], 0
	v_mov_b64 v[178:179], 0
	v_mov_b64 v[180:181], 0
	v_mov_b64 v[174:175], 0
	v_mov_b64 v[176:177], 0
	v_mov_b64 v[166:167], 0
	v_mov_b64 v[168:169], 0
	v_mov_b64 v[158:159], 0
	v_mov_b64 v[160:161], 0
	v_mov_b64 v[150:151], 0
	v_mov_b64 v[152:153], 0
	v_mov_b64 v[142:143], 0
	v_mov_b64 v[144:145], 0
	v_mov_b64 v[134:135], 0
	v_mov_b64 v[136:137], 0
	v_mov_b64 v[122:123], 0
	v_mov_b64 v[124:125], 0
	v_mov_b64 v[114:115], 0
	v_mov_b64 v[116:117], 0
	v_mov_b64 v[106:107], 0
	v_mov_b64 v[108:109], 0
	v_mov_b64 v[98:99], 0
	v_mov_b64 v[100:101], 0
	v_mov_b64 v[90:91], 0
	v_mov_b64 v[92:93], 0
	v_mov_b64 v[82:83], 0
	v_mov_b64 v[84:85], 0
	v_mov_b64 v[74:75], 0
	v_mov_b64 v[76:77], 0
	v_mov_b64 v[66:67], 0
	v_mov_b64 v[68:69], 0
	v_mov_b64 v[126:127], 0
	v_mov_b64 v[128:129], 0
	v_mov_b64 v[118:119], 0
	v_mov_b64 v[120:121], 0
	v_mov_b64 v[110:111], 0
	v_mov_b64 v[112:113], 0
	v_mov_b64 v[102:103], 0
	v_mov_b64 v[104:105], 0
	v_mov_b64 v[94:95], 0
	v_mov_b64 v[96:97], 0
	v_mov_b64 v[86:87], 0
	v_mov_b64 v[88:89], 0
	v_mov_b64 v[78:79], 0
	v_mov_b64 v[80:81], 0
	v_mov_b64 v[70:71], 0
	v_mov_b64 v[72:73], 0
	s_add_u32 s24, s36, s6
	s_addc_u32 s25, s37, s7
	v_lshlrev_b32_e32 v7, 4, v6
	v_xor_b32_e32 v7, v7, v6
	v_lshlrev_b32_e32 v6, 8, v6
	s_add_i32 s23, s39, 0
	v_and_b32_e32 v6, 0xfffff800, v6
	s_mov_b64 s[6:7], s[24:25]
	s_add_i32 m0, s23, 0x10000
	s_movk_i32 s38, 0x70
	v_lshl_add_u32 v6, s33, 19, v6
	v_and_or_b32 v198, v7, s38, v6
	global_load_lds_dwordx4 v194, s[6:7]
	s_add_i32 m0, s23, 0x12000
	s_add_i32 s40, s23, 0x2000
	global_load_lds_dwordx4 v196, s[6:7]
	s_mov_b64 s[6:7], s[0:1]
	s_mov_b32 m0, s23
	v_add_u32_e32 v206, 0x20000, v198
	v_add_u32_e32 v210, 0x40000, v198
	global_load_lds_dwordx4 v198, s[6:7]
	s_mov_b32 m0, s40
	v_add_u32_e32 v208, 0x60000, v198
	global_load_lds_dwordx4 v206, s[6:7]
	s_add_u32 s6, s24, 0x40000
	s_addc_u32 s7, s25, 0
	s_add_i32 s41, s23, 0x14000
	s_mov_b32 m0, s41
	s_add_i32 s42, s23, 0x16000
	s_add_i32 s43, s23, 0x4000
	global_load_lds_dwordx4 v194, s[6:7]
	s_mov_b32 m0, s42
	s_add_i32 s44, s23, 0x6000
	global_load_lds_dwordx4 v196, s[6:7]
	s_mov_b64 s[6:7], s[0:1]
	s_mov_b32 m0, s43
	v_mov_b32_e32 v199, 0
	global_load_lds_dwordx4 v210, s[6:7]
	s_mov_b32 m0, s44
	s_mov_b32 s5, 0
	global_load_lds_dwordx4 v208, s[6:7]
	v_mov_b32_e32 v195, v199
	v_mov_b32_e32 v197, v199
	s_cmp_lg_u32 s4, 1
	v_mov_b32_e32 v207, v199
	s_cbranch_scc1 .LBB0_2418
	s_barrier

; __device__ __forceinline__ int otid() { int t = threadIdx.x; asm volatile("" : "+v"(t)); return t; }
; __device__ __forceinline__ unsigned xb_ld(unsigned* p)              { return __hip_atomic_load(p, __ATOMIC_RELAXED, __HIP_MEMORY_SCOPE_AGENT); }
; __device__ __forceinline__ void xcd_barrier_complete(unsigned* bar, unsigned x, unsigned& nloc, unsigned& nx) {
;     const unsigned G = gridDim.x * gridDim.y * gridDim.z;
;     unsigned sum, cnt, mine, sp = 0u;
;     for (;;) {
;         sum = 0u; cnt = 0u; mine = 0u;
; #pragma unroll
;         for (unsigned j = 0; j < 16; ++j) { const unsigned c = xb_ld(&bar[XB_XCNT(j)]); sum += c; cnt += (c > 0u) ? 1u : 0u; mine = (j == x) ? c : mine; }
;         if (sum == G) break;
;         __builtin_amdgcn_s_sleep(1);
;         if ((++sp & 255u) == 0u) { if (xb_ld(&bar[XB_TMO])) break; if (sp > XB_SPIN_CAP) { atomicAdd(&bar[XB_TMO], 1u); break; } }
;     }
;     nloc = mine > 0u ? mine : 1u; nx = cnt > 0u ? cnt : 1u;
; }
; __device__ __forceinline__ void xcd_barrier(const XcdBarrier& b) {
;     asm volatile("s_waitcnt vmcnt(0)" ::: "memory");
;     __syncthreads();
;     if (otid() == 0) {
;         unsigned* bar = b.bar;
;         __builtin_amdgcn_s_waitcnt(0);
;         unsigned nloc = b.st[0], nx = b.st[1];
;         if (nloc == 0u) { xcd_barrier_complete(bar, b.x, nloc, nx); b.st[0] = nloc; b.st[1] = nx; }
.LBB0_2449:
	s_mov_b64 s[0:1], s[24:25]
	s_mov_b32 s0, s100
	s_waitcnt lgkmcnt(0)
	s_cmp_gt_i32 s0, 16
	s_cbranch_scc1 .LBB0_2507
	s_mov_b64 s[0:1], s[24:25]
	s_mov_b32 s0, s101
	s_waitcnt lgkmcnt(0)
	s_cmp_lt_i32 s0, 17
	s_cbranch_scc1 .LBB0_2506
	v_readlane_b32 s0, v255, 0
	v_readlane_b32 s1, v255, 1
	s_mov_b32 s0, s100
	s_waitcnt lgkmcnt(0)
	s_cmp_gt_i32 s0, 17
	s_cbranch_scc1 .LBB0_2506
	v_readlane_b32 s0, v255, 0
	v_readlane_b32 s1, v255, 1
	s_mov_b32 s0, s101
	s_waitcnt lgkmcnt(0)
	s_cmp_lt_i32 s0, 18
	s_cbranch_scc1 .LBB0_2506
	v_readlane_b32 s2, v255, 0
	v_readlane_b32 s3, v255, 1
	s_getreg_b32 s4, hwreg(HW_REG_XCC_ID, 0, 4)
	s_waitcnt vmcnt(0)
	v_mov_b32_e32 v1, v0
	s_waitcnt vmcnt(0)
	s_barrier
	s_nop 0
	v_cmp_eq_u32_e32 vcc, 0, v1
	s_and_saveexec_b64 s[0:1], vcc
	s_cbranch_execz .LBB0_2505
	s_add_i32 s5, 0, 0x20020
	v_mov_b32_e32 v1, s5
	s_mov_b64 s[2:3], s[98:99]
	s_waitcnt vmcnt(0) expcnt(0) lgkmcnt(0)
	ds_read_b32 v3, v1
	s_add_i32 s5, 0, 0x20024
	v_mov_b32_e32 v1, s5
	ds_read_b32 v1, v1
	s_and_b32 s33, s4, 15
	s_waitcnt lgkmcnt(1)
	v_cmp_ne_u32_e32 vcc, 0, v3
	s_cbranch_vccnz .LBB0_2469
	v_readlane_b32 s4, v255, 0
	v_readlane_b32 s5, v255, 1
	s_load_dwordx2 s[8:9], s[4:5], 0xe0
	s_load_dword s7, s[4:5], 0xe8
	s_add_u32 s4, s2, 0x4200
	s_addc_u32 s5, s3, 0
	s_add_u32 s6, s2, 0x4400
	s_waitcnt lgkmcnt(0)
	s_mul_i32 s46, s9, s8
	s_mul_i32 s46, s46, s7
	s_addc_u32 s7, s3, 0
	s_add_u32 s8, s2, 0x4500
	s_addc_u32 s9, s3, 0
	s_add_u32 s10, s2, 0x4600
	s_addc_u32 s11, s3, 0
	s_add_u32 s12, s2, 0x4700
	s_addc_u32 s13, s3, 0
	s_add_u32 s14, s2, 0x4800
	s_addc_u32 s15, s3, 0
	s_add_u32 s16, s2, 0x4900
	s_addc_u32 s17, s3, 0
	s_add_u32 s18, s2, 0x4a00
	s_addc_u32 s19, s3, 0
	s_add_u32 s20, s2, 0x4b00
	s_addc_u32 s21, s3, 0
	s_add_u32 s22, s2, 0x4c00
	s_addc_u32 s23, s3, 0
	s_add_u32 s24, s2, 0x4d00
	s_addc_u32 s25, s3, 0
	s_add_u32 s26, s2, 0x4e00
	s_addc_u32 s27, s3, 0
	s_add_u32 s28, s2, 0x4f00
	s_addc_u32 s29, s3, 0
	s_add_u32 s30, s2, 0x5000
	s_addc_u32 s31, s3, 0
	s_add_u32 s34, s2, 0x5100
	s_addc_u32 s35, s3, 0
	s_add_u32 s36, s2, 0x5200
	s_addc_u32 s37, s3, 0
	s_add_u32 s38, s2, 0x5300
	s_addc_u32 s39, s3, 0
	s_mov_b32 s47, 1
	v_mov_b32_e32 v17, 0
	s_branch .LBB0_2457

; template <class P, class MK = NoChain>
; __device__ __forceinline__ void gemm_phase(LAS unsigned char* lds, const P& p, const MK& mk = MK(), bool chain_out = false, bool chained_in = false) {
;     ...
;     int tid = threadIdx.x; asm volatile("" : "+v"(tid));
;     const int wid = __builtin_amdgcn_readfirstlane(tid >> 6), lane = tid & 63, wr = wid >> 2, wc = wid & 3, fr = lane & 15, fq = lane >> 4;
;     unsigned voffB[2], vA[2][2], nvA[2][2], nvB[2]; typedef decltype(mk()) NP; constexpr int NES = NP::FP8 ? 1 : 2; constexpr int NBMODE = bmode_of<NP>::value; constexpr size_t nhstepB = (size_t)(NBMODE == 1 ? 8 : (NBMODE == 2 ? 16 : HALF)) * NP::LDB * NES;
;     constexpr size_t kstep = (size_t)(BK * 2);
;     constexpr int BMODE = bmode_of<P>::value;
;     constexpr size_t hstep = (size_t)(BMODE == 1 ? 8 : (BMODE == 2 ? 16 : HALF)) * LDB * ES, hstepA = (size_t)HALF * LDA * ES;
; #pragma unroll
;     for (int i = 0; i < 2; ++i) { int R, C; stage_rc(tid * 16 + i * 8192, R, C); const int rho_ = R & 31;
;         const int fq_ = (rho_ & 15) >> 2, n_ = rho_ >> 4, q_ = rho_ & 3;
;         const int Rb = BMODE == 1 ? ((R >> 5) * 64 + fq_ * 16 + 4 * n_ + q_) : (BMODE == 2 ? ((R >> 5) * 64 + 32 * (fq_ >> 1) + 8 * n_ + 4 * (fq_ & 1) + q_) : (P::PERM ? ((R & ~31) + perm32(R & 31)) : R));
;         voffB[i] = (unsigned)(Rb * LDB * ES + C * 2); vA[0][i] = (unsigned)(R * LDA * ES + C * 2); vA[1][i] = vA[0][i] + (unsigned)hstepA; nvA[0][i] = vA[0][i]; nvA[1][i] = vA[1][i]; nvB[i] = voffB[i]; }
;     const unsigned ldsw = (unsigned)wid * 1024u;
;     const int aoff = lds_byte(wr * 64 + fr, fq * 8), boff = lds_byte(wc * 32 + fr, fq * 8); const int aoff1 = aoff ^ 64, boff1 = boff ^ 64;
;     ...
;     Unit cur, nxt; int ui = 0;
;     if (!p.next(0, cur)) return;
;     Acc acc;
;     if constexpr (!PEEL) {
; #pragma unroll
;     for (int a = 0; a < 2; ++a)
; #pragma unroll
;         for (int b = 0; b < 2; ++b)
; #pragma unroll
;             for (int m = 0; m < 4; ++m)
; #pragma unroll
;                 for (int n = 0; n < 2; ++n) { typedef double d2_ __attribute__((ext_vector_type(2))); d2_ z_; asm volatile("v_mov_b64 %0, 0" : "=v"(z_.x)); asm volatile("v_mov_b64 %0, 0" : "=v"(z_.y)); acc[a][b][m][n] = __builtin_bit_cast(f32x4, z_); }
;     }
;     typedef int v8i_ __attribute__((ext_vector_type(8))); typedef int v4i_ __attribute__((ext_vector_type(4)));
.LBB0_2507:
	s_mov_b64 s[0:1], s[24:25]
	s_mov_b32 s0, s100
	s_waitcnt lgkmcnt(0)
	s_cmp_gt_i32 s0, 17
	s_cbranch_scc1 .LBB0_2545
	s_mov_b64 s[0:1], s[24:25]
	s_mov_b32 s0, s101
	s_waitcnt lgkmcnt(0)
	s_cmp_lt_i32 s0, 18
	s_cbranch_scc1 .LBB0_2545
	s_cmpk_lt_i32 s95, 0x100
	s_mov_b64 s[0:1], s[24:25]
	v_mov_b32_e32 v2, v0
	s_cselect_b64 s[2:3], -1, 0
	s_cmpk_gt_i32 s95, 0xff
	s_nop 0
	v_readfirstlane_b32 s13, v2
	s_cbranch_scc1 .LBB0_2511
	s_lshl_b32 s4, s96, 3
	s_sub_i32 s4, s95, s4
	s_lshl_b32 s6, s4, 5
	s_mul_i32 s5, s4, 33
	s_cmp_lt_i32 s4, 0
	s_cselect_b32 s4, s5, s6
	s_add_i32 s4, s4, s96
	s_ashr_i32 s5, s4, 31
	s_lshr_b32 s5, s5, 26
	s_add_i32 s5, s4, s5
	s_ashr_i32 s6, s5, 6
	s_and_b32 s5, s5, 0xffc0
	s_sub_i32 s4, s4, s5
	s_bfe_i32 s5, s4, 0x80000
	s_bfe_u32 s5, s5, 0x3000c
	s_add_i32 s5, s4, s5
	s_bfe_i32 s7, s5, 0x80000
	s_and_b32 s5, s5, 0xf8
	s_sub_i32 s4, s4, s5
	s_lshl_b32 s6, s6, 3
	s_sext_i32_i16 s7, s7
	s_sext_i32_i8 s4, s4
	s_add_i32 s33, s6, s4
	s_ashr_i32 s18, s7, 3
.LBB0_2511:
	v_readlane_b32 s24, v255, 0
	s_andn2_b64 vcc, exec, s[2:3]
	v_readlane_b32 s25, v255, 1
	s_cbranch_vccnz .LBB0_2545
	s_mov_b64 s[2:3], s[98:99]
	v_lshlrev_b32_e32 v1, 4, v2
	v_lshlrev_b32_e32 v3, 8, v2
	v_xor_b32_e32 v1, v1, v2
	v_and_b32_e32 v3, 0xfffff800, v3
	s_waitcnt lgkmcnt(0)
	s_add_u32 s0, s2, 0x36400000
	s_addc_u32 s1, s3, 0
	s_add_u32 s30, s2, 0x35000000
	s_addc_u32 s31, s3, 0
	s_movk_i32 s34, 0x70
	s_ashr_i32 s8, s13, 6
	s_ashr_i32 s19, s18, 31
	s_ashr_i32 s4, s13, 8
	v_and_or_b32 v194, v1, s34, v3
	s_lshl_b32 s35, s8, 10
	s_lshl_b64 s[6:7], s[18:19], 19
	v_mov_b32_e32 v1, v0
	v_mov_b64 v[178:179], 0
	v_mov_b64 v[180:181], 0
	v_mov_b64 v[182:183], 0
	v_mov_b64 v[184:185], 0
	v_mov_b64 v[162:163], 0
	v_mov_b64 v[164:165], 0
	v_mov_b64 v[166:167], 0
	v_mov_b64 v[168:169], 0
	v_mov_b64 v[146:147], 0
	v_mov_b64 v[148:149], 0
	v_mov_b64 v[150:151], 0
	v_mov_b64 v[152:153], 0
	v_mov_b64 v[122:123], 0
	v_mov_b64 v[124:125], 0
	v_mov_b64 v[126:127], 0
	v_mov_b64 v[128:129], 0
	v_mov_b64 v[186:187], 0
	v_mov_b64 v[188:189], 0
	v_mov_b64 v[190:191], 0
	v_mov_b64 v[192:193], 0
	v_mov_b64 v[170:171], 0
	v_mov_b64 v[172:173], 0
	v_mov_b64 v[174:175], 0
	v_mov_b64 v[176:177], 0
	v_mov_b64 v[154:155], 0
	v_mov_b64 v[156:157], 0
	v_mov_b64 v[158:159], 0
	v_mov_b64 v[160:161], 0
	v_mov_b64 v[138:139], 0
	v_mov_b64 v[140:141], 0
	v_mov_b64 v[142:143], 0
	v_mov_b64 v[144:145], 0
	v_mov_b64 v[114:115], 0
	v_mov_b64 v[116:117], 0
	v_mov_b64 v[118:119], 0
	v_mov_b64 v[120:121], 0
	v_mov_b64 v[98:99], 0
	v_mov_b64 v[100:101], 0
	v_mov_b64 v[102:103], 0
	v_mov_b64 v[104:105], 0
	v_mov_b64 v[82:83], 0
	v_mov_b64 v[84:85], 0
	v_mov_b64 v[86:87], 0
	v_mov_b64 v[88:89], 0
	v_mov_b64 v[66:67], 0
	v_mov_b64 v[68:69], 0
	v_mov_b64 v[70:71], 0
	v_mov_b64 v[72:73], 0
	v_mov_b64 v[130:131], 0
	v_mov_b64 v[132:133], 0
	v_mov_b64 v[134:135], 0
	v_mov_b64 v[136:137], 0
	v_mov_b64 v[106:107], 0
	v_mov_b64 v[108:109], 0
	v_mov_b64 v[110:111], 0
	v_mov_b64 v[112:113], 0
	v_mov_b64 v[90:91], 0
	v_mov_b64 v[92:93], 0
	v_mov_b64 v[94:95], 0
	v_mov_b64 v[96:97], 0
	v_mov_b64 v[74:75], 0
	v_mov_b64 v[76:77], 0
	v_mov_b64 v[78:79], 0
	v_mov_b64 v[80:81], 0
	s_add_u32 s20, s30, s6
	s_addc_u32 s21, s31, s7
	v_lshlrev_b32_e32 v3, 4, v1
	v_xor_b32_e32 v3, v3, v1
	v_lshlrev_b32_e32 v1, 8, v1
	s_add_i32 s36, s35, 0
	v_and_b32_e32 v1, 0xfffff800, v1
	s_mov_b64 s[6:7], s[20:21]
	s_add_i32 m0, s36, 0x10000
	v_add_u32_e32 v196, 0x20000, v194
	v_lshl_add_u32 v1, s33, 19, v1
	v_and_or_b32 v198, v3, s34, v1
	global_load_lds_dwordx4 v194, s[6:7]
	s_add_i32 m0, s36, 0x12000
	s_add_i32 s37, s36, 0x2000
	global_load_lds_dwordx4 v196, s[6:7]
	s_mov_b64 s[6:7], s[0:1]
	s_mov_b32 m0, s36
	v_add_u32_e32 v208, 0x20000, v198
	v_add_u32_e32 v212, 0x40000, v198
	global_load_lds_dwordx4 v198, s[6:7]
	s_mov_b32 m0, s37
	v_add_u32_e32 v210, 0x60000, v198
	global_load_lds_dwordx4 v208, s[6:7]
	s_add_u32 s6, s20, 0x40000
	s_addc_u32 s7, s21, 0
	s_add_i32 s38, s36, 0x14000
	s_mov_b32 m0, s38
	s_add_i32 s39, s36, 0x16000
	s_add_i32 s40, s36, 0x4000
	global_load_lds_dwordx4 v194, s[6:7]
	s_mov_b32 m0, s39
	s_add_i32 s41, s36, 0x6000
	global_load_lds_dwordx4 v196, s[6:7]
	s_mov_b64 s[6:7], s[0:1]
	s_mov_b32 m0, s40
	v_mov_b32_e32 v199, 0
	global_load_lds_dwordx4 v212, s[6:7]
	s_mov_b32 m0, s41
	s_mov_b32 s5, 0
	global_load_lds_dwordx4 v210, s[6:7]
	v_mov_b32_e32 v195, v199
	v_mov_b32_e32 v197, v199
	s_cmp_lg_u32 s4, 1
	v_mov_b32_e32 v209, v199
	s_cbranch_scc1 .LBB0_2514
	s_barrier

; __device__ __forceinline__ int otid() { int t = threadIdx.x; asm volatile("" : "+v"(t)); return t; }
; __device__ __forceinline__ unsigned xb_ld(unsigned* p)              { return __hip_atomic_load(p, __ATOMIC_RELAXED, __HIP_MEMORY_SCOPE_AGENT); }
; __device__ __forceinline__ void xcd_barrier_complete(unsigned* bar, unsigned x, unsigned& nloc, unsigned& nx) {
;     const unsigned G = gridDim.x * gridDim.y * gridDim.z;
;     unsigned sum, cnt, mine, sp = 0u;
;     for (;;) {
;         sum = 0u; cnt = 0u; mine = 0u;
; #pragma unroll
;         for (unsigned j = 0; j < 16; ++j) { const unsigned c = xb_ld(&bar[XB_XCNT(j)]); sum += c; cnt += (c > 0u) ? 1u : 0u; mine = (j == x) ? c : mine; }
;         if (sum == G) break;
;         __builtin_amdgcn_s_sleep(1);
;         if ((++sp & 255u) == 0u) { if (xb_ld(&bar[XB_TMO])) break; if (sp > XB_SPIN_CAP) { atomicAdd(&bar[XB_TMO], 1u); break; } }
;     }
;     nloc = mine > 0u ? mine : 1u; nx = cnt > 0u ? cnt : 1u;
; }
; __device__ __forceinline__ void xcd_barrier(const XcdBarrier& b) {
;     asm volatile("s_waitcnt vmcnt(0)" ::: "memory");
;     __syncthreads();
;     if (otid() == 0) {
;         unsigned* bar = b.bar;
;         __builtin_amdgcn_s_waitcnt(0);
;         unsigned nloc = b.st[0], nx = b.st[1];
;         if (nloc == 0u) { xcd_barrier_complete(bar, b.x, nloc, nx); b.st[0] = nloc; b.st[1] = nx; }
.LBB0_2545:
	s_mov_b64 s[0:1], s[24:25]
	s_mov_b32 s0, s100
	s_waitcnt lgkmcnt(0)
	s_cmp_gt_i32 s0, 17
	s_cbranch_scc1 .LBB0_2603
	s_mov_b64 s[0:1], s[24:25]
	s_mov_b32 s0, s101
	s_waitcnt lgkmcnt(0)
	s_cmp_lt_i32 s0, 18
	s_cbranch_scc1 .LBB0_2602
	v_readlane_b32 s0, v255, 0
	v_readlane_b32 s1, v255, 1
	s_mov_b32 s0, s100
	s_waitcnt lgkmcnt(0)
	s_cmp_gt_i32 s0, 18
	s_cbranch_scc1 .LBB0_2602
	v_readlane_b32 s0, v255, 0
	v_readlane_b32 s1, v255, 1
	s_mov_b32 s0, s101
	s_waitcnt lgkmcnt(0)
	s_cmp_lt_i32 s0, 19
	s_cbranch_scc1 .LBB0_2602
	v_readlane_b32 s2, v255, 0
	v_readlane_b32 s3, v255, 1
	s_getreg_b32 s4, hwreg(HW_REG_XCC_ID, 0, 4)
	s_waitcnt vmcnt(0)
	v_mov_b32_e32 v1, v0
	s_waitcnt vmcnt(0)
	s_barrier
	s_nop 0
	v_cmp_eq_u32_e32 vcc, 0, v1
	s_and_saveexec_b64 s[0:1], vcc
	s_cbranch_execz .LBB0_2601
	s_add_i32 s5, 0, 0x20020
	v_mov_b32_e32 v1, s5
	s_mov_b64 s[2:3], s[98:99]
	s_waitcnt vmcnt(0) expcnt(0) lgkmcnt(0)
	ds_read_b32 v3, v1
	s_add_i32 s5, 0, 0x20024
	v_mov_b32_e32 v1, s5
	ds_read_b32 v1, v1
	s_and_b32 s33, s4, 15
	s_waitcnt lgkmcnt(1)
	v_cmp_ne_u32_e32 vcc, 0, v3
	s_cbranch_vccnz .LBB0_2565
	v_readlane_b32 s4, v255, 0
	v_readlane_b32 s5, v255, 1
	s_load_dwordx2 s[8:9], s[4:5], 0xe0
	s_load_dword s7, s[4:5], 0xe8
	s_add_u32 s4, s2, 0x4200
	s_addc_u32 s5, s3, 0
	s_add_u32 s6, s2, 0x4400
	s_waitcnt lgkmcnt(0)
	s_mul_i32 s46, s9, s8
	s_mul_i32 s46, s46, s7
	s_addc_u32 s7, s3, 0
	s_add_u32 s8, s2, 0x4500
	s_addc_u32 s9, s3, 0
	s_add_u32 s10, s2, 0x4600
	s_addc_u32 s11, s3, 0
	s_add_u32 s12, s2, 0x4700
	s_addc_u32 s13, s3, 0
	s_add_u32 s14, s2, 0x4800
	s_addc_u32 s15, s3, 0
	s_add_u32 s16, s2, 0x4900
	s_addc_u32 s17, s3, 0
	s_add_u32 s18, s2, 0x4a00
	s_addc_u32 s19, s3, 0
	s_add_u32 s20, s2, 0x4b00
	s_addc_u32 s21, s3, 0
	s_add_u32 s22, s2, 0x4c00
	s_addc_u32 s23, s3, 0
	s_add_u32 s24, s2, 0x4d00
	s_addc_u32 s25, s3, 0
	s_add_u32 s26, s2, 0x4e00
	s_addc_u32 s27, s3, 0
	s_add_u32 s28, s2, 0x4f00
	s_addc_u32 s29, s3, 0
	s_add_u32 s30, s2, 0x5000
	s_addc_u32 s31, s3, 0
	s_add_u32 s34, s2, 0x5100
	s_addc_u32 s35, s3, 0
	s_add_u32 s36, s2, 0x5200
	s_addc_u32 s37, s3, 0
	s_add_u32 s38, s2, 0x5300
	s_addc_u32 s39, s3, 0
	s_mov_b32 s47, 1
	v_mov_b32_e32 v17, 0
	s_branch .LBB0_2553

; #define LAS __attribute__((address_space(3)))
; #define IN(k) (fresh_args()->ph_lo <= (k) && (k) < fresh_args()->ph_hi)
; #define SEAM(k) do { if (IN(k) && IN((k) + 1)) { XcdBarrier bar; bar.bar = (unsigned*)(fresh_args()->ws + WS_CTL) + CW_BAR; bar.x = xb_xcc_id(); bar.st = (volatile LAS unsigned*)(lds + LDS_TAB) + 8; xcd_barrier(bar); } } while (0)
; #define PHASE_ARGS() CArgs* A_p = fresh_args(); CArgs& A = *A_p; unsigned char* ws = A.ws; (void)ws;
; __device__ __forceinline__ void nmr_phase(CArgs& A, const float* xin, int l, int vcu, LAS unsigned char* lds) {
;     int tid = threadIdx.x; asm volatile("" : "+v"(tid));
;     const int lane = tid & 63, wave = __builtin_amdgcn_readfirstlane(tid >> 6);
;     bf16* H = (bf16*)(A.ws + WS_H); int* LIST = (int*)(A.ws + WS_LIST);
;     unsigned* ASG = (unsigned*)(A.ws + WS_ASG); float* ASGW = (float*)(A.ws + WS_ASG + 512 * 1024);
;     unsigned* cnt = (unsigned*)(A.ws + WS_CTL) + CW_CNT + l * 64;
;     const int t0 = vcu * 32;
;     {
;         const float* g = A.in[I_GFFN] + (size_t)l * DM;
;         for (int r = 0; r < 4; ++r) { const int t = t0 + wave * 4 + r; const int b = t / SEQ; Row x; row_load_f32(x, xin + (size_t)t * DM, lane);
;             row_norm_mod_store(x, g, mod_ptr(A, l, b, 3), mod_ptr(A, l, b, 4), H + (size_t)t * DM, lane, A.ws + WS_H8 + (size_t)t * DM); }
; template <int l> __device__ __forceinline__ void layer_body(LAS unsigned char* lds, unsigned char* lds_raw, int bx, int vcu) {
;     ...
;         if (KEN(8) && IN(pb + 6)) { PHASE_ARGS(); nmr_phase(A, (const float*)(ws + WS_X), l, vcu, lds); } SEAM(pb + 6);
.LBB0_2603:
	s_mov_b64 s[0:1], s[24:25]
	s_mov_b32 s0, s100
	s_waitcnt lgkmcnt(0)
	s_cmp_gt_i32 s0, 18
	s_cbranch_scc1 .LBB0_2626
	s_mov_b64 s[0:1], s[24:25]
	s_mov_b32 s0, s101
	s_waitcnt lgkmcnt(0)
	s_cmp_lt_i32 s0, 19
	s_cbranch_scc1 .LBB0_2626
	s_mov_b64 s[4:5], s[24:25]
	v_mov_b32_e32 v38, v0
	s_mov_b64 s[2:3], s[98:99]
	s_load_dwordx2 s[0:1], s[4:5], 0x78
	v_readfirstlane_b32 s6, v38
	v_and_b32_e32 v1, 63, v38
	s_ashr_i32 s22, s6, 6
	s_lshl_b32 s8, s97, 5
	s_waitcnt lgkmcnt(0)
	s_add_u32 s0, s0, 0x2000
	v_lshlrev_b32_e32 v2, 3, v1
	s_addc_u32 s1, s1, 0
	s_lshl_b32 s23, s22, 2
	v_mov_b32_e32 v5, 0
	v_or_b32_e32 v6, 0x200, v2
	s_add_i32 s8, s23, s8
	v_lshlrev_b32_e32 v8, 2, v6
	v_mov_b32_e32 v9, v5
	s_add_u32 s24, s2, 0x10000
	v_lshl_add_u64 v[12:13], s[0:1], 0, v[8:9]
	v_or_b32_e32 v8, 0x400, v2
	v_or_b32_e32 v24, 0x600, v2
	s_addc_u32 s25, s3, 0
	v_lshlrev_b32_e32 v4, 5, v1
	v_lshlrev_b32_e32 v14, 2, v8
	v_mov_b32_e32 v15, v5
	v_lshlrev_b32_e32 v16, 2, v24
	v_mov_b32_e32 v17, v5
	s_ashr_i32 s9, s8, 31
	v_lshl_add_u64 v[10:11], s[0:1], 0, v[4:5]
	v_lshl_add_u64 v[14:15], s[0:1], 0, v[14:15]
	v_lshl_add_u64 v[16:17], s[0:1], 0, v[16:17]
	s_lshl_b64 s[0:1], s[8:9], 11
	v_or_b32_e32 v18, s0, v2
	v_mov_b32_e32 v19, s1
	s_lshl_b64 s[0:1], s[8:9], 12
	v_lshl_or_b32 v20, v1, 4, s0
	v_mov_b32_e32 v21, s1
	s_lshl_b64 s[0:1], s[8:9], 13
	s_mov_b64 s[6:7], 0x2000
	v_or_b32_e32 v22, s0, v4
	v_mov_b32_e32 v23, s1
	s_mov_b32 s9, 0
	s_mov_b64 s[10:11], 0x38400000
	s_mov_b64 s[12:13], 0x38400800
	s_mov_b64 s[14:15], 0x38401000
	s_mov_b32 s26, 0x38401000
	s_mov_b64 s[16:17], 0x38401800
	v_mov_b32_e32 v39, 0x358637bd
	s_mov_b32 s27, 0x800000
	v_lshlrev_b32_e32 v40, 2, v2
	v_lshlrev_b32_e32 v41, 2, v6
	v_lshlrev_b32_e32 v42, 2, v8
	v_lshlrev_b32_e32 v43, 2, v24
	s_mov_b32 s28, 0x3c400000
	s_mov_b32 s29, 0x30c00000
	s_mov_b64 s[18:19], 0x800
	s_mov_b64 s[20:21], 0x1000

; __device__ __forceinline__ int otid() { int t = threadIdx.x; asm volatile("" : "+v"(t)); return t; }
; __device__ __forceinline__ unsigned xb_ld(unsigned* p)              { return __hip_atomic_load(p, __ATOMIC_RELAXED, __HIP_MEMORY_SCOPE_AGENT); }
; __device__ __forceinline__ void xcd_barrier_complete(unsigned* bar, unsigned x, unsigned& nloc, unsigned& nx) {
;     const unsigned G = gridDim.x * gridDim.y * gridDim.z;
;     unsigned sum, cnt, mine, sp = 0u;
;     for (;;) {
;         sum = 0u; cnt = 0u; mine = 0u;
; #pragma unroll
;         for (unsigned j = 0; j < 16; ++j) { const unsigned c = xb_ld(&bar[XB_XCNT(j)]); sum += c; cnt += (c > 0u) ? 1u : 0u; mine = (j == x) ? c : mine; }
;         if (sum == G) break;
;         __builtin_amdgcn_s_sleep(1);
;         if ((++sp & 255u) == 0u) { if (xb_ld(&bar[XB_TMO])) break; if (sp > XB_SPIN_CAP) { atomicAdd(&bar[XB_TMO], 1u); break; } }
;     }
;     nloc = mine > 0u ? mine : 1u; nx = cnt > 0u ? cnt : 1u;
; }
; __device__ __forceinline__ void xcd_barrier(const XcdBarrier& b) {
;     asm volatile("s_waitcnt vmcnt(0)" ::: "memory");
;     __syncthreads();
;     if (otid() == 0) {
;         unsigned* bar = b.bar;
;         __builtin_amdgcn_s_waitcnt(0);
;         unsigned nloc = b.st[0], nx = b.st[1];
;         if (nloc == 0u) { xcd_barrier_complete(bar, b.x, nloc, nx); b.st[0] = nloc; b.st[1] = nx; }
.LBB0_2626:
	s_mov_b64 s[0:1], s[24:25]
	s_mov_b32 s0, s100
	s_waitcnt lgkmcnt(0)
	s_cmp_gt_i32 s0, 18
	s_cbranch_scc1 .LBB0_2684
	s_mov_b64 s[0:1], s[24:25]
	s_mov_b32 s0, s101
	s_waitcnt lgkmcnt(0)
	s_cmp_lt_i32 s0, 19
	s_cbranch_scc1 .LBB0_2683
	v_readlane_b32 s0, v255, 0
	v_readlane_b32 s1, v255, 1
	s_mov_b32 s0, s100
	s_waitcnt lgkmcnt(0)
	s_cmp_gt_i32 s0, 19
	s_cbranch_scc1 .LBB0_2683
	v_readlane_b32 s0, v255, 0
	v_readlane_b32 s1, v255, 1
	s_mov_b32 s0, s101
	s_waitcnt lgkmcnt(0)
	s_cmp_lt_i32 s0, 20
	s_cbranch_scc1 .LBB0_2683
	v_readlane_b32 s2, v255, 0
	v_readlane_b32 s3, v255, 1
	s_getreg_b32 s4, hwreg(HW_REG_XCC_ID, 0, 4)
	s_waitcnt vmcnt(0)
	v_mov_b32_e32 v1, v0
	s_waitcnt vmcnt(0)
	s_barrier
	s_nop 0
	v_cmp_eq_u32_e32 vcc, 0, v1
	s_and_saveexec_b64 s[0:1], vcc
	s_cbranch_execz .LBB0_2682
	s_add_i32 s5, 0, 0x20020
	v_mov_b32_e32 v1, s5
	s_mov_b64 s[2:3], s[98:99]
	s_waitcnt vmcnt(0) expcnt(0) lgkmcnt(0)
	ds_read_b32 v3, v1
	s_add_i32 s5, 0, 0x20024
	v_mov_b32_e32 v1, s5
	ds_read_b32 v1, v1
	s_and_b32 s33, s4, 15
	s_waitcnt lgkmcnt(1)
	v_cmp_ne_u32_e32 vcc, 0, v3
	s_cbranch_vccnz .LBB0_2646
	v_readlane_b32 s4, v255, 0
	v_readlane_b32 s5, v255, 1
	s_load_dwordx2 s[8:9], s[4:5], 0xe0
	s_load_dword s7, s[4:5], 0xe8
	s_add_u32 s4, s2, 0x4200
	s_addc_u32 s5, s3, 0
	s_add_u32 s6, s2, 0x4400
	s_waitcnt lgkmcnt(0)
	s_mul_i32 s46, s9, s8
	s_mul_i32 s46, s46, s7
	s_addc_u32 s7, s3, 0
	s_add_u32 s8, s2, 0x4500
	s_addc_u32 s9, s3, 0
	s_add_u32 s10, s2, 0x4600
	s_addc_u32 s11, s3, 0
	s_add_u32 s12, s2, 0x4700
	s_addc_u32 s13, s3, 0
	s_add_u32 s14, s2, 0x4800
	s_addc_u32 s15, s3, 0
	s_add_u32 s16, s2, 0x4900
	s_addc_u32 s17, s3, 0
	s_add_u32 s18, s2, 0x4a00
	s_addc_u32 s19, s3, 0
	s_add_u32 s20, s2, 0x4b00
	s_addc_u32 s21, s3, 0
	s_add_u32 s22, s2, 0x4c00
	s_addc_u32 s23, s3, 0
	s_add_u32 s24, s2, 0x4d00
	s_addc_u32 s25, s3, 0
	s_add_u32 s26, s2, 0x4e00
	s_addc_u32 s27, s3, 0
	s_add_u32 s28, s2, 0x4f00
	s_addc_u32 s29, s3, 0
	s_add_u32 s30, s2, 0x5000
	s_addc_u32 s31, s3, 0
	s_add_u32 s34, s2, 0x5100
	s_addc_u32 s35, s3, 0
	s_add_u32 s36, s2, 0x5200
	s_addc_u32 s37, s3, 0
	s_add_u32 s38, s2, 0x5300
	s_addc_u32 s39, s3, 0
	s_mov_b32 s47, 1
	v_mov_b32_e32 v17, 0
	s_branch .LBB0_2634

; #define LAS __attribute__((address_space(3)))
; __device__ __forceinline__ int otid() { int t = threadIdx.x; asm volatile("" : "+v"(t)); return t; }
; #define REP(k) for (int rep_ = 0; rep_ < ((REP_KIND == (k)) ? REP_N : 1); ++rep_)
; #define IN(k) (fresh_args()->ph_lo <= (k) && (k) < fresh_args()->ph_hi)
; #define PHASE_ARGS() CArgs* A_p = fresh_args(); CArgs& A = *A_p; unsigned char* ws = A.ws; (void)ws;
; __device__ __forceinline__ MoeTab moe_tables(CArgs& A, int l, LAS unsigned char* lds, bool want_order) {
;     MoeTab T; T.cnt = (LAS int*)(lds + LDS_TAB + 256); T.ts = T.cnt + 64; T.ord = (LAS int*)(lds + LDS_TAB + 1024) + 1;
;     unsigned* cg = (unsigned*)(A.ws + WS_CTL) + CW_CNT + l * 64;
;     const int tt = otid();
;     __syncthreads();
;     if (tt < 64) {
;         const int e = tt; const int c = (int)__hip_atomic_load(cg + e, RLX_AGENT);
;         T.cnt[e] = c;
;         const int nall = (c + 255) >> 8; const int ia = wave_incl_scan(nall, e);
;         T.ts[e] = ia - nall; if (e == 63) T.ts[64] = ia;
;         if (want_order) {
;             const int nfull = c >> 8, rem = c & 255;
;             const int n1 = nfull + (rem > 128 ? 1 : 0), nh = (rem != 0 && rem <= 128) ? 1 : 0;
;             const int p1 = wave_incl_scan(n1, e), ph = wave_incl_scan(nh, e);
;             const int tot1 = __builtin_amdgcn_readlane(p1, 63), toth = __builtin_amdgcn_readlane(ph, 63);
;             if (e < NT / 256) T.ord[e] = 64 | (e << 8);
;             const int pos = NT / 256 + p1 - n1;
; #pragma nounroll
;             for (int m = 0; m < n1; ++m) T.ord[pos + m] = e | (m << 8);
;             if (nh) T.ord[NT / 256 + tot1 + ph - 1] = e | (nfull << 8) | (1 << 16);
;             if (e == 0) T.ord[-1] = NT / 256 + tot1 + toth;
;         }
;     }
;     __syncthreads();
;     return T;
; }
; template <int l> __device__ __forceinline__ void layer_body(LAS unsigned char* lds, unsigned char* lds_raw, int bx, int vcu) {
;     ...
;         if (KEN(9) && IN(pb + 7)) REP(9) { PHASE_ARGS();
;             Moe1P P; P.H = (const char*)(ws + WS_H8); P.W = (const char*)(ws + WS_W13E) + (size_t)l * NE * 1024 * DM; P.WSH = (const char*)(ws + WS_WSH8) + (size_t)l * 1024 * DM; P.LIST = (const int*)(ws + WS_LIST); P.ACT = (bf16*)(ws + WS_ACT); P.SACT = (bf16*)(ws + WS_SACT); P.T = moe_tables(A, l, lds, true); P.G = G; P.c = bx;
.LBB0_2684:
	s_mov_b64 s[0:1], s[24:25]
	s_mov_b32 s0, s100
	s_waitcnt lgkmcnt(0)
	s_cmp_gt_i32 s0, 19
	s_cbranch_scc1 .LBB0_2798
	s_mov_b64 s[0:1], s[24:25]
	s_mov_b32 s0, s101
	s_waitcnt lgkmcnt(0)
	s_cmp_lt_i32 s0, 20
	s_cbranch_scc1 .LBB0_2798
	s_mov_b64 s[0:1], s[24:25]
	s_mov_b64 s[14:15], s[98:99]
	v_mov_b32_e32 v2, v0
	s_waitcnt vmcnt(0) lgkmcnt(0)
	v_cmp_gt_i32_e32 vcc, 64, v2
	s_barrier
	s_and_saveexec_b64 s[16:17], vcc
	s_cbranch_execz .LBB0_2705
	v_ashrrev_i32_e32 v3, 31, v2
	v_mul_u32_u24_e32 v4, 0x1100, v2
	v_mov_b32_e32 v5, 0
	v_lshl_add_u64 v[4:5], v[4:5], 0, s[14:15]
	v_add_co_u32_e32 v4, vcc, 0xc4000, v4
	v_cmp_lt_i32_e64 s[0:1], 0, v2
	s_nop 0
	v_addc_co_u32_e32 v5, vcc, 0, v5, vcc
	global_load_dword v3, v[4:5], off sc1
	v_mbcnt_lo_u32_b32 v4, -1, 0
	v_mbcnt_hi_u32_b32 v4, -1, v4
	v_and_b32_e32 v10, 64, v4
	v_add_u32_e32 v5, -1, v4
	v_cmp_lt_i32_e32 vcc, v5, v10
	v_add_u32_e32 v6, -2, v4
	v_add_u32_e32 v7, -4, v4
	v_cndmask_b32_e32 v5, v5, v4, vcc
	v_lshlrev_b32_e32 v5, 2, v5
	v_cmp_lt_i32_e32 vcc, v6, v10
	v_cmp_gt_i32_e64 s[2:3], 2, v2
	v_add_u32_e32 v8, -8, v4
	v_cndmask_b32_e32 v6, v6, v4, vcc
	v_lshlrev_b32_e32 v6, 2, v6
	v_cmp_lt_i32_e32 vcc, v7, v10
	v_cmp_gt_i32_e64 s[4:5], 4, v2
	v_add_u32_e32 v9, -16, v4
	v_cndmask_b32_e32 v7, v7, v4, vcc
	v_lshlrev_b32_e32 v7, 2, v7
	v_cmp_lt_i32_e32 vcc, v8, v10
	v_cmp_gt_i32_e64 s[6:7], 8, v2
	v_subrev_u32_e32 v11, 32, v4
	v_cndmask_b32_e32 v8, v8, v4, vcc
	v_lshlrev_b32_e32 v8, 2, v8
	v_cmp_lt_i32_e32 vcc, v9, v10
	v_cmp_gt_i32_e64 s[8:9], 16, v2
	v_cmp_gt_i32_e64 s[10:11], 32, v2
	v_cndmask_b32_e32 v9, v9, v4, vcc
	v_lshlrev_b32_e32 v9, 2, v9
	v_cmp_lt_i32_e32 vcc, v11, v10
	v_lshl_add_u32 v1, v2, 2, 0
	s_waitcnt vmcnt(0)
	v_add_u32_e32 v12, 0xff, v3
	v_ashrrev_i32_e32 v12, 8, v12
	ds_bpermute_b32 v13, v5, v12
	v_cndmask_b32_e32 v4, v11, v4, vcc
	v_lshlrev_b32_e32 v10, 2, v4
	v_cmp_eq_u32_e32 vcc, 63, v2
	s_waitcnt lgkmcnt(0)
	v_cndmask_b32_e64 v13, 0, v13, s[0:1]
	v_add_u32_e32 v13, v13, v12
	ds_bpermute_b32 v14, v6, v13
	s_waitcnt lgkmcnt(0)
	v_cndmask_b32_e64 v14, v14, 0, s[2:3]
	v_add_u32_e32 v13, v14, v13
	ds_bpermute_b32 v14, v7, v13
	s_waitcnt lgkmcnt(0)
	v_cndmask_b32_e64 v14, v14, 0, s[4:5]
	v_add_u32_e32 v13, v14, v13
	ds_bpermute_b32 v14, v8, v13
	s_waitcnt lgkmcnt(0)
	v_cndmask_b32_e64 v14, v14, 0, s[6:7]
	v_add_u32_e32 v13, v14, v13
	ds_bpermute_b32 v14, v9, v13
	s_waitcnt lgkmcnt(0)
	v_cndmask_b32_e64 v4, v14, 0, s[8:9]
	v_add_u32_e32 v4, v4, v13
	ds_bpermute_b32 v11, v10, v4
	v_add_u32_e32 v13, 0x20100, v1
	v_add_u32_e32 v14, 0x20200, v1
	ds_write_b32 v13, v3
	s_waitcnt lgkmcnt(1)
	v_cndmask_b32_e64 v11, v11, 0, s[10:11]
	v_add_u32_e32 v4, v11, v4
	v_sub_u32_e32 v11, v4, v12
	ds_write_b32 v14, v11
	s_and_saveexec_b64 s[12:13], vcc
	s_add_i32 s18, 0, 0x20300
	v_mov_b32_e32 v11, s18
	ds_write_b32 v11, v4
	s_or_b64 exec, exec, s[12:13]
	s_movk_i32 s18, 0x80
	v_ashrrev_i32_e32 v12, 8, v3
	v_cmp_gt_u32_sdwa s[12:13], v3, s18 src0_sel:BYTE_0 src1_sel:DWORD
	v_mov_b32_e32 v11, -1
	v_add_u32_sdwa v11, v3, v11 dst_sel:DWORD dst_unused:UNUSED_PAD src0_sel:BYTE_0 src1_sel:DWORD
	v_addc_co_u32_e64 v4, vcc, 0, v12, s[12:13]
	v_cmp_gt_u32_e32 vcc, s18, v11
	ds_bpermute_b32 v13, v5, v4
	s_nop 0
	v_cndmask_b32_e64 v11, 0, 1, vcc
	ds_bpermute_b32 v5, v5, v11
	s_waitcnt lgkmcnt(1)
	v_cndmask_b32_e64 v11, 0, v13, s[0:1]
	v_addc_co_u32_e64 v12, s[12:13], v11, v12, s[12:13]
	s_waitcnt lgkmcnt(0)
	v_cndmask_b32_e64 v5, 0, v5, s[0:1]
	v_addc_co_u32_e64 v14, s[0:1], 0, v5, vcc
	ds_bpermute_b32 v13, v6, v12
	ds_bpermute_b32 v14, v6, v14
	s_waitcnt lgkmcnt(1)
	v_cndmask_b32_e64 v6, v13, 0, s[2:3]
	s_waitcnt lgkmcnt(0)
	v_cndmask_b32_e64 v14, v14, 0, s[2:3]
	v_add_u32_e32 v12, v6, v12
	v_addc_co_u32_e64 v5, s[0:1], v14, v5, vcc
	ds_bpermute_b32 v13, v7, v12
	ds_bpermute_b32 v14, v7, v5
	s_waitcnt lgkmcnt(1)
	v_cndmask_b32_e64 v7, v13, 0, s[4:5]
	s_waitcnt lgkmcnt(0)
	v_cndmask_b32_e64 v14, v14, 0, s[4:5]
	v_add_u32_e32 v13, v7, v12
	v_add_u32_e32 v5, v14, v5
	ds_bpermute_b32 v12, v8, v13
	ds_bpermute_b32 v8, v8, v5
	s_waitcnt lgkmcnt(1)
	v_cndmask_b32_e64 v12, v12, 0, s[6:7]
	s_waitcnt lgkmcnt(0)
	v_cndmask_b32_e64 v8, v8, 0, s[6:7]
	v_add_u32_e32 v13, v12, v13
	v_add_u32_e32 v5, v8, v5
	ds_bpermute_b32 v14, v9, v13
	ds_bpermute_b32 v8, v9, v5
	s_waitcnt lgkmcnt(1)
	v_cndmask_b32_e64 v9, v14, 0, s[8:9]
	s_waitcnt lgkmcnt(0)
	v_cndmask_b32_e64 v8, v8, 0, s[8:9]
	v_add_u32_e32 v13, v9, v13
	v_add_u32_e32 v5, v8, v5
	ds_bpermute_b32 v14, v10, v13
	ds_bpermute_b32 v10, v10, v5
	s_waitcnt lgkmcnt(1)
	v_cndmask_b32_e64 v8, v14, 0, s[10:11]
	s_waitcnt lgkmcnt(0)
	v_cndmask_b32_e64 v10, v10, 0, s[10:11]
	v_add_u32_e32 v13, v8, v13
	v_add_u32_e32 v5, v10, v5
	v_readlane_b32 s8, v13, 63
	v_readlane_b32 s9, v5, 63
	s_and_saveexec_b64 s[0:1], s[10:11]
	v_add_u32_e32 v1, 0x20404, v1
	v_lshl_or_b32 v10, v2, 8, 64
	ds_write_b32 v1, v10
	s_or_b64 exec, exec, s[0:1]
	v_cmp_lt_i32_e64 s[0:1], 0, v4
	s_and_saveexec_b64 s[2:3], s[0:1]
	s_cbranch_execz .LBB0_2701
	v_add3_u32 v1, v11, v6, v7
	s_mov_b32 s10, 1
	v_cmp_ne_u32_e64 s[0:1], 1, v4
	s_mov_b64 s[6:7], 0
	v_add3_u32 v9, v1, v12, v9
	s_and_saveexec_b64 s[4:5], s[0:1]
	s_xor_b64 s[4:5], exec, s[4:5]
	s_cbranch_execnz .LBB0_2695
	s_andn2_saveexec_b64 s[0:1], s[4:5]
	s_cbranch_execnz .LBB0_2698

; __device__ __forceinline__ int otid() { int t = threadIdx.x; asm volatile("" : "+v"(t)); return t; }
; __device__ __forceinline__ unsigned xb_ld(unsigned* p)              { return __hip_atomic_load(p, __ATOMIC_RELAXED, __HIP_MEMORY_SCOPE_AGENT); }
; __device__ __forceinline__ void xcd_barrier_complete(unsigned* bar, unsigned x, unsigned& nloc, unsigned& nx) {
;     const unsigned G = gridDim.x * gridDim.y * gridDim.z;
;     unsigned sum, cnt, mine, sp = 0u;
;     for (;;) {
;         sum = 0u; cnt = 0u; mine = 0u;
; #pragma unroll
;         for (unsigned j = 0; j < 16; ++j) { const unsigned c = xb_ld(&bar[XB_XCNT(j)]); sum += c; cnt += (c > 0u) ? 1u : 0u; mine = (j == x) ? c : mine; }
;         if (sum == G) break;
;         __builtin_amdgcn_s_sleep(1);
;         if ((++sp & 255u) == 0u) { if (xb_ld(&bar[XB_TMO])) break; if (sp > XB_SPIN_CAP) { atomicAdd(&bar[XB_TMO], 1u); break; } }
;     }
;     nloc = mine > 0u ? mine : 1u; nx = cnt > 0u ? cnt : 1u;
; }
; __device__ __forceinline__ void xcd_barrier(const XcdBarrier& b) {
;     asm volatile("s_waitcnt vmcnt(0)" ::: "memory");
;     __syncthreads();
;     if (otid() == 0) {
;         unsigned* bar = b.bar;
;         __builtin_amdgcn_s_waitcnt(0);
;         unsigned nloc = b.st[0], nx = b.st[1];
;         if (nloc == 0u) { xcd_barrier_complete(bar, b.x, nloc, nx); b.st[0] = nloc; b.st[1] = nx; }
.LBB0_2798:
	s_mov_b64 s[0:1], s[24:25]
	s_mov_b32 s0, s100
	s_waitcnt lgkmcnt(0)
	s_cmp_gt_i32 s0, 19
	s_cbranch_scc1 .LBB0_2856
	s_mov_b64 s[0:1], s[24:25]
	s_mov_b32 s0, s101
	s_waitcnt lgkmcnt(0)
	s_cmp_lt_i32 s0, 20
	s_cbranch_scc1 .LBB0_2855
	v_readlane_b32 s0, v255, 0
	v_readlane_b32 s1, v255, 1
	s_mov_b32 s0, s100
	s_waitcnt lgkmcnt(0)
	s_cmp_gt_i32 s0, 20
	s_cbranch_scc1 .LBB0_2855
	v_readlane_b32 s0, v255, 0
	v_readlane_b32 s1, v255, 1
	s_mov_b32 s0, s101
	s_waitcnt lgkmcnt(0)
	s_cmp_lt_i32 s0, 21
	s_cbranch_scc1 .LBB0_2855
	v_readlane_b32 s2, v255, 0
	v_readlane_b32 s3, v255, 1
	s_getreg_b32 s4, hwreg(HW_REG_XCC_ID, 0, 4)
	s_waitcnt vmcnt(0)
	v_mov_b32_e32 v1, v0
	s_waitcnt vmcnt(0)
	s_barrier
	s_nop 0
	v_cmp_eq_u32_e32 vcc, 0, v1
	s_and_saveexec_b64 s[0:1], vcc
	s_cbranch_execz .LBB0_2854
	s_add_i32 s5, 0, 0x20020
	v_mov_b32_e32 v1, s5
	s_mov_b64 s[2:3], s[98:99]
	s_waitcnt vmcnt(0) expcnt(0) lgkmcnt(0)
	ds_read_b32 v3, v1
	s_add_i32 s5, 0, 0x20024
	v_mov_b32_e32 v1, s5
	ds_read_b32 v1, v1
	s_and_b32 s33, s4, 15
	s_waitcnt lgkmcnt(1)
	v_cmp_ne_u32_e32 vcc, 0, v3
	s_cbranch_vccnz .LBB0_2818
	v_readlane_b32 s4, v255, 0
	v_readlane_b32 s5, v255, 1
	s_load_dwordx2 s[8:9], s[4:5], 0xe0
	s_load_dword s7, s[4:5], 0xe8
	s_add_u32 s4, s2, 0x4200
	s_addc_u32 s5, s3, 0
	s_add_u32 s6, s2, 0x4400
	s_waitcnt lgkmcnt(0)
	s_mul_i32 s46, s9, s8
	s_mul_i32 s46, s46, s7
	s_addc_u32 s7, s3, 0
	s_add_u32 s8, s2, 0x4500
	s_addc_u32 s9, s3, 0
	s_add_u32 s10, s2, 0x4600
	s_addc_u32 s11, s3, 0
	s_add_u32 s12, s2, 0x4700
	s_addc_u32 s13, s3, 0
	s_add_u32 s14, s2, 0x4800
	s_addc_u32 s15, s3, 0
	s_add_u32 s16, s2, 0x4900
	s_addc_u32 s17, s3, 0
	s_add_u32 s18, s2, 0x4a00
	s_addc_u32 s19, s3, 0
	s_add_u32 s20, s2, 0x4b00
	s_addc_u32 s21, s3, 0
	s_add_u32 s22, s2, 0x4c00
	s_addc_u32 s23, s3, 0
	s_add_u32 s24, s2, 0x4d00
	s_addc_u32 s25, s3, 0
	s_add_u32 s26, s2, 0x4e00
	s_addc_u32 s27, s3, 0
	s_add_u32 s28, s2, 0x4f00
	s_addc_u32 s29, s3, 0
	s_add_u32 s30, s2, 0x5000
	s_addc_u32 s31, s3, 0
	s_add_u32 s34, s2, 0x5100
	s_addc_u32 s35, s3, 0
	s_add_u32 s36, s2, 0x5200
	s_addc_u32 s37, s3, 0
	s_add_u32 s38, s2, 0x5300
	s_addc_u32 s39, s3, 0
	s_mov_b32 s47, 1
	v_mov_b32_e32 v17, 0
	s_branch .LBB0_2806

; #define LAS __attribute__((address_space(3)))
; __device__ __forceinline__ int otid() { int t = threadIdx.x; asm volatile("" : "+v"(t)); return t; }
; #define REP(k) for (int rep_ = 0; rep_ < ((REP_KIND == (k)) ? REP_N : 1); ++rep_)
; #define IN(k) (fresh_args()->ph_lo <= (k) && (k) < fresh_args()->ph_hi)
; #define PHASE_ARGS() CArgs* A_p = fresh_args(); CArgs& A = *A_p; unsigned char* ws = A.ws; (void)ws;
; __device__ __forceinline__ MoeTab moe_tables(CArgs& A, int l, LAS unsigned char* lds, bool want_order) {
;     MoeTab T; T.cnt = (LAS int*)(lds + LDS_TAB + 256); T.ts = T.cnt + 64; T.ord = (LAS int*)(lds + LDS_TAB + 1024) + 1;
;     unsigned* cg = (unsigned*)(A.ws + WS_CTL) + CW_CNT + l * 64;
;     const int tt = otid();
;     __syncthreads();
;     if (tt < 64) {
;         const int e = tt; const int c = (int)__hip_atomic_load(cg + e, RLX_AGENT);
;         T.cnt[e] = c;
;         const int nall = (c + 255) >> 8; const int ia = wave_incl_scan(nall, e);
;         T.ts[e] = ia - nall; if (e == 63) T.ts[64] = ia;
;         if (want_order) {
;             const int nfull = c >> 8, rem = c & 255;
;             const int n1 = nfull + (rem > 128 ? 1 : 0), nh = (rem != 0 && rem <= 128) ? 1 : 0;
;             const int p1 = wave_incl_scan(n1, e), ph = wave_incl_scan(nh, e);
;             const int tot1 = __builtin_amdgcn_readlane(p1, 63), toth = __builtin_amdgcn_readlane(ph, 63);
;             if (e < NT / 256) T.ord[e] = 64 | (e << 8);
;             const int pos = NT / 256 + p1 - n1;
; #pragma nounroll
;             for (int m = 0; m < n1; ++m) T.ord[pos + m] = e | (m << 8);
;             if (nh) T.ord[NT / 256 + tot1 + ph - 1] = e | (nfull << 8) | (1 << 16);
;             if (e == 0) T.ord[-1] = NT / 256 + tot1 + toth;
;         }
;     }
;     __syncthreads();
;     return T;
; }
; template <int l> __device__ __forceinline__ void layer_body(LAS unsigned char* lds, unsigned char* lds_raw, int bx, int vcu) {
;     ...
;         if (KEN(10) && IN(pb + 8)) REP(10) { PHASE_ARGS();
;             Moe2P P; P.ACT = (const char*)(ws + WS_ACT); P.SACT = (const char*)(ws + WS_SACT); P.W = (const char*)(ws + WS_W2E) + (size_t)l * NE * DM * DE; P.WS2 = (const char*)(ws + WS_W2S) + (size_t)l * DM * DS;
;             P.OUT2 = (bf16*)(ws + WS_OUT2); P.T = moe_tables(A, l, lds, true); P.G = G; P.c = bx;
.LBB0_2856:
	s_mov_b64 s[0:1], s[24:25]
	s_mov_b32 s0, s100
	s_waitcnt lgkmcnt(0)
	s_cmp_gt_i32 s0, 20
	s_cbranch_scc1 .LBB0_2932
	s_mov_b64 s[0:1], s[24:25]
	s_mov_b32 s0, s101
	s_waitcnt lgkmcnt(0)
	s_cmp_lt_i32 s0, 21
	s_cbranch_scc1 .LBB0_2932
	s_mov_b64 s[0:1], s[24:25]
	s_mov_b64 s[14:15], s[98:99]
	v_mov_b32_e32 v2, v0
	s_waitcnt vmcnt(0) lgkmcnt(0)
	v_cmp_gt_i32_e32 vcc, 64, v2
	s_barrier
	s_and_saveexec_b64 s[16:17], vcc
	s_cbranch_execz .LBB0_2877
	v_ashrrev_i32_e32 v3, 31, v2
	v_mul_u32_u24_e32 v4, 0x1100, v2
	v_mov_b32_e32 v5, 0
	v_lshl_add_u64 v[4:5], v[4:5], 0, s[14:15]
	v_add_co_u32_e32 v4, vcc, 0xc4000, v4
	v_cmp_lt_i32_e64 s[0:1], 0, v2
	s_nop 0
	v_addc_co_u32_e32 v5, vcc, 0, v5, vcc
	global_load_dword v3, v[4:5], off sc1
	v_mbcnt_lo_u32_b32 v4, -1, 0
	v_mbcnt_hi_u32_b32 v4, -1, v4
	v_and_b32_e32 v10, 64, v4
	v_add_u32_e32 v5, -1, v4
	v_cmp_lt_i32_e32 vcc, v5, v10
	v_add_u32_e32 v6, -2, v4
	v_add_u32_e32 v7, -4, v4
	v_cndmask_b32_e32 v5, v5, v4, vcc
	v_lshlrev_b32_e32 v5, 2, v5
	v_cmp_lt_i32_e32 vcc, v6, v10
	v_cmp_gt_i32_e64 s[2:3], 2, v2
	v_add_u32_e32 v8, -8, v4
	v_cndmask_b32_e32 v6, v6, v4, vcc
	v_lshlrev_b32_e32 v6, 2, v6
	v_cmp_lt_i32_e32 vcc, v7, v10
	v_cmp_gt_i32_e64 s[4:5], 4, v2
	v_add_u32_e32 v9, -16, v4
	v_cndmask_b32_e32 v7, v7, v4, vcc
	v_lshlrev_b32_e32 v7, 2, v7
	v_cmp_lt_i32_e32 vcc, v8, v10
	v_cmp_gt_i32_e64 s[6:7], 8, v2
	v_subrev_u32_e32 v11, 32, v4
	v_cndmask_b32_e32 v8, v8, v4, vcc
	v_lshlrev_b32_e32 v8, 2, v8
	v_cmp_lt_i32_e32 vcc, v9, v10
	v_cmp_gt_i32_e64 s[8:9], 16, v2
	v_cmp_gt_i32_e64 s[10:11], 32, v2
	v_cndmask_b32_e32 v9, v9, v4, vcc
	v_lshlrev_b32_e32 v9, 2, v9
	v_cmp_lt_i32_e32 vcc, v11, v10
	v_lshl_add_u32 v1, v2, 2, 0
	s_waitcnt vmcnt(0)
	v_add_u32_e32 v12, 0xff, v3
	v_ashrrev_i32_e32 v12, 8, v12
	ds_bpermute_b32 v13, v5, v12
	v_cndmask_b32_e32 v4, v11, v4, vcc
	v_lshlrev_b32_e32 v10, 2, v4
	v_cmp_eq_u32_e32 vcc, 63, v2
	s_waitcnt lgkmcnt(0)
	v_cndmask_b32_e64 v13, 0, v13, s[0:1]
	v_add_u32_e32 v13, v13, v12
	ds_bpermute_b32 v14, v6, v13
	s_waitcnt lgkmcnt(0)
	v_cndmask_b32_e64 v14, v14, 0, s[2:3]
	v_add_u32_e32 v13, v14, v13
	ds_bpermute_b32 v14, v7, v13
	s_waitcnt lgkmcnt(0)
	v_cndmask_b32_e64 v14, v14, 0, s[4:5]
	v_add_u32_e32 v13, v14, v13
	ds_bpermute_b32 v14, v8, v13
	s_waitcnt lgkmcnt(0)
	v_cndmask_b32_e64 v14, v14, 0, s[6:7]
	v_add_u32_e32 v13, v14, v13
	ds_bpermute_b32 v14, v9, v13
	s_waitcnt lgkmcnt(0)
	v_cndmask_b32_e64 v4, v14, 0, s[8:9]
	v_add_u32_e32 v4, v4, v13
	ds_bpermute_b32 v11, v10, v4
	v_add_u32_e32 v13, 0x20100, v1
	v_add_u32_e32 v14, 0x20200, v1
	ds_write_b32 v13, v3
	s_waitcnt lgkmcnt(1)
	v_cndmask_b32_e64 v11, v11, 0, s[10:11]
	v_add_u32_e32 v4, v11, v4
	v_sub_u32_e32 v11, v4, v12
	ds_write_b32 v14, v11
	s_and_saveexec_b64 s[12:13], vcc
	s_add_i32 s18, 0, 0x20300
	v_mov_b32_e32 v11, s18
	ds_write_b32 v11, v4
	s_or_b64 exec, exec, s[12:13]
	s_movk_i32 s18, 0x80
	v_ashrrev_i32_e32 v12, 8, v3
	v_cmp_gt_u32_sdwa s[12:13], v3, s18 src0_sel:BYTE_0 src1_sel:DWORD
	v_mov_b32_e32 v11, -1
	v_add_u32_sdwa v11, v3, v11 dst_sel:DWORD dst_unused:UNUSED_PAD src0_sel:BYTE_0 src1_sel:DWORD
	v_addc_co_u32_e64 v4, vcc, 0, v12, s[12:13]
	v_cmp_gt_u32_e32 vcc, s18, v11
	ds_bpermute_b32 v13, v5, v4
	s_nop 0
	v_cndmask_b32_e64 v11, 0, 1, vcc
	ds_bpermute_b32 v5, v5, v11
	s_waitcnt lgkmcnt(1)
	v_cndmask_b32_e64 v11, 0, v13, s[0:1]
	v_addc_co_u32_e64 v12, s[12:13], v11, v12, s[12:13]
	s_waitcnt lgkmcnt(0)
	v_cndmask_b32_e64 v5, 0, v5, s[0:1]
	v_addc_co_u32_e64 v14, s[0:1], 0, v5, vcc
	ds_bpermute_b32 v13, v6, v12
	ds_bpermute_b32 v14, v6, v14
	s_waitcnt lgkmcnt(1)
	v_cndmask_b32_e64 v6, v13, 0, s[2:3]
	s_waitcnt lgkmcnt(0)
	v_cndmask_b32_e64 v14, v14, 0, s[2:3]
	v_add_u32_e32 v12, v6, v12
	v_addc_co_u32_e64 v5, s[0:1], v14, v5, vcc
	ds_bpermute_b32 v13, v7, v12
	ds_bpermute_b32 v14, v7, v5
	s_waitcnt lgkmcnt(1)
	v_cndmask_b32_e64 v7, v13, 0, s[4:5]
	s_waitcnt lgkmcnt(0)
	v_cndmask_b32_e64 v14, v14, 0, s[4:5]
	v_add_u32_e32 v13, v7, v12
	v_add_u32_e32 v5, v14, v5
	ds_bpermute_b32 v12, v8, v13
	ds_bpermute_b32 v8, v8, v5
	s_waitcnt lgkmcnt(1)
	v_cndmask_b32_e64 v12, v12, 0, s[6:7]
	s_waitcnt lgkmcnt(0)
	v_cndmask_b32_e64 v8, v8, 0, s[6:7]
	v_add_u32_e32 v13, v12, v13
	v_add_u32_e32 v5, v8, v5
	ds_bpermute_b32 v14, v9, v13
	ds_bpermute_b32 v8, v9, v5
	s_waitcnt lgkmcnt(1)
	v_cndmask_b32_e64 v9, v14, 0, s[8:9]
	s_waitcnt lgkmcnt(0)
	v_cndmask_b32_e64 v8, v8, 0, s[8:9]
	v_add_u32_e32 v13, v9, v13
	v_add_u32_e32 v5, v8, v5
	ds_bpermute_b32 v14, v10, v13
	ds_bpermute_b32 v10, v10, v5
	s_waitcnt lgkmcnt(1)
	v_cndmask_b32_e64 v8, v14, 0, s[10:11]
	s_waitcnt lgkmcnt(0)
	v_cndmask_b32_e64 v10, v10, 0, s[10:11]
	v_add_u32_e32 v13, v8, v13
	v_add_u32_e32 v5, v10, v5
	v_readlane_b32 s8, v13, 63
	v_readlane_b32 s9, v5, 63
	s_and_saveexec_b64 s[0:1], s[10:11]
	v_add_u32_e32 v1, 0x20404, v1
	v_lshl_or_b32 v10, v2, 8, 64
	ds_write_b32 v1, v10
	s_or_b64 exec, exec, s[0:1]
	v_cmp_lt_i32_e64 s[0:1], 0, v4
	s_and_saveexec_b64 s[2:3], s[0:1]
	s_cbranch_execz .LBB0_2873
	v_add3_u32 v1, v11, v6, v7
	s_mov_b32 s10, 1
	v_cmp_ne_u32_e64 s[0:1], 1, v4
	s_mov_b64 s[6:7], 0
	v_add3_u32 v9, v1, v12, v9
	s_and_saveexec_b64 s[4:5], s[0:1]
	s_xor_b64 s[4:5], exec, s[4:5]
	s_cbranch_execnz .LBB0_2867
	s_andn2_saveexec_b64 s[0:1], s[4:5]
	s_cbranch_execnz .LBB0_2870

; __device__ __forceinline__ int otid() { int t = threadIdx.x; asm volatile("" : "+v"(t)); return t; }
; __device__ __forceinline__ unsigned xb_ld(unsigned* p)              { return __hip_atomic_load(p, __ATOMIC_RELAXED, __HIP_MEMORY_SCOPE_AGENT); }
; __device__ __forceinline__ void xcd_barrier_complete(unsigned* bar, unsigned x, unsigned& nloc, unsigned& nx) {
;     const unsigned G = gridDim.x * gridDim.y * gridDim.z;
;     unsigned sum, cnt, mine, sp = 0u;
;     for (;;) {
;         sum = 0u; cnt = 0u; mine = 0u;
; #pragma unroll
;         for (unsigned j = 0; j < 16; ++j) { const unsigned c = xb_ld(&bar[XB_XCNT(j)]); sum += c; cnt += (c > 0u) ? 1u : 0u; mine = (j == x) ? c : mine; }
;         if (sum == G) break;
;         __builtin_amdgcn_s_sleep(1);
;         if ((++sp & 255u) == 0u) { if (xb_ld(&bar[XB_TMO])) break; if (sp > XB_SPIN_CAP) { atomicAdd(&bar[XB_TMO], 1u); break; } }
;     }
;     nloc = mine > 0u ? mine : 1u; nx = cnt > 0u ? cnt : 1u;
; }
; __device__ __forceinline__ void xcd_barrier(const XcdBarrier& b) {
;     asm volatile("s_waitcnt vmcnt(0)" ::: "memory");
;     __syncthreads();
;     if (otid() == 0) {
;         unsigned* bar = b.bar;
;         __builtin_amdgcn_s_waitcnt(0);
;         unsigned nloc = b.st[0], nx = b.st[1];
;         if (nloc == 0u) { xcd_barrier_complete(bar, b.x, nloc, nx); b.st[0] = nloc; b.st[1] = nx; }
.LBB0_2932:
	s_mov_b64 s[0:1], s[24:25]
	s_mov_b32 s0, s100
	s_waitcnt lgkmcnt(0)
	s_cmp_gt_i32 s0, 20
	s_cbranch_scc1 .LBB0_2990
	s_mov_b64 s[0:1], s[24:25]
	s_mov_b32 s0, s101
	s_waitcnt lgkmcnt(0)
	s_cmp_lt_i32 s0, 21
	s_cbranch_scc1 .LBB0_2989
	v_readlane_b32 s0, v255, 0
	v_readlane_b32 s1, v255, 1
	s_mov_b32 s0, s100
	s_waitcnt lgkmcnt(0)
	s_cmp_gt_i32 s0, 21
	s_cbranch_scc1 .LBB0_2989
	v_readlane_b32 s0, v255, 0
	v_readlane_b32 s1, v255, 1
	s_mov_b32 s0, s101
	s_waitcnt lgkmcnt(0)
	s_cmp_lt_i32 s0, 22
	s_cbranch_scc1 .LBB0_2989
	v_readlane_b32 s2, v255, 0
	v_readlane_b32 s3, v255, 1
	s_getreg_b32 s4, hwreg(HW_REG_XCC_ID, 0, 4)
	s_waitcnt vmcnt(0)
	v_mov_b32_e32 v1, v0
	s_waitcnt vmcnt(0)
	s_barrier
	s_nop 0
	v_cmp_eq_u32_e32 vcc, 0, v1
	s_and_saveexec_b64 s[0:1], vcc
	s_cbranch_execz .LBB0_2988
	s_add_i32 s5, 0, 0x20020
	v_mov_b32_e32 v1, s5
	s_mov_b64 s[2:3], s[98:99]
	s_waitcnt vmcnt(0) expcnt(0) lgkmcnt(0)
	ds_read_b32 v3, v1
	s_add_i32 s5, 0, 0x20024
	v_mov_b32_e32 v1, s5
	ds_read_b32 v1, v1
	s_and_b32 s33, s4, 15
	s_waitcnt lgkmcnt(1)
	v_cmp_ne_u32_e32 vcc, 0, v3
	s_cbranch_vccnz .LBB0_2952
	v_readlane_b32 s4, v255, 0
	v_readlane_b32 s5, v255, 1
	s_load_dwordx2 s[8:9], s[4:5], 0xe0
	s_load_dword s7, s[4:5], 0xe8
	s_add_u32 s4, s2, 0x4200
	s_addc_u32 s5, s3, 0
	s_add_u32 s6, s2, 0x4400
	s_waitcnt lgkmcnt(0)
	s_mul_i32 s46, s9, s8
	s_mul_i32 s46, s46, s7
	s_addc_u32 s7, s3, 0
	s_add_u32 s8, s2, 0x4500
	s_addc_u32 s9, s3, 0
	s_add_u32 s10, s2, 0x4600
	s_addc_u32 s11, s3, 0
	s_add_u32 s12, s2, 0x4700
	s_addc_u32 s13, s3, 0
	s_add_u32 s14, s2, 0x4800
	s_addc_u32 s15, s3, 0
	s_add_u32 s16, s2, 0x4900
	s_addc_u32 s17, s3, 0
	s_add_u32 s18, s2, 0x4a00
	s_addc_u32 s19, s3, 0
	s_add_u32 s20, s2, 0x4b00
	s_addc_u32 s21, s3, 0
	s_add_u32 s22, s2, 0x4c00
	s_addc_u32 s23, s3, 0
	s_add_u32 s24, s2, 0x4d00
	s_addc_u32 s25, s3, 0
	s_add_u32 s26, s2, 0x4e00
	s_addc_u32 s27, s3, 0
	s_add_u32 s28, s2, 0x4f00
	s_addc_u32 s29, s3, 0
	s_add_u32 s30, s2, 0x5000
	s_addc_u32 s31, s3, 0
	s_add_u32 s34, s2, 0x5100
	s_addc_u32 s35, s3, 0
	s_add_u32 s36, s2, 0x5200
	s_addc_u32 s37, s3, 0
	s_add_u32 s38, s2, 0x5300
	s_addc_u32 s39, s3, 0
	s_mov_b32 s47, 1
	v_mov_b32_e32 v17, 0
	s_branch .LBB0_2940

; #define LAS __attribute__((address_space(3)))
; __device__ __forceinline__ int otid() { int t = threadIdx.x; asm volatile("" : "+v"(t)); return t; }
; __device__ __forceinline__ MoeTab moe_tables(CArgs& A, int l, LAS unsigned char* lds, bool want_order) {
;     MoeTab T; T.cnt = (LAS int*)(lds + LDS_TAB + 256); T.ts = T.cnt + 64; T.ord = (LAS int*)(lds + LDS_TAB + 1024) + 1;
;     unsigned* cg = (unsigned*)(A.ws + WS_CTL) + CW_CNT + l * 64;
;     const int tt = otid();
;     __syncthreads();
;     if (tt < 64) {
;         const int e = tt; const int c = (int)__hip_atomic_load(cg + e, RLX_AGENT);
;         T.cnt[e] = c;
;         const int nall = (c + 255) >> 8; const int ia = wave_incl_scan(nall, e);
;         T.ts[e] = ia - nall; if (e == 63) T.ts[64] = ia;
; __device__ __forceinline__ void combine_phase(CArgs& A, int l, const float* xin, LAS unsigned char* lds, int vcu, int G) {
;     int tid = threadIdx.x; asm volatile("" : "+v"(tid));
;     const int lane = tid & 63, wave = __builtin_amdgcn_readfirstlane(tid >> 6);
;     const MoeTab T = moe_tables(A, l, lds, false);
.LBB0_2990:
	s_mov_b64 s[0:1], s[24:25]
	s_mov_b32 s0, s100
	s_waitcnt lgkmcnt(0)
	s_cmp_gt_i32 s0, 21
	s_cbranch_scc1 .LBB0_2999
	s_mov_b64 s[0:1], s[24:25]
	s_mov_b32 s0, s101
	s_waitcnt lgkmcnt(0)
	s_cmp_lt_i32 s0, 22
	s_cbranch_scc1 .LBB0_2999
	s_mov_b64 s[10:11], s[24:25]
	s_mov_b64 s[4:5], s[98:99]
	v_mov_b32_e32 v1, v0
	v_mov_b32_e32 v2, v0
	s_waitcnt vmcnt(0) lgkmcnt(0)
	v_readfirstlane_b32 s2, v1
	v_cmp_gt_i32_e32 vcc, 64, v2
	s_barrier
	s_and_saveexec_b64 s[0:1], vcc
	s_cbranch_execz .LBB0_2995
	v_ashrrev_i32_e32 v3, 31, v2
	v_mul_u32_u24_e32 v4, 0x1100, v2
	v_mov_b32_e32 v5, 0
	v_lshl_add_u64 v[4:5], v[4:5], 0, s[4:5]
	v_add_co_u32_e32 v4, vcc, 0xc4000, v4
	s_nop 1
	v_addc_co_u32_e32 v5, vcc, 0, v5, vcc
	global_load_dword v3, v[4:5], off sc1
	v_mbcnt_lo_u32_b32 v5, -1, 0
	v_mbcnt_hi_u32_b32 v5, -1, v5
	v_and_b32_e32 v6, 64, v5
	v_add_u32_e32 v7, -1, v5
	v_cmp_lt_i32_e32 vcc, v7, v6
	v_add_u32_e32 v8, -2, v5
	v_add_u32_e32 v9, -4, v5
	v_cndmask_b32_e32 v7, v7, v5, vcc
	v_lshlrev_b32_e32 v7, 2, v7
	v_cmp_lt_i32_e32 vcc, v8, v6
	v_add_u32_e32 v10, -8, v5
	v_add_u32_e32 v11, -16, v5
	v_cndmask_b32_e32 v8, v8, v5, vcc
	v_cmp_lt_i32_e32 vcc, 0, v2
	v_lshlrev_b32_e32 v8, 2, v8
	v_subrev_u32_e32 v12, 32, v5
	v_lshl_add_u32 v4, v2, 2, 0
	s_waitcnt vmcnt(0)
	v_add_u32_e32 v13, 0xff, v3
	v_ashrrev_i32_e32 v13, 8, v13
	ds_bpermute_b32 v7, v7, v13
	s_waitcnt lgkmcnt(0)
	v_cndmask_b32_e32 v7, 0, v7, vcc
	v_add_u32_e32 v7, v7, v13
	ds_bpermute_b32 v8, v8, v7
	v_cmp_lt_i32_e32 vcc, v9, v6
	s_nop 1
	v_cndmask_b32_e32 v9, v9, v5, vcc
	v_cmp_lt_i32_e32 vcc, 1, v2
	v_lshlrev_b32_e32 v9, 2, v9
	s_waitcnt lgkmcnt(0)
	v_cndmask_b32_e32 v8, 0, v8, vcc
	v_add_u32_e32 v7, v8, v7
	ds_bpermute_b32 v8, v9, v7
	v_cmp_lt_i32_e32 vcc, v10, v6
	s_nop 1
	v_cndmask_b32_e32 v9, v10, v5, vcc
	v_cmp_lt_i32_e32 vcc, 3, v2
	v_lshlrev_b32_e32 v9, 2, v9
	s_waitcnt lgkmcnt(0)
	v_cndmask_b32_e32 v8, 0, v8, vcc
	v_add_u32_e32 v7, v8, v7
	ds_bpermute_b32 v8, v9, v7
	v_cmp_lt_i32_e32 vcc, v11, v6
	s_nop 1
	v_cndmask_b32_e32 v9, v11, v5, vcc
	v_cmp_lt_i32_e32 vcc, 7, v2
	v_lshlrev_b32_e32 v9, 2, v9
	s_waitcnt lgkmcnt(0)
	v_cndmask_b32_e32 v8, 0, v8, vcc
	v_add_u32_e32 v7, v8, v7
	ds_bpermute_b32 v8, v9, v7
	v_cmp_lt_i32_e32 vcc, v12, v6
	s_nop 1
	v_cndmask_b32_e32 v5, v12, v5, vcc
	v_cmp_lt_i32_e32 vcc, 15, v2
	v_lshlrev_b32_e32 v5, 2, v5
	s_waitcnt lgkmcnt(0)
	v_cndmask_b32_e32 v6, 0, v8, vcc
	v_add_u32_e32 v6, v6, v7
	ds_bpermute_b32 v5, v5, v6
	v_add_u32_e32 v7, 0x20100, v4
	v_cmp_lt_i32_e32 vcc, 31, v2
	ds_write_b32 v7, v3
	v_add_u32_e32 v4, 0x20200, v4
	s_waitcnt lgkmcnt(1)
	v_cndmask_b32_e32 v3, 0, v5, vcc
	v_add_u32_e32 v3, v3, v6
	v_sub_u32_e32 v5, v3, v13
	v_cmp_eq_u32_e32 vcc, 63, v2
	ds_write_b32 v4, v5
	s_and_b64 exec, exec, vcc
	s_add_i32 s3, 0, 0x20300
	v_mov_b32_e32 v2, s3
	ds_write_b32 v2, v3

; __device__ __forceinline__ int otid() { int t = threadIdx.x; asm volatile("" : "+v"(t)); return t; }
; __device__ __forceinline__ unsigned xb_ld(unsigned* p)              { return __hip_atomic_load(p, __ATOMIC_RELAXED, __HIP_MEMORY_SCOPE_AGENT); }
; __device__ __forceinline__ void xcd_barrier_complete(unsigned* bar, unsigned x, unsigned& nloc, unsigned& nx) {
;     const unsigned G = gridDim.x * gridDim.y * gridDim.z;
;     unsigned sum, cnt, mine, sp = 0u;
;     for (;;) {
;         sum = 0u; cnt = 0u; mine = 0u;
; #pragma unroll
;         for (unsigned j = 0; j < 16; ++j) { const unsigned c = xb_ld(&bar[XB_XCNT(j)]); sum += c; cnt += (c > 0u) ? 1u : 0u; mine = (j == x) ? c : mine; }
;         if (sum == G) break;
;         __builtin_amdgcn_s_sleep(1);
;         if ((++sp & 255u) == 0u) { if (xb_ld(&bar[XB_TMO])) break; if (sp > XB_SPIN_CAP) { atomicAdd(&bar[XB_TMO], 1u); break; } }
;     }
;     nloc = mine > 0u ? mine : 1u; nx = cnt > 0u ? cnt : 1u;
; }
; __device__ __forceinline__ void xcd_barrier(const XcdBarrier& b) {
;     asm volatile("s_waitcnt vmcnt(0)" ::: "memory");
;     __syncthreads();
;     if (otid() == 0) {
;         unsigned* bar = b.bar;
;         __builtin_amdgcn_s_waitcnt(0);
;         unsigned nloc = b.st[0], nx = b.st[1];
;         if (nloc == 0u) { xcd_barrier_complete(bar, b.x, nloc, nx); b.st[0] = nloc; b.st[1] = nx; }
.LBB0_2999:
	s_mov_b64 s[0:1], s[24:25]
	s_mov_b32 s0, s100
	s_waitcnt lgkmcnt(0)
	s_cmp_gt_i32 s0, 21
	s_cbranch_scc1 .LBB0_3056
	s_mov_b64 s[0:1], s[24:25]
	s_mov_b32 s0, s101
	s_waitcnt lgkmcnt(0)
	s_cmp_lt_i32 s0, 22
	s_cbranch_scc1 .LBB0_3056
	s_mov_b64 s[0:1], s[24:25]
	s_mov_b32 s0, s100
	s_waitcnt lgkmcnt(0)
	s_cmp_gt_i32 s0, 22
	s_cbranch_scc1 .LBB0_3056
	s_mov_b64 s[0:1], s[24:25]
	s_mov_b32 s0, s101
	s_waitcnt lgkmcnt(0)
	s_cmp_lt_i32 s0, 23
	s_cbranch_scc1 .LBB0_3056
	s_mov_b64 s[2:3], s[24:25]
	s_getreg_b32 s4, hwreg(HW_REG_XCC_ID, 0, 4)
	s_waitcnt vmcnt(0)
	s_waitcnt vmcnt(0)
	s_barrier
	s_nop 0
	v_cmp_eq_u32_e32 vcc, 0, v0
	s_and_saveexec_b64 s[0:1], vcc
	s_cbranch_execz .LBB0_3055
	s_add_i32 s5, 0, 0x20020
	v_mov_b32_e32 v0, s5
	s_mov_b64 s[2:3], s[98:99]
	s_waitcnt vmcnt(0) expcnt(0) lgkmcnt(0)
	ds_read_b32 v2, v0
	s_add_i32 s5, 0, 0x20024
	v_mov_b32_e32 v0, s5
	ds_read_b32 v0, v0
	s_and_b32 s33, s4, 15
	s_waitcnt lgkmcnt(1)
	v_cmp_ne_u32_e32 vcc, 0, v2
	s_cbranch_vccnz .LBB0_3019
	v_readlane_b32 s4, v255, 0
	v_readlane_b32 s5, v255, 1
	s_load_dwordx2 s[8:9], s[4:5], 0xe0
	s_load_dword s7, s[4:5], 0xe8
	s_add_u32 s4, s2, 0x4200
	s_addc_u32 s5, s3, 0
	s_add_u32 s6, s2, 0x4400
	s_waitcnt lgkmcnt(0)
	s_mul_i32 s46, s9, s8
	s_mul_i32 s46, s46, s7
	s_addc_u32 s7, s3, 0
	s_add_u32 s8, s2, 0x4500
	s_addc_u32 s9, s3, 0
	s_add_u32 s10, s2, 0x4600
	s_addc_u32 s11, s3, 0
	s_add_u32 s12, s2, 0x4700
	s_addc_u32 s13, s3, 0
	s_add_u32 s14, s2, 0x4800
	s_addc_u32 s15, s3, 0
	s_add_u32 s16, s2, 0x4900
	s_addc_u32 s17, s3, 0
	s_add_u32 s18, s2, 0x4a00
	s_addc_u32 s19, s3, 0
	s_add_u32 s20, s2, 0x4b00
	s_addc_u32 s21, s3, 0
	s_add_u32 s22, s2, 0x4c00
	s_addc_u32 s23, s3, 0
	s_add_u32 s24, s2, 0x4d00
	s_addc_u32 s25, s3, 0
	s_add_u32 s26, s2, 0x4e00
	s_addc_u32 s27, s3, 0
	s_add_u32 s28, s2, 0x4f00
	s_addc_u32 s29, s3, 0
	s_add_u32 s30, s2, 0x5000
	s_addc_u32 s31, s3, 0
	s_add_u32 s34, s2, 0x5100
	s_addc_u32 s35, s3, 0
	s_add_u32 s36, s2, 0x5200
	s_addc_u32 s37, s3, 0
	s_add_u32 s38, s2, 0x5300
	s_addc_u32 s39, s3, 0
	s_mov_b32 s47, 1
	v_mov_b32_e32 v16, 0
	s_branch .LBB0_3007

; #define LAS __attribute__((address_space(3)))
; __global__ void __launch_bounds__(NTHREADS, 2) fwd_kernel(const Args A_unused) {
;     extern __shared__ __attribute__((aligned(16))) unsigned char lds_raw[];
;     LAS unsigned char* lds = (LAS unsigned char*)lds_raw;
;     constexpr int G = 256;
;     const int bx = blockIdx.x; const int vcu = (bx % 8) * (G / 8) + bx / 8;
	.amdhsa_kernel _Z10fwd_kernel4Args
		.amdhsa_group_segment_fixed_size 0
		.amdhsa_private_segment_fixed_size 0
		.amdhsa_kernarg_size 480
		.amdhsa_user_sgpr_count 2
		.amdhsa_user_sgpr_dispatch_ptr 0
		.amdhsa_user_sgpr_queue_ptr 0
		.amdhsa_user_sgpr_kernarg_segment_ptr 1
		.amdhsa_user_sgpr_dispatch_id 0
		.amdhsa_user_sgpr_kernarg_preload_length 0
		.amdhsa_user_sgpr_kernarg_preload_offset 0
		.amdhsa_user_sgpr_private_segment_size 0
		.amdhsa_uses_dynamic_stack 0
		.amdhsa_enable_private_segment 0
		.amdhsa_system_sgpr_workgroup_id_x 1
		.amdhsa_system_sgpr_workgroup_id_y 0
		.amdhsa_system_sgpr_workgroup_id_z 0
		.amdhsa_system_sgpr_workgroup_info 0
		.amdhsa_system_vgpr_workitem_id 0
		.amdhsa_next_free_vgpr 256
		.amdhsa_next_free_sgpr 102
		.amdhsa_accum_offset 256
		.amdhsa_reserve_vcc 1
		.amdhsa_float_round_mode_32 0
		.amdhsa_float_round_mode_16_64 0
		.amdhsa_float_denorm_mode_32 3
		.amdhsa_float_denorm_mode_16_64 3
		.amdhsa_dx10_clamp 1
		.amdhsa_ieee_mode 1
		.amdhsa_fp16_overflow 0
		.amdhsa_tg_split 0
		.amdhsa_exception_fp_ieee_invalid_op 0
		.amdhsa_exception_fp_denorm_src 0
		.amdhsa_exception_fp_ieee_div_zero 0
		.amdhsa_exception_fp_ieee_overflow 0
		.amdhsa_exception_fp_ieee_underflow 0
		.amdhsa_exception_fp_ieee_inexact 0
		.amdhsa_exception_int_div_zero 0
	.end_amdhsa_kernel

; __global__ void __launch_bounds__(NTHREADS, 2) fwd_kernel(const Args A_unused) {
amdhsa.kernels:
  - .agpr_count:     0
    .args:
      - .offset:         0
        .size:           224
        .value_kind:     by_value
      - .offset:         224
        .size:           4
        .value_kind:     hidden_block_count_x
      - .offset:         228
        .size:           4
        .value_kind:     hidden_block_count_y
      - .offset:         232
        .size:           4
        .value_kind:     hidden_block_count_z
      - .offset:         236
        .size:           2
        .value_kind:     hidden_group_size_x
      - .offset:         238
        .size:           2
        .value_kind:     hidden_group_size_y
      - .offset:         240
        .size:           2
        .value_kind:     hidden_group_size_z
      - .offset:         242
        .size:           2
        .value_kind:     hidden_remainder_x
      - .offset:         244
        .size:           2
        .value_kind:     hidden_remainder_y
      - .offset:         246
        .size:           2
        .value_kind:     hidden_remainder_z
      - .offset:         264
        .size:           8
        .value_kind:     hidden_global_offset_x
      - .offset:         272
        .size:           8
        .value_kind:     hidden_global_offset_y
      - .offset:         280
        .size:           8
        .value_kind:     hidden_global_offset_z
      - .offset:         288
        .size:           2
        .value_kind:     hidden_grid_dims
      - .offset:         344
        .size:           4
        .value_kind:     hidden_dynamic_lds_size
    .group_segment_fixed_size: 0
    .kernarg_segment_align: 8
    .kernarg_segment_size: 480
    .language:       OpenCL C
    .language_version:
      - 2
      - 0
    .max_flat_workgroup_size: 512
    .name:           _Z10fwd_kernel4Args
    .private_segment_fixed_size: 0
    .sgpr_count:     108
    .sgpr_spill_count: 109
    .symbol:         _Z10fwd_kernel4Args.kd
    .uniform_work_group_size: 1
    .uses_dynamic_stack: false
    .vgpr_count:     256
    .vgpr_spill_count: 0
    .wavefront_size: 64
